# v18 + light K-loop load phases: LDS-DMA issue starts at the top of the phase, ds_reads interleaved behind the m0 writes (s_nop pads removed); reads only move later
# speedup vs baseline: 1.0061x; 1.0061x over previous
;     __device__ __forceinline__ unsigned a_off(const Unit& u, const Gemm& g) const { return (unsigned)u.pm * (unsigned)(BM * 2) * (unsigned)g.K; }
; template <class Epi, class Sched, bool ALIGN_EPI = false, bool SP2 = false, bool FP8 = false>
; __device__ __forceinline__ void gemm_phase(LAS unsigned char* lds, const Gemm g, const Sched& S, const Epi& E, int wbase) {
;     ...
;         const bool has_next = S.next(ui + 1, nxt);
;         const unsigned nA = has_next ? S.a_off(nxt, g) : cA, nB = has_next ? S.b_off(nxt, g) : cB;
;         const rsrc_t rAn = (Sched::TWO && has_next) ? (nxt.part ? rA1 : rA0) : rAc, rBn = (Sched::TWO && has_next) ? (nxt.part ? rB1 : rB0) : rBc;
;         float pre_[8] = {0.f, 0.f, 0.f, 0.f, 0.f, 0.f, 0.f, 0.f};
;         if constexpr (Epi::HAS_PRE) E.pre_load(pre_, cur, wr);
;         for (int t = 0; t < nt; t += 2) {
;             const bool last = (t == nt - 2);
;             const unsigned a1 = cA + (unsigned)(t + 1) * kstep;
;             const unsigned a2 = last ? nA : cA + (unsigned)(t + 2) * kstep, b2 = last ? nB : cB + (unsigned)(t + 2) * kstep; const rsrc_t rA2 = (Sched::TWO && last) ? rAn : rAc, rB2 = (Sched::TWO && last) ? rBn : rBc;
;             const unsigned a3 = a2 + kstep, b3 = b2 + kstep;
;             if (last && has_next) S.a_ready(nxt);
;             if constexpr (SP2) {
;             PG8_LDB(B0, 0, 0); PG8_LDB(B1, 0, 1); PG8_SCHED; PG8_LDA(At, 0, 0); PG8_STAGE(PG8_SA(1, 1), rAc, a1 + hstep, voffA);
;             PG8_WAIT_V(8); PG8_WAIT_L(0); PG8_BAR; PG8_MMA(0, 0, At, B0); PG8_MMA(0, 1, At, B1); PG8_BAR; PG8_SCHED;
;             PG8_LDA(At, 0, 1); PG8_STAGE(PG8_SB(0, 0), rB2, b2, voffB); PG8_STAGE(PG8_SB(0, 1), rB2, b2 + hstep, voffB); PG8_STAGE(PG8_SA(0, 0), rA2, a2, voffA);
;             PG8_WAIT_V(8); PG8_WAIT_L(0); PG8_BAR; PG8_MMA(1, 0, At, B0); PG8_MMA(1, 1, At, B1); PG8_BAR; PG8_SCHED;
;             PG8_LDB(B0, 1, 0); PG8_LDB(B1, 1, 1); PG8_SCHED; PG8_LDA(At, 1, 0); PG8_STAGE(PG8_SA(0, 1), rA2, a2 + hstep, voffA);
;             PG8_WAIT_V(8); PG8_WAIT_L(0); PG8_BAR; PG8_MMA(0, 0, At, B0); PG8_MMA(0, 1, At, B1); PG8_BAR; PG8_SCHED;
;             PG8_LDA(At, 1, 1); PG8_STAGE(PG8_SB(1, 0), rB2, b3, voffB); PG8_STAGE(PG8_SB(1, 1), rB2, b3 + hstep, voffB); PG8_STAGE(PG8_SA(1, 0), rA2, a3, voffA);
;             PG8_WAIT_V(8); PG8_WAIT_L(0); PG8_BAR; PG8_MMA(1, 0, At, B0); PG8_MMA(1, 1, At, B1); PG8_BAR; PG8_SCHED;
.LBB0_256:
	s_lshl_b32 s82, s1, 18
	s_andn2_b64 vcc, exec, s[66:67]
	s_lshl_b32 s83, s21, 18
	s_cbranch_vccnz .LBB0_260
	s_and_b64 s[2:3], s[26:27], exec
	s_waitcnt vmcnt(37)
	s_waitcnt vmcnt(36)
	s_waitcnt vmcnt(35)
	s_waitcnt vmcnt(32)
	s_waitcnt vmcnt(31)
	s_waitcnt vmcnt(28)
	s_waitcnt vmcnt(27)
	s_waitcnt vmcnt(24)
	s_waitcnt vmcnt(23)
	s_waitcnt vmcnt(22)
	v_mov_b32_e32 v231, v164
	v_mov_b32_e32 v230, 0xff61b1e6
	v_mov_b32_e32 v175, v233
	s_cselect_b32 s2, s82, s29
	s_cselect_b32 s3, s83, s28
	s_add_i32 s16, s29, 0x80
	s_addk_i32 s28, 0x100
	s_mov_b32 s29, 0
	ds_read_b128 v[128:131], v252
	ds_read_b128 v[132:135], v252 offset:1024
	ds_read_b128 v[136:139], v252 offset:2048
	ds_read_b128 v[140:143], v252 offset:3072
	ds_read_b128 v[144:147], v225
	ds_read_b128 v[148:151], v225 offset:1024
	ds_read_b128 v[152:155], v225 offset:2048
	ds_read_b128 v[156:159], v225 offset:3072
	s_add_i32 s6, s16, 0x80
	s_cmp_eq_u32 s18, s29
	s_cselect_b32 s46, s2, s6
	s_cselect_b32 s31, s3, s28
	s_or_b32 s30, s46, 0x80
	s_add_i32 s6, s41, s16
	s_mov_b32 m0, s19
	ds_read_b128 v[176:179], v172
	ds_read_b128 v[180:183], v172 offset:1024
	ds_read_b128 v[184:187], v172 offset:2048
	ds_read_b128 v[188:191], v172 offset:3072
	ds_read_b128 v[194:197], v172 offset:4096
	ds_read_b128 v[198:201], v172 offset:5120
	ds_read_b128 v[202:205], v172 offset:6144
	ds_read_b128 v[206:209], v172 offset:7168
	buffer_load_dwordx4 v192, s[36:39], s6 offen lds
	s_mov_b32 m0, s20
	s_nop 0
	buffer_load_dwordx4 v223, s[36:39], s6 offen lds
	s_waitcnt vmcnt(8)
	s_waitcnt lgkmcnt(0)
	s_barrier
	s_setprio 1
	v_mfma_f32_16x16x128_f8f6f4 v[124:127], v[128:135], v[176:183], 0
	v_mfma_f32_16x16x128_f8f6f4 v[120:123], v[136:143], v[176:183], 0
	v_mfma_f32_16x16x128_f8f6f4 v[108:111], v[128:135], v[184:191], 0
	v_mfma_f32_16x16x128_f8f6f4 v[104:107], v[136:143], v[184:191], 0
	v_mfma_f32_16x16x128_f8f6f4 v[160:163], v[128:135], v[194:201], 0
	v_mfma_f32_16x16x128_f8f6f4 v[210:213], v[136:143], v[194:201], 0
	v_mfma_f32_16x16x128_f8f6f4 v[214:217], v[128:135], v[202:209], 0
	v_mfma_f32_16x16x128_f8f6f4 v[218:221], v[136:143], v[202:209], 0
	v_mfma_f32_16x16x128_f8f6f4 v[116:119], v[144:151], v[176:183], 0
	v_mfma_f32_16x16x128_f8f6f4 v[112:115], v[152:159], v[176:183], 0
	v_mfma_f32_16x16x128_f8f6f4 v[100:103], v[144:151], v[184:191], 0
	v_mfma_f32_16x16x128_f8f6f4 v[96:99], v[152:159], v[184:191], 0
	v_mfma_f32_16x16x128_f8f6f4 v[176:179], v[144:151], v[194:201], 0
	v_mfma_f32_16x16x128_f8f6f4 v[180:183], v[152:159], v[194:201], 0
	v_mfma_f32_16x16x128_f8f6f4 v[184:187], v[144:151], v[202:209], 0
	v_mfma_f32_16x16x128_f8f6f4 v[188:191], v[152:159], v[202:209], 0
	s_setprio 0
	s_barrier
	s_mov_b32 m0, s43
	s_mov_b32 s6, s38
	s_mov_b32 s7, s39
	s_nop 1
	buffer_load_dwordx4 v222, s[4:7], s31 offen lds
	s_mov_b32 m0, s44
	ds_read_b128 v[64:67], v172 offset:16384
	s_add_i32 s47, s31, s41
	buffer_load_dwordx4 v193, s[4:7], s31 offen lds
	s_mov_b32 m0, s45
	ds_read_b128 v[68:71], v172 offset:17408
	buffer_load_dwordx4 v222, s[4:7], s47 offen lds
	s_mov_b32 m0, s52
	ds_read_b128 v[72:75], v172 offset:18432
	buffer_load_dwordx4 v193, s[4:7], s47 offen lds
	s_mov_b32 m0, s42
	ds_read_b128 v[76:79], v172 offset:19456
	buffer_load_dwordx4 v192, s[36:39], s46 offen lds
	s_mov_b32 m0, s53
	ds_read_b128 v[80:83], v172 offset:20480
	buffer_load_dwordx4 v223, s[36:39], s46 offen lds
	ds_read_b128 v[84:87], v172 offset:21504
	ds_read_b128 v[88:91], v172 offset:22528
	ds_read_b128 v[92:95], v172 offset:23552
	s_waitcnt vmcnt(8)
	s_waitcnt lgkmcnt(0)
	s_barrier
	s_setprio 1
	v_mfma_f32_16x16x128_f8f6f4 v[60:63], v[128:135], v[64:71], 0
	v_mfma_f32_16x16x128_f8f6f4 v[56:59], v[136:143], v[64:71], 0
	v_mfma_f32_16x16x128_f8f6f4 v[194:197], v[128:135], v[72:79], 0
	v_mfma_f32_16x16x128_f8f6f4 v[198:201], v[136:143], v[72:79], 0
	v_mfma_f32_16x16x128_f8f6f4 v[202:205], v[128:135], v[80:87], 0
	v_mfma_f32_16x16x128_f8f6f4 v[206:209], v[136:143], v[80:87], 0
	v_mfma_f32_16x16x128_f8f6f4 v[236:239], v[128:135], v[88:95], 0
	v_mfma_f32_16x16x128_f8f6f4 v[240:243], v[136:143], v[88:95], 0
	v_mfma_f32_16x16x128_f8f6f4 v[52:55], v[144:151], v[64:71], 0
	v_mfma_f32_16x16x128_f8f6f4 v[48:51], v[152:159], v[64:71], 0
	v_mfma_f32_16x16x128_f8f6f4 v[244:247], v[144:151], v[72:79], 0
	v_mfma_f32_16x16x128_f8f6f4 v[248:251], v[152:159], v[72:79], 0
	v_mfma_f32_16x16x128_f8f6f4 v[226:229], v[144:151], v[80:87], 0
	v_mfma_f32_16x16x128_f8f6f4 v[232:235], v[152:159], v[80:87], 0
	v_mfma_f32_16x16x128_f8f6f4 v[164:167], v[144:151], v[88:95], 0
	v_mfma_f32_16x16x128_f8f6f4 v[168:171], v[152:159], v[88:95], 0
	s_setprio 0
	s_barrier
	s_nop 4
	ds_read_b128 v[0:3], v173
	ds_read_b128 v[4:7], v173 offset:1024
	ds_read_b128 v[16:19], v173 offset:2048
	ds_read_b128 v[20:23], v173 offset:3072
	ds_read_b128 v[128:131], v174
	ds_read_b128 v[132:135], v174 offset:1024
	ds_read_b128 v[136:139], v174 offset:2048
	ds_read_b128 v[140:143], v174 offset:3072
	s_add_i32 s46, s46, s41
	s_mov_b32 m0, s56
	ds_read_b128 v[8:11], v172 offset:32768
	ds_read_b128 v[12:15], v172 offset:33792
	ds_read_b128 v[24:27], v172 offset:34816
	ds_read_b128 v[28:31], v172 offset:35840
	ds_read_b128 v[32:35], v172 offset:36864
	ds_read_b128 v[36:39], v172 offset:37888
	ds_read_b128 v[40:43], v172 offset:38912
	ds_read_b128 v[44:47], v172 offset:39936
	buffer_load_dwordx4 v192, s[36:39], s46 offen lds
	s_mov_b32 m0, s57
	s_nop 0
	buffer_load_dwordx4 v223, s[36:39], s46 offen lds
	s_waitcnt vmcnt(8)
	s_waitcnt lgkmcnt(0)
	s_barrier
; #define PG8_STAGE(bufoff, rs_, soff_, voff) do { _Pragma("unroll") for (int _i = 0; _i < 2; ++_i) \
;         __builtin_amdgcn_raw_ptr_buffer_load_lds(rs_, (LAS void*)(lds + (bufoff) + ldsw + _i * 8192), 16, (int)(voff)[_i], (int)(soff_), 0, 0); } while (0)
; #define PG8_LDA(dst, b, h) do { _Pragma("unroll") for (int m = 0; m < 4; ++m) dst[m] = PG8_LD2(lds + PG8_SA(b, h) + aoff + m * 2048); } while (0)
; #define PG8_LDB(dst, b, h) do { _Pragma("unroll") for (int n = 0; n < 2; ++n) dst[n] = PG8_LD2(lds + PG8_SB(b, h) + boff + n * 2048); } while (0)
; #define PG8_WAIT_V(n) asm volatile("s_waitcnt vmcnt(" #n ")" ::: "memory")
; #define PG8_WAIT_L(n) asm volatile("s_waitcnt lgkmcnt(" #n ")" ::: "memory")
; #define PG8_BAR __builtin_amdgcn_s_barrier()
; #define PG8_SCHED __builtin_amdgcn_sched_barrier(0)
; template <class Epi, class Sched, bool ALIGN_EPI = false, bool SP2 = false, bool FP8 = false>
; __device__ __forceinline__ void gemm_phase(LAS unsigned char* lds, const Gemm g, const Sched& S, const Epi& E, int wbase) {
;     ...
;             PG8_LDB(B0, 0, 0); PG8_LDB(B1, 0, 1); PG8_SCHED; PG8_LDA(At, 0, 0); PG8_STAGE(PG8_SA(1, 1), rAc, a1 + hstep, voffA);
;             PG8_WAIT_V(8); PG8_WAIT_L(0); PG8_BAR; PG8_MMA(0, 0, At, B0); PG8_MMA(0, 1, At, B1); PG8_BAR; PG8_SCHED;
;             PG8_LDA(At, 0, 1); PG8_STAGE(PG8_SB(0, 0), rB2, b2, voffB); PG8_STAGE(PG8_SB(0, 1), rB2, b2 + hstep, voffB); PG8_STAGE(PG8_SA(0, 0), rA2, a2, voffA);
;             PG8_WAIT_V(8); PG8_WAIT_L(0); PG8_BAR; PG8_MMA(1, 0, At, B0); PG8_MMA(1, 1, At, B1); PG8_BAR; PG8_SCHED;
;             PG8_LDB(B0, 1, 0); PG8_LDB(B1, 1, 1); PG8_SCHED; PG8_LDA(At, 1, 0); PG8_STAGE(PG8_SA(0, 1), rA2, a2 + hstep, voffA);
;             PG8_WAIT_V(8); PG8_WAIT_L(0); PG8_BAR; PG8_MMA(0, 0, At, B0); PG8_MMA(0, 1, At, B1); PG8_BAR; PG8_SCHED;
;             PG8_LDA(At, 1, 1); PG8_STAGE(PG8_SB(1, 0), rB2, b3, voffB); PG8_STAGE(PG8_SB(1, 1), rB2, b3 + hstep, voffB); PG8_STAGE(PG8_SA(1, 0), rA2, a3, voffA);
;             PG8_WAIT_V(8); PG8_WAIT_L(0); PG8_BAR; PG8_MMA(1, 0, At, B0); PG8_MMA(1, 1, At, B1); PG8_BAR; PG8_SCHED;
	s_setprio 1
	v_mfma_f32_16x16x128_f8f6f4 v[124:127], v[0:7], v[8:15], v[124:127]
	v_mfma_f32_16x16x128_f8f6f4 v[120:123], v[16:23], v[8:15], v[120:123]
	v_mfma_f32_16x16x128_f8f6f4 v[108:111], v[0:7], v[24:31], v[108:111]
	v_mfma_f32_16x16x128_f8f6f4 v[104:107], v[16:23], v[24:31], v[104:107]
	v_mfma_f32_16x16x128_f8f6f4 v[92:95], v[0:7], v[32:39], v[160:163]
	v_mfma_f32_16x16x128_f8f6f4 v[88:91], v[16:23], v[32:39], v[210:213]
	v_mfma_f32_16x16x128_f8f6f4 v[76:79], v[0:7], v[40:47], v[214:217]
	v_mfma_f32_16x16x128_f8f6f4 v[72:75], v[16:23], v[40:47], v[218:221]
	v_mfma_f32_16x16x128_f8f6f4 v[116:119], v[128:135], v[8:15], v[116:119]
	v_mfma_f32_16x16x128_f8f6f4 v[112:115], v[136:143], v[8:15], v[112:115]
	v_mfma_f32_16x16x128_f8f6f4 v[100:103], v[128:135], v[24:31], v[100:103]
	v_mfma_f32_16x16x128_f8f6f4 v[96:99], v[136:143], v[24:31], v[96:99]
	v_mfma_f32_16x16x128_f8f6f4 v[84:87], v[128:135], v[32:39], v[176:179]
	v_mfma_f32_16x16x128_f8f6f4 v[80:83], v[136:143], v[32:39], v[180:183]
	v_mfma_f32_16x16x128_f8f6f4 v[68:71], v[128:135], v[40:47], v[184:187]
	v_mfma_f32_16x16x128_f8f6f4 v[64:67], v[136:143], v[40:47], v[188:191]
	s_setprio 0
	s_barrier
	s_mov_b32 m0, s58
	s_bitset1_b32 s31, 7
	buffer_load_dwordx4 v222, s[4:7], s31 offen lds
	s_mov_b32 m0, s59
	ds_read_b128 v[32:35], v172 offset:49152
	buffer_load_dwordx4 v193, s[4:7], s31 offen lds
	s_add_i32 s31, s31, s41
	s_mov_b32 m0, s65
	ds_read_b128 v[36:39], v172 offset:50176
	buffer_load_dwordx4 v222, s[4:7], s31 offen lds
	s_mov_b32 m0, s33
	ds_read_b128 v[144:147], v172 offset:51200
	buffer_load_dwordx4 v193, s[4:7], s31 offen lds
	s_mov_b32 m0, s12
	ds_read_b128 v[148:151], v172 offset:52224
	buffer_load_dwordx4 v192, s[36:39], s30 offen lds
	s_mov_b32 m0, s13
	ds_read_b128 v[152:155], v172 offset:53248
	buffer_load_dwordx4 v223, s[36:39], s30 offen lds
	ds_read_b128 v[156:159], v172 offset:54272
	ds_read_b128 v[176:179], v172 offset:55296
	ds_read_b128 v[180:183], v172 offset:56320
	s_waitcnt vmcnt(8)
	s_waitcnt lgkmcnt(0)
	s_barrier
	s_setprio 1
	v_mfma_f32_16x16x128_f8f6f4 v[60:63], v[0:7], v[32:39], v[60:63]
	v_mfma_f32_16x16x128_f8f6f4 v[56:59], v[16:23], v[32:39], v[56:59]
	v_mfma_f32_16x16x128_f8f6f4 v[44:47], v[0:7], v[144:151], v[194:197]
	v_mfma_f32_16x16x128_f8f6f4 v[40:43], v[16:23], v[144:151], v[198:201]
	v_mfma_f32_16x16x128_f8f6f4 v[28:31], v[0:7], v[152:159], v[202:205]
	v_mfma_f32_16x16x128_f8f6f4 v[24:27], v[16:23], v[152:159], v[206:209]
	v_mfma_f32_16x16x128_f8f6f4 v[12:15], v[0:7], v[176:183], v[236:239]
	v_mfma_f32_16x16x128_f8f6f4 v[8:11], v[16:23], v[176:183], v[240:243]
	v_mfma_f32_16x16x128_f8f6f4 v[52:55], v[128:135], v[32:39], v[52:55]
	v_mfma_f32_16x16x128_f8f6f4 v[48:51], v[136:143], v[32:39], v[48:51]
	v_mfma_f32_16x16x128_f8f6f4 v[36:39], v[128:135], v[144:151], v[244:247]
	v_mfma_f32_16x16x128_f8f6f4 v[32:35], v[136:143], v[144:151], v[248:251]
	v_mfma_f32_16x16x128_f8f6f4 v[20:23], v[128:135], v[152:159], v[226:229]
	v_mfma_f32_16x16x128_f8f6f4 v[16:19], v[136:143], v[152:159], v[232:235]
	v_mfma_f32_16x16x128_f8f6f4 v[4:7], v[128:135], v[176:183], v[164:167]
	v_mfma_f32_16x16x128_f8f6f4 v[0:3], v[136:143], v[176:183], v[168:171]
	s_setprio 0
	s_barrier
	s_add_i32 s29, s29, 2
	s_addk_i32 s16, 0x100
	s_addk_i32 s28, 0x100
	s_cmp_ge_i32 s29, s77
	s_cbranch_scc0 .LBB0_258
	s_branch .Lzp_after_258
.LBB0_258:
	ds_read_b128 v[128:131], v252
	ds_read_b128 v[132:135], v252 offset:1024
	ds_read_b128 v[136:139], v252 offset:2048
	ds_read_b128 v[140:143], v252 offset:3072
	ds_read_b128 v[144:147], v225
	ds_read_b128 v[148:151], v225 offset:1024
	ds_read_b128 v[152:155], v225 offset:2048
	ds_read_b128 v[156:159], v225 offset:3072
	s_add_i32 s6, s16, 0x80
	s_cmp_eq_u32 s18, s29
	s_cselect_b32 s46, s2, s6
	s_cselect_b32 s31, s3, s28
	s_or_b32 s30, s46, 0x80
	s_add_i32 s6, s41, s16
	s_mov_b32 m0, s19
	ds_read_b128 v[176:179], v172
	ds_read_b128 v[180:183], v172 offset:1024
	ds_read_b128 v[184:187], v172 offset:2048
	ds_read_b128 v[188:191], v172 offset:3072
	ds_read_b128 v[194:197], v172 offset:4096
	ds_read_b128 v[198:201], v172 offset:5120
	ds_read_b128 v[202:205], v172 offset:6144
	ds_read_b128 v[206:209], v172 offset:7168
	buffer_load_dwordx4 v192, s[36:39], s6 offen lds
	s_mov_b32 m0, s20
	s_nop 0
	buffer_load_dwordx4 v223, s[36:39], s6 offen lds
	s_waitcnt vmcnt(8)
	s_waitcnt lgkmcnt(0)
	s_barrier
	s_setprio 1
	v_mfma_f32_16x16x128_f8f6f4 v[124:127], v[128:135], v[176:183], v[124:127]
	v_mfma_f32_16x16x128_f8f6f4 v[120:123], v[136:143], v[176:183], v[120:123]
	v_mfma_f32_16x16x128_f8f6f4 v[108:111], v[128:135], v[184:191], v[108:111]
	v_mfma_f32_16x16x128_f8f6f4 v[104:107], v[136:143], v[184:191], v[104:107]
	v_mfma_f32_16x16x128_f8f6f4 v[160:163], v[128:135], v[194:201], v[92:95]
	v_mfma_f32_16x16x128_f8f6f4 v[210:213], v[136:143], v[194:201], v[88:91]
	v_mfma_f32_16x16x128_f8f6f4 v[214:217], v[128:135], v[202:209], v[76:79]
	v_mfma_f32_16x16x128_f8f6f4 v[218:221], v[136:143], v[202:209], v[72:75]
	v_mfma_f32_16x16x128_f8f6f4 v[116:119], v[144:151], v[176:183], v[116:119]
	v_mfma_f32_16x16x128_f8f6f4 v[112:115], v[152:159], v[176:183], v[112:115]
	v_mfma_f32_16x16x128_f8f6f4 v[100:103], v[144:151], v[184:191], v[100:103]
	v_mfma_f32_16x16x128_f8f6f4 v[96:99], v[152:159], v[184:191], v[96:99]
	v_mfma_f32_16x16x128_f8f6f4 v[176:179], v[144:151], v[194:201], v[84:87]
	v_mfma_f32_16x16x128_f8f6f4 v[180:183], v[152:159], v[194:201], v[80:83]
	v_mfma_f32_16x16x128_f8f6f4 v[184:187], v[144:151], v[202:209], v[68:71]
	v_mfma_f32_16x16x128_f8f6f4 v[188:191], v[152:159], v[202:209], v[64:67]
	s_setprio 0
	s_barrier
; #define PG8_STAGE(bufoff, rs_, soff_, voff) do { _Pragma("unroll") for (int _i = 0; _i < 2; ++_i) \
;         __builtin_amdgcn_raw_ptr_buffer_load_lds(rs_, (LAS void*)(lds + (bufoff) + ldsw + _i * 8192), 16, (int)(voff)[_i], (int)(soff_), 0, 0); } while (0)
; #define PG8_LDA(dst, b, h) do { _Pragma("unroll") for (int m = 0; m < 4; ++m) dst[m] = PG8_LD2(lds + PG8_SA(b, h) + aoff + m * 2048); } while (0)
; #define PG8_LDB(dst, b, h) do { _Pragma("unroll") for (int n = 0; n < 2; ++n) dst[n] = PG8_LD2(lds + PG8_SB(b, h) + boff + n * 2048); } while (0)
; #define PG8_WAIT_V(n) asm volatile("s_waitcnt vmcnt(" #n ")" ::: "memory")
; #define PG8_WAIT_L(n) asm volatile("s_waitcnt lgkmcnt(" #n ")" ::: "memory")
; #define PG8_BAR __builtin_amdgcn_s_barrier()
; #define PG8_SCHED __builtin_amdgcn_sched_barrier(0)
; template <class Epi, class Sched, bool ALIGN_EPI = false, bool SP2 = false, bool FP8 = false>
; __device__ __forceinline__ void gemm_phase(LAS unsigned char* lds, const Gemm g, const Sched& S, const Epi& E, int wbase) {
;     ...
;             PG8_LDB(B0, 0, 0); PG8_LDB(B1, 0, 1); PG8_SCHED; PG8_LDA(At, 0, 0); PG8_STAGE(PG8_SA(1, 1), rAc, a1 + hstep, voffA);
;             PG8_WAIT_V(8); PG8_WAIT_L(0); PG8_BAR; PG8_MMA(0, 0, At, B0); PG8_MMA(0, 1, At, B1); PG8_BAR; PG8_SCHED;
;             PG8_LDA(At, 0, 1); PG8_STAGE(PG8_SB(0, 0), rB2, b2, voffB); PG8_STAGE(PG8_SB(0, 1), rB2, b2 + hstep, voffB); PG8_STAGE(PG8_SA(0, 0), rA2, a2, voffA);
;             PG8_WAIT_V(8); PG8_WAIT_L(0); PG8_BAR; PG8_MMA(1, 0, At, B0); PG8_MMA(1, 1, At, B1); PG8_BAR; PG8_SCHED;
;             PG8_LDB(B0, 1, 0); PG8_LDB(B1, 1, 1); PG8_SCHED; PG8_LDA(At, 1, 0); PG8_STAGE(PG8_SA(0, 1), rA2, a2 + hstep, voffA);
;             PG8_WAIT_V(8); PG8_WAIT_L(0); PG8_BAR; PG8_MMA(0, 0, At, B0); PG8_MMA(0, 1, At, B1); PG8_BAR; PG8_SCHED;
;             PG8_LDA(At, 1, 1); PG8_STAGE(PG8_SB(1, 0), rB2, b3, voffB); PG8_STAGE(PG8_SB(1, 1), rB2, b3 + hstep, voffB); PG8_STAGE(PG8_SA(1, 0), rA2, a3, voffA);
;             PG8_WAIT_V(8); PG8_WAIT_L(0); PG8_BAR; PG8_MMA(1, 0, At, B0); PG8_MMA(1, 1, At, B1); PG8_BAR; PG8_SCHED;
	s_mov_b32 m0, s43
	s_mov_b32 s6, s38
	s_mov_b32 s7, s39
	s_nop 1
	buffer_load_dwordx4 v222, s[4:7], s31 offen lds
	s_mov_b32 m0, s44
	ds_read_b128 v[64:67], v172 offset:16384
	s_add_i32 s47, s31, s41
	buffer_load_dwordx4 v193, s[4:7], s31 offen lds
	s_mov_b32 m0, s45
	ds_read_b128 v[68:71], v172 offset:17408
	buffer_load_dwordx4 v222, s[4:7], s47 offen lds
	s_mov_b32 m0, s52
	ds_read_b128 v[72:75], v172 offset:18432
	buffer_load_dwordx4 v193, s[4:7], s47 offen lds
	s_mov_b32 m0, s42
	ds_read_b128 v[76:79], v172 offset:19456
	buffer_load_dwordx4 v192, s[36:39], s46 offen lds
	s_mov_b32 m0, s53
	ds_read_b128 v[80:83], v172 offset:20480
	buffer_load_dwordx4 v223, s[36:39], s46 offen lds
	ds_read_b128 v[84:87], v172 offset:21504
	ds_read_b128 v[88:91], v172 offset:22528
	ds_read_b128 v[92:95], v172 offset:23552
	s_waitcnt vmcnt(8)
	s_waitcnt lgkmcnt(0)
	s_barrier
	s_setprio 1
	v_mfma_f32_16x16x128_f8f6f4 v[60:63], v[128:135], v[64:71], v[60:63]
	v_mfma_f32_16x16x128_f8f6f4 v[56:59], v[136:143], v[64:71], v[56:59]
	v_mfma_f32_16x16x128_f8f6f4 v[194:197], v[128:135], v[72:79], v[44:47]
	v_mfma_f32_16x16x128_f8f6f4 v[198:201], v[136:143], v[72:79], v[40:43]
	v_mfma_f32_16x16x128_f8f6f4 v[202:205], v[128:135], v[80:87], v[28:31]
	v_mfma_f32_16x16x128_f8f6f4 v[206:209], v[136:143], v[80:87], v[24:27]
	v_mfma_f32_16x16x128_f8f6f4 v[236:239], v[128:135], v[88:95], v[12:15]
	v_mfma_f32_16x16x128_f8f6f4 v[240:243], v[136:143], v[88:95], v[8:11]
	v_mfma_f32_16x16x128_f8f6f4 v[52:55], v[144:151], v[64:71], v[52:55]
	v_mfma_f32_16x16x128_f8f6f4 v[48:51], v[152:159], v[64:71], v[48:51]
	v_mfma_f32_16x16x128_f8f6f4 v[244:247], v[144:151], v[72:79], v[36:39]
	v_mfma_f32_16x16x128_f8f6f4 v[248:251], v[152:159], v[72:79], v[32:35]
	v_mfma_f32_16x16x128_f8f6f4 v[226:229], v[144:151], v[80:87], v[20:23]
	v_mfma_f32_16x16x128_f8f6f4 v[232:235], v[152:159], v[80:87], v[16:19]
	v_mfma_f32_16x16x128_f8f6f4 v[164:167], v[144:151], v[88:95], v[4:7]
	v_mfma_f32_16x16x128_f8f6f4 v[168:171], v[152:159], v[88:95], v[0:3]
	s_setprio 0
	s_barrier
	s_nop 4
	ds_read_b128 v[0:3], v173
	ds_read_b128 v[4:7], v173 offset:1024
	ds_read_b128 v[16:19], v173 offset:2048
	ds_read_b128 v[20:23], v173 offset:3072
	ds_read_b128 v[128:131], v174
	ds_read_b128 v[132:135], v174 offset:1024
	ds_read_b128 v[136:139], v174 offset:2048
	ds_read_b128 v[140:143], v174 offset:3072
	s_add_i32 s46, s46, s41
	s_mov_b32 m0, s56
	ds_read_b128 v[8:11], v172 offset:32768
	ds_read_b128 v[12:15], v172 offset:33792
	ds_read_b128 v[24:27], v172 offset:34816
	ds_read_b128 v[28:31], v172 offset:35840
	ds_read_b128 v[32:35], v172 offset:36864
	ds_read_b128 v[36:39], v172 offset:37888
	ds_read_b128 v[40:43], v172 offset:38912
	ds_read_b128 v[44:47], v172 offset:39936
	buffer_load_dwordx4 v192, s[36:39], s46 offen lds
	s_mov_b32 m0, s57
	s_nop 0
	buffer_load_dwordx4 v223, s[36:39], s46 offen lds
	s_waitcnt vmcnt(8)
	s_waitcnt lgkmcnt(0)
	s_barrier
	s_setprio 1
	v_mfma_f32_16x16x128_f8f6f4 v[124:127], v[0:7], v[8:15], v[124:127]
	v_mfma_f32_16x16x128_f8f6f4 v[120:123], v[16:23], v[8:15], v[120:123]
	v_mfma_f32_16x16x128_f8f6f4 v[108:111], v[0:7], v[24:31], v[108:111]
	v_mfma_f32_16x16x128_f8f6f4 v[104:107], v[16:23], v[24:31], v[104:107]
	v_mfma_f32_16x16x128_f8f6f4 v[92:95], v[0:7], v[32:39], v[160:163]
	v_mfma_f32_16x16x128_f8f6f4 v[88:91], v[16:23], v[32:39], v[210:213]
	v_mfma_f32_16x16x128_f8f6f4 v[76:79], v[0:7], v[40:47], v[214:217]
	v_mfma_f32_16x16x128_f8f6f4 v[72:75], v[16:23], v[40:47], v[218:221]
	v_mfma_f32_16x16x128_f8f6f4 v[116:119], v[128:135], v[8:15], v[116:119]
	v_mfma_f32_16x16x128_f8f6f4 v[112:115], v[136:143], v[8:15], v[112:115]
	v_mfma_f32_16x16x128_f8f6f4 v[100:103], v[128:135], v[24:31], v[100:103]
	v_mfma_f32_16x16x128_f8f6f4 v[96:99], v[136:143], v[24:31], v[96:99]
	v_mfma_f32_16x16x128_f8f6f4 v[84:87], v[128:135], v[32:39], v[176:179]
	v_mfma_f32_16x16x128_f8f6f4 v[80:83], v[136:143], v[32:39], v[180:183]
	v_mfma_f32_16x16x128_f8f6f4 v[68:71], v[128:135], v[40:47], v[184:187]
	v_mfma_f32_16x16x128_f8f6f4 v[64:67], v[136:143], v[40:47], v[188:191]
	s_setprio 0
	s_barrier
	s_mov_b32 m0, s58
	s_bitset1_b32 s31, 7
	buffer_load_dwordx4 v222, s[4:7], s31 offen lds
	s_mov_b32 m0, s59
	ds_read_b128 v[32:35], v172 offset:49152
	buffer_load_dwordx4 v193, s[4:7], s31 offen lds
	s_add_i32 s31, s31, s41
	s_mov_b32 m0, s65
	ds_read_b128 v[36:39], v172 offset:50176
	buffer_load_dwordx4 v222, s[4:7], s31 offen lds
	s_mov_b32 m0, s33
	ds_read_b128 v[144:147], v172 offset:51200
	buffer_load_dwordx4 v193, s[4:7], s31 offen lds
	s_mov_b32 m0, s12
	ds_read_b128 v[148:151], v172 offset:52224
	buffer_load_dwordx4 v192, s[36:39], s30 offen lds
	s_mov_b32 m0, s13
	ds_read_b128 v[152:155], v172 offset:53248
	buffer_load_dwordx4 v223, s[36:39], s30 offen lds
	ds_read_b128 v[156:159], v172 offset:54272
	ds_read_b128 v[176:179], v172 offset:55296
	ds_read_b128 v[180:183], v172 offset:56320
	s_waitcnt vmcnt(8)
	s_waitcnt lgkmcnt(0)
	s_barrier
	s_setprio 1
	v_mfma_f32_16x16x128_f8f6f4 v[60:63], v[0:7], v[32:39], v[60:63]
	v_mfma_f32_16x16x128_f8f6f4 v[56:59], v[16:23], v[32:39], v[56:59]
	v_mfma_f32_16x16x128_f8f6f4 v[44:47], v[0:7], v[144:151], v[194:197]
	v_mfma_f32_16x16x128_f8f6f4 v[40:43], v[16:23], v[144:151], v[198:201]
	v_mfma_f32_16x16x128_f8f6f4 v[28:31], v[0:7], v[152:159], v[202:205]
	v_mfma_f32_16x16x128_f8f6f4 v[24:27], v[16:23], v[152:159], v[206:209]
	v_mfma_f32_16x16x128_f8f6f4 v[12:15], v[0:7], v[176:183], v[236:239]
	v_mfma_f32_16x16x128_f8f6f4 v[8:11], v[16:23], v[176:183], v[240:243]
	v_mfma_f32_16x16x128_f8f6f4 v[52:55], v[128:135], v[32:39], v[52:55]
	v_mfma_f32_16x16x128_f8f6f4 v[48:51], v[136:143], v[32:39], v[48:51]
	v_mfma_f32_16x16x128_f8f6f4 v[36:39], v[128:135], v[144:151], v[244:247]
	v_mfma_f32_16x16x128_f8f6f4 v[32:35], v[136:143], v[144:151], v[248:251]
	v_mfma_f32_16x16x128_f8f6f4 v[20:23], v[128:135], v[152:159], v[226:229]
	v_mfma_f32_16x16x128_f8f6f4 v[16:19], v[136:143], v[152:159], v[232:235]
	v_mfma_f32_16x16x128_f8f6f4 v[4:7], v[128:135], v[176:183], v[164:167]
	v_mfma_f32_16x16x128_f8f6f4 v[0:3], v[136:143], v[176:183], v[168:171]
	s_setprio 0
	s_barrier
	s_add_i32 s29, s29, 2
	s_addk_i32 s16, 0x100
	s_addk_i32 s28, 0x100
	s_cmp_ge_i32 s29, s77
	s_cbranch_scc0 .LBB0_258

;     __device__ __forceinline__ unsigned a_off(const Unit& u, const Gemm& g) const { return (unsigned)u.pm * (unsigned)(BM * 2) * (unsigned)g.K; }
; template <class Epi, class Sched, bool ALIGN_EPI = false, bool SP2 = false, bool FP8 = false>
; __device__ __forceinline__ void gemm_phase(LAS unsigned char* lds, const Gemm g, const Sched& S, const Epi& E, int wbase) {
;     ...
;         const bool has_next = S.next(ui + 1, nxt);
;         const unsigned nA = has_next ? S.a_off(nxt, g) : cA, nB = has_next ? S.b_off(nxt, g) : cB;
;         const rsrc_t rAn = (Sched::TWO && has_next) ? (nxt.part ? rA1 : rA0) : rAc, rBn = (Sched::TWO && has_next) ? (nxt.part ? rB1 : rB0) : rBc;
;         float pre_[8] = {0.f, 0.f, 0.f, 0.f, 0.f, 0.f, 0.f, 0.f};
;         if constexpr (Epi::HAS_PRE) E.pre_load(pre_, cur, wr);
;         for (int t = 0; t < nt; t += 2) {
;             const bool last = (t == nt - 2);
;             const unsigned a1 = cA + (unsigned)(t + 1) * kstep;
;             const unsigned a2 = last ? nA : cA + (unsigned)(t + 2) * kstep, b2 = last ? nB : cB + (unsigned)(t + 2) * kstep; const rsrc_t rA2 = (Sched::TWO && last) ? rAn : rAc, rB2 = (Sched::TWO && last) ? rBn : rBc;
;             const unsigned a3 = a2 + kstep, b3 = b2 + kstep;
;             if (last && has_next) S.a_ready(nxt);
;             if constexpr (SP2) {
;             PG8_LDB(B0, 0, 0); PG8_LDB(B1, 0, 1); PG8_SCHED; PG8_LDA(At, 0, 0); PG8_STAGE(PG8_SA(1, 1), rAc, a1 + hstep, voffA);
;             PG8_WAIT_V(8); PG8_WAIT_L(0); PG8_BAR; PG8_MMA(0, 0, At, B0); PG8_MMA(0, 1, At, B1); PG8_BAR; PG8_SCHED;
;             PG8_LDA(At, 0, 1); PG8_STAGE(PG8_SB(0, 0), rB2, b2, voffB); PG8_STAGE(PG8_SB(0, 1), rB2, b2 + hstep, voffB); PG8_STAGE(PG8_SA(0, 0), rA2, a2, voffA);
;             PG8_WAIT_V(8); PG8_WAIT_L(0); PG8_BAR; PG8_MMA(1, 0, At, B0); PG8_MMA(1, 1, At, B1); PG8_BAR; PG8_SCHED;
;             PG8_LDB(B0, 1, 0); PG8_LDB(B1, 1, 1); PG8_SCHED; PG8_LDA(At, 1, 0); PG8_STAGE(PG8_SA(0, 1), rA2, a2 + hstep, voffA);
;             PG8_WAIT_V(8); PG8_WAIT_L(0); PG8_BAR; PG8_MMA(0, 0, At, B0); PG8_MMA(0, 1, At, B1); PG8_BAR; PG8_SCHED;
;             PG8_LDA(At, 1, 1); PG8_STAGE(PG8_SB(1, 0), rB2, b3, voffB); PG8_STAGE(PG8_SB(1, 1), rB2, b3 + hstep, voffB); PG8_STAGE(PG8_SA(1, 0), rA2, a3, voffA);
;             PG8_WAIT_V(8); PG8_WAIT_L(0); PG8_BAR; PG8_MMA(1, 0, At, B0); PG8_MMA(1, 1, At, B1); PG8_BAR; PG8_SCHED;
.LBB0_350:
	s_lshl_b32 s20, s19, 19
	s_andn2_b64 vcc, exec, s[66:67]
	s_lshl_b32 s21, s18, 19
	s_cbranch_vccnz .LBB0_430
	s_and_b64 s[2:3], s[26:27], exec
	s_waitcnt vmcnt(37)
	s_waitcnt vmcnt(36)
	s_waitcnt vmcnt(35)
	s_waitcnt vmcnt(32)
	s_waitcnt vmcnt(31)
	s_waitcnt vmcnt(28)
	s_waitcnt vmcnt(27)
	s_waitcnt vmcnt(24)
	s_waitcnt vmcnt(23)
	s_waitcnt vmcnt(22)
	s_cselect_b32 s2, s20, s29
	s_cselect_b32 s3, s21, s28
	s_add_i32 s16, s29, 0x80
	s_addk_i32 s28, 0x100
	s_mov_b32 s29, 0
	v_add_u32_e32 v140, 0x10000, v170
	v_add_u32_e32 v156, 0x14000, v170
	ds_read_b128 v[128:131], v140
	ds_read_b128 v[132:135], v140 offset:1024
	ds_read_b128 v[136:139], v140 offset:2048
	ds_read_b128 v[140:143], v140 offset:3072
	ds_read_b128 v[144:147], v156
	ds_read_b128 v[148:151], v156 offset:1024
	ds_read_b128 v[152:155], v156 offset:2048
	ds_read_b128 v[156:159], v156 offset:3072
	s_add_i32 s6, s16, 0x80
	s_cmp_eq_u32 s12, s29
	s_cselect_b32 s46, s2, s6
	s_cselect_b32 s31, s3, s28
	s_or_b32 s30, s46, 0x80
	s_add_i32 s6, s33, s16
	s_mov_b32 m0, s13
	ds_read_b128 v[160:163], v171
	ds_read_b128 v[172:175], v171 offset:1024
	ds_read_b128 v[176:179], v171 offset:2048
	ds_read_b128 v[180:183], v171 offset:3072
	ds_read_b128 v[184:187], v171 offset:4096
	ds_read_b128 v[188:191], v171 offset:5120
	ds_read_b128 v[194:197], v171 offset:6144
	ds_read_b128 v[198:201], v171 offset:7168
	buffer_load_dwordx4 v164, s[36:39], s6 offen lds
	s_mov_b32 m0, s83
	s_nop 0
	buffer_load_dwordx4 v166, s[36:39], s6 offen lds
	s_waitcnt vmcnt(8)
	s_waitcnt lgkmcnt(0)
	s_barrier
	s_setprio 1
	v_mfma_f32_16x16x32_bf16 v[124:127], v[128:131], v[160:163], 0
	v_mfma_f32_16x16x32_bf16 v[120:123], v[136:139], v[160:163], 0
	v_mfma_f32_16x16x32_bf16 v[108:111], v[128:131], v[176:179], 0
	v_mfma_f32_16x16x32_bf16 v[104:107], v[136:139], v[176:179], 0
	v_mfma_f32_16x16x32_bf16 v[92:95], v[128:131], v[184:187], 0
	v_mfma_f32_16x16x32_bf16 v[88:91], v[136:139], v[184:187], 0
	v_mfma_f32_16x16x32_bf16 v[76:79], v[128:131], v[194:197], 0
	v_mfma_f32_16x16x32_bf16 v[72:75], v[136:139], v[194:197], 0
	v_mfma_f32_16x16x32_bf16 v[124:127], v[132:135], v[172:175], v[124:127]
	v_mfma_f32_16x16x32_bf16 v[120:123], v[140:143], v[172:175], v[120:123]
	v_mfma_f32_16x16x32_bf16 v[108:111], v[132:135], v[180:183], v[108:111]
	v_mfma_f32_16x16x32_bf16 v[104:107], v[140:143], v[180:183], v[104:107]
	v_mfma_f32_16x16x32_bf16 v[92:95], v[132:135], v[188:191], v[92:95]
	v_mfma_f32_16x16x32_bf16 v[88:91], v[140:143], v[188:191], v[88:91]
	v_mfma_f32_16x16x32_bf16 v[76:79], v[132:135], v[198:201], v[76:79]
	v_mfma_f32_16x16x32_bf16 v[72:75], v[140:143], v[198:201], v[72:75]
	v_mfma_f32_16x16x32_bf16 v[116:119], v[144:147], v[160:163], 0
	v_mfma_f32_16x16x32_bf16 v[112:115], v[152:155], v[160:163], 0
	v_mfma_f32_16x16x32_bf16 v[100:103], v[144:147], v[176:179], 0
	v_mfma_f32_16x16x32_bf16 v[96:99], v[152:155], v[176:179], 0
	v_mfma_f32_16x16x32_bf16 v[84:87], v[144:147], v[184:187], 0
	v_mfma_f32_16x16x32_bf16 v[80:83], v[152:155], v[184:187], 0
	v_mfma_f32_16x16x32_bf16 v[68:71], v[144:147], v[194:197], 0
	v_mfma_f32_16x16x32_bf16 v[64:67], v[152:155], v[194:197], 0
	v_mfma_f32_16x16x32_bf16 v[116:119], v[148:151], v[172:175], v[116:119]
	v_mfma_f32_16x16x32_bf16 v[112:115], v[156:159], v[172:175], v[112:115]
	v_mfma_f32_16x16x32_bf16 v[100:103], v[148:151], v[180:183], v[100:103]
	v_mfma_f32_16x16x32_bf16 v[96:99], v[156:159], v[180:183], v[96:99]
	v_mfma_f32_16x16x32_bf16 v[84:87], v[148:151], v[188:191], v[84:87]
	v_mfma_f32_16x16x32_bf16 v[80:83], v[156:159], v[188:191], v[80:83]
	v_mfma_f32_16x16x32_bf16 v[68:71], v[148:151], v[198:201], v[68:71]
	v_mfma_f32_16x16x32_bf16 v[64:67], v[156:159], v[198:201], v[64:67]
	s_setprio 0
	s_barrier
	s_mov_b32 m0, s42
	s_mov_b32 s6, s38
	s_mov_b32 s7, s39
	buffer_load_dwordx4 v165, s[4:7], s31 offen lds
	s_mov_b32 m0, s43
	ds_read_b128 v[160:163], v171 offset:16384
	s_add_i32 s47, s31, s33
	buffer_load_dwordx4 v167, s[4:7], s31 offen lds
	s_mov_b32 m0, s44
	ds_read_b128 v[172:175], v171 offset:17408
	buffer_load_dwordx4 v165, s[4:7], s47 offen lds
	s_mov_b32 m0, s45
	ds_read_b128 v[176:179], v171 offset:18432
	buffer_load_dwordx4 v167, s[4:7], s47 offen lds
	s_mov_b32 m0, s41
	ds_read_b128 v[180:183], v171 offset:19456
	buffer_load_dwordx4 v164, s[36:39], s46 offen lds
	s_mov_b32 m0, s52
	ds_read_b128 v[184:187], v171 offset:20480
	buffer_load_dwordx4 v166, s[36:39], s46 offen lds
	ds_read_b128 v[188:191], v171 offset:21504
	ds_read_b128 v[194:197], v171 offset:22528
	ds_read_b128 v[198:201], v171 offset:23552
	s_waitcnt vmcnt(8)
	s_waitcnt lgkmcnt(0)
	s_barrier
; #define PG8_STAGE(bufoff, rs_, soff_, voff) do { _Pragma("unroll") for (int _i = 0; _i < 2; ++_i) \
;         __builtin_amdgcn_raw_ptr_buffer_load_lds(rs_, (LAS void*)(lds + (bufoff) + ldsw + _i * 8192), 16, (int)(voff)[_i], (int)(soff_), 0, 0); } while (0)
; #define PG8_LDA(dst, b, h) do { _Pragma("unroll") for (int m = 0; m < 4; ++m) dst[m] = PG8_LD2(lds + PG8_SA(b, h) + aoff + m * 2048); } while (0)
; #define PG8_LDB(dst, b, h) do { _Pragma("unroll") for (int n = 0; n < 2; ++n) dst[n] = PG8_LD2(lds + PG8_SB(b, h) + boff + n * 2048); } while (0)
; #define PG8_WAIT_V(n) asm volatile("s_waitcnt vmcnt(" #n ")" ::: "memory")
; #define PG8_WAIT_L(n) asm volatile("s_waitcnt lgkmcnt(" #n ")" ::: "memory")
; #define PG8_BAR __builtin_amdgcn_s_barrier()
; #define PG8_SCHED __builtin_amdgcn_sched_barrier(0)
; template <class Epi, class Sched, bool ALIGN_EPI = false, bool SP2 = false, bool FP8 = false>
; __device__ __forceinline__ void gemm_phase(LAS unsigned char* lds, const Gemm g, const Sched& S, const Epi& E, int wbase) {
;     ...
;             PG8_LDB(B0, 0, 0); PG8_LDB(B1, 0, 1); PG8_SCHED; PG8_LDA(At, 0, 0); PG8_STAGE(PG8_SA(1, 1), rAc, a1 + hstep, voffA);
;             PG8_WAIT_V(8); PG8_WAIT_L(0); PG8_BAR; PG8_MMA(0, 0, At, B0); PG8_MMA(0, 1, At, B1); PG8_BAR; PG8_SCHED;
;             PG8_LDA(At, 0, 1); PG8_STAGE(PG8_SB(0, 0), rB2, b2, voffB); PG8_STAGE(PG8_SB(0, 1), rB2, b2 + hstep, voffB); PG8_STAGE(PG8_SA(0, 0), rA2, a2, voffA);
;             PG8_WAIT_V(8); PG8_WAIT_L(0); PG8_BAR; PG8_MMA(1, 0, At, B0); PG8_MMA(1, 1, At, B1); PG8_BAR; PG8_SCHED;
;             PG8_LDB(B0, 1, 0); PG8_LDB(B1, 1, 1); PG8_SCHED; PG8_LDA(At, 1, 0); PG8_STAGE(PG8_SA(0, 1), rA2, a2 + hstep, voffA);
;             PG8_WAIT_V(8); PG8_WAIT_L(0); PG8_BAR; PG8_MMA(0, 0, At, B0); PG8_MMA(0, 1, At, B1); PG8_BAR; PG8_SCHED;
;             PG8_LDA(At, 1, 1); PG8_STAGE(PG8_SB(1, 0), rB2, b3, voffB); PG8_STAGE(PG8_SB(1, 1), rB2, b3 + hstep, voffB); PG8_STAGE(PG8_SA(1, 0), rA2, a3, voffA);
;             PG8_WAIT_V(8); PG8_WAIT_L(0); PG8_BAR; PG8_MMA(1, 0, At, B0); PG8_MMA(1, 1, At, B1); PG8_BAR; PG8_SCHED;
	s_setprio 1
	v_mfma_f32_16x16x32_bf16 v[60:63], v[128:131], v[160:163], 0
	v_mfma_f32_16x16x32_bf16 v[56:59], v[136:139], v[160:163], 0
	v_mfma_f32_16x16x32_bf16 v[44:47], v[128:131], v[176:179], 0
	v_mfma_f32_16x16x32_bf16 v[40:43], v[136:139], v[176:179], 0
	v_mfma_f32_16x16x32_bf16 v[28:31], v[128:131], v[184:187], 0
	v_mfma_f32_16x16x32_bf16 v[24:27], v[136:139], v[184:187], 0
	v_mfma_f32_16x16x32_bf16 v[12:15], v[128:131], v[194:197], 0
	v_mfma_f32_16x16x32_bf16 v[8:11], v[136:139], v[194:197], 0
	v_mfma_f32_16x16x32_bf16 v[60:63], v[132:135], v[172:175], v[60:63]
	v_mfma_f32_16x16x32_bf16 v[56:59], v[140:143], v[172:175], v[56:59]
	v_mfma_f32_16x16x32_bf16 v[44:47], v[132:135], v[180:183], v[44:47]
	v_mfma_f32_16x16x32_bf16 v[40:43], v[140:143], v[180:183], v[40:43]
	v_mfma_f32_16x16x32_bf16 v[28:31], v[132:135], v[188:191], v[28:31]
	v_mfma_f32_16x16x32_bf16 v[24:27], v[140:143], v[188:191], v[24:27]
	v_mfma_f32_16x16x32_bf16 v[12:15], v[132:135], v[198:201], v[12:15]
	v_mfma_f32_16x16x32_bf16 v[8:11], v[140:143], v[198:201], v[8:11]
	v_mfma_f32_16x16x32_bf16 v[52:55], v[144:147], v[160:163], 0
	v_mfma_f32_16x16x32_bf16 v[48:51], v[152:155], v[160:163], 0
	v_mfma_f32_16x16x32_bf16 v[36:39], v[144:147], v[176:179], 0
	v_mfma_f32_16x16x32_bf16 v[32:35], v[152:155], v[176:179], 0
	v_mfma_f32_16x16x32_bf16 v[20:23], v[144:147], v[184:187], 0
	v_mfma_f32_16x16x32_bf16 v[16:19], v[152:155], v[184:187], 0
	v_mfma_f32_16x16x32_bf16 v[4:7], v[144:147], v[194:197], 0
	v_mfma_f32_16x16x32_bf16 v[0:3], v[152:155], v[194:197], 0
	v_mfma_f32_16x16x32_bf16 v[52:55], v[148:151], v[172:175], v[52:55]
	v_mfma_f32_16x16x32_bf16 v[48:51], v[156:159], v[172:175], v[48:51]
	v_mfma_f32_16x16x32_bf16 v[36:39], v[148:151], v[180:183], v[36:39]
	v_mfma_f32_16x16x32_bf16 v[32:35], v[156:159], v[180:183], v[32:35]
	v_mfma_f32_16x16x32_bf16 v[20:23], v[148:151], v[188:191], v[20:23]
	v_mfma_f32_16x16x32_bf16 v[16:19], v[156:159], v[188:191], v[16:19]
	v_mfma_f32_16x16x32_bf16 v[4:7], v[148:151], v[198:201], v[4:7]
	v_mfma_f32_16x16x32_bf16 v[0:3], v[156:159], v[198:201], v[0:3]
	s_setprio 0
	s_barrier
	v_add_u32_e32 v140, 0x18000, v170
	v_add_u32_e32 v156, 0x1c000, v170
	ds_read_b128 v[128:131], v140
	ds_read_b128 v[132:135], v140 offset:1024
	ds_read_b128 v[136:139], v140 offset:2048
	ds_read_b128 v[140:143], v140 offset:3072
	ds_read_b128 v[144:147], v156
	ds_read_b128 v[148:151], v156 offset:1024
	ds_read_b128 v[152:155], v156 offset:2048
	ds_read_b128 v[156:159], v156 offset:3072
	s_add_i32 s46, s46, s33
	s_mov_b32 m0, s53
	ds_read_b128 v[160:163], v171 offset:32768
	ds_read_b128 v[172:175], v171 offset:33792
	ds_read_b128 v[176:179], v171 offset:34816
	ds_read_b128 v[180:183], v171 offset:35840
	ds_read_b128 v[184:187], v171 offset:36864
	ds_read_b128 v[188:191], v171 offset:37888
	ds_read_b128 v[194:197], v171 offset:38912
	ds_read_b128 v[198:201], v171 offset:39936
	buffer_load_dwordx4 v164, s[36:39], s46 offen lds
	s_mov_b32 m0, s1
	s_nop 0
	buffer_load_dwordx4 v166, s[36:39], s46 offen lds
	s_waitcnt vmcnt(8)
	s_waitcnt lgkmcnt(0)
	s_barrier
	s_setprio 1
	v_mfma_f32_16x16x32_bf16 v[124:127], v[128:131], v[160:163], v[124:127]
	v_mfma_f32_16x16x32_bf16 v[120:123], v[136:139], v[160:163], v[120:123]
	v_mfma_f32_16x16x32_bf16 v[108:111], v[128:131], v[176:179], v[108:111]
	v_mfma_f32_16x16x32_bf16 v[104:107], v[136:139], v[176:179], v[104:107]
	v_mfma_f32_16x16x32_bf16 v[92:95], v[128:131], v[184:187], v[92:95]
	v_mfma_f32_16x16x32_bf16 v[88:91], v[136:139], v[184:187], v[88:91]
	v_mfma_f32_16x16x32_bf16 v[76:79], v[128:131], v[194:197], v[76:79]
	v_mfma_f32_16x16x32_bf16 v[72:75], v[136:139], v[194:197], v[72:75]
	v_mfma_f32_16x16x32_bf16 v[124:127], v[132:135], v[172:175], v[124:127]
	v_mfma_f32_16x16x32_bf16 v[120:123], v[140:143], v[172:175], v[120:123]
	v_mfma_f32_16x16x32_bf16 v[108:111], v[132:135], v[180:183], v[108:111]
	v_mfma_f32_16x16x32_bf16 v[104:107], v[140:143], v[180:183], v[104:107]
	v_mfma_f32_16x16x32_bf16 v[92:95], v[132:135], v[188:191], v[92:95]
	v_mfma_f32_16x16x32_bf16 v[88:91], v[140:143], v[188:191], v[88:91]
	v_mfma_f32_16x16x32_bf16 v[76:79], v[132:135], v[198:201], v[76:79]
	v_mfma_f32_16x16x32_bf16 v[72:75], v[140:143], v[198:201], v[72:75]
	v_mfma_f32_16x16x32_bf16 v[116:119], v[144:147], v[160:163], v[116:119]
	v_mfma_f32_16x16x32_bf16 v[112:115], v[152:155], v[160:163], v[112:115]
	v_mfma_f32_16x16x32_bf16 v[100:103], v[144:147], v[176:179], v[100:103]
	v_mfma_f32_16x16x32_bf16 v[96:99], v[152:155], v[176:179], v[96:99]
	v_mfma_f32_16x16x32_bf16 v[84:87], v[144:147], v[184:187], v[84:87]
	v_mfma_f32_16x16x32_bf16 v[80:83], v[152:155], v[184:187], v[80:83]
	v_mfma_f32_16x16x32_bf16 v[68:71], v[144:147], v[194:197], v[68:71]
	v_mfma_f32_16x16x32_bf16 v[64:67], v[152:155], v[194:197], v[64:67]
	v_mfma_f32_16x16x32_bf16 v[116:119], v[148:151], v[172:175], v[116:119]
	v_mfma_f32_16x16x32_bf16 v[112:115], v[156:159], v[172:175], v[112:115]
	v_mfma_f32_16x16x32_bf16 v[100:103], v[148:151], v[180:183], v[100:103]
	v_mfma_f32_16x16x32_bf16 v[96:99], v[156:159], v[180:183], v[96:99]
	v_mfma_f32_16x16x32_bf16 v[84:87], v[148:151], v[188:191], v[84:87]
	v_mfma_f32_16x16x32_bf16 v[80:83], v[156:159], v[188:191], v[80:83]
	v_mfma_f32_16x16x32_bf16 v[68:71], v[148:151], v[198:201], v[68:71]
	v_mfma_f32_16x16x32_bf16 v[64:67], v[156:159], v[198:201], v[64:67]
	s_setprio 0
	s_barrier
; #define PG8_STAGE(bufoff, rs_, soff_, voff) do { _Pragma("unroll") for (int _i = 0; _i < 2; ++_i) \
;         __builtin_amdgcn_raw_ptr_buffer_load_lds(rs_, (LAS void*)(lds + (bufoff) + ldsw + _i * 8192), 16, (int)(voff)[_i], (int)(soff_), 0, 0); } while (0)
; #define PG8_LDA(dst, b, h) do { _Pragma("unroll") for (int m = 0; m < 4; ++m) dst[m] = PG8_LD2(lds + PG8_SA(b, h) + aoff + m * 2048); } while (0)
; #define PG8_LDB(dst, b, h) do { _Pragma("unroll") for (int n = 0; n < 2; ++n) dst[n] = PG8_LD2(lds + PG8_SB(b, h) + boff + n * 2048); } while (0)
; #define PG8_WAIT_V(n) asm volatile("s_waitcnt vmcnt(" #n ")" ::: "memory")
; #define PG8_WAIT_L(n) asm volatile("s_waitcnt lgkmcnt(" #n ")" ::: "memory")
; #define PG8_BAR __builtin_amdgcn_s_barrier()
; #define PG8_SCHED __builtin_amdgcn_sched_barrier(0)
; template <class Epi, class Sched, bool ALIGN_EPI = false, bool SP2 = false, bool FP8 = false>
; __device__ __forceinline__ void gemm_phase(LAS unsigned char* lds, const Gemm g, const Sched& S, const Epi& E, int wbase) {
;     ...
;             PG8_LDB(B0, 0, 0); PG8_LDB(B1, 0, 1); PG8_SCHED; PG8_LDA(At, 0, 0); PG8_STAGE(PG8_SA(1, 1), rAc, a1 + hstep, voffA);
;             PG8_WAIT_V(8); PG8_WAIT_L(0); PG8_BAR; PG8_MMA(0, 0, At, B0); PG8_MMA(0, 1, At, B1); PG8_BAR; PG8_SCHED;
;             PG8_LDA(At, 0, 1); PG8_STAGE(PG8_SB(0, 0), rB2, b2, voffB); PG8_STAGE(PG8_SB(0, 1), rB2, b2 + hstep, voffB); PG8_STAGE(PG8_SA(0, 0), rA2, a2, voffA);
;             PG8_WAIT_V(8); PG8_WAIT_L(0); PG8_BAR; PG8_MMA(1, 0, At, B0); PG8_MMA(1, 1, At, B1); PG8_BAR; PG8_SCHED;
;             PG8_LDB(B0, 1, 0); PG8_LDB(B1, 1, 1); PG8_SCHED; PG8_LDA(At, 1, 0); PG8_STAGE(PG8_SA(0, 1), rA2, a2 + hstep, voffA);
;             PG8_WAIT_V(8); PG8_WAIT_L(0); PG8_BAR; PG8_MMA(0, 0, At, B0); PG8_MMA(0, 1, At, B1); PG8_BAR; PG8_SCHED;
;             PG8_LDA(At, 1, 1); PG8_STAGE(PG8_SB(1, 0), rB2, b3, voffB); PG8_STAGE(PG8_SB(1, 1), rB2, b3 + hstep, voffB); PG8_STAGE(PG8_SA(1, 0), rA2, a3, voffA);
;             PG8_WAIT_V(8); PG8_WAIT_L(0); PG8_BAR; PG8_MMA(1, 0, At, B0); PG8_MMA(1, 1, At, B1); PG8_BAR; PG8_SCHED;
	s_mov_b32 m0, s56
	s_bitset1_b32 s31, 7
	buffer_load_dwordx4 v165, s[4:7], s31 offen lds
	s_mov_b32 m0, s57
	ds_read_b128 v[160:163], v171 offset:49152
	buffer_load_dwordx4 v167, s[4:7], s31 offen lds
	s_add_i32 s31, s31, s33
	s_mov_b32 m0, s65
	ds_read_b128 v[172:175], v171 offset:50176
	buffer_load_dwordx4 v165, s[4:7], s31 offen lds
	s_mov_b32 m0, s76
	ds_read_b128 v[176:179], v171 offset:51200
	buffer_load_dwordx4 v167, s[4:7], s31 offen lds
	s_mov_b32 m0, s58
	ds_read_b128 v[180:183], v171 offset:52224
	buffer_load_dwordx4 v164, s[36:39], s30 offen lds
	s_mov_b32 m0, s59
	ds_read_b128 v[184:187], v171 offset:53248
	buffer_load_dwordx4 v166, s[36:39], s30 offen lds
	ds_read_b128 v[188:191], v171 offset:54272
	ds_read_b128 v[194:197], v171 offset:55296
	ds_read_b128 v[198:201], v171 offset:56320
	s_waitcnt vmcnt(8)
	s_waitcnt lgkmcnt(0)
	s_barrier
	s_setprio 1
	v_mfma_f32_16x16x32_bf16 v[60:63], v[128:131], v[160:163], v[60:63]
	v_mfma_f32_16x16x32_bf16 v[56:59], v[136:139], v[160:163], v[56:59]
	v_mfma_f32_16x16x32_bf16 v[44:47], v[128:131], v[176:179], v[44:47]
	v_mfma_f32_16x16x32_bf16 v[40:43], v[136:139], v[176:179], v[40:43]
	v_mfma_f32_16x16x32_bf16 v[28:31], v[128:131], v[184:187], v[28:31]
	v_mfma_f32_16x16x32_bf16 v[24:27], v[136:139], v[184:187], v[24:27]
	v_mfma_f32_16x16x32_bf16 v[12:15], v[128:131], v[194:197], v[12:15]
	v_mfma_f32_16x16x32_bf16 v[8:11], v[136:139], v[194:197], v[8:11]
	v_mfma_f32_16x16x32_bf16 v[60:63], v[132:135], v[172:175], v[60:63]
	v_mfma_f32_16x16x32_bf16 v[56:59], v[140:143], v[172:175], v[56:59]
	v_mfma_f32_16x16x32_bf16 v[44:47], v[132:135], v[180:183], v[44:47]
	v_mfma_f32_16x16x32_bf16 v[40:43], v[140:143], v[180:183], v[40:43]
	v_mfma_f32_16x16x32_bf16 v[28:31], v[132:135], v[188:191], v[28:31]
	v_mfma_f32_16x16x32_bf16 v[24:27], v[140:143], v[188:191], v[24:27]
	v_mfma_f32_16x16x32_bf16 v[12:15], v[132:135], v[198:201], v[12:15]
	v_mfma_f32_16x16x32_bf16 v[8:11], v[140:143], v[198:201], v[8:11]
	v_mfma_f32_16x16x32_bf16 v[52:55], v[144:147], v[160:163], v[52:55]
	v_mfma_f32_16x16x32_bf16 v[48:51], v[152:155], v[160:163], v[48:51]
	v_mfma_f32_16x16x32_bf16 v[36:39], v[144:147], v[176:179], v[36:39]
	v_mfma_f32_16x16x32_bf16 v[32:35], v[152:155], v[176:179], v[32:35]
	v_mfma_f32_16x16x32_bf16 v[20:23], v[144:147], v[184:187], v[20:23]
	v_mfma_f32_16x16x32_bf16 v[16:19], v[152:155], v[184:187], v[16:19]
	v_mfma_f32_16x16x32_bf16 v[4:7], v[144:147], v[194:197], v[4:7]
	v_mfma_f32_16x16x32_bf16 v[0:3], v[152:155], v[194:197], v[0:3]
	v_mfma_f32_16x16x32_bf16 v[52:55], v[148:151], v[172:175], v[52:55]
	v_mfma_f32_16x16x32_bf16 v[48:51], v[156:159], v[172:175], v[48:51]
	v_mfma_f32_16x16x32_bf16 v[36:39], v[148:151], v[180:183], v[36:39]
	v_mfma_f32_16x16x32_bf16 v[32:35], v[156:159], v[180:183], v[32:35]
	v_mfma_f32_16x16x32_bf16 v[20:23], v[148:151], v[188:191], v[20:23]
	v_mfma_f32_16x16x32_bf16 v[16:19], v[156:159], v[188:191], v[16:19]
	v_mfma_f32_16x16x32_bf16 v[4:7], v[148:151], v[198:201], v[4:7]
	v_mfma_f32_16x16x32_bf16 v[0:3], v[156:159], v[198:201], v[0:3]
	s_setprio 0
	s_barrier
	s_add_i32 s29, s29, 2
	s_addk_i32 s16, 0x100
	s_addk_i32 s28, 0x100
	s_cmp_ge_i32 s29, s82
	s_cbranch_scc0 .LBB0_352
	s_branch .Lzp_after_352
.LBB0_352:
	v_add_u32_e32 v140, 0x10000, v170
	v_add_u32_e32 v156, 0x14000, v170
	ds_read_b128 v[128:131], v140
	ds_read_b128 v[132:135], v140 offset:1024
	ds_read_b128 v[136:139], v140 offset:2048
	ds_read_b128 v[140:143], v140 offset:3072
	ds_read_b128 v[144:147], v156
	ds_read_b128 v[148:151], v156 offset:1024
	ds_read_b128 v[152:155], v156 offset:2048
	ds_read_b128 v[156:159], v156 offset:3072
	s_add_i32 s6, s16, 0x80
	s_cmp_eq_u32 s12, s29
	s_cselect_b32 s46, s2, s6
	s_cselect_b32 s31, s3, s28
	s_or_b32 s30, s46, 0x80
	s_add_i32 s6, s33, s16
	s_mov_b32 m0, s13
	ds_read_b128 v[160:163], v171
	ds_read_b128 v[172:175], v171 offset:1024
	ds_read_b128 v[176:179], v171 offset:2048
	ds_read_b128 v[180:183], v171 offset:3072
	ds_read_b128 v[184:187], v171 offset:4096
	ds_read_b128 v[188:191], v171 offset:5120
	ds_read_b128 v[194:197], v171 offset:6144
	ds_read_b128 v[198:201], v171 offset:7168
	buffer_load_dwordx4 v164, s[36:39], s6 offen lds
	s_mov_b32 m0, s83
	s_nop 0
	buffer_load_dwordx4 v166, s[36:39], s6 offen lds
	s_waitcnt vmcnt(8)
	s_waitcnt lgkmcnt(0)
	s_barrier
	s_setprio 1
	v_mfma_f32_16x16x32_bf16 v[124:127], v[128:131], v[160:163], v[124:127]
	v_mfma_f32_16x16x32_bf16 v[120:123], v[136:139], v[160:163], v[120:123]
	v_mfma_f32_16x16x32_bf16 v[108:111], v[128:131], v[176:179], v[108:111]
	v_mfma_f32_16x16x32_bf16 v[104:107], v[136:139], v[176:179], v[104:107]
	v_mfma_f32_16x16x32_bf16 v[92:95], v[128:131], v[184:187], v[92:95]
	v_mfma_f32_16x16x32_bf16 v[88:91], v[136:139], v[184:187], v[88:91]
	v_mfma_f32_16x16x32_bf16 v[76:79], v[128:131], v[194:197], v[76:79]
	v_mfma_f32_16x16x32_bf16 v[72:75], v[136:139], v[194:197], v[72:75]
	v_mfma_f32_16x16x32_bf16 v[124:127], v[132:135], v[172:175], v[124:127]
	v_mfma_f32_16x16x32_bf16 v[120:123], v[140:143], v[172:175], v[120:123]
	v_mfma_f32_16x16x32_bf16 v[108:111], v[132:135], v[180:183], v[108:111]
	v_mfma_f32_16x16x32_bf16 v[104:107], v[140:143], v[180:183], v[104:107]
	v_mfma_f32_16x16x32_bf16 v[92:95], v[132:135], v[188:191], v[92:95]
	v_mfma_f32_16x16x32_bf16 v[88:91], v[140:143], v[188:191], v[88:91]
	v_mfma_f32_16x16x32_bf16 v[76:79], v[132:135], v[198:201], v[76:79]
	v_mfma_f32_16x16x32_bf16 v[72:75], v[140:143], v[198:201], v[72:75]
	v_mfma_f32_16x16x32_bf16 v[116:119], v[144:147], v[160:163], v[116:119]
	v_mfma_f32_16x16x32_bf16 v[112:115], v[152:155], v[160:163], v[112:115]
	v_mfma_f32_16x16x32_bf16 v[100:103], v[144:147], v[176:179], v[100:103]
	v_mfma_f32_16x16x32_bf16 v[96:99], v[152:155], v[176:179], v[96:99]
	v_mfma_f32_16x16x32_bf16 v[84:87], v[144:147], v[184:187], v[84:87]
	v_mfma_f32_16x16x32_bf16 v[80:83], v[152:155], v[184:187], v[80:83]
	v_mfma_f32_16x16x32_bf16 v[68:71], v[144:147], v[194:197], v[68:71]
	v_mfma_f32_16x16x32_bf16 v[64:67], v[152:155], v[194:197], v[64:67]
	v_mfma_f32_16x16x32_bf16 v[116:119], v[148:151], v[172:175], v[116:119]
	v_mfma_f32_16x16x32_bf16 v[112:115], v[156:159], v[172:175], v[112:115]
	v_mfma_f32_16x16x32_bf16 v[100:103], v[148:151], v[180:183], v[100:103]
	v_mfma_f32_16x16x32_bf16 v[96:99], v[156:159], v[180:183], v[96:99]
	v_mfma_f32_16x16x32_bf16 v[84:87], v[148:151], v[188:191], v[84:87]
	v_mfma_f32_16x16x32_bf16 v[80:83], v[156:159], v[188:191], v[80:83]
	v_mfma_f32_16x16x32_bf16 v[68:71], v[148:151], v[198:201], v[68:71]
	v_mfma_f32_16x16x32_bf16 v[64:67], v[156:159], v[198:201], v[64:67]
	s_setprio 0
	s_barrier
; #define PG8_STAGE(bufoff, rs_, soff_, voff) do { _Pragma("unroll") for (int _i = 0; _i < 2; ++_i) \
;         __builtin_amdgcn_raw_ptr_buffer_load_lds(rs_, (LAS void*)(lds + (bufoff) + ldsw + _i * 8192), 16, (int)(voff)[_i], (int)(soff_), 0, 0); } while (0)
; #define PG8_LDA(dst, b, h) do { _Pragma("unroll") for (int m = 0; m < 4; ++m) dst[m] = PG8_LD2(lds + PG8_SA(b, h) + aoff + m * 2048); } while (0)
; #define PG8_LDB(dst, b, h) do { _Pragma("unroll") for (int n = 0; n < 2; ++n) dst[n] = PG8_LD2(lds + PG8_SB(b, h) + boff + n * 2048); } while (0)
; #define PG8_WAIT_V(n) asm volatile("s_waitcnt vmcnt(" #n ")" ::: "memory")
; #define PG8_WAIT_L(n) asm volatile("s_waitcnt lgkmcnt(" #n ")" ::: "memory")
; #define PG8_BAR __builtin_amdgcn_s_barrier()
; #define PG8_SCHED __builtin_amdgcn_sched_barrier(0)
; template <class Epi, class Sched, bool ALIGN_EPI = false, bool SP2 = false, bool FP8 = false>
; __device__ __forceinline__ void gemm_phase(LAS unsigned char* lds, const Gemm g, const Sched& S, const Epi& E, int wbase) {
;     ...
;             PG8_LDB(B0, 0, 0); PG8_LDB(B1, 0, 1); PG8_SCHED; PG8_LDA(At, 0, 0); PG8_STAGE(PG8_SA(1, 1), rAc, a1 + hstep, voffA);
;             PG8_WAIT_V(8); PG8_WAIT_L(0); PG8_BAR; PG8_MMA(0, 0, At, B0); PG8_MMA(0, 1, At, B1); PG8_BAR; PG8_SCHED;
;             PG8_LDA(At, 0, 1); PG8_STAGE(PG8_SB(0, 0), rB2, b2, voffB); PG8_STAGE(PG8_SB(0, 1), rB2, b2 + hstep, voffB); PG8_STAGE(PG8_SA(0, 0), rA2, a2, voffA);
;             PG8_WAIT_V(8); PG8_WAIT_L(0); PG8_BAR; PG8_MMA(1, 0, At, B0); PG8_MMA(1, 1, At, B1); PG8_BAR; PG8_SCHED;
;             PG8_LDB(B0, 1, 0); PG8_LDB(B1, 1, 1); PG8_SCHED; PG8_LDA(At, 1, 0); PG8_STAGE(PG8_SA(0, 1), rA2, a2 + hstep, voffA);
;             PG8_WAIT_V(8); PG8_WAIT_L(0); PG8_BAR; PG8_MMA(0, 0, At, B0); PG8_MMA(0, 1, At, B1); PG8_BAR; PG8_SCHED;
;             PG8_LDA(At, 1, 1); PG8_STAGE(PG8_SB(1, 0), rB2, b3, voffB); PG8_STAGE(PG8_SB(1, 1), rB2, b3 + hstep, voffB); PG8_STAGE(PG8_SA(1, 0), rA2, a3, voffA);
;             PG8_WAIT_V(8); PG8_WAIT_L(0); PG8_BAR; PG8_MMA(1, 0, At, B0); PG8_MMA(1, 1, At, B1); PG8_BAR; PG8_SCHED;
	s_mov_b32 m0, s42
	s_mov_b32 s6, s38
	s_mov_b32 s7, s39
	buffer_load_dwordx4 v165, s[4:7], s31 offen lds
	s_mov_b32 m0, s43
	ds_read_b128 v[160:163], v171 offset:16384
	s_add_i32 s47, s31, s33
	buffer_load_dwordx4 v167, s[4:7], s31 offen lds
	s_mov_b32 m0, s44
	ds_read_b128 v[172:175], v171 offset:17408
	buffer_load_dwordx4 v165, s[4:7], s47 offen lds
	s_mov_b32 m0, s45
	ds_read_b128 v[176:179], v171 offset:18432
	buffer_load_dwordx4 v167, s[4:7], s47 offen lds
	s_mov_b32 m0, s41
	ds_read_b128 v[180:183], v171 offset:19456
	buffer_load_dwordx4 v164, s[36:39], s46 offen lds
	s_mov_b32 m0, s52
	ds_read_b128 v[184:187], v171 offset:20480
	buffer_load_dwordx4 v166, s[36:39], s46 offen lds
	ds_read_b128 v[188:191], v171 offset:21504
	ds_read_b128 v[194:197], v171 offset:22528
	ds_read_b128 v[198:201], v171 offset:23552
	s_waitcnt vmcnt(8)
	s_waitcnt lgkmcnt(0)
	s_barrier
	s_setprio 1
	v_mfma_f32_16x16x32_bf16 v[60:63], v[128:131], v[160:163], v[60:63]
	v_mfma_f32_16x16x32_bf16 v[56:59], v[136:139], v[160:163], v[56:59]
	v_mfma_f32_16x16x32_bf16 v[44:47], v[128:131], v[176:179], v[44:47]
	v_mfma_f32_16x16x32_bf16 v[40:43], v[136:139], v[176:179], v[40:43]
	v_mfma_f32_16x16x32_bf16 v[28:31], v[128:131], v[184:187], v[28:31]
	v_mfma_f32_16x16x32_bf16 v[24:27], v[136:139], v[184:187], v[24:27]
	v_mfma_f32_16x16x32_bf16 v[12:15], v[128:131], v[194:197], v[12:15]
	v_mfma_f32_16x16x32_bf16 v[8:11], v[136:139], v[194:197], v[8:11]
	v_mfma_f32_16x16x32_bf16 v[60:63], v[132:135], v[172:175], v[60:63]
	v_mfma_f32_16x16x32_bf16 v[56:59], v[140:143], v[172:175], v[56:59]
	v_mfma_f32_16x16x32_bf16 v[44:47], v[132:135], v[180:183], v[44:47]
	v_mfma_f32_16x16x32_bf16 v[40:43], v[140:143], v[180:183], v[40:43]
	v_mfma_f32_16x16x32_bf16 v[28:31], v[132:135], v[188:191], v[28:31]
	v_mfma_f32_16x16x32_bf16 v[24:27], v[140:143], v[188:191], v[24:27]
	v_mfma_f32_16x16x32_bf16 v[12:15], v[132:135], v[198:201], v[12:15]
	v_mfma_f32_16x16x32_bf16 v[8:11], v[140:143], v[198:201], v[8:11]
	v_mfma_f32_16x16x32_bf16 v[52:55], v[144:147], v[160:163], v[52:55]
	v_mfma_f32_16x16x32_bf16 v[48:51], v[152:155], v[160:163], v[48:51]
	v_mfma_f32_16x16x32_bf16 v[36:39], v[144:147], v[176:179], v[36:39]
	v_mfma_f32_16x16x32_bf16 v[32:35], v[152:155], v[176:179], v[32:35]
	v_mfma_f32_16x16x32_bf16 v[20:23], v[144:147], v[184:187], v[20:23]
	v_mfma_f32_16x16x32_bf16 v[16:19], v[152:155], v[184:187], v[16:19]
	v_mfma_f32_16x16x32_bf16 v[4:7], v[144:147], v[194:197], v[4:7]
	v_mfma_f32_16x16x32_bf16 v[0:3], v[152:155], v[194:197], v[0:3]
	v_mfma_f32_16x16x32_bf16 v[52:55], v[148:151], v[172:175], v[52:55]
	v_mfma_f32_16x16x32_bf16 v[48:51], v[156:159], v[172:175], v[48:51]
	v_mfma_f32_16x16x32_bf16 v[36:39], v[148:151], v[180:183], v[36:39]
	v_mfma_f32_16x16x32_bf16 v[32:35], v[156:159], v[180:183], v[32:35]
	v_mfma_f32_16x16x32_bf16 v[20:23], v[148:151], v[188:191], v[20:23]
	v_mfma_f32_16x16x32_bf16 v[16:19], v[156:159], v[188:191], v[16:19]
	v_mfma_f32_16x16x32_bf16 v[4:7], v[148:151], v[198:201], v[4:7]
	v_mfma_f32_16x16x32_bf16 v[0:3], v[156:159], v[198:201], v[0:3]
	s_setprio 0
	s_barrier
	v_add_u32_e32 v140, 0x18000, v170
	v_add_u32_e32 v156, 0x1c000, v170
	ds_read_b128 v[128:131], v140
	ds_read_b128 v[132:135], v140 offset:1024
	ds_read_b128 v[136:139], v140 offset:2048
	ds_read_b128 v[140:143], v140 offset:3072
	ds_read_b128 v[144:147], v156
	ds_read_b128 v[148:151], v156 offset:1024
	ds_read_b128 v[152:155], v156 offset:2048
	ds_read_b128 v[156:159], v156 offset:3072
	s_add_i32 s46, s46, s33
	s_mov_b32 m0, s53
	ds_read_b128 v[160:163], v171 offset:32768
	ds_read_b128 v[172:175], v171 offset:33792
	ds_read_b128 v[176:179], v171 offset:34816
	ds_read_b128 v[180:183], v171 offset:35840
	ds_read_b128 v[184:187], v171 offset:36864
	ds_read_b128 v[188:191], v171 offset:37888
	ds_read_b128 v[194:197], v171 offset:38912
	ds_read_b128 v[198:201], v171 offset:39936
	buffer_load_dwordx4 v164, s[36:39], s46 offen lds
	s_mov_b32 m0, s1
	s_nop 0
	buffer_load_dwordx4 v166, s[36:39], s46 offen lds
	s_waitcnt vmcnt(8)
	s_waitcnt lgkmcnt(0)
	s_barrier
; #define PG8_STAGE(bufoff, rs_, soff_, voff) do { _Pragma("unroll") for (int _i = 0; _i < 2; ++_i) \
;         __builtin_amdgcn_raw_ptr_buffer_load_lds(rs_, (LAS void*)(lds + (bufoff) + ldsw + _i * 8192), 16, (int)(voff)[_i], (int)(soff_), 0, 0); } while (0)
; #define PG8_LDA(dst, b, h) do { _Pragma("unroll") for (int m = 0; m < 4; ++m) dst[m] = PG8_LD2(lds + PG8_SA(b, h) + aoff + m * 2048); } while (0)
; #define PG8_LDB(dst, b, h) do { _Pragma("unroll") for (int n = 0; n < 2; ++n) dst[n] = PG8_LD2(lds + PG8_SB(b, h) + boff + n * 2048); } while (0)
; #define PG8_WAIT_V(n) asm volatile("s_waitcnt vmcnt(" #n ")" ::: "memory")
; #define PG8_WAIT_L(n) asm volatile("s_waitcnt lgkmcnt(" #n ")" ::: "memory")
; #define PG8_BAR __builtin_amdgcn_s_barrier()
; #define PG8_SCHED __builtin_amdgcn_sched_barrier(0)
; template <class Epi, class Sched, bool ALIGN_EPI = false, bool SP2 = false, bool FP8 = false>
; __device__ __forceinline__ void gemm_phase(LAS unsigned char* lds, const Gemm g, const Sched& S, const Epi& E, int wbase) {
;     ...
;             PG8_LDB(B0, 0, 0); PG8_LDB(B1, 0, 1); PG8_SCHED; PG8_LDA(At, 0, 0); PG8_STAGE(PG8_SA(1, 1), rAc, a1 + hstep, voffA);
;             PG8_WAIT_V(8); PG8_WAIT_L(0); PG8_BAR; PG8_MMA(0, 0, At, B0); PG8_MMA(0, 1, At, B1); PG8_BAR; PG8_SCHED;
;             PG8_LDA(At, 0, 1); PG8_STAGE(PG8_SB(0, 0), rB2, b2, voffB); PG8_STAGE(PG8_SB(0, 1), rB2, b2 + hstep, voffB); PG8_STAGE(PG8_SA(0, 0), rA2, a2, voffA);
;             PG8_WAIT_V(8); PG8_WAIT_L(0); PG8_BAR; PG8_MMA(1, 0, At, B0); PG8_MMA(1, 1, At, B1); PG8_BAR; PG8_SCHED;
;             PG8_LDB(B0, 1, 0); PG8_LDB(B1, 1, 1); PG8_SCHED; PG8_LDA(At, 1, 0); PG8_STAGE(PG8_SA(0, 1), rA2, a2 + hstep, voffA);
;             PG8_WAIT_V(8); PG8_WAIT_L(0); PG8_BAR; PG8_MMA(0, 0, At, B0); PG8_MMA(0, 1, At, B1); PG8_BAR; PG8_SCHED;
;             PG8_LDA(At, 1, 1); PG8_STAGE(PG8_SB(1, 0), rB2, b3, voffB); PG8_STAGE(PG8_SB(1, 1), rB2, b3 + hstep, voffB); PG8_STAGE(PG8_SA(1, 0), rA2, a3, voffA);
;             PG8_WAIT_V(8); PG8_WAIT_L(0); PG8_BAR; PG8_MMA(1, 0, At, B0); PG8_MMA(1, 1, At, B1); PG8_BAR; PG8_SCHED;
	s_setprio 1
	v_mfma_f32_16x16x32_bf16 v[124:127], v[128:131], v[160:163], v[124:127]
	v_mfma_f32_16x16x32_bf16 v[120:123], v[136:139], v[160:163], v[120:123]
	v_mfma_f32_16x16x32_bf16 v[108:111], v[128:131], v[176:179], v[108:111]
	v_mfma_f32_16x16x32_bf16 v[104:107], v[136:139], v[176:179], v[104:107]
	v_mfma_f32_16x16x32_bf16 v[92:95], v[128:131], v[184:187], v[92:95]
	v_mfma_f32_16x16x32_bf16 v[88:91], v[136:139], v[184:187], v[88:91]
	v_mfma_f32_16x16x32_bf16 v[76:79], v[128:131], v[194:197], v[76:79]
	v_mfma_f32_16x16x32_bf16 v[72:75], v[136:139], v[194:197], v[72:75]
	v_mfma_f32_16x16x32_bf16 v[124:127], v[132:135], v[172:175], v[124:127]
	v_mfma_f32_16x16x32_bf16 v[120:123], v[140:143], v[172:175], v[120:123]
	v_mfma_f32_16x16x32_bf16 v[108:111], v[132:135], v[180:183], v[108:111]
	v_mfma_f32_16x16x32_bf16 v[104:107], v[140:143], v[180:183], v[104:107]
	v_mfma_f32_16x16x32_bf16 v[92:95], v[132:135], v[188:191], v[92:95]
	v_mfma_f32_16x16x32_bf16 v[88:91], v[140:143], v[188:191], v[88:91]
	v_mfma_f32_16x16x32_bf16 v[76:79], v[132:135], v[198:201], v[76:79]
	v_mfma_f32_16x16x32_bf16 v[72:75], v[140:143], v[198:201], v[72:75]
	v_mfma_f32_16x16x32_bf16 v[116:119], v[144:147], v[160:163], v[116:119]
	v_mfma_f32_16x16x32_bf16 v[112:115], v[152:155], v[160:163], v[112:115]
	v_mfma_f32_16x16x32_bf16 v[100:103], v[144:147], v[176:179], v[100:103]
	v_mfma_f32_16x16x32_bf16 v[96:99], v[152:155], v[176:179], v[96:99]
	v_mfma_f32_16x16x32_bf16 v[84:87], v[144:147], v[184:187], v[84:87]
	v_mfma_f32_16x16x32_bf16 v[80:83], v[152:155], v[184:187], v[80:83]
	v_mfma_f32_16x16x32_bf16 v[68:71], v[144:147], v[194:197], v[68:71]
	v_mfma_f32_16x16x32_bf16 v[64:67], v[152:155], v[194:197], v[64:67]
	v_mfma_f32_16x16x32_bf16 v[116:119], v[148:151], v[172:175], v[116:119]
	v_mfma_f32_16x16x32_bf16 v[112:115], v[156:159], v[172:175], v[112:115]
	v_mfma_f32_16x16x32_bf16 v[100:103], v[148:151], v[180:183], v[100:103]
	v_mfma_f32_16x16x32_bf16 v[96:99], v[156:159], v[180:183], v[96:99]
	v_mfma_f32_16x16x32_bf16 v[84:87], v[148:151], v[188:191], v[84:87]
	v_mfma_f32_16x16x32_bf16 v[80:83], v[156:159], v[188:191], v[80:83]
	v_mfma_f32_16x16x32_bf16 v[68:71], v[148:151], v[198:201], v[68:71]
	v_mfma_f32_16x16x32_bf16 v[64:67], v[156:159], v[198:201], v[64:67]
	s_setprio 0
	s_barrier
	s_mov_b32 m0, s56
	s_bitset1_b32 s31, 7
	buffer_load_dwordx4 v165, s[4:7], s31 offen lds
	s_mov_b32 m0, s57
	ds_read_b128 v[160:163], v171 offset:49152
	buffer_load_dwordx4 v167, s[4:7], s31 offen lds
	s_add_i32 s31, s31, s33
	s_mov_b32 m0, s65
	ds_read_b128 v[172:175], v171 offset:50176
	buffer_load_dwordx4 v165, s[4:7], s31 offen lds
	s_mov_b32 m0, s76
	ds_read_b128 v[176:179], v171 offset:51200
	buffer_load_dwordx4 v167, s[4:7], s31 offen lds
	s_mov_b32 m0, s58
	ds_read_b128 v[180:183], v171 offset:52224
	buffer_load_dwordx4 v164, s[36:39], s30 offen lds
	s_mov_b32 m0, s59
	ds_read_b128 v[184:187], v171 offset:53248
	buffer_load_dwordx4 v166, s[36:39], s30 offen lds
	ds_read_b128 v[188:191], v171 offset:54272
	ds_read_b128 v[194:197], v171 offset:55296
	ds_read_b128 v[198:201], v171 offset:56320
	s_waitcnt vmcnt(8)
	s_waitcnt lgkmcnt(0)
	s_barrier
	s_setprio 1
	v_mfma_f32_16x16x32_bf16 v[60:63], v[128:131], v[160:163], v[60:63]
	v_mfma_f32_16x16x32_bf16 v[56:59], v[136:139], v[160:163], v[56:59]
	v_mfma_f32_16x16x32_bf16 v[44:47], v[128:131], v[176:179], v[44:47]
	v_mfma_f32_16x16x32_bf16 v[40:43], v[136:139], v[176:179], v[40:43]
	v_mfma_f32_16x16x32_bf16 v[28:31], v[128:131], v[184:187], v[28:31]
	v_mfma_f32_16x16x32_bf16 v[24:27], v[136:139], v[184:187], v[24:27]
	v_mfma_f32_16x16x32_bf16 v[12:15], v[128:131], v[194:197], v[12:15]
	v_mfma_f32_16x16x32_bf16 v[8:11], v[136:139], v[194:197], v[8:11]
	v_mfma_f32_16x16x32_bf16 v[60:63], v[132:135], v[172:175], v[60:63]
	v_mfma_f32_16x16x32_bf16 v[56:59], v[140:143], v[172:175], v[56:59]
	v_mfma_f32_16x16x32_bf16 v[44:47], v[132:135], v[180:183], v[44:47]
	v_mfma_f32_16x16x32_bf16 v[40:43], v[140:143], v[180:183], v[40:43]
	v_mfma_f32_16x16x32_bf16 v[28:31], v[132:135], v[188:191], v[28:31]
	v_mfma_f32_16x16x32_bf16 v[24:27], v[140:143], v[188:191], v[24:27]
	v_mfma_f32_16x16x32_bf16 v[12:15], v[132:135], v[198:201], v[12:15]
	v_mfma_f32_16x16x32_bf16 v[8:11], v[140:143], v[198:201], v[8:11]
	v_mfma_f32_16x16x32_bf16 v[52:55], v[144:147], v[160:163], v[52:55]
	v_mfma_f32_16x16x32_bf16 v[48:51], v[152:155], v[160:163], v[48:51]
	v_mfma_f32_16x16x32_bf16 v[36:39], v[144:147], v[176:179], v[36:39]
	v_mfma_f32_16x16x32_bf16 v[32:35], v[152:155], v[176:179], v[32:35]
	v_mfma_f32_16x16x32_bf16 v[20:23], v[144:147], v[184:187], v[20:23]
	v_mfma_f32_16x16x32_bf16 v[16:19], v[152:155], v[184:187], v[16:19]
	v_mfma_f32_16x16x32_bf16 v[4:7], v[144:147], v[194:197], v[4:7]
	v_mfma_f32_16x16x32_bf16 v[0:3], v[152:155], v[194:197], v[0:3]
	v_mfma_f32_16x16x32_bf16 v[52:55], v[148:151], v[172:175], v[52:55]
	v_mfma_f32_16x16x32_bf16 v[48:51], v[156:159], v[172:175], v[48:51]
	v_mfma_f32_16x16x32_bf16 v[36:39], v[148:151], v[180:183], v[36:39]
	v_mfma_f32_16x16x32_bf16 v[32:35], v[156:159], v[180:183], v[32:35]
	v_mfma_f32_16x16x32_bf16 v[20:23], v[148:151], v[188:191], v[20:23]
	v_mfma_f32_16x16x32_bf16 v[16:19], v[156:159], v[188:191], v[16:19]
	v_mfma_f32_16x16x32_bf16 v[4:7], v[148:151], v[198:201], v[4:7]
	v_mfma_f32_16x16x32_bf16 v[0:3], v[156:159], v[198:201], v[0:3]
	s_setprio 0
	s_barrier
	s_add_i32 s29, s29, 2
	s_addk_i32 s16, 0x100
	s_addk_i32 s28, 0x100
	s_cmp_ge_i32 s29, s82
	s_cbranch_scc0 .LBB0_352

;     __device__ __forceinline__ unsigned a_off(const Unit& u, const Gemm& g) const { return (unsigned)u.pm * (unsigned)(BM * 2) * (unsigned)g.K; }
; template <class Epi, class Sched, bool ALIGN_EPI = false, bool SP2 = false, bool FP8 = false>
; __device__ __forceinline__ void gemm_phase(LAS unsigned char* lds, const Gemm g, const Sched& S, const Epi& E, int wbase) {
;     ...
;         const bool has_next = S.next(ui + 1, nxt);
;         const unsigned nA = has_next ? S.a_off(nxt, g) : cA, nB = has_next ? S.b_off(nxt, g) : cB;
;         const rsrc_t rAn = (Sched::TWO && has_next) ? (nxt.part ? rA1 : rA0) : rAc, rBn = (Sched::TWO && has_next) ? (nxt.part ? rB1 : rB0) : rBc;
;         float pre_[8] = {0.f, 0.f, 0.f, 0.f, 0.f, 0.f, 0.f, 0.f};
;         if constexpr (Epi::HAS_PRE) E.pre_load(pre_, cur, wr);
;         for (int t = 0; t < nt; t += 2) {
;             const bool last = (t == nt - 2);
;             const unsigned a1 = cA + (unsigned)(t + 1) * kstep;
;             const unsigned a2 = last ? nA : cA + (unsigned)(t + 2) * kstep, b2 = last ? nB : cB + (unsigned)(t + 2) * kstep; const rsrc_t rA2 = (Sched::TWO && last) ? rAn : rAc, rB2 = (Sched::TWO && last) ? rBn : rBc;
;             const unsigned a3 = a2 + kstep, b3 = b2 + kstep;
;             if (last && has_next) S.a_ready(nxt);
;             if constexpr (SP2) {
;             PG8_LDB(B0, 0, 0); PG8_LDB(B1, 0, 1); PG8_SCHED; PG8_LDA(At, 0, 0); PG8_STAGE(PG8_SA(1, 1), rAc, a1 + hstep, voffA);
;             PG8_WAIT_V(8); PG8_WAIT_L(0); PG8_BAR; PG8_MMA(0, 0, At, B0); PG8_MMA(0, 1, At, B1); PG8_BAR; PG8_SCHED;
;             PG8_LDA(At, 0, 1); PG8_STAGE(PG8_SB(0, 0), rB2, b2, voffB); PG8_STAGE(PG8_SB(0, 1), rB2, b2 + hstep, voffB); PG8_STAGE(PG8_SA(0, 0), rA2, a2, voffA);
;             PG8_WAIT_V(8); PG8_WAIT_L(0); PG8_BAR; PG8_MMA(1, 0, At, B0); PG8_MMA(1, 1, At, B1); PG8_BAR; PG8_SCHED;
;             PG8_LDB(B0, 1, 0); PG8_LDB(B1, 1, 1); PG8_SCHED; PG8_LDA(At, 1, 0); PG8_STAGE(PG8_SA(0, 1), rA2, a2 + hstep, voffA);
;             PG8_WAIT_V(8); PG8_WAIT_L(0); PG8_BAR; PG8_MMA(0, 0, At, B0); PG8_MMA(0, 1, At, B1); PG8_BAR; PG8_SCHED;
;             PG8_LDA(At, 1, 1); PG8_STAGE(PG8_SB(1, 0), rB2, b3, voffB); PG8_STAGE(PG8_SB(1, 1), rB2, b3 + hstep, voffB); PG8_STAGE(PG8_SA(1, 0), rA2, a3, voffA);
;             PG8_WAIT_V(8); PG8_WAIT_L(0); PG8_BAR; PG8_MMA(1, 0, At, B0); PG8_MMA(1, 1, At, B1); PG8_BAR; PG8_SCHED;
.LBB0_448:
	s_lshl_b32 s48, s47, 17
	s_andn2_b64 vcc, exec, s[10:11]
	s_lshl_b32 s52, s46, 17
	s_cbranch_vccnz .LBB0_456
	s_and_b64 s[6:7], s[16:17], exec
	s_waitcnt vmcnt(37)
	s_waitcnt vmcnt(36)
	s_waitcnt vmcnt(35)
	s_waitcnt vmcnt(32)
	s_waitcnt vmcnt(31)
	s_waitcnt vmcnt(28)
	s_waitcnt vmcnt(27)
	s_waitcnt vmcnt(24)
	s_waitcnt vmcnt(23)
	s_waitcnt vmcnt(22)
	s_cselect_b32 s56, s48, s55
	s_cselect_b32 s57, s52, s54
	s_add_i32 s58, s55, 0x80
	s_add_i32 s59, s54, 0x100
	s_mov_b32 s60, 0
	v_add_u32_e32 v148, 0x10000, v138
	v_add_u32_e32 v164, 0x14000, v138
	ds_read_b128 v[128:131], v148
	ds_read_b128 v[140:143], v148 offset:1024
	ds_read_b128 v[144:147], v148 offset:2048
	ds_read_b128 v[148:151], v148 offset:3072
	ds_read_b128 v[152:155], v164
	ds_read_b128 v[156:159], v164 offset:1024
	ds_read_b128 v[160:163], v164 offset:2048
	ds_read_b128 v[164:167], v164 offset:3072
	s_add_i32 s6, s58, 0x80
	s_cmp_eq_u32 s42, s60
	s_cselect_b32 s61, s56, s6
	s_cselect_b32 s55, s57, s59
	s_or_b32 s54, s61, 0x80
	s_add_i32 s6, s19, s58
	s_mov_b32 m0, s43
	ds_read_b128 v[168:171], v139
	ds_read_b128 v[172:175], v139 offset:1024
	ds_read_b128 v[176:179], v139 offset:2048
	ds_read_b128 v[180:183], v139 offset:3072
	ds_read_b128 v[184:187], v139 offset:4096
	ds_read_b128 v[188:191], v139 offset:5120
	ds_read_b128 v[194:197], v139 offset:6144
	ds_read_b128 v[198:201], v139 offset:7168
	buffer_load_dwordx4 v132, s[36:39], s6 offen lds
	s_mov_b32 m0, s44
	s_nop 0
	buffer_load_dwordx4 v134, s[36:39], s6 offen lds
	s_waitcnt vmcnt(8)
	s_waitcnt lgkmcnt(0)
	s_barrier
	s_setprio 1
	v_mfma_f32_16x16x32_bf16 v[124:127], v[128:131], v[168:171], 0
	v_mfma_f32_16x16x32_bf16 v[120:123], v[144:147], v[168:171], 0
	v_mfma_f32_16x16x32_bf16 v[108:111], v[128:131], v[176:179], 0
	v_mfma_f32_16x16x32_bf16 v[104:107], v[144:147], v[176:179], 0
	v_mfma_f32_16x16x32_bf16 v[92:95], v[128:131], v[184:187], 0
	v_mfma_f32_16x16x32_bf16 v[88:91], v[144:147], v[184:187], 0
	v_mfma_f32_16x16x32_bf16 v[76:79], v[128:131], v[194:197], 0
	v_mfma_f32_16x16x32_bf16 v[72:75], v[144:147], v[194:197], 0
	v_mfma_f32_16x16x32_bf16 v[124:127], v[140:143], v[172:175], v[124:127]
	v_mfma_f32_16x16x32_bf16 v[120:123], v[148:151], v[172:175], v[120:123]
	v_mfma_f32_16x16x32_bf16 v[108:111], v[140:143], v[180:183], v[108:111]
	v_mfma_f32_16x16x32_bf16 v[104:107], v[148:151], v[180:183], v[104:107]
	v_mfma_f32_16x16x32_bf16 v[92:95], v[140:143], v[188:191], v[92:95]
	v_mfma_f32_16x16x32_bf16 v[88:91], v[148:151], v[188:191], v[88:91]
	v_mfma_f32_16x16x32_bf16 v[76:79], v[140:143], v[198:201], v[76:79]
	v_mfma_f32_16x16x32_bf16 v[72:75], v[148:151], v[198:201], v[72:75]
	v_mfma_f32_16x16x32_bf16 v[116:119], v[152:155], v[168:171], 0
	v_mfma_f32_16x16x32_bf16 v[112:115], v[160:163], v[168:171], 0
	v_mfma_f32_16x16x32_bf16 v[100:103], v[152:155], v[176:179], 0
	v_mfma_f32_16x16x32_bf16 v[96:99], v[160:163], v[176:179], 0
	v_mfma_f32_16x16x32_bf16 v[84:87], v[152:155], v[184:187], 0
	v_mfma_f32_16x16x32_bf16 v[80:83], v[160:163], v[184:187], 0
	v_mfma_f32_16x16x32_bf16 v[68:71], v[152:155], v[194:197], 0
	v_mfma_f32_16x16x32_bf16 v[64:67], v[160:163], v[194:197], 0
	v_mfma_f32_16x16x32_bf16 v[116:119], v[156:159], v[172:175], v[116:119]
	v_mfma_f32_16x16x32_bf16 v[112:115], v[164:167], v[172:175], v[112:115]
	v_mfma_f32_16x16x32_bf16 v[100:103], v[156:159], v[180:183], v[100:103]
	v_mfma_f32_16x16x32_bf16 v[96:99], v[164:167], v[180:183], v[96:99]
	v_mfma_f32_16x16x32_bf16 v[84:87], v[156:159], v[188:191], v[84:87]
	v_mfma_f32_16x16x32_bf16 v[80:83], v[164:167], v[188:191], v[80:83]
	v_mfma_f32_16x16x32_bf16 v[68:71], v[156:159], v[198:201], v[68:71]
	v_mfma_f32_16x16x32_bf16 v[64:67], v[164:167], v[198:201], v[64:67]
	s_setprio 0
	s_barrier
	s_mov_b32 m0, s21
	s_mov_b32 s6, s38
	s_mov_b32 s7, s39
	buffer_load_dwordx4 v133, s[4:7], s55 offen lds
	s_mov_b32 m0, s22
	ds_read_b128 v[168:171], v139 offset:16384
	s_add_i32 s62, s55, s19
	buffer_load_dwordx4 v135, s[4:7], s55 offen lds
	s_mov_b32 m0, s23
	ds_read_b128 v[172:175], v139 offset:17408
	buffer_load_dwordx4 v133, s[4:7], s62 offen lds
	s_mov_b32 m0, s24
	ds_read_b128 v[176:179], v139 offset:18432
	buffer_load_dwordx4 v135, s[4:7], s62 offen lds
	s_mov_b32 m0, s20
	ds_read_b128 v[180:183], v139 offset:19456
	buffer_load_dwordx4 v132, s[36:39], s61 offen lds
	s_mov_b32 m0, s25
	ds_read_b128 v[184:187], v139 offset:20480
	buffer_load_dwordx4 v134, s[36:39], s61 offen lds
	ds_read_b128 v[188:191], v139 offset:21504
	ds_read_b128 v[194:197], v139 offset:22528
	ds_read_b128 v[198:201], v139 offset:23552
	s_waitcnt vmcnt(8)
	s_waitcnt lgkmcnt(0)
	s_barrier
; #define PG8_STAGE(bufoff, rs_, soff_, voff) do { _Pragma("unroll") for (int _i = 0; _i < 2; ++_i) \
;         __builtin_amdgcn_raw_ptr_buffer_load_lds(rs_, (LAS void*)(lds + (bufoff) + ldsw + _i * 8192), 16, (int)(voff)[_i], (int)(soff_), 0, 0); } while (0)
; #define PG8_LDA(dst, b, h) do { _Pragma("unroll") for (int m = 0; m < 4; ++m) dst[m] = PG8_LD2(lds + PG8_SA(b, h) + aoff + m * 2048); } while (0)
; #define PG8_LDB(dst, b, h) do { _Pragma("unroll") for (int n = 0; n < 2; ++n) dst[n] = PG8_LD2(lds + PG8_SB(b, h) + boff + n * 2048); } while (0)
; #define PG8_WAIT_V(n) asm volatile("s_waitcnt vmcnt(" #n ")" ::: "memory")
; #define PG8_WAIT_L(n) asm volatile("s_waitcnt lgkmcnt(" #n ")" ::: "memory")
; #define PG8_BAR __builtin_amdgcn_s_barrier()
; #define PG8_SCHED __builtin_amdgcn_sched_barrier(0)
; template <class Epi, class Sched, bool ALIGN_EPI = false, bool SP2 = false, bool FP8 = false>
; __device__ __forceinline__ void gemm_phase(LAS unsigned char* lds, const Gemm g, const Sched& S, const Epi& E, int wbase) {
;     ...
;             PG8_LDB(B0, 0, 0); PG8_LDB(B1, 0, 1); PG8_SCHED; PG8_LDA(At, 0, 0); PG8_STAGE(PG8_SA(1, 1), rAc, a1 + hstep, voffA);
;             PG8_WAIT_V(8); PG8_WAIT_L(0); PG8_BAR; PG8_MMA(0, 0, At, B0); PG8_MMA(0, 1, At, B1); PG8_BAR; PG8_SCHED;
;             PG8_LDA(At, 0, 1); PG8_STAGE(PG8_SB(0, 0), rB2, b2, voffB); PG8_STAGE(PG8_SB(0, 1), rB2, b2 + hstep, voffB); PG8_STAGE(PG8_SA(0, 0), rA2, a2, voffA);
;             PG8_WAIT_V(8); PG8_WAIT_L(0); PG8_BAR; PG8_MMA(1, 0, At, B0); PG8_MMA(1, 1, At, B1); PG8_BAR; PG8_SCHED;
;             PG8_LDB(B0, 1, 0); PG8_LDB(B1, 1, 1); PG8_SCHED; PG8_LDA(At, 1, 0); PG8_STAGE(PG8_SA(0, 1), rA2, a2 + hstep, voffA);
;             PG8_WAIT_V(8); PG8_WAIT_L(0); PG8_BAR; PG8_MMA(0, 0, At, B0); PG8_MMA(0, 1, At, B1); PG8_BAR; PG8_SCHED;
;             PG8_LDA(At, 1, 1); PG8_STAGE(PG8_SB(1, 0), rB2, b3, voffB); PG8_STAGE(PG8_SB(1, 1), rB2, b3 + hstep, voffB); PG8_STAGE(PG8_SA(1, 0), rA2, a3, voffA);
;             PG8_WAIT_V(8); PG8_WAIT_L(0); PG8_BAR; PG8_MMA(1, 0, At, B0); PG8_MMA(1, 1, At, B1); PG8_BAR; PG8_SCHED;
	s_setprio 1
	v_mfma_f32_16x16x32_bf16 v[60:63], v[128:131], v[168:171], 0
	v_mfma_f32_16x16x32_bf16 v[56:59], v[144:147], v[168:171], 0
	v_mfma_f32_16x16x32_bf16 v[44:47], v[128:131], v[176:179], 0
	v_mfma_f32_16x16x32_bf16 v[40:43], v[144:147], v[176:179], 0
	v_mfma_f32_16x16x32_bf16 v[28:31], v[128:131], v[184:187], 0
	v_mfma_f32_16x16x32_bf16 v[24:27], v[144:147], v[184:187], 0
	v_mfma_f32_16x16x32_bf16 v[12:15], v[128:131], v[194:197], 0
	v_mfma_f32_16x16x32_bf16 v[8:11], v[144:147], v[194:197], 0
	v_mfma_f32_16x16x32_bf16 v[60:63], v[140:143], v[172:175], v[60:63]
	v_mfma_f32_16x16x32_bf16 v[56:59], v[148:151], v[172:175], v[56:59]
	v_mfma_f32_16x16x32_bf16 v[44:47], v[140:143], v[180:183], v[44:47]
	v_mfma_f32_16x16x32_bf16 v[40:43], v[148:151], v[180:183], v[40:43]
	v_mfma_f32_16x16x32_bf16 v[28:31], v[140:143], v[188:191], v[28:31]
	v_mfma_f32_16x16x32_bf16 v[24:27], v[148:151], v[188:191], v[24:27]
	v_mfma_f32_16x16x32_bf16 v[12:15], v[140:143], v[198:201], v[12:15]
	v_mfma_f32_16x16x32_bf16 v[8:11], v[148:151], v[198:201], v[8:11]
	v_mfma_f32_16x16x32_bf16 v[52:55], v[152:155], v[168:171], 0
	v_mfma_f32_16x16x32_bf16 v[48:51], v[160:163], v[168:171], 0
	v_mfma_f32_16x16x32_bf16 v[36:39], v[152:155], v[176:179], 0
	v_mfma_f32_16x16x32_bf16 v[32:35], v[160:163], v[176:179], 0
	v_mfma_f32_16x16x32_bf16 v[20:23], v[152:155], v[184:187], 0
	v_mfma_f32_16x16x32_bf16 v[16:19], v[160:163], v[184:187], 0
	v_mfma_f32_16x16x32_bf16 v[4:7], v[152:155], v[194:197], 0
	v_mfma_f32_16x16x32_bf16 v[0:3], v[160:163], v[194:197], 0
	v_mfma_f32_16x16x32_bf16 v[52:55], v[156:159], v[172:175], v[52:55]
	v_mfma_f32_16x16x32_bf16 v[48:51], v[164:167], v[172:175], v[48:51]
	v_mfma_f32_16x16x32_bf16 v[36:39], v[156:159], v[180:183], v[36:39]
	v_mfma_f32_16x16x32_bf16 v[32:35], v[164:167], v[180:183], v[32:35]
	v_mfma_f32_16x16x32_bf16 v[20:23], v[156:159], v[188:191], v[20:23]
	v_mfma_f32_16x16x32_bf16 v[16:19], v[164:167], v[188:191], v[16:19]
	v_mfma_f32_16x16x32_bf16 v[4:7], v[156:159], v[198:201], v[4:7]
	v_mfma_f32_16x16x32_bf16 v[0:3], v[164:167], v[198:201], v[0:3]
	s_setprio 0
	s_barrier
	v_add_u32_e32 v148, 0x18000, v138
	v_add_u32_e32 v164, 0x1c000, v138
	ds_read_b128 v[128:131], v148
	ds_read_b128 v[140:143], v148 offset:1024
	ds_read_b128 v[144:147], v148 offset:2048
	ds_read_b128 v[148:151], v148 offset:3072
	ds_read_b128 v[152:155], v164
	ds_read_b128 v[156:159], v164 offset:1024
	ds_read_b128 v[160:163], v164 offset:2048
	ds_read_b128 v[164:167], v164 offset:3072
	s_add_i32 s61, s61, s19
	s_mov_b32 m0, s26
	ds_read_b128 v[168:171], v139 offset:32768
	ds_read_b128 v[172:175], v139 offset:33792
	ds_read_b128 v[176:179], v139 offset:34816
	ds_read_b128 v[180:183], v139 offset:35840
	ds_read_b128 v[184:187], v139 offset:36864
	ds_read_b128 v[188:191], v139 offset:37888
	ds_read_b128 v[194:197], v139 offset:38912
	ds_read_b128 v[198:201], v139 offset:39936
	buffer_load_dwordx4 v132, s[36:39], s61 offen lds
	s_mov_b32 m0, s27
	s_nop 0
	buffer_load_dwordx4 v134, s[36:39], s61 offen lds
	s_waitcnt vmcnt(8)
	s_waitcnt lgkmcnt(0)
	s_barrier
	s_setprio 1
	v_mfma_f32_16x16x32_bf16 v[124:127], v[128:131], v[168:171], v[124:127]
	v_mfma_f32_16x16x32_bf16 v[120:123], v[144:147], v[168:171], v[120:123]
	v_mfma_f32_16x16x32_bf16 v[108:111], v[128:131], v[176:179], v[108:111]
	v_mfma_f32_16x16x32_bf16 v[104:107], v[144:147], v[176:179], v[104:107]
	v_mfma_f32_16x16x32_bf16 v[92:95], v[128:131], v[184:187], v[92:95]
	v_mfma_f32_16x16x32_bf16 v[88:91], v[144:147], v[184:187], v[88:91]
	v_mfma_f32_16x16x32_bf16 v[76:79], v[128:131], v[194:197], v[76:79]
	v_mfma_f32_16x16x32_bf16 v[72:75], v[144:147], v[194:197], v[72:75]
	v_mfma_f32_16x16x32_bf16 v[124:127], v[140:143], v[172:175], v[124:127]
	v_mfma_f32_16x16x32_bf16 v[120:123], v[148:151], v[172:175], v[120:123]
	v_mfma_f32_16x16x32_bf16 v[108:111], v[140:143], v[180:183], v[108:111]
	v_mfma_f32_16x16x32_bf16 v[104:107], v[148:151], v[180:183], v[104:107]
	v_mfma_f32_16x16x32_bf16 v[92:95], v[140:143], v[188:191], v[92:95]
	v_mfma_f32_16x16x32_bf16 v[88:91], v[148:151], v[188:191], v[88:91]
	v_mfma_f32_16x16x32_bf16 v[76:79], v[140:143], v[198:201], v[76:79]
	v_mfma_f32_16x16x32_bf16 v[72:75], v[148:151], v[198:201], v[72:75]
	v_mfma_f32_16x16x32_bf16 v[116:119], v[152:155], v[168:171], v[116:119]
	v_mfma_f32_16x16x32_bf16 v[112:115], v[160:163], v[168:171], v[112:115]
	v_mfma_f32_16x16x32_bf16 v[100:103], v[152:155], v[176:179], v[100:103]
	v_mfma_f32_16x16x32_bf16 v[96:99], v[160:163], v[176:179], v[96:99]
	v_mfma_f32_16x16x32_bf16 v[84:87], v[152:155], v[184:187], v[84:87]
	v_mfma_f32_16x16x32_bf16 v[80:83], v[160:163], v[184:187], v[80:83]
	v_mfma_f32_16x16x32_bf16 v[68:71], v[152:155], v[194:197], v[68:71]
	v_mfma_f32_16x16x32_bf16 v[64:67], v[160:163], v[194:197], v[64:67]
	v_mfma_f32_16x16x32_bf16 v[116:119], v[156:159], v[172:175], v[116:119]
	v_mfma_f32_16x16x32_bf16 v[112:115], v[164:167], v[172:175], v[112:115]
	v_mfma_f32_16x16x32_bf16 v[100:103], v[156:159], v[180:183], v[100:103]
	v_mfma_f32_16x16x32_bf16 v[96:99], v[164:167], v[180:183], v[96:99]
	v_mfma_f32_16x16x32_bf16 v[84:87], v[156:159], v[188:191], v[84:87]
	v_mfma_f32_16x16x32_bf16 v[80:83], v[164:167], v[188:191], v[80:83]
	v_mfma_f32_16x16x32_bf16 v[68:71], v[156:159], v[198:201], v[68:71]
	v_mfma_f32_16x16x32_bf16 v[64:67], v[164:167], v[198:201], v[64:67]
	s_setprio 0
	s_barrier
; #define PG8_STAGE(bufoff, rs_, soff_, voff) do { _Pragma("unroll") for (int _i = 0; _i < 2; ++_i) \
;         __builtin_amdgcn_raw_ptr_buffer_load_lds(rs_, (LAS void*)(lds + (bufoff) + ldsw + _i * 8192), 16, (int)(voff)[_i], (int)(soff_), 0, 0); } while (0)
; #define PG8_LDA(dst, b, h) do { _Pragma("unroll") for (int m = 0; m < 4; ++m) dst[m] = PG8_LD2(lds + PG8_SA(b, h) + aoff + m * 2048); } while (0)
; #define PG8_LDB(dst, b, h) do { _Pragma("unroll") for (int n = 0; n < 2; ++n) dst[n] = PG8_LD2(lds + PG8_SB(b, h) + boff + n * 2048); } while (0)
; #define PG8_WAIT_V(n) asm volatile("s_waitcnt vmcnt(" #n ")" ::: "memory")
; #define PG8_WAIT_L(n) asm volatile("s_waitcnt lgkmcnt(" #n ")" ::: "memory")
; #define PG8_BAR __builtin_amdgcn_s_barrier()
; #define PG8_SCHED __builtin_amdgcn_sched_barrier(0)
; template <class Epi, class Sched, bool ALIGN_EPI = false, bool SP2 = false, bool FP8 = false>
; __device__ __forceinline__ void gemm_phase(LAS unsigned char* lds, const Gemm g, const Sched& S, const Epi& E, int wbase) {
;     ...
;             PG8_LDB(B0, 0, 0); PG8_LDB(B1, 0, 1); PG8_SCHED; PG8_LDA(At, 0, 0); PG8_STAGE(PG8_SA(1, 1), rAc, a1 + hstep, voffA);
;             PG8_WAIT_V(8); PG8_WAIT_L(0); PG8_BAR; PG8_MMA(0, 0, At, B0); PG8_MMA(0, 1, At, B1); PG8_BAR; PG8_SCHED;
;             PG8_LDA(At, 0, 1); PG8_STAGE(PG8_SB(0, 0), rB2, b2, voffB); PG8_STAGE(PG8_SB(0, 1), rB2, b2 + hstep, voffB); PG8_STAGE(PG8_SA(0, 0), rA2, a2, voffA);
;             PG8_WAIT_V(8); PG8_WAIT_L(0); PG8_BAR; PG8_MMA(1, 0, At, B0); PG8_MMA(1, 1, At, B1); PG8_BAR; PG8_SCHED;
;             PG8_LDB(B0, 1, 0); PG8_LDB(B1, 1, 1); PG8_SCHED; PG8_LDA(At, 1, 0); PG8_STAGE(PG8_SA(0, 1), rA2, a2 + hstep, voffA);
;             PG8_WAIT_V(8); PG8_WAIT_L(0); PG8_BAR; PG8_MMA(0, 0, At, B0); PG8_MMA(0, 1, At, B1); PG8_BAR; PG8_SCHED;
;             PG8_LDA(At, 1, 1); PG8_STAGE(PG8_SB(1, 0), rB2, b3, voffB); PG8_STAGE(PG8_SB(1, 1), rB2, b3 + hstep, voffB); PG8_STAGE(PG8_SA(1, 0), rA2, a3, voffA);
;             PG8_WAIT_V(8); PG8_WAIT_L(0); PG8_BAR; PG8_MMA(1, 0, At, B0); PG8_MMA(1, 1, At, B1); PG8_BAR; PG8_SCHED;
	s_mov_b32 m0, s28
	s_bitset1_b32 s55, 7
	buffer_load_dwordx4 v133, s[4:7], s55 offen lds
	s_mov_b32 m0, s29
	ds_read_b128 v[168:171], v139 offset:49152
	buffer_load_dwordx4 v135, s[4:7], s55 offen lds
	s_add_i32 s55, s55, s19
	s_mov_b32 m0, s33
	ds_read_b128 v[172:175], v139 offset:50176
	buffer_load_dwordx4 v133, s[4:7], s55 offen lds
	s_mov_b32 m0, s34
	ds_read_b128 v[176:179], v139 offset:51200
	buffer_load_dwordx4 v135, s[4:7], s55 offen lds
	s_mov_b32 m0, s30
	ds_read_b128 v[180:183], v139 offset:52224
	buffer_load_dwordx4 v132, s[36:39], s54 offen lds
	s_mov_b32 m0, s31
	ds_read_b128 v[184:187], v139 offset:53248
	buffer_load_dwordx4 v134, s[36:39], s54 offen lds
	ds_read_b128 v[188:191], v139 offset:54272
	ds_read_b128 v[194:197], v139 offset:55296
	ds_read_b128 v[198:201], v139 offset:56320
	s_waitcnt vmcnt(8)
	s_waitcnt lgkmcnt(0)
	s_barrier
	s_setprio 1
	v_mfma_f32_16x16x32_bf16 v[60:63], v[128:131], v[168:171], v[60:63]
	v_mfma_f32_16x16x32_bf16 v[56:59], v[144:147], v[168:171], v[56:59]
	v_mfma_f32_16x16x32_bf16 v[44:47], v[128:131], v[176:179], v[44:47]
	v_mfma_f32_16x16x32_bf16 v[40:43], v[144:147], v[176:179], v[40:43]
	v_mfma_f32_16x16x32_bf16 v[28:31], v[128:131], v[184:187], v[28:31]
	v_mfma_f32_16x16x32_bf16 v[24:27], v[144:147], v[184:187], v[24:27]
	v_mfma_f32_16x16x32_bf16 v[12:15], v[128:131], v[194:197], v[12:15]
	v_mfma_f32_16x16x32_bf16 v[8:11], v[144:147], v[194:197], v[8:11]
	v_mfma_f32_16x16x32_bf16 v[60:63], v[140:143], v[172:175], v[60:63]
	v_mfma_f32_16x16x32_bf16 v[56:59], v[148:151], v[172:175], v[56:59]
	v_mfma_f32_16x16x32_bf16 v[44:47], v[140:143], v[180:183], v[44:47]
	v_mfma_f32_16x16x32_bf16 v[40:43], v[148:151], v[180:183], v[40:43]
	v_mfma_f32_16x16x32_bf16 v[28:31], v[140:143], v[188:191], v[28:31]
	v_mfma_f32_16x16x32_bf16 v[24:27], v[148:151], v[188:191], v[24:27]
	v_mfma_f32_16x16x32_bf16 v[12:15], v[140:143], v[198:201], v[12:15]
	v_mfma_f32_16x16x32_bf16 v[8:11], v[148:151], v[198:201], v[8:11]
	v_mfma_f32_16x16x32_bf16 v[52:55], v[152:155], v[168:171], v[52:55]
	v_mfma_f32_16x16x32_bf16 v[48:51], v[160:163], v[168:171], v[48:51]
	v_mfma_f32_16x16x32_bf16 v[36:39], v[152:155], v[176:179], v[36:39]
	v_mfma_f32_16x16x32_bf16 v[32:35], v[160:163], v[176:179], v[32:35]
	v_mfma_f32_16x16x32_bf16 v[20:23], v[152:155], v[184:187], v[20:23]
	v_mfma_f32_16x16x32_bf16 v[16:19], v[160:163], v[184:187], v[16:19]
	v_mfma_f32_16x16x32_bf16 v[4:7], v[152:155], v[194:197], v[4:7]
	v_mfma_f32_16x16x32_bf16 v[0:3], v[160:163], v[194:197], v[0:3]
	v_mfma_f32_16x16x32_bf16 v[52:55], v[156:159], v[172:175], v[52:55]
	v_mfma_f32_16x16x32_bf16 v[48:51], v[164:167], v[172:175], v[48:51]
	v_mfma_f32_16x16x32_bf16 v[36:39], v[156:159], v[180:183], v[36:39]
	v_mfma_f32_16x16x32_bf16 v[32:35], v[164:167], v[180:183], v[32:35]
	v_mfma_f32_16x16x32_bf16 v[20:23], v[156:159], v[188:191], v[20:23]
	v_mfma_f32_16x16x32_bf16 v[16:19], v[164:167], v[188:191], v[16:19]
	v_mfma_f32_16x16x32_bf16 v[4:7], v[156:159], v[198:201], v[4:7]
	v_mfma_f32_16x16x32_bf16 v[0:3], v[164:167], v[198:201], v[0:3]
	s_setprio 0
	s_barrier
	s_add_i32 s60, s60, 2
	s_addk_i32 s58, 0x100
	s_addk_i32 s59, 0x100
	s_cmp_ge_i32 s60, s35
	s_cbranch_scc0 .LBB0_450
	s_branch .Lzp_after_450
.LBB0_450:
	v_add_u32_e32 v148, 0x10000, v138
	v_add_u32_e32 v164, 0x14000, v138
	ds_read_b128 v[128:131], v148
	ds_read_b128 v[140:143], v148 offset:1024
	ds_read_b128 v[144:147], v148 offset:2048
	ds_read_b128 v[148:151], v148 offset:3072
	ds_read_b128 v[152:155], v164
	ds_read_b128 v[156:159], v164 offset:1024
	ds_read_b128 v[160:163], v164 offset:2048
	ds_read_b128 v[164:167], v164 offset:3072
	s_add_i32 s6, s58, 0x80
	s_cmp_eq_u32 s42, s60
	s_cselect_b32 s61, s56, s6
	s_cselect_b32 s55, s57, s59
	s_or_b32 s54, s61, 0x80
	s_add_i32 s6, s19, s58
	s_mov_b32 m0, s43
	ds_read_b128 v[168:171], v139
	ds_read_b128 v[172:175], v139 offset:1024
	ds_read_b128 v[176:179], v139 offset:2048
	ds_read_b128 v[180:183], v139 offset:3072
	ds_read_b128 v[184:187], v139 offset:4096
	ds_read_b128 v[188:191], v139 offset:5120
	ds_read_b128 v[194:197], v139 offset:6144
	ds_read_b128 v[198:201], v139 offset:7168
	buffer_load_dwordx4 v132, s[36:39], s6 offen lds
	s_mov_b32 m0, s44
	s_nop 0
	buffer_load_dwordx4 v134, s[36:39], s6 offen lds
	s_waitcnt vmcnt(8)
	s_waitcnt lgkmcnt(0)
	s_barrier
	s_setprio 1
	v_mfma_f32_16x16x32_bf16 v[124:127], v[128:131], v[168:171], v[124:127]
	v_mfma_f32_16x16x32_bf16 v[120:123], v[144:147], v[168:171], v[120:123]
	v_mfma_f32_16x16x32_bf16 v[108:111], v[128:131], v[176:179], v[108:111]
	v_mfma_f32_16x16x32_bf16 v[104:107], v[144:147], v[176:179], v[104:107]
	v_mfma_f32_16x16x32_bf16 v[92:95], v[128:131], v[184:187], v[92:95]
	v_mfma_f32_16x16x32_bf16 v[88:91], v[144:147], v[184:187], v[88:91]
	v_mfma_f32_16x16x32_bf16 v[76:79], v[128:131], v[194:197], v[76:79]
	v_mfma_f32_16x16x32_bf16 v[72:75], v[144:147], v[194:197], v[72:75]
	v_mfma_f32_16x16x32_bf16 v[124:127], v[140:143], v[172:175], v[124:127]
	v_mfma_f32_16x16x32_bf16 v[120:123], v[148:151], v[172:175], v[120:123]
	v_mfma_f32_16x16x32_bf16 v[108:111], v[140:143], v[180:183], v[108:111]
	v_mfma_f32_16x16x32_bf16 v[104:107], v[148:151], v[180:183], v[104:107]
	v_mfma_f32_16x16x32_bf16 v[92:95], v[140:143], v[188:191], v[92:95]
	v_mfma_f32_16x16x32_bf16 v[88:91], v[148:151], v[188:191], v[88:91]
	v_mfma_f32_16x16x32_bf16 v[76:79], v[140:143], v[198:201], v[76:79]
	v_mfma_f32_16x16x32_bf16 v[72:75], v[148:151], v[198:201], v[72:75]
	v_mfma_f32_16x16x32_bf16 v[116:119], v[152:155], v[168:171], v[116:119]
	v_mfma_f32_16x16x32_bf16 v[112:115], v[160:163], v[168:171], v[112:115]
	v_mfma_f32_16x16x32_bf16 v[100:103], v[152:155], v[176:179], v[100:103]
	v_mfma_f32_16x16x32_bf16 v[96:99], v[160:163], v[176:179], v[96:99]
	v_mfma_f32_16x16x32_bf16 v[84:87], v[152:155], v[184:187], v[84:87]
	v_mfma_f32_16x16x32_bf16 v[80:83], v[160:163], v[184:187], v[80:83]
	v_mfma_f32_16x16x32_bf16 v[68:71], v[152:155], v[194:197], v[68:71]
	v_mfma_f32_16x16x32_bf16 v[64:67], v[160:163], v[194:197], v[64:67]
	v_mfma_f32_16x16x32_bf16 v[116:119], v[156:159], v[172:175], v[116:119]
	v_mfma_f32_16x16x32_bf16 v[112:115], v[164:167], v[172:175], v[112:115]
	v_mfma_f32_16x16x32_bf16 v[100:103], v[156:159], v[180:183], v[100:103]
	v_mfma_f32_16x16x32_bf16 v[96:99], v[164:167], v[180:183], v[96:99]
	v_mfma_f32_16x16x32_bf16 v[84:87], v[156:159], v[188:191], v[84:87]
	v_mfma_f32_16x16x32_bf16 v[80:83], v[164:167], v[188:191], v[80:83]
	v_mfma_f32_16x16x32_bf16 v[68:71], v[156:159], v[198:201], v[68:71]
	v_mfma_f32_16x16x32_bf16 v[64:67], v[164:167], v[198:201], v[64:67]
	s_setprio 0
	s_barrier
; #define PG8_STAGE(bufoff, rs_, soff_, voff) do { _Pragma("unroll") for (int _i = 0; _i < 2; ++_i) \
;         __builtin_amdgcn_raw_ptr_buffer_load_lds(rs_, (LAS void*)(lds + (bufoff) + ldsw + _i * 8192), 16, (int)(voff)[_i], (int)(soff_), 0, 0); } while (0)
; #define PG8_LDA(dst, b, h) do { _Pragma("unroll") for (int m = 0; m < 4; ++m) dst[m] = PG8_LD2(lds + PG8_SA(b, h) + aoff + m * 2048); } while (0)
; #define PG8_LDB(dst, b, h) do { _Pragma("unroll") for (int n = 0; n < 2; ++n) dst[n] = PG8_LD2(lds + PG8_SB(b, h) + boff + n * 2048); } while (0)
; #define PG8_WAIT_V(n) asm volatile("s_waitcnt vmcnt(" #n ")" ::: "memory")
; #define PG8_WAIT_L(n) asm volatile("s_waitcnt lgkmcnt(" #n ")" ::: "memory")
; #define PG8_BAR __builtin_amdgcn_s_barrier()
; #define PG8_SCHED __builtin_amdgcn_sched_barrier(0)
; template <class Epi, class Sched, bool ALIGN_EPI = false, bool SP2 = false, bool FP8 = false>
; __device__ __forceinline__ void gemm_phase(LAS unsigned char* lds, const Gemm g, const Sched& S, const Epi& E, int wbase) {
;     ...
;             PG8_LDB(B0, 0, 0); PG8_LDB(B1, 0, 1); PG8_SCHED; PG8_LDA(At, 0, 0); PG8_STAGE(PG8_SA(1, 1), rAc, a1 + hstep, voffA);
;             PG8_WAIT_V(8); PG8_WAIT_L(0); PG8_BAR; PG8_MMA(0, 0, At, B0); PG8_MMA(0, 1, At, B1); PG8_BAR; PG8_SCHED;
;             PG8_LDA(At, 0, 1); PG8_STAGE(PG8_SB(0, 0), rB2, b2, voffB); PG8_STAGE(PG8_SB(0, 1), rB2, b2 + hstep, voffB); PG8_STAGE(PG8_SA(0, 0), rA2, a2, voffA);
;             PG8_WAIT_V(8); PG8_WAIT_L(0); PG8_BAR; PG8_MMA(1, 0, At, B0); PG8_MMA(1, 1, At, B1); PG8_BAR; PG8_SCHED;
;             PG8_LDB(B0, 1, 0); PG8_LDB(B1, 1, 1); PG8_SCHED; PG8_LDA(At, 1, 0); PG8_STAGE(PG8_SA(0, 1), rA2, a2 + hstep, voffA);
;             PG8_WAIT_V(8); PG8_WAIT_L(0); PG8_BAR; PG8_MMA(0, 0, At, B0); PG8_MMA(0, 1, At, B1); PG8_BAR; PG8_SCHED;
;             PG8_LDA(At, 1, 1); PG8_STAGE(PG8_SB(1, 0), rB2, b3, voffB); PG8_STAGE(PG8_SB(1, 1), rB2, b3 + hstep, voffB); PG8_STAGE(PG8_SA(1, 0), rA2, a3, voffA);
;             PG8_WAIT_V(8); PG8_WAIT_L(0); PG8_BAR; PG8_MMA(1, 0, At, B0); PG8_MMA(1, 1, At, B1); PG8_BAR; PG8_SCHED;
	s_mov_b32 m0, s21
	s_mov_b32 s6, s38
	s_mov_b32 s7, s39
	buffer_load_dwordx4 v133, s[4:7], s55 offen lds
	s_mov_b32 m0, s22
	ds_read_b128 v[168:171], v139 offset:16384
	s_add_i32 s62, s55, s19
	buffer_load_dwordx4 v135, s[4:7], s55 offen lds
	s_mov_b32 m0, s23
	ds_read_b128 v[172:175], v139 offset:17408
	buffer_load_dwordx4 v133, s[4:7], s62 offen lds
	s_mov_b32 m0, s24
	ds_read_b128 v[176:179], v139 offset:18432
	buffer_load_dwordx4 v135, s[4:7], s62 offen lds
	s_mov_b32 m0, s20
	ds_read_b128 v[180:183], v139 offset:19456
	buffer_load_dwordx4 v132, s[36:39], s61 offen lds
	s_mov_b32 m0, s25
	ds_read_b128 v[184:187], v139 offset:20480
	buffer_load_dwordx4 v134, s[36:39], s61 offen lds
	ds_read_b128 v[188:191], v139 offset:21504
	ds_read_b128 v[194:197], v139 offset:22528
	ds_read_b128 v[198:201], v139 offset:23552
	s_waitcnt vmcnt(8)
	s_waitcnt lgkmcnt(0)
	s_barrier
	s_setprio 1
	v_mfma_f32_16x16x32_bf16 v[60:63], v[128:131], v[168:171], v[60:63]
	v_mfma_f32_16x16x32_bf16 v[56:59], v[144:147], v[168:171], v[56:59]
	v_mfma_f32_16x16x32_bf16 v[44:47], v[128:131], v[176:179], v[44:47]
	v_mfma_f32_16x16x32_bf16 v[40:43], v[144:147], v[176:179], v[40:43]
	v_mfma_f32_16x16x32_bf16 v[28:31], v[128:131], v[184:187], v[28:31]
	v_mfma_f32_16x16x32_bf16 v[24:27], v[144:147], v[184:187], v[24:27]
	v_mfma_f32_16x16x32_bf16 v[12:15], v[128:131], v[194:197], v[12:15]
	v_mfma_f32_16x16x32_bf16 v[8:11], v[144:147], v[194:197], v[8:11]
	v_mfma_f32_16x16x32_bf16 v[60:63], v[140:143], v[172:175], v[60:63]
	v_mfma_f32_16x16x32_bf16 v[56:59], v[148:151], v[172:175], v[56:59]
	v_mfma_f32_16x16x32_bf16 v[44:47], v[140:143], v[180:183], v[44:47]
	v_mfma_f32_16x16x32_bf16 v[40:43], v[148:151], v[180:183], v[40:43]
	v_mfma_f32_16x16x32_bf16 v[28:31], v[140:143], v[188:191], v[28:31]
	v_mfma_f32_16x16x32_bf16 v[24:27], v[148:151], v[188:191], v[24:27]
	v_mfma_f32_16x16x32_bf16 v[12:15], v[140:143], v[198:201], v[12:15]
	v_mfma_f32_16x16x32_bf16 v[8:11], v[148:151], v[198:201], v[8:11]
	v_mfma_f32_16x16x32_bf16 v[52:55], v[152:155], v[168:171], v[52:55]
	v_mfma_f32_16x16x32_bf16 v[48:51], v[160:163], v[168:171], v[48:51]
	v_mfma_f32_16x16x32_bf16 v[36:39], v[152:155], v[176:179], v[36:39]
	v_mfma_f32_16x16x32_bf16 v[32:35], v[160:163], v[176:179], v[32:35]
	v_mfma_f32_16x16x32_bf16 v[20:23], v[152:155], v[184:187], v[20:23]
	v_mfma_f32_16x16x32_bf16 v[16:19], v[160:163], v[184:187], v[16:19]
	v_mfma_f32_16x16x32_bf16 v[4:7], v[152:155], v[194:197], v[4:7]
	v_mfma_f32_16x16x32_bf16 v[0:3], v[160:163], v[194:197], v[0:3]
	v_mfma_f32_16x16x32_bf16 v[52:55], v[156:159], v[172:175], v[52:55]
	v_mfma_f32_16x16x32_bf16 v[48:51], v[164:167], v[172:175], v[48:51]
	v_mfma_f32_16x16x32_bf16 v[36:39], v[156:159], v[180:183], v[36:39]
	v_mfma_f32_16x16x32_bf16 v[32:35], v[164:167], v[180:183], v[32:35]
	v_mfma_f32_16x16x32_bf16 v[20:23], v[156:159], v[188:191], v[20:23]
	v_mfma_f32_16x16x32_bf16 v[16:19], v[164:167], v[188:191], v[16:19]
	v_mfma_f32_16x16x32_bf16 v[4:7], v[156:159], v[198:201], v[4:7]
	v_mfma_f32_16x16x32_bf16 v[0:3], v[164:167], v[198:201], v[0:3]
	s_setprio 0
	s_barrier
	v_add_u32_e32 v148, 0x18000, v138
	v_add_u32_e32 v164, 0x1c000, v138
	ds_read_b128 v[128:131], v148
	ds_read_b128 v[140:143], v148 offset:1024
	ds_read_b128 v[144:147], v148 offset:2048
	ds_read_b128 v[148:151], v148 offset:3072
	ds_read_b128 v[152:155], v164
	ds_read_b128 v[156:159], v164 offset:1024
	ds_read_b128 v[160:163], v164 offset:2048
	ds_read_b128 v[164:167], v164 offset:3072
	s_add_i32 s61, s61, s19
	s_mov_b32 m0, s26
	ds_read_b128 v[168:171], v139 offset:32768
	ds_read_b128 v[172:175], v139 offset:33792
	ds_read_b128 v[176:179], v139 offset:34816
	ds_read_b128 v[180:183], v139 offset:35840
	ds_read_b128 v[184:187], v139 offset:36864
	ds_read_b128 v[188:191], v139 offset:37888
	ds_read_b128 v[194:197], v139 offset:38912
	ds_read_b128 v[198:201], v139 offset:39936
	buffer_load_dwordx4 v132, s[36:39], s61 offen lds
	s_mov_b32 m0, s27
	s_nop 0
	buffer_load_dwordx4 v134, s[36:39], s61 offen lds
	s_waitcnt vmcnt(8)
	s_waitcnt lgkmcnt(0)
	s_barrier
; #define PG8_STAGE(bufoff, rs_, soff_, voff) do { _Pragma("unroll") for (int _i = 0; _i < 2; ++_i) \
;         __builtin_amdgcn_raw_ptr_buffer_load_lds(rs_, (LAS void*)(lds + (bufoff) + ldsw + _i * 8192), 16, (int)(voff)[_i], (int)(soff_), 0, 0); } while (0)
; #define PG8_LDA(dst, b, h) do { _Pragma("unroll") for (int m = 0; m < 4; ++m) dst[m] = PG8_LD2(lds + PG8_SA(b, h) + aoff + m * 2048); } while (0)
; #define PG8_LDB(dst, b, h) do { _Pragma("unroll") for (int n = 0; n < 2; ++n) dst[n] = PG8_LD2(lds + PG8_SB(b, h) + boff + n * 2048); } while (0)
; #define PG8_WAIT_V(n) asm volatile("s_waitcnt vmcnt(" #n ")" ::: "memory")
; #define PG8_WAIT_L(n) asm volatile("s_waitcnt lgkmcnt(" #n ")" ::: "memory")
; #define PG8_BAR __builtin_amdgcn_s_barrier()
; #define PG8_SCHED __builtin_amdgcn_sched_barrier(0)
; template <class Epi, class Sched, bool ALIGN_EPI = false, bool SP2 = false, bool FP8 = false>
; __device__ __forceinline__ void gemm_phase(LAS unsigned char* lds, const Gemm g, const Sched& S, const Epi& E, int wbase) {
;     ...
;             PG8_LDB(B0, 0, 0); PG8_LDB(B1, 0, 1); PG8_SCHED; PG8_LDA(At, 0, 0); PG8_STAGE(PG8_SA(1, 1), rAc, a1 + hstep, voffA);
;             PG8_WAIT_V(8); PG8_WAIT_L(0); PG8_BAR; PG8_MMA(0, 0, At, B0); PG8_MMA(0, 1, At, B1); PG8_BAR; PG8_SCHED;
;             PG8_LDA(At, 0, 1); PG8_STAGE(PG8_SB(0, 0), rB2, b2, voffB); PG8_STAGE(PG8_SB(0, 1), rB2, b2 + hstep, voffB); PG8_STAGE(PG8_SA(0, 0), rA2, a2, voffA);
;             PG8_WAIT_V(8); PG8_WAIT_L(0); PG8_BAR; PG8_MMA(1, 0, At, B0); PG8_MMA(1, 1, At, B1); PG8_BAR; PG8_SCHED;
;             PG8_LDB(B0, 1, 0); PG8_LDB(B1, 1, 1); PG8_SCHED; PG8_LDA(At, 1, 0); PG8_STAGE(PG8_SA(0, 1), rA2, a2 + hstep, voffA);
;             PG8_WAIT_V(8); PG8_WAIT_L(0); PG8_BAR; PG8_MMA(0, 0, At, B0); PG8_MMA(0, 1, At, B1); PG8_BAR; PG8_SCHED;
;             PG8_LDA(At, 1, 1); PG8_STAGE(PG8_SB(1, 0), rB2, b3, voffB); PG8_STAGE(PG8_SB(1, 1), rB2, b3 + hstep, voffB); PG8_STAGE(PG8_SA(1, 0), rA2, a3, voffA);
;             PG8_WAIT_V(8); PG8_WAIT_L(0); PG8_BAR; PG8_MMA(1, 0, At, B0); PG8_MMA(1, 1, At, B1); PG8_BAR; PG8_SCHED;
	s_setprio 1
	v_mfma_f32_16x16x32_bf16 v[124:127], v[128:131], v[168:171], v[124:127]
	v_mfma_f32_16x16x32_bf16 v[120:123], v[144:147], v[168:171], v[120:123]
	v_mfma_f32_16x16x32_bf16 v[108:111], v[128:131], v[176:179], v[108:111]
	v_mfma_f32_16x16x32_bf16 v[104:107], v[144:147], v[176:179], v[104:107]
	v_mfma_f32_16x16x32_bf16 v[92:95], v[128:131], v[184:187], v[92:95]
	v_mfma_f32_16x16x32_bf16 v[88:91], v[144:147], v[184:187], v[88:91]
	v_mfma_f32_16x16x32_bf16 v[76:79], v[128:131], v[194:197], v[76:79]
	v_mfma_f32_16x16x32_bf16 v[72:75], v[144:147], v[194:197], v[72:75]
	v_mfma_f32_16x16x32_bf16 v[124:127], v[140:143], v[172:175], v[124:127]
	v_mfma_f32_16x16x32_bf16 v[120:123], v[148:151], v[172:175], v[120:123]
	v_mfma_f32_16x16x32_bf16 v[108:111], v[140:143], v[180:183], v[108:111]
	v_mfma_f32_16x16x32_bf16 v[104:107], v[148:151], v[180:183], v[104:107]
	v_mfma_f32_16x16x32_bf16 v[92:95], v[140:143], v[188:191], v[92:95]
	v_mfma_f32_16x16x32_bf16 v[88:91], v[148:151], v[188:191], v[88:91]
	v_mfma_f32_16x16x32_bf16 v[76:79], v[140:143], v[198:201], v[76:79]
	v_mfma_f32_16x16x32_bf16 v[72:75], v[148:151], v[198:201], v[72:75]
	v_mfma_f32_16x16x32_bf16 v[116:119], v[152:155], v[168:171], v[116:119]
	v_mfma_f32_16x16x32_bf16 v[112:115], v[160:163], v[168:171], v[112:115]
	v_mfma_f32_16x16x32_bf16 v[100:103], v[152:155], v[176:179], v[100:103]
	v_mfma_f32_16x16x32_bf16 v[96:99], v[160:163], v[176:179], v[96:99]
	v_mfma_f32_16x16x32_bf16 v[84:87], v[152:155], v[184:187], v[84:87]
	v_mfma_f32_16x16x32_bf16 v[80:83], v[160:163], v[184:187], v[80:83]
	v_mfma_f32_16x16x32_bf16 v[68:71], v[152:155], v[194:197], v[68:71]
	v_mfma_f32_16x16x32_bf16 v[64:67], v[160:163], v[194:197], v[64:67]
	v_mfma_f32_16x16x32_bf16 v[116:119], v[156:159], v[172:175], v[116:119]
	v_mfma_f32_16x16x32_bf16 v[112:115], v[164:167], v[172:175], v[112:115]
	v_mfma_f32_16x16x32_bf16 v[100:103], v[156:159], v[180:183], v[100:103]
	v_mfma_f32_16x16x32_bf16 v[96:99], v[164:167], v[180:183], v[96:99]
	v_mfma_f32_16x16x32_bf16 v[84:87], v[156:159], v[188:191], v[84:87]
	v_mfma_f32_16x16x32_bf16 v[80:83], v[164:167], v[188:191], v[80:83]
	v_mfma_f32_16x16x32_bf16 v[68:71], v[156:159], v[198:201], v[68:71]
	v_mfma_f32_16x16x32_bf16 v[64:67], v[164:167], v[198:201], v[64:67]
	s_setprio 0
	s_barrier
	s_mov_b32 m0, s28
	s_bitset1_b32 s55, 7
	buffer_load_dwordx4 v133, s[4:7], s55 offen lds
	s_mov_b32 m0, s29
	ds_read_b128 v[168:171], v139 offset:49152
	buffer_load_dwordx4 v135, s[4:7], s55 offen lds
	s_add_i32 s55, s55, s19
	s_mov_b32 m0, s33
	ds_read_b128 v[172:175], v139 offset:50176
	buffer_load_dwordx4 v133, s[4:7], s55 offen lds
	s_mov_b32 m0, s34
	ds_read_b128 v[176:179], v139 offset:51200
	buffer_load_dwordx4 v135, s[4:7], s55 offen lds
	s_mov_b32 m0, s30
	ds_read_b128 v[180:183], v139 offset:52224
	buffer_load_dwordx4 v132, s[36:39], s54 offen lds
	s_mov_b32 m0, s31
	ds_read_b128 v[184:187], v139 offset:53248
	buffer_load_dwordx4 v134, s[36:39], s54 offen lds
	ds_read_b128 v[188:191], v139 offset:54272
	ds_read_b128 v[194:197], v139 offset:55296
	ds_read_b128 v[198:201], v139 offset:56320
	s_waitcnt vmcnt(8)
	s_waitcnt lgkmcnt(0)
	s_barrier
	s_setprio 1
	v_mfma_f32_16x16x32_bf16 v[60:63], v[128:131], v[168:171], v[60:63]
	v_mfma_f32_16x16x32_bf16 v[56:59], v[144:147], v[168:171], v[56:59]
	v_mfma_f32_16x16x32_bf16 v[44:47], v[128:131], v[176:179], v[44:47]
	v_mfma_f32_16x16x32_bf16 v[40:43], v[144:147], v[176:179], v[40:43]
	v_mfma_f32_16x16x32_bf16 v[28:31], v[128:131], v[184:187], v[28:31]
	v_mfma_f32_16x16x32_bf16 v[24:27], v[144:147], v[184:187], v[24:27]
	v_mfma_f32_16x16x32_bf16 v[12:15], v[128:131], v[194:197], v[12:15]
	v_mfma_f32_16x16x32_bf16 v[8:11], v[144:147], v[194:197], v[8:11]
	v_mfma_f32_16x16x32_bf16 v[60:63], v[140:143], v[172:175], v[60:63]
	v_mfma_f32_16x16x32_bf16 v[56:59], v[148:151], v[172:175], v[56:59]
	v_mfma_f32_16x16x32_bf16 v[44:47], v[140:143], v[180:183], v[44:47]
	v_mfma_f32_16x16x32_bf16 v[40:43], v[148:151], v[180:183], v[40:43]
	v_mfma_f32_16x16x32_bf16 v[28:31], v[140:143], v[188:191], v[28:31]
	v_mfma_f32_16x16x32_bf16 v[24:27], v[148:151], v[188:191], v[24:27]
	v_mfma_f32_16x16x32_bf16 v[12:15], v[140:143], v[198:201], v[12:15]
	v_mfma_f32_16x16x32_bf16 v[8:11], v[148:151], v[198:201], v[8:11]
	v_mfma_f32_16x16x32_bf16 v[52:55], v[152:155], v[168:171], v[52:55]
	v_mfma_f32_16x16x32_bf16 v[48:51], v[160:163], v[168:171], v[48:51]
	v_mfma_f32_16x16x32_bf16 v[36:39], v[152:155], v[176:179], v[36:39]
	v_mfma_f32_16x16x32_bf16 v[32:35], v[160:163], v[176:179], v[32:35]
	v_mfma_f32_16x16x32_bf16 v[20:23], v[152:155], v[184:187], v[20:23]
	v_mfma_f32_16x16x32_bf16 v[16:19], v[160:163], v[184:187], v[16:19]
	v_mfma_f32_16x16x32_bf16 v[4:7], v[152:155], v[194:197], v[4:7]
	v_mfma_f32_16x16x32_bf16 v[0:3], v[160:163], v[194:197], v[0:3]
	v_mfma_f32_16x16x32_bf16 v[52:55], v[156:159], v[172:175], v[52:55]
	v_mfma_f32_16x16x32_bf16 v[48:51], v[164:167], v[172:175], v[48:51]
	v_mfma_f32_16x16x32_bf16 v[36:39], v[156:159], v[180:183], v[36:39]
	v_mfma_f32_16x16x32_bf16 v[32:35], v[164:167], v[180:183], v[32:35]
	v_mfma_f32_16x16x32_bf16 v[20:23], v[156:159], v[188:191], v[20:23]
	v_mfma_f32_16x16x32_bf16 v[16:19], v[164:167], v[188:191], v[16:19]
	v_mfma_f32_16x16x32_bf16 v[4:7], v[156:159], v[198:201], v[4:7]
	v_mfma_f32_16x16x32_bf16 v[0:3], v[164:167], v[198:201], v[0:3]
	s_setprio 0
	s_barrier
	s_add_i32 s60, s60, 2
	s_addk_i32 s58, 0x100
	s_addk_i32 s59, 0x100
	s_cmp_ge_i32 s60, s35
	s_cbranch_scc0 .LBB0_450

;     __device__ __forceinline__ unsigned a_off(const Unit& u, const Gemm& g) const { return (unsigned)u.pm * (unsigned)(BM * 2) * (unsigned)g.K; }
; template <class Epi, class Sched, bool ALIGN_EPI = false, bool SP2 = false, bool FP8 = false>
; __device__ __forceinline__ void gemm_phase(LAS unsigned char* lds, const Gemm g, const Sched& S, const Epi& E, int wbase) {
;     ...
;         const bool has_next = S.next(ui + 1, nxt);
;         const unsigned nA = has_next ? S.a_off(nxt, g) : cA, nB = has_next ? S.b_off(nxt, g) : cB;
;         const rsrc_t rAn = (Sched::TWO && has_next) ? (nxt.part ? rA1 : rA0) : rAc, rBn = (Sched::TWO && has_next) ? (nxt.part ? rB1 : rB0) : rBc;
;         float pre_[8] = {0.f, 0.f, 0.f, 0.f, 0.f, 0.f, 0.f, 0.f};
;         if constexpr (Epi::HAS_PRE) E.pre_load(pre_, cur, wr);
;         for (int t = 0; t < nt; t += 2) {
;             const bool last = (t == nt - 2);
;             const unsigned a1 = cA + (unsigned)(t + 1) * kstep;
;             const unsigned a2 = last ? nA : cA + (unsigned)(t + 2) * kstep, b2 = last ? nB : cB + (unsigned)(t + 2) * kstep; const rsrc_t rA2 = (Sched::TWO && last) ? rAn : rAc, rB2 = (Sched::TWO && last) ? rBn : rBc;
;             const unsigned a3 = a2 + kstep, b3 = b2 + kstep;
;             if (last && has_next) S.a_ready(nxt);
;             if constexpr (SP2) {
;             PG8_LDB(B0, 0, 0); PG8_LDB(B1, 0, 1); PG8_SCHED; PG8_LDA(At, 0, 0); PG8_STAGE(PG8_SA(1, 1), rAc, a1 + hstep, voffA);
;             PG8_WAIT_V(8); PG8_WAIT_L(0); PG8_BAR; PG8_MMA(0, 0, At, B0); PG8_MMA(0, 1, At, B1); PG8_BAR; PG8_SCHED;
;             PG8_LDA(At, 0, 1); PG8_STAGE(PG8_SB(0, 0), rB2, b2, voffB); PG8_STAGE(PG8_SB(0, 1), rB2, b2 + hstep, voffB); PG8_STAGE(PG8_SA(0, 0), rA2, a2, voffA);
;             PG8_WAIT_V(8); PG8_WAIT_L(0); PG8_BAR; PG8_MMA(1, 0, At, B0); PG8_MMA(1, 1, At, B1); PG8_BAR; PG8_SCHED;
;             PG8_LDB(B0, 1, 0); PG8_LDB(B1, 1, 1); PG8_SCHED; PG8_LDA(At, 1, 0); PG8_STAGE(PG8_SA(0, 1), rA2, a2 + hstep, voffA);
;             PG8_WAIT_V(8); PG8_WAIT_L(0); PG8_BAR; PG8_MMA(0, 0, At, B0); PG8_MMA(0, 1, At, B1); PG8_BAR; PG8_SCHED;
;             PG8_LDA(At, 1, 1); PG8_STAGE(PG8_SB(1, 0), rB2, b3, voffB); PG8_STAGE(PG8_SB(1, 1), rB2, b3 + hstep, voffB); PG8_STAGE(PG8_SA(1, 0), rA2, a3, voffA);
;             PG8_WAIT_V(8); PG8_WAIT_L(0); PG8_BAR; PG8_MMA(1, 0, At, B0); PG8_MMA(1, 1, At, B1); PG8_BAR; PG8_SCHED;
.LBB0_813:
	s_add_i32 s20, vcc_hi, 0x80
	v_add_u32_e32 v140, 0x10000, v240
	v_add_u32_e32 v156, 0x14000, v240
	s_cmp_eq_u32 s41, s78
	ds_read_b128 v[128:131], v140
	ds_read_b128 v[132:135], v140 offset:1024
	ds_read_b128 v[136:139], v140 offset:2048
	ds_read_b128 v[140:143], v140 offset:3072
	ds_read_b128 v[144:147], v156
	ds_read_b128 v[148:151], v156 offset:1024
	ds_read_b128 v[152:155], v156 offset:2048
	ds_read_b128 v[156:159], v156 offset:3072
	s_cselect_b64 s[16:17], -1, 0
	s_and_b64 s[18:19], s[16:17], exec
	s_cselect_b32 s68, s67, s20
	s_cselect_b32 s54, vcc_lo, s3
	s_and_b64 s[20:21], s[44:45], s[16:17]
	s_and_b64 s[16:17], s[20:21], exec
	s_cselect_b32 s18, s52, s14
	s_cselect_b32 s19, s53, s15
	s_cselect_b32 s17, s35, s13
	s_cselect_b32 s16, s34, s12
	s_or_b32 s55, s68, 0x80
	s_and_b64 s[20:21], s[20:21], exec
	s_cselect_b32 s23, s53, s31
	s_cselect_b32 s22, s52, s30
	s_cselect_b32 s21, s11, s59
	s_cselect_b32 s20, s10, s58
	s_add_i32 s69, s46, vcc_hi
	s_mov_b32 m0, s61
	ds_read_b128 v[160:163], v241
	ds_read_b128 v[164:167], v241 offset:1024
	ds_read_b128 v[168:171], v241 offset:2048
	ds_read_b128 v[172:175], v241 offset:3072
	ds_read_b128 v[176:179], v241 offset:4096
	ds_read_b128 v[180:183], v241 offset:5120
	ds_read_b128 v[184:187], v241 offset:6144
	ds_read_b128 v[188:191], v241 offset:7168
	buffer_load_dwordx4 v192, s[12:15], s69 offen lds
	s_mov_b32 m0, s62
	s_nop 0
	buffer_load_dwordx4 v236, s[12:15], s69 offen lds
	s_waitcnt vmcnt(8)
	s_waitcnt lgkmcnt(0)
	s_barrier
	s_setprio 1
	v_mfma_f32_16x16x128_f8f6f4 v[124:127], v[128:135], v[160:167], v[124:127]
	v_mfma_f32_16x16x128_f8f6f4 v[120:123], v[136:143], v[160:167], v[120:123]
	v_mfma_f32_16x16x128_f8f6f4 v[116:119], v[128:135], v[168:175], v[116:119]
	v_mfma_f32_16x16x128_f8f6f4 v[112:115], v[136:143], v[168:175], v[112:115]
	v_mfma_f32_16x16x128_f8f6f4 v[108:111], v[128:135], v[176:183], v[108:111]
	v_mfma_f32_16x16x128_f8f6f4 v[104:107], v[136:143], v[176:183], v[104:107]
	v_mfma_f32_16x16x128_f8f6f4 v[100:103], v[128:135], v[184:191], v[100:103]
	v_mfma_f32_16x16x128_f8f6f4 v[96:99], v[136:143], v[184:191], v[96:99]
	v_mfma_f32_16x16x128_f8f6f4 v[194:197], v[144:151], v[160:167], v[92:95]
	v_mfma_f32_16x16x128_f8f6f4 v[160:163], v[152:159], v[160:167], v[88:91]
	v_mfma_f32_16x16x128_f8f6f4 v[164:167], v[144:151], v[168:175], v[84:87]
	v_mfma_f32_16x16x128_f8f6f4 v[168:171], v[152:159], v[168:175], v[80:83]
	v_mfma_f32_16x16x128_f8f6f4 v[172:175], v[144:151], v[176:183], v[76:79]
	v_mfma_f32_16x16x128_f8f6f4 v[176:179], v[152:159], v[176:183], v[72:75]
	v_mfma_f32_16x16x128_f8f6f4 v[180:183], v[144:151], v[184:191], v[68:71]
	v_mfma_f32_16x16x128_f8f6f4 v[184:187], v[152:159], v[184:191], v[64:67]
	s_setprio 0
	s_barrier
	s_mov_b32 m0, s48
	s_nop 3
	buffer_load_dwordx4 v235, s[20:23], s54 offen lds
	s_mov_b32 m0, s56
	ds_read_b128 v[64:67], v241 offset:16384
	s_add_i32 s69, s54, s46
	buffer_load_dwordx4 v237, s[20:23], s54 offen lds
	s_mov_b32 m0, s57
	ds_read_b128 v[68:71], v241 offset:17408
	buffer_load_dwordx4 v235, s[20:23], s69 offen lds
	s_mov_b32 m0, s65
	ds_read_b128 v[72:75], v241 offset:18432
	buffer_load_dwordx4 v237, s[20:23], s69 offen lds
	s_mov_b32 m0, s47
	ds_read_b128 v[76:79], v241 offset:19456
	buffer_load_dwordx4 v192, s[16:19], s68 offen lds
	s_mov_b32 m0, s76
	ds_read_b128 v[80:83], v241 offset:20480
	buffer_load_dwordx4 v236, s[16:19], s68 offen lds
	ds_read_b128 v[84:87], v241 offset:21504
	ds_read_b128 v[88:91], v241 offset:22528
	ds_read_b128 v[92:95], v241 offset:23552
	s_waitcnt vmcnt(8)
	s_waitcnt lgkmcnt(0)
	s_barrier
	s_setprio 1
	v_mfma_f32_16x16x128_f8f6f4 v[60:63], v[128:135], v[64:71], v[60:63]
	v_mfma_f32_16x16x128_f8f6f4 v[56:59], v[136:143], v[64:71], v[56:59]
	v_mfma_f32_16x16x128_f8f6f4 v[52:55], v[128:135], v[72:79], v[52:55]
	v_mfma_f32_16x16x128_f8f6f4 v[48:51], v[136:143], v[72:79], v[48:51]
	v_mfma_f32_16x16x128_f8f6f4 v[188:191], v[128:135], v[80:87], v[44:47]
	v_mfma_f32_16x16x128_f8f6f4 v[198:201], v[136:143], v[80:87], v[40:43]
	v_mfma_f32_16x16x128_f8f6f4 v[202:205], v[128:135], v[88:95], v[36:39]
	v_mfma_f32_16x16x128_f8f6f4 v[206:209], v[136:143], v[88:95], v[32:35]
	v_mfma_f32_16x16x128_f8f6f4 v[210:213], v[144:151], v[64:71], v[28:31]
	v_mfma_f32_16x16x128_f8f6f4 v[214:217], v[152:159], v[64:71], v[24:27]
	v_mfma_f32_16x16x128_f8f6f4 v[218:221], v[144:151], v[72:79], v[20:23]
	v_mfma_f32_16x16x128_f8f6f4 v[226:229], v[152:159], v[72:79], v[16:19]
	v_mfma_f32_16x16x128_f8f6f4 v[242:245], v[144:151], v[80:87], v[12:15]
	v_mfma_f32_16x16x128_f8f6f4 v[246:249], v[152:159], v[80:87], v[8:11]
	v_mfma_f32_16x16x128_f8f6f4 v[250:253], v[144:151], v[88:95], v[4:7]
	v_mfma_f32_16x16x128_f8f6f4 v[230:233], v[152:159], v[88:95], v[0:3]
	s_setprio 0
	s_barrier
; #define PG8_STAGE(bufoff, rs_, soff_, voff) do { _Pragma("unroll") for (int _i = 0; _i < 2; ++_i) \
;         __builtin_amdgcn_raw_ptr_buffer_load_lds(rs_, (LAS void*)(lds + (bufoff) + ldsw + _i * 8192), 16, (int)(voff)[_i], (int)(soff_), 0, 0); } while (0)
; #define PG8_LDA(dst, b, h) do { _Pragma("unroll") for (int m = 0; m < 4; ++m) dst[m] = PG8_LD2(lds + PG8_SA(b, h) + aoff + m * 2048); } while (0)
; #define PG8_LDB(dst, b, h) do { _Pragma("unroll") for (int n = 0; n < 2; ++n) dst[n] = PG8_LD2(lds + PG8_SB(b, h) + boff + n * 2048); } while (0)
; #define PG8_WAIT_V(n) asm volatile("s_waitcnt vmcnt(" #n ")" ::: "memory")
; #define PG8_WAIT_L(n) asm volatile("s_waitcnt lgkmcnt(" #n ")" ::: "memory")
; #define PG8_BAR __builtin_amdgcn_s_barrier()
; #define PG8_SCHED __builtin_amdgcn_sched_barrier(0)
; template <class Epi, class Sched, bool ALIGN_EPI = false, bool SP2 = false, bool FP8 = false>
; __device__ __forceinline__ void gemm_phase(LAS unsigned char* lds, const Gemm g, const Sched& S, const Epi& E, int wbase) {
;     ...
;             PG8_LDB(B0, 0, 0); PG8_LDB(B1, 0, 1); PG8_SCHED; PG8_LDA(At, 0, 0); PG8_STAGE(PG8_SA(1, 1), rAc, a1 + hstep, voffA);
;             PG8_WAIT_V(8); PG8_WAIT_L(0); PG8_BAR; PG8_MMA(0, 0, At, B0); PG8_MMA(0, 1, At, B1); PG8_BAR; PG8_SCHED;
;             PG8_LDA(At, 0, 1); PG8_STAGE(PG8_SB(0, 0), rB2, b2, voffB); PG8_STAGE(PG8_SB(0, 1), rB2, b2 + hstep, voffB); PG8_STAGE(PG8_SA(0, 0), rA2, a2, voffA);
;             PG8_WAIT_V(8); PG8_WAIT_L(0); PG8_BAR; PG8_MMA(1, 0, At, B0); PG8_MMA(1, 1, At, B1); PG8_BAR; PG8_SCHED;
;             PG8_LDB(B0, 1, 0); PG8_LDB(B1, 1, 1); PG8_SCHED; PG8_LDA(At, 1, 0); PG8_STAGE(PG8_SA(0, 1), rA2, a2 + hstep, voffA);
;             PG8_WAIT_V(8); PG8_WAIT_L(0); PG8_BAR; PG8_MMA(0, 0, At, B0); PG8_MMA(0, 1, At, B1); PG8_BAR; PG8_SCHED;
;             PG8_LDA(At, 1, 1); PG8_STAGE(PG8_SB(1, 0), rB2, b3, voffB); PG8_STAGE(PG8_SB(1, 1), rB2, b3 + hstep, voffB); PG8_STAGE(PG8_SA(1, 0), rA2, a3, voffA);
;             PG8_WAIT_V(8); PG8_WAIT_L(0); PG8_BAR; PG8_MMA(1, 0, At, B0); PG8_MMA(1, 1, At, B1); PG8_BAR; PG8_SCHED;
	s_nop 1
	v_add_u32_e32 v12, 0x18000, v240
	v_add_u32_e32 v16, 0x1c000, v240
	s_nop 0
	ds_read_b128 v[0:3], v12
	ds_read_b128 v[4:7], v12 offset:1024
	ds_read_b128 v[8:11], v12 offset:2048
	ds_read_b128 v[12:15], v12 offset:3072
	ds_read_b128 v[128:131], v16
	ds_read_b128 v[132:135], v16 offset:1024
	ds_read_b128 v[136:139], v16 offset:2048
	ds_read_b128 v[140:143], v16 offset:3072
	s_add_i32 s68, s68, s46
	s_mov_b32 m0, s77
	ds_read_b128 v[16:19], v241 offset:32768
	ds_read_b128 v[20:23], v241 offset:33792
	ds_read_b128 v[24:27], v241 offset:34816
	ds_read_b128 v[28:31], v241 offset:35840
	ds_read_b128 v[32:35], v241 offset:36864
	ds_read_b128 v[36:39], v241 offset:37888
	ds_read_b128 v[40:43], v241 offset:38912
	ds_read_b128 v[44:47], v241 offset:39936
	buffer_load_dwordx4 v192, s[16:19], s68 offen lds
	s_mov_b32 m0, s79
	s_nop 0
	buffer_load_dwordx4 v236, s[16:19], s68 offen lds
	s_waitcnt vmcnt(8)
	s_waitcnt lgkmcnt(0)
	s_barrier
	s_setprio 1
	v_mfma_f32_16x16x128_f8f6f4 v[124:127], v[0:7], v[16:23], v[124:127]
	v_mfma_f32_16x16x128_f8f6f4 v[120:123], v[8:15], v[16:23], v[120:123]
	v_mfma_f32_16x16x128_f8f6f4 v[116:119], v[0:7], v[24:31], v[116:119]
	v_mfma_f32_16x16x128_f8f6f4 v[112:115], v[8:15], v[24:31], v[112:115]
	v_mfma_f32_16x16x128_f8f6f4 v[108:111], v[0:7], v[32:39], v[108:111]
	v_mfma_f32_16x16x128_f8f6f4 v[104:107], v[8:15], v[32:39], v[104:107]
	v_mfma_f32_16x16x128_f8f6f4 v[100:103], v[0:7], v[40:47], v[100:103]
	v_mfma_f32_16x16x128_f8f6f4 v[96:99], v[8:15], v[40:47], v[96:99]
	v_mfma_f32_16x16x128_f8f6f4 v[92:95], v[128:135], v[16:23], v[194:197]
	v_mfma_f32_16x16x128_f8f6f4 v[88:91], v[136:143], v[16:23], v[160:163]
	v_mfma_f32_16x16x128_f8f6f4 v[84:87], v[128:135], v[24:31], v[164:167]
	v_mfma_f32_16x16x128_f8f6f4 v[80:83], v[136:143], v[24:31], v[168:171]
	v_mfma_f32_16x16x128_f8f6f4 v[76:79], v[128:135], v[32:39], v[172:175]
	v_mfma_f32_16x16x128_f8f6f4 v[72:75], v[136:143], v[32:39], v[176:179]
	v_mfma_f32_16x16x128_f8f6f4 v[68:71], v[128:135], v[40:47], v[180:183]
	v_mfma_f32_16x16x128_f8f6f4 v[64:67], v[136:143], v[40:47], v[184:187]
	s_setprio 0
	s_barrier
	s_mov_b32 m0, s84
	s_bitset1_b32 s54, 7
	buffer_load_dwordx4 v235, s[20:23], s54 offen lds
	s_mov_b32 m0, s85
	ds_read_b128 v[16:19], v241 offset:49152
	buffer_load_dwordx4 v237, s[20:23], s54 offen lds
	s_add_i32 s54, s54, s46
	s_mov_b32 m0, s96
	ds_read_b128 v[20:23], v241 offset:50176
	buffer_load_dwordx4 v235, s[20:23], s54 offen lds
	s_mov_b32 m0, s97
	ds_read_b128 v[144:147], v241 offset:51200
	buffer_load_dwordx4 v237, s[20:23], s54 offen lds
	s_mov_b32 m0, s94
	ds_read_b128 v[148:151], v241 offset:52224
	buffer_load_dwordx4 v192, s[16:19], s55 offen lds
	s_mov_b32 m0, s95
	ds_read_b128 v[152:155], v241 offset:53248
	buffer_load_dwordx4 v236, s[16:19], s55 offen lds
	ds_read_b128 v[156:159], v241 offset:54272
	ds_read_b128 v[160:163], v241 offset:55296
	ds_read_b128 v[164:167], v241 offset:56320
	s_waitcnt vmcnt(8)
	s_waitcnt lgkmcnt(0)
	s_barrier
	s_setprio 1
	v_mfma_f32_16x16x128_f8f6f4 v[60:63], v[0:7], v[16:23], v[60:63]
	v_mfma_f32_16x16x128_f8f6f4 v[56:59], v[8:15], v[16:23], v[56:59]
	v_mfma_f32_16x16x128_f8f6f4 v[52:55], v[0:7], v[144:151], v[52:55]
	v_mfma_f32_16x16x128_f8f6f4 v[48:51], v[8:15], v[144:151], v[48:51]
	v_mfma_f32_16x16x128_f8f6f4 v[44:47], v[0:7], v[152:159], v[188:191]
	v_mfma_f32_16x16x128_f8f6f4 v[40:43], v[8:15], v[152:159], v[198:201]
	v_mfma_f32_16x16x128_f8f6f4 v[36:39], v[0:7], v[160:167], v[202:205]
	v_mfma_f32_16x16x128_f8f6f4 v[32:35], v[8:15], v[160:167], v[206:209]
	v_mfma_f32_16x16x128_f8f6f4 v[28:31], v[128:135], v[16:23], v[210:213]
	v_mfma_f32_16x16x128_f8f6f4 v[24:27], v[136:143], v[16:23], v[214:217]
	v_mfma_f32_16x16x128_f8f6f4 v[20:23], v[128:135], v[144:151], v[218:221]
	v_mfma_f32_16x16x128_f8f6f4 v[16:19], v[136:143], v[144:151], v[226:229]
	v_mfma_f32_16x16x128_f8f6f4 v[12:15], v[128:135], v[152:159], v[242:245]
	v_mfma_f32_16x16x128_f8f6f4 v[8:11], v[136:143], v[152:159], v[246:249]
	v_mfma_f32_16x16x128_f8f6f4 v[4:7], v[128:135], v[160:167], v[250:253]
	v_mfma_f32_16x16x128_f8f6f4 v[0:3], v[136:143], v[160:167], v[230:233]
	s_setprio 0
	s_barrier
	s_add_i32 s78, s78, 2
	s_addk_i32 vcc_hi, 0x100
	s_addk_i32 s3, 0x100
	s_cmp_ge_i32 s78, s60
	s_cbranch_scc0 .LBB0_813
	v_readlane_b32 s68, v255, 22
	v_readlane_b32 s54, v255, 25
	v_readlane_b32 s69, v255, 23
	v_readlane_b32 s55, v255, 26
	v_mov_b32_e32 v230, v193
	v_mov_b32_e32 v231, v222

;     __device__ __forceinline__ unsigned a_off(const Unit& u, const Gemm& g) const { return (unsigned)u.pm * (unsigned)(BM * 2) * (unsigned)g.K; }
; template <class Epi, class Sched, bool ALIGN_EPI = false, bool SP2 = false, bool FP8 = false>
; __device__ __forceinline__ void gemm_phase(LAS unsigned char* lds, const Gemm g, const Sched& S, const Epi& E, int wbase) {
;     ...
;         const bool has_next = S.next(ui + 1, nxt);
;         const unsigned nA = has_next ? S.a_off(nxt, g) : cA, nB = has_next ? S.b_off(nxt, g) : cB;
;         const rsrc_t rAn = (Sched::TWO && has_next) ? (nxt.part ? rA1 : rA0) : rAc, rBn = (Sched::TWO && has_next) ? (nxt.part ? rB1 : rB0) : rBc;
;         float pre_[8] = {0.f, 0.f, 0.f, 0.f, 0.f, 0.f, 0.f, 0.f};
;         if constexpr (Epi::HAS_PRE) E.pre_load(pre_, cur, wr);
;         for (int t = 0; t < nt; t += 2) {
;             const bool last = (t == nt - 2);
;             const unsigned a1 = cA + (unsigned)(t + 1) * kstep;
;             const unsigned a2 = last ? nA : cA + (unsigned)(t + 2) * kstep, b2 = last ? nB : cB + (unsigned)(t + 2) * kstep; const rsrc_t rA2 = (Sched::TWO && last) ? rAn : rAc, rB2 = (Sched::TWO && last) ? rBn : rBc;
;             const unsigned a3 = a2 + kstep, b3 = b2 + kstep;
;             if (last && has_next) S.a_ready(nxt);
;             if constexpr (SP2) {
;             PG8_LDB(B0, 0, 0); PG8_LDB(B1, 0, 1); PG8_SCHED; PG8_LDA(At, 0, 0); PG8_STAGE(PG8_SA(1, 1), rAc, a1 + hstep, voffA);
;             PG8_WAIT_V(8); PG8_WAIT_L(0); PG8_BAR; PG8_MMA(0, 0, At, B0); PG8_MMA(0, 1, At, B1); PG8_BAR; PG8_SCHED;
;             PG8_LDA(At, 0, 1); PG8_STAGE(PG8_SB(0, 0), rB2, b2, voffB); PG8_STAGE(PG8_SB(0, 1), rB2, b2 + hstep, voffB); PG8_STAGE(PG8_SA(0, 0), rA2, a2, voffA);
;             PG8_WAIT_V(8); PG8_WAIT_L(0); PG8_BAR; PG8_MMA(1, 0, At, B0); PG8_MMA(1, 1, At, B1); PG8_BAR; PG8_SCHED;
;             PG8_LDB(B0, 1, 0); PG8_LDB(B1, 1, 1); PG8_SCHED; PG8_LDA(At, 1, 0); PG8_STAGE(PG8_SA(0, 1), rA2, a2 + hstep, voffA);
;             PG8_WAIT_V(8); PG8_WAIT_L(0); PG8_BAR; PG8_MMA(0, 0, At, B0); PG8_MMA(0, 1, At, B1); PG8_BAR; PG8_SCHED;
;             PG8_LDA(At, 1, 1); PG8_STAGE(PG8_SB(1, 0), rB2, b3, voffB); PG8_STAGE(PG8_SB(1, 1), rB2, b3 + hstep, voffB); PG8_STAGE(PG8_SA(1, 0), rA2, a3, voffA);
;             PG8_WAIT_V(8); PG8_WAIT_L(0); PG8_BAR; PG8_MMA(1, 0, At, B0); PG8_MMA(1, 1, At, B1); PG8_BAR; PG8_SCHED;
.LBB0_847:
	s_add_i32 s20, vcc_lo, 0x80
	v_add_u32_e32 v140, 0x10000, v238
	v_add_u32_e32 v156, 0x14000, v238
	s_cmp_eq_u32 s88, s85
	ds_read_b128 v[128:131], v140
	ds_read_b128 v[132:135], v140 offset:1024
	ds_read_b128 v[136:139], v140 offset:2048
	ds_read_b128 v[140:143], v140 offset:3072
	ds_read_b128 v[144:147], v156
	ds_read_b128 v[148:151], v156 offset:1024
	ds_read_b128 v[152:155], v156 offset:2048
	ds_read_b128 v[156:159], v156 offset:3072
	s_cselect_b64 s[16:17], -1, 0
	s_and_b64 s[18:19], s[16:17], exec
	s_cselect_b32 s68, s67, s20
	s_cselect_b32 s54, s78, vcc_hi
	s_and_b64 s[20:21], s[58:59], s[16:17]
	s_and_b64 s[16:17], s[20:21], exec
	s_cselect_b32 s18, s30, s14
	s_cselect_b32 s19, s31, s15
	s_cselect_b32 s17, s35, s13
	s_cselect_b32 s16, s34, s12
	s_or_b32 s55, s68, 0x80
	s_and_b64 s[20:21], s[20:21], exec
	s_cselect_b32 s23, s31, s53
	s_cselect_b32 s22, s30, s52
	s_cselect_b32 s21, s45, s11
	s_cselect_b32 s20, s44, s10
	s_add_i32 s69, s41, vcc_lo
	s_mov_b32 m0, s89
	ds_read_b128 v[160:163], v239
	ds_read_b128 v[164:167], v239 offset:1024
	ds_read_b128 v[168:171], v239 offset:2048
	ds_read_b128 v[172:175], v239 offset:3072
	ds_read_b128 v[176:179], v239 offset:4096
	ds_read_b128 v[180:183], v239 offset:5120
	ds_read_b128 v[184:187], v239 offset:6144
	ds_read_b128 v[188:191], v239 offset:7168
	buffer_load_dwordx4 v192, s[12:15], s69 offen lds
	s_mov_b32 m0, s92
	s_nop 0
	buffer_load_dwordx4 v223, s[12:15], s69 offen lds
	s_waitcnt vmcnt(8)
	s_waitcnt lgkmcnt(0)
	s_barrier
	s_setprio 1
	v_mfma_f32_16x16x32_bf16 v[124:127], v[128:131], v[160:163], v[124:127]
	v_mfma_f32_16x16x32_bf16 v[120:123], v[136:139], v[160:163], v[120:123]
	v_mfma_f32_16x16x32_bf16 v[116:119], v[128:131], v[168:171], v[116:119]
	v_mfma_f32_16x16x32_bf16 v[112:115], v[136:139], v[168:171], v[112:115]
	v_mfma_f32_16x16x32_bf16 v[108:111], v[128:131], v[176:179], v[108:111]
	v_mfma_f32_16x16x32_bf16 v[104:107], v[136:139], v[176:179], v[104:107]
	v_mfma_f32_16x16x32_bf16 v[100:103], v[128:131], v[184:187], v[100:103]
	v_mfma_f32_16x16x32_bf16 v[96:99], v[136:139], v[184:187], v[96:99]
	v_mfma_f32_16x16x32_bf16 v[124:127], v[132:135], v[164:167], v[124:127]
	v_mfma_f32_16x16x32_bf16 v[120:123], v[140:143], v[164:167], v[120:123]
	v_mfma_f32_16x16x32_bf16 v[116:119], v[132:135], v[172:175], v[116:119]
	v_mfma_f32_16x16x32_bf16 v[112:115], v[140:143], v[172:175], v[112:115]
	v_mfma_f32_16x16x32_bf16 v[108:111], v[132:135], v[180:183], v[108:111]
	v_mfma_f32_16x16x32_bf16 v[104:107], v[140:143], v[180:183], v[104:107]
	v_mfma_f32_16x16x32_bf16 v[100:103], v[132:135], v[188:191], v[100:103]
	v_mfma_f32_16x16x32_bf16 v[96:99], v[140:143], v[188:191], v[96:99]
	v_mfma_f32_16x16x32_bf16 v[92:95], v[144:147], v[160:163], v[92:95]
	v_mfma_f32_16x16x32_bf16 v[88:91], v[152:155], v[160:163], v[88:91]
	v_mfma_f32_16x16x32_bf16 v[84:87], v[144:147], v[168:171], v[84:87]
	v_mfma_f32_16x16x32_bf16 v[80:83], v[152:155], v[168:171], v[80:83]
	v_mfma_f32_16x16x32_bf16 v[76:79], v[144:147], v[176:179], v[76:79]
	v_mfma_f32_16x16x32_bf16 v[72:75], v[152:155], v[176:179], v[72:75]
	v_mfma_f32_16x16x32_bf16 v[68:71], v[144:147], v[184:187], v[68:71]
	v_mfma_f32_16x16x32_bf16 v[64:67], v[152:155], v[184:187], v[64:67]
	v_mfma_f32_16x16x32_bf16 v[92:95], v[148:151], v[164:167], v[92:95]
	v_mfma_f32_16x16x32_bf16 v[88:91], v[156:159], v[164:167], v[88:91]
	v_mfma_f32_16x16x32_bf16 v[84:87], v[148:151], v[172:175], v[84:87]
	v_mfma_f32_16x16x32_bf16 v[80:83], v[156:159], v[172:175], v[80:83]
	v_mfma_f32_16x16x32_bf16 v[76:79], v[148:151], v[180:183], v[76:79]
	v_mfma_f32_16x16x32_bf16 v[72:75], v[156:159], v[180:183], v[72:75]
	v_mfma_f32_16x16x32_bf16 v[68:71], v[148:151], v[188:191], v[68:71]
	v_mfma_f32_16x16x32_bf16 v[64:67], v[156:159], v[188:191], v[64:67]
	s_setprio 0
	s_barrier
	s_mov_b32 m0, s43
	ds_read_b128 v[160:163], v239 offset:16384
	buffer_load_dwordx4 v222, s[20:23], s54 offen lds
	s_mov_b32 m0, s46
	ds_read_b128 v[164:167], v239 offset:17408
	s_add_i32 s69, s54, s41
	buffer_load_dwordx4 v235, s[20:23], s54 offen lds
	s_mov_b32 m0, s47
	ds_read_b128 v[168:171], v239 offset:18432
	buffer_load_dwordx4 v222, s[20:23], s69 offen lds
	s_mov_b32 m0, s48
	ds_read_b128 v[172:175], v239 offset:19456
	buffer_load_dwordx4 v235, s[20:23], s69 offen lds
	s_mov_b32 m0, s42
	ds_read_b128 v[176:179], v239 offset:20480
	buffer_load_dwordx4 v192, s[16:19], s68 offen lds
	s_mov_b32 m0, s56
	ds_read_b128 v[180:183], v239 offset:21504
	buffer_load_dwordx4 v223, s[16:19], s68 offen lds
	ds_read_b128 v[184:187], v239 offset:22528
	ds_read_b128 v[188:191], v239 offset:23552
	s_waitcnt vmcnt(8)
	s_waitcnt lgkmcnt(0)
	s_barrier
; #define PG8_STAGE(bufoff, rs_, soff_, voff) do { _Pragma("unroll") for (int _i = 0; _i < 2; ++_i) \
;         __builtin_amdgcn_raw_ptr_buffer_load_lds(rs_, (LAS void*)(lds + (bufoff) + ldsw + _i * 8192), 16, (int)(voff)[_i], (int)(soff_), 0, 0); } while (0)
; #define PG8_LDA(dst, b, h) do { _Pragma("unroll") for (int m = 0; m < 4; ++m) dst[m] = PG8_LD2(lds + PG8_SA(b, h) + aoff + m * 2048); } while (0)
; #define PG8_LDB(dst, b, h) do { _Pragma("unroll") for (int n = 0; n < 2; ++n) dst[n] = PG8_LD2(lds + PG8_SB(b, h) + boff + n * 2048); } while (0)
; #define PG8_WAIT_V(n) asm volatile("s_waitcnt vmcnt(" #n ")" ::: "memory")
; #define PG8_WAIT_L(n) asm volatile("s_waitcnt lgkmcnt(" #n ")" ::: "memory")
; #define PG8_BAR __builtin_amdgcn_s_barrier()
; #define PG8_SCHED __builtin_amdgcn_sched_barrier(0)
; template <class Epi, class Sched, bool ALIGN_EPI = false, bool SP2 = false, bool FP8 = false>
; __device__ __forceinline__ void gemm_phase(LAS unsigned char* lds, const Gemm g, const Sched& S, const Epi& E, int wbase) {
;     ...
;             PG8_LDB(B0, 0, 0); PG8_LDB(B1, 0, 1); PG8_SCHED; PG8_LDA(At, 0, 0); PG8_STAGE(PG8_SA(1, 1), rAc, a1 + hstep, voffA);
;             PG8_WAIT_V(8); PG8_WAIT_L(0); PG8_BAR; PG8_MMA(0, 0, At, B0); PG8_MMA(0, 1, At, B1); PG8_BAR; PG8_SCHED;
;             PG8_LDA(At, 0, 1); PG8_STAGE(PG8_SB(0, 0), rB2, b2, voffB); PG8_STAGE(PG8_SB(0, 1), rB2, b2 + hstep, voffB); PG8_STAGE(PG8_SA(0, 0), rA2, a2, voffA);
;             PG8_WAIT_V(8); PG8_WAIT_L(0); PG8_BAR; PG8_MMA(1, 0, At, B0); PG8_MMA(1, 1, At, B1); PG8_BAR; PG8_SCHED;
;             PG8_LDB(B0, 1, 0); PG8_LDB(B1, 1, 1); PG8_SCHED; PG8_LDA(At, 1, 0); PG8_STAGE(PG8_SA(0, 1), rA2, a2 + hstep, voffA);
;             PG8_WAIT_V(8); PG8_WAIT_L(0); PG8_BAR; PG8_MMA(0, 0, At, B0); PG8_MMA(0, 1, At, B1); PG8_BAR; PG8_SCHED;
;             PG8_LDA(At, 1, 1); PG8_STAGE(PG8_SB(1, 0), rB2, b3, voffB); PG8_STAGE(PG8_SB(1, 1), rB2, b3 + hstep, voffB); PG8_STAGE(PG8_SA(1, 0), rA2, a3, voffA);
;             PG8_WAIT_V(8); PG8_WAIT_L(0); PG8_BAR; PG8_MMA(1, 0, At, B0); PG8_MMA(1, 1, At, B1); PG8_BAR; PG8_SCHED;
	s_setprio 1
	v_mfma_f32_16x16x32_bf16 v[60:63], v[128:131], v[160:163], v[60:63]
	v_mfma_f32_16x16x32_bf16 v[56:59], v[136:139], v[160:163], v[56:59]
	v_mfma_f32_16x16x32_bf16 v[52:55], v[128:131], v[168:171], v[52:55]
	v_mfma_f32_16x16x32_bf16 v[48:51], v[136:139], v[168:171], v[48:51]
	v_mfma_f32_16x16x32_bf16 v[44:47], v[128:131], v[176:179], v[44:47]
	v_mfma_f32_16x16x32_bf16 v[40:43], v[136:139], v[176:179], v[40:43]
	v_mfma_f32_16x16x32_bf16 v[36:39], v[128:131], v[184:187], v[36:39]
	v_mfma_f32_16x16x32_bf16 v[32:35], v[136:139], v[184:187], v[32:35]
	v_mfma_f32_16x16x32_bf16 v[60:63], v[132:135], v[164:167], v[60:63]
	v_mfma_f32_16x16x32_bf16 v[56:59], v[140:143], v[164:167], v[56:59]
	v_mfma_f32_16x16x32_bf16 v[52:55], v[132:135], v[172:175], v[52:55]
	v_mfma_f32_16x16x32_bf16 v[48:51], v[140:143], v[172:175], v[48:51]
	v_mfma_f32_16x16x32_bf16 v[44:47], v[132:135], v[180:183], v[44:47]
	v_mfma_f32_16x16x32_bf16 v[40:43], v[140:143], v[180:183], v[40:43]
	v_mfma_f32_16x16x32_bf16 v[36:39], v[132:135], v[188:191], v[36:39]
	v_mfma_f32_16x16x32_bf16 v[32:35], v[140:143], v[188:191], v[32:35]
	v_mfma_f32_16x16x32_bf16 v[28:31], v[144:147], v[160:163], v[28:31]
	v_mfma_f32_16x16x32_bf16 v[24:27], v[152:155], v[160:163], v[24:27]
	v_mfma_f32_16x16x32_bf16 v[20:23], v[144:147], v[168:171], v[20:23]
	v_mfma_f32_16x16x32_bf16 v[16:19], v[152:155], v[168:171], v[16:19]
	v_mfma_f32_16x16x32_bf16 v[12:15], v[144:147], v[176:179], v[12:15]
	v_mfma_f32_16x16x32_bf16 v[8:11], v[152:155], v[176:179], v[8:11]
	v_mfma_f32_16x16x32_bf16 v[4:7], v[144:147], v[184:187], v[4:7]
	v_mfma_f32_16x16x32_bf16 v[0:3], v[152:155], v[184:187], v[0:3]
	v_mfma_f32_16x16x32_bf16 v[28:31], v[148:151], v[164:167], v[28:31]
	v_mfma_f32_16x16x32_bf16 v[24:27], v[156:159], v[164:167], v[24:27]
	v_mfma_f32_16x16x32_bf16 v[20:23], v[148:151], v[172:175], v[20:23]
	v_mfma_f32_16x16x32_bf16 v[16:19], v[156:159], v[172:175], v[16:19]
	v_mfma_f32_16x16x32_bf16 v[12:15], v[148:151], v[180:183], v[12:15]
	v_mfma_f32_16x16x32_bf16 v[8:11], v[156:159], v[180:183], v[8:11]
	v_mfma_f32_16x16x32_bf16 v[4:7], v[148:151], v[188:191], v[4:7]
	v_mfma_f32_16x16x32_bf16 v[0:3], v[156:159], v[188:191], v[0:3]
	s_setprio 0
	s_barrier
	v_add_u32_e32 v140, 0x18000, v238
	v_add_u32_e32 v156, 0x1c000, v238
	ds_read_b128 v[128:131], v140
	ds_read_b128 v[132:135], v140 offset:1024
	ds_read_b128 v[136:139], v140 offset:2048
	ds_read_b128 v[140:143], v140 offset:3072
	ds_read_b128 v[144:147], v156
	ds_read_b128 v[148:151], v156 offset:1024
	ds_read_b128 v[152:155], v156 offset:2048
	ds_read_b128 v[156:159], v156 offset:3072
	s_add_i32 s68, s68, s41
	s_mov_b32 m0, s57
	ds_read_b128 v[160:163], v239 offset:32768
	ds_read_b128 v[164:167], v239 offset:33792
	ds_read_b128 v[168:171], v239 offset:34816
	ds_read_b128 v[172:175], v239 offset:35840
	ds_read_b128 v[176:179], v239 offset:36864
	ds_read_b128 v[180:183], v239 offset:37888
	ds_read_b128 v[184:187], v239 offset:38912
	ds_read_b128 v[188:191], v239 offset:39936
	buffer_load_dwordx4 v192, s[16:19], s68 offen lds
	s_mov_b32 m0, s60
	s_nop 0
	buffer_load_dwordx4 v223, s[16:19], s68 offen lds
	s_waitcnt vmcnt(8)
	s_waitcnt lgkmcnt(0)
	s_barrier
	s_setprio 1
	v_mfma_f32_16x16x32_bf16 v[124:127], v[128:131], v[160:163], v[124:127]
	v_mfma_f32_16x16x32_bf16 v[120:123], v[136:139], v[160:163], v[120:123]
	v_mfma_f32_16x16x32_bf16 v[116:119], v[128:131], v[168:171], v[116:119]
	v_mfma_f32_16x16x32_bf16 v[112:115], v[136:139], v[168:171], v[112:115]
	v_mfma_f32_16x16x32_bf16 v[108:111], v[128:131], v[176:179], v[108:111]
	v_mfma_f32_16x16x32_bf16 v[104:107], v[136:139], v[176:179], v[104:107]
	v_mfma_f32_16x16x32_bf16 v[100:103], v[128:131], v[184:187], v[100:103]
	v_mfma_f32_16x16x32_bf16 v[96:99], v[136:139], v[184:187], v[96:99]
	v_mfma_f32_16x16x32_bf16 v[124:127], v[132:135], v[164:167], v[124:127]
	v_mfma_f32_16x16x32_bf16 v[120:123], v[140:143], v[164:167], v[120:123]
	v_mfma_f32_16x16x32_bf16 v[116:119], v[132:135], v[172:175], v[116:119]
	v_mfma_f32_16x16x32_bf16 v[112:115], v[140:143], v[172:175], v[112:115]
	v_mfma_f32_16x16x32_bf16 v[108:111], v[132:135], v[180:183], v[108:111]
	v_mfma_f32_16x16x32_bf16 v[104:107], v[140:143], v[180:183], v[104:107]
	v_mfma_f32_16x16x32_bf16 v[100:103], v[132:135], v[188:191], v[100:103]
	v_mfma_f32_16x16x32_bf16 v[96:99], v[140:143], v[188:191], v[96:99]
	v_mfma_f32_16x16x32_bf16 v[92:95], v[144:147], v[160:163], v[92:95]
	v_mfma_f32_16x16x32_bf16 v[88:91], v[152:155], v[160:163], v[88:91]
	v_mfma_f32_16x16x32_bf16 v[84:87], v[144:147], v[168:171], v[84:87]
	v_mfma_f32_16x16x32_bf16 v[80:83], v[152:155], v[168:171], v[80:83]
	v_mfma_f32_16x16x32_bf16 v[76:79], v[144:147], v[176:179], v[76:79]
	v_mfma_f32_16x16x32_bf16 v[72:75], v[152:155], v[176:179], v[72:75]
	v_mfma_f32_16x16x32_bf16 v[68:71], v[144:147], v[184:187], v[68:71]
	v_mfma_f32_16x16x32_bf16 v[64:67], v[152:155], v[184:187], v[64:67]
	v_mfma_f32_16x16x32_bf16 v[92:95], v[148:151], v[164:167], v[92:95]
	v_mfma_f32_16x16x32_bf16 v[88:91], v[156:159], v[164:167], v[88:91]
	v_mfma_f32_16x16x32_bf16 v[84:87], v[148:151], v[172:175], v[84:87]
	v_mfma_f32_16x16x32_bf16 v[80:83], v[156:159], v[172:175], v[80:83]
	v_mfma_f32_16x16x32_bf16 v[76:79], v[148:151], v[180:183], v[76:79]
	v_mfma_f32_16x16x32_bf16 v[72:75], v[156:159], v[180:183], v[72:75]
	v_mfma_f32_16x16x32_bf16 v[68:71], v[148:151], v[188:191], v[68:71]
	v_mfma_f32_16x16x32_bf16 v[64:67], v[156:159], v[188:191], v[64:67]
	s_setprio 0
	s_barrier
; #define PG8_STAGE(bufoff, rs_, soff_, voff) do { _Pragma("unroll") for (int _i = 0; _i < 2; ++_i) \
;         __builtin_amdgcn_raw_ptr_buffer_load_lds(rs_, (LAS void*)(lds + (bufoff) + ldsw + _i * 8192), 16, (int)(voff)[_i], (int)(soff_), 0, 0); } while (0)
; #define PG8_LDA(dst, b, h) do { _Pragma("unroll") for (int m = 0; m < 4; ++m) dst[m] = PG8_LD2(lds + PG8_SA(b, h) + aoff + m * 2048); } while (0)
; #define PG8_LDB(dst, b, h) do { _Pragma("unroll") for (int n = 0; n < 2; ++n) dst[n] = PG8_LD2(lds + PG8_SB(b, h) + boff + n * 2048); } while (0)
; #define PG8_WAIT_V(n) asm volatile("s_waitcnt vmcnt(" #n ")" ::: "memory")
; #define PG8_WAIT_L(n) asm volatile("s_waitcnt lgkmcnt(" #n ")" ::: "memory")
; #define PG8_BAR __builtin_amdgcn_s_barrier()
; #define PG8_SCHED __builtin_amdgcn_sched_barrier(0)
; template <class Epi, class Sched, bool ALIGN_EPI = false, bool SP2 = false, bool FP8 = false>
; __device__ __forceinline__ void gemm_phase(LAS unsigned char* lds, const Gemm g, const Sched& S, const Epi& E, int wbase) {
;     ...
;             PG8_LDB(B0, 0, 0); PG8_LDB(B1, 0, 1); PG8_SCHED; PG8_LDA(At, 0, 0); PG8_STAGE(PG8_SA(1, 1), rAc, a1 + hstep, voffA);
;             PG8_WAIT_V(8); PG8_WAIT_L(0); PG8_BAR; PG8_MMA(0, 0, At, B0); PG8_MMA(0, 1, At, B1); PG8_BAR; PG8_SCHED;
;             PG8_LDA(At, 0, 1); PG8_STAGE(PG8_SB(0, 0), rB2, b2, voffB); PG8_STAGE(PG8_SB(0, 1), rB2, b2 + hstep, voffB); PG8_STAGE(PG8_SA(0, 0), rA2, a2, voffA);
;             PG8_WAIT_V(8); PG8_WAIT_L(0); PG8_BAR; PG8_MMA(1, 0, At, B0); PG8_MMA(1, 1, At, B1); PG8_BAR; PG8_SCHED;
;             PG8_LDB(B0, 1, 0); PG8_LDB(B1, 1, 1); PG8_SCHED; PG8_LDA(At, 1, 0); PG8_STAGE(PG8_SA(0, 1), rA2, a2 + hstep, voffA);
;             PG8_WAIT_V(8); PG8_WAIT_L(0); PG8_BAR; PG8_MMA(0, 0, At, B0); PG8_MMA(0, 1, At, B1); PG8_BAR; PG8_SCHED;
;             PG8_LDA(At, 1, 1); PG8_STAGE(PG8_SB(1, 0), rB2, b3, voffB); PG8_STAGE(PG8_SB(1, 1), rB2, b3 + hstep, voffB); PG8_STAGE(PG8_SA(1, 0), rA2, a3, voffA);
;             PG8_WAIT_V(8); PG8_WAIT_L(0); PG8_BAR; PG8_MMA(1, 0, At, B0); PG8_MMA(1, 1, At, B1); PG8_BAR; PG8_SCHED;
	s_mov_b32 m0, s63
	s_bitset1_b32 s54, 7
	buffer_load_dwordx4 v222, s[20:23], s54 offen lds
	s_mov_b32 m0, s65
	ds_read_b128 v[160:163], v239 offset:49152
	buffer_load_dwordx4 v235, s[20:23], s54 offen lds
	s_add_i32 s54, s54, s41
	s_mov_b32 m0, s79
	ds_read_b128 v[164:167], v239 offset:50176
	buffer_load_dwordx4 v222, s[20:23], s54 offen lds
	s_mov_b32 m0, s80
	ds_read_b128 v[168:171], v239 offset:51200
	buffer_load_dwordx4 v235, s[20:23], s54 offen lds
	s_mov_b32 m0, s76
	ds_read_b128 v[172:175], v239 offset:52224
	buffer_load_dwordx4 v192, s[16:19], s55 offen lds
	s_mov_b32 m0, s77
	ds_read_b128 v[176:179], v239 offset:53248
	buffer_load_dwordx4 v223, s[16:19], s55 offen lds
	ds_read_b128 v[180:183], v239 offset:54272
	ds_read_b128 v[184:187], v239 offset:55296
	ds_read_b128 v[188:191], v239 offset:56320
	s_waitcnt vmcnt(8)
	s_waitcnt lgkmcnt(0)
	s_barrier
	s_setprio 1
	v_mfma_f32_16x16x32_bf16 v[60:63], v[128:131], v[160:163], v[60:63]
	v_mfma_f32_16x16x32_bf16 v[56:59], v[136:139], v[160:163], v[56:59]
	v_mfma_f32_16x16x32_bf16 v[52:55], v[128:131], v[168:171], v[52:55]
	v_mfma_f32_16x16x32_bf16 v[48:51], v[136:139], v[168:171], v[48:51]
	v_mfma_f32_16x16x32_bf16 v[44:47], v[128:131], v[176:179], v[44:47]
	v_mfma_f32_16x16x32_bf16 v[40:43], v[136:139], v[176:179], v[40:43]
	v_mfma_f32_16x16x32_bf16 v[36:39], v[128:131], v[184:187], v[36:39]
	v_mfma_f32_16x16x32_bf16 v[32:35], v[136:139], v[184:187], v[32:35]
	v_mfma_f32_16x16x32_bf16 v[60:63], v[132:135], v[164:167], v[60:63]
	v_mfma_f32_16x16x32_bf16 v[56:59], v[140:143], v[164:167], v[56:59]
	v_mfma_f32_16x16x32_bf16 v[52:55], v[132:135], v[172:175], v[52:55]
	v_mfma_f32_16x16x32_bf16 v[48:51], v[140:143], v[172:175], v[48:51]
	v_mfma_f32_16x16x32_bf16 v[44:47], v[132:135], v[180:183], v[44:47]
	v_mfma_f32_16x16x32_bf16 v[40:43], v[140:143], v[180:183], v[40:43]
	v_mfma_f32_16x16x32_bf16 v[36:39], v[132:135], v[188:191], v[36:39]
	v_mfma_f32_16x16x32_bf16 v[32:35], v[140:143], v[188:191], v[32:35]
	v_mfma_f32_16x16x32_bf16 v[28:31], v[144:147], v[160:163], v[28:31]
	v_mfma_f32_16x16x32_bf16 v[24:27], v[152:155], v[160:163], v[24:27]
	v_mfma_f32_16x16x32_bf16 v[20:23], v[144:147], v[168:171], v[20:23]
	v_mfma_f32_16x16x32_bf16 v[16:19], v[152:155], v[168:171], v[16:19]
	v_mfma_f32_16x16x32_bf16 v[12:15], v[144:147], v[176:179], v[12:15]
	v_mfma_f32_16x16x32_bf16 v[8:11], v[152:155], v[176:179], v[8:11]
	v_mfma_f32_16x16x32_bf16 v[4:7], v[144:147], v[184:187], v[4:7]
	v_mfma_f32_16x16x32_bf16 v[0:3], v[152:155], v[184:187], v[0:3]
	v_mfma_f32_16x16x32_bf16 v[28:31], v[148:151], v[164:167], v[28:31]
	v_mfma_f32_16x16x32_bf16 v[24:27], v[156:159], v[164:167], v[24:27]
	v_mfma_f32_16x16x32_bf16 v[20:23], v[148:151], v[172:175], v[20:23]
	v_mfma_f32_16x16x32_bf16 v[16:19], v[156:159], v[172:175], v[16:19]
	v_mfma_f32_16x16x32_bf16 v[12:15], v[148:151], v[180:183], v[12:15]
	v_mfma_f32_16x16x32_bf16 v[8:11], v[156:159], v[180:183], v[8:11]
	v_mfma_f32_16x16x32_bf16 v[4:7], v[148:151], v[188:191], v[4:7]
	v_mfma_f32_16x16x32_bf16 v[0:3], v[156:159], v[188:191], v[0:3]
	s_setprio 0
	s_barrier
	s_add_i32 s85, s85, 2
	s_addk_i32 vcc_lo, 0x100
	s_addk_i32 vcc_hi, 0x100
	s_cmp_ge_i32 s85, s81
	s_cbranch_scc0 .LBB0_847
	v_readlane_b32 s68, v255, 22
	v_readlane_b32 s54, v255, 25
	v_readlane_b32 s69, v255, 23
	v_readlane_b32 s55, v255, 26

;     __device__ __forceinline__ unsigned a_off(const Unit& u, const Gemm& g) const { return (unsigned)u.pm * (unsigned)(BM * 2) * (unsigned)g.K; }
; template <class Epi, class Sched, bool ALIGN_EPI = false, bool SP2 = false, bool FP8 = false>
; __device__ __forceinline__ void gemm_phase(LAS unsigned char* lds, const Gemm g, const Sched& S, const Epi& E, int wbase) {
;     ...
;         const bool has_next = S.next(ui + 1, nxt);
;         const unsigned nA = has_next ? S.a_off(nxt, g) : cA, nB = has_next ? S.b_off(nxt, g) : cB;
;         const rsrc_t rAn = (Sched::TWO && has_next) ? (nxt.part ? rA1 : rA0) : rAc, rBn = (Sched::TWO && has_next) ? (nxt.part ? rB1 : rB0) : rBc;
;         float pre_[8] = {0.f, 0.f, 0.f, 0.f, 0.f, 0.f, 0.f, 0.f};
;         if constexpr (Epi::HAS_PRE) E.pre_load(pre_, cur, wr);
;         for (int t = 0; t < nt; t += 2) {
;             const bool last = (t == nt - 2);
;             const unsigned a1 = cA + (unsigned)(t + 1) * kstep;
;             const unsigned a2 = last ? nA : cA + (unsigned)(t + 2) * kstep, b2 = last ? nB : cB + (unsigned)(t + 2) * kstep; const rsrc_t rA2 = (Sched::TWO && last) ? rAn : rAc, rB2 = (Sched::TWO && last) ? rBn : rBc;
;             const unsigned a3 = a2 + kstep, b3 = b2 + kstep;
;             if (last && has_next) S.a_ready(nxt);
;             if constexpr (SP2) {
;             PG8_LDB(B0, 0, 0); PG8_LDB(B1, 0, 1); PG8_SCHED; PG8_LDA(At, 0, 0); PG8_STAGE(PG8_SA(1, 1), rAc, a1 + hstep, voffA);
;             PG8_WAIT_V(8); PG8_WAIT_L(0); PG8_BAR; PG8_MMA(0, 0, At, B0); PG8_MMA(0, 1, At, B1); PG8_BAR; PG8_SCHED;
;             PG8_LDA(At, 0, 1); PG8_STAGE(PG8_SB(0, 0), rB2, b2, voffB); PG8_STAGE(PG8_SB(0, 1), rB2, b2 + hstep, voffB); PG8_STAGE(PG8_SA(0, 0), rA2, a2, voffA);
;             PG8_WAIT_V(8); PG8_WAIT_L(0); PG8_BAR; PG8_MMA(1, 0, At, B0); PG8_MMA(1, 1, At, B1); PG8_BAR; PG8_SCHED;
;             PG8_LDB(B0, 1, 0); PG8_LDB(B1, 1, 1); PG8_SCHED; PG8_LDA(At, 1, 0); PG8_STAGE(PG8_SA(0, 1), rA2, a2 + hstep, voffA);
;             PG8_WAIT_V(8); PG8_WAIT_L(0); PG8_BAR; PG8_MMA(0, 0, At, B0); PG8_MMA(0, 1, At, B1); PG8_BAR; PG8_SCHED;
;             PG8_LDA(At, 1, 1); PG8_STAGE(PG8_SB(1, 0), rB2, b3, voffB); PG8_STAGE(PG8_SB(1, 1), rB2, b3 + hstep, voffB); PG8_STAGE(PG8_SA(1, 0), rA2, a3, voffA);
;             PG8_WAIT_V(8); PG8_WAIT_L(0); PG8_BAR; PG8_MMA(1, 0, At, B0); PG8_MMA(1, 1, At, B1); PG8_BAR; PG8_SCHED;
.LBB0_924:
	s_lshl_b32 s79, s77, 18
	s_andn2_b64 vcc, exec, s[22:23]
	s_lshl_b32 s80, s76, 18
	s_cbranch_vccnz .LBB0_928
	s_and_b64 s[2:3], s[26:27], exec
	s_waitcnt vmcnt(37)
	s_waitcnt vmcnt(36)
	s_waitcnt vmcnt(35)
	s_waitcnt vmcnt(32)
	s_waitcnt vmcnt(31)
	s_waitcnt vmcnt(28)
	s_waitcnt vmcnt(27)
	s_waitcnt vmcnt(24)
	s_waitcnt vmcnt(23)
	v_mov_b32_e32 v159, v233
	s_cselect_b32 s2, s79, s4
	s_cselect_b32 s3, s80, s5
	s_addk_i32 s4, 0x80
	s_addk_i32 s5, 0x100
	s_mov_b32 s11, 0
	s_waitcnt vmcnt(0)
	v_add_u32_e32 v120, 0x10000, v160
	ds_read_b128 v[132:135], v120
	ds_read_b128 v[136:139], v120 offset:1024
	ds_read_b128 v[140:143], v120 offset:2048
	ds_read_b128 v[144:147], v120 offset:3072
	v_add_u32_e32 v120, 0x14000, v160
	ds_read_b128 v[162:165], v120
	ds_read_b128 v[166:169], v120 offset:1024
	ds_read_b128 v[170:173], v120 offset:2048
	ds_read_b128 v[174:177], v120 offset:3072
	s_add_i32 s14, s4, 0x80
	s_cmp_eq_u32 s60, s11
	s_cselect_b32 s66, s2, s14
	s_cselect_b32 s55, s3, s5
	s_or_b32 s54, s66, 0x80
	s_add_i32 s14, s30, s4
	s_mov_b32 m0, s61
	ds_read_b128 v[178:181], v161
	ds_read_b128 v[182:185], v161 offset:1024
	ds_read_b128 v[194:197], v161 offset:2048
	ds_read_b128 v[198:201], v161 offset:3072
	ds_read_b128 v[202:205], v161 offset:4096
	ds_read_b128 v[206:209], v161 offset:5120
	ds_read_b128 v[210:213], v161 offset:6144
	ds_read_b128 v[214:217], v161 offset:7168
	buffer_load_dwordx4 v222, s[36:39], s14 offen lds
	s_mov_b32 m0, s62
	s_nop 0
	buffer_load_dwordx4 v156, s[36:39], s14 offen lds
	s_waitcnt vmcnt(8)
	s_waitcnt lgkmcnt(0)
	s_barrier
	s_setprio 1
	v_mfma_f32_16x16x128_f8f6f4 v[124:127], v[140:147], v[178:185], 0
	v_mfma_f32_16x16x128_f8f6f4 v[108:111], v[132:139], v[194:201], 0
	v_mfma_f32_16x16x128_f8f6f4 v[104:107], v[140:147], v[194:201], 0
	v_mfma_f32_16x16x128_f8f6f4 v[120:123], v[132:139], v[178:185], 0
	v_mfma_f32_16x16x128_f8f6f4 v[148:151], v[132:139], v[202:209], 0
	v_mfma_f32_16x16x128_f8f6f4 v[186:189], v[140:147], v[202:209], 0
	v_mfma_f32_16x16x128_f8f6f4 v[218:221], v[132:139], v[210:217], 0
	v_mfma_f32_16x16x128_f8f6f4 v[226:229], v[140:147], v[210:217], 0
	v_mfma_f32_16x16x128_f8f6f4 v[116:119], v[162:169], v[178:185], 0
	v_mfma_f32_16x16x128_f8f6f4 v[112:115], v[170:177], v[178:185], 0
	v_mfma_f32_16x16x128_f8f6f4 v[100:103], v[162:169], v[194:201], 0
	v_mfma_f32_16x16x128_f8f6f4 v[96:99], v[170:177], v[194:201], 0
	v_mfma_f32_16x16x128_f8f6f4 v[178:181], v[162:169], v[202:209], 0
	v_mfma_f32_16x16x128_f8f6f4 v[182:185], v[170:177], v[202:209], 0
	v_mfma_f32_16x16x128_f8f6f4 v[194:197], v[162:169], v[210:217], 0
	v_mfma_f32_16x16x128_f8f6f4 v[198:201], v[170:177], v[210:217], 0
	s_setprio 0
	s_barrier
	s_mov_b32 m0, s33
	s_mov_b32 s14, s38
	s_mov_b32 s15, s39
	s_nop 1
	buffer_load_dwordx4 v223, s[12:15], s55 offen lds
	s_mov_b32 m0, s34
	ds_read_b128 v[64:67], v161 offset:16384
	s_add_i32 s67, s55, s30
	buffer_load_dwordx4 v157, s[12:15], s55 offen lds
	s_mov_b32 m0, s35
	ds_read_b128 v[68:71], v161 offset:17408
	buffer_load_dwordx4 v223, s[12:15], s67 offen lds
	s_mov_b32 m0, s41
	ds_read_b128 v[72:75], v161 offset:18432
	buffer_load_dwordx4 v157, s[12:15], s67 offen lds
	s_mov_b32 m0, s31
	ds_read_b128 v[76:79], v161 offset:19456
	buffer_load_dwordx4 v222, s[36:39], s66 offen lds
	s_mov_b32 m0, s42
	ds_read_b128 v[80:83], v161 offset:20480
	buffer_load_dwordx4 v156, s[36:39], s66 offen lds
	ds_read_b128 v[84:87], v161 offset:21504
	ds_read_b128 v[88:91], v161 offset:22528
	ds_read_b128 v[92:95], v161 offset:23552
	s_waitcnt vmcnt(8)
	s_waitcnt lgkmcnt(0)
	s_barrier
	s_setprio 1
	v_mfma_f32_16x16x128_f8f6f4 v[60:63], v[132:139], v[64:71], 0
	v_mfma_f32_16x16x128_f8f6f4 v[56:59], v[140:147], v[64:71], 0
	v_mfma_f32_16x16x128_f8f6f4 v[202:205], v[132:139], v[72:79], 0
	v_mfma_f32_16x16x128_f8f6f4 v[206:209], v[140:147], v[72:79], 0
	v_mfma_f32_16x16x128_f8f6f4 v[210:213], v[132:139], v[80:87], 0
	v_mfma_f32_16x16x128_f8f6f4 v[214:217], v[140:147], v[80:87], 0
	v_mfma_f32_16x16x128_f8f6f4 v[230:233], v[132:139], v[88:95], 0
	v_mfma_f32_16x16x128_f8f6f4 v[234:237], v[140:147], v[88:95], 0
	v_mfma_f32_16x16x128_f8f6f4 v[52:55], v[162:169], v[64:71], 0
	v_mfma_f32_16x16x128_f8f6f4 v[48:51], v[170:177], v[64:71], 0
	v_mfma_f32_16x16x128_f8f6f4 v[238:241], v[162:169], v[72:79], 0
	v_mfma_f32_16x16x128_f8f6f4 v[242:245], v[170:177], v[72:79], 0
	v_mfma_f32_16x16x128_f8f6f4 v[246:249], v[162:169], v[80:87], 0
	v_mfma_f32_16x16x128_f8f6f4 v[250:253], v[170:177], v[80:87], 0
	v_mfma_f32_16x16x128_f8f6f4 v[190:193], v[162:169], v[88:95], 0
	v_mfma_f32_16x16x128_f8f6f4 v[152:155], v[170:177], v[88:95], 0
	s_setprio 0
	s_barrier
	v_add_u32_e32 v8, 0x18000, v160
	s_nop 3
	ds_read_b128 v[0:3], v8
	ds_read_b128 v[4:7], v8 offset:1024
	ds_read_b128 v[16:19], v8 offset:2048
	ds_read_b128 v[20:23], v8 offset:3072
	v_add_u32_e32 v8, 0x1c000, v160
	ds_read_b128 v[132:135], v8
	ds_read_b128 v[136:139], v8 offset:1024
	ds_read_b128 v[140:143], v8 offset:2048
	ds_read_b128 v[144:147], v8 offset:3072
	s_add_i32 s66, s66, s30
	s_mov_b32 m0, s43
	ds_read_b128 v[8:11], v161 offset:32768
	ds_read_b128 v[12:15], v161 offset:33792
	ds_read_b128 v[24:27], v161 offset:34816
	ds_read_b128 v[28:31], v161 offset:35840
	ds_read_b128 v[32:35], v161 offset:36864
	ds_read_b128 v[36:39], v161 offset:37888
	ds_read_b128 v[40:43], v161 offset:38912
	ds_read_b128 v[44:47], v161 offset:39936
	buffer_load_dwordx4 v222, s[36:39], s66 offen lds
	s_mov_b32 m0, s44
	s_nop 0
	buffer_load_dwordx4 v156, s[36:39], s66 offen lds
	s_waitcnt vmcnt(8)
	s_waitcnt lgkmcnt(0)
	s_barrier
; #define PG8_STAGE(bufoff, rs_, soff_, voff) do { _Pragma("unroll") for (int _i = 0; _i < 2; ++_i) \
;         __builtin_amdgcn_raw_ptr_buffer_load_lds(rs_, (LAS void*)(lds + (bufoff) + ldsw + _i * 8192), 16, (int)(voff)[_i], (int)(soff_), 0, 0); } while (0)
; #define PG8_LDA(dst, b, h) do { _Pragma("unroll") for (int m = 0; m < 4; ++m) dst[m] = PG8_LD2(lds + PG8_SA(b, h) + aoff + m * 2048); } while (0)
; #define PG8_LDB(dst, b, h) do { _Pragma("unroll") for (int n = 0; n < 2; ++n) dst[n] = PG8_LD2(lds + PG8_SB(b, h) + boff + n * 2048); } while (0)
; #define PG8_WAIT_V(n) asm volatile("s_waitcnt vmcnt(" #n ")" ::: "memory")
; #define PG8_WAIT_L(n) asm volatile("s_waitcnt lgkmcnt(" #n ")" ::: "memory")
; #define PG8_BAR __builtin_amdgcn_s_barrier()
; #define PG8_SCHED __builtin_amdgcn_sched_barrier(0)
; template <class Epi, class Sched, bool ALIGN_EPI = false, bool SP2 = false, bool FP8 = false>
; __device__ __forceinline__ void gemm_phase(LAS unsigned char* lds, const Gemm g, const Sched& S, const Epi& E, int wbase) {
;     ...
;             PG8_LDB(B0, 0, 0); PG8_LDB(B1, 0, 1); PG8_SCHED; PG8_LDA(At, 0, 0); PG8_STAGE(PG8_SA(1, 1), rAc, a1 + hstep, voffA);
;             PG8_WAIT_V(8); PG8_WAIT_L(0); PG8_BAR; PG8_MMA(0, 0, At, B0); PG8_MMA(0, 1, At, B1); PG8_BAR; PG8_SCHED;
;             PG8_LDA(At, 0, 1); PG8_STAGE(PG8_SB(0, 0), rB2, b2, voffB); PG8_STAGE(PG8_SB(0, 1), rB2, b2 + hstep, voffB); PG8_STAGE(PG8_SA(0, 0), rA2, a2, voffA);
;             PG8_WAIT_V(8); PG8_WAIT_L(0); PG8_BAR; PG8_MMA(1, 0, At, B0); PG8_MMA(1, 1, At, B1); PG8_BAR; PG8_SCHED;
;             PG8_LDB(B0, 1, 0); PG8_LDB(B1, 1, 1); PG8_SCHED; PG8_LDA(At, 1, 0); PG8_STAGE(PG8_SA(0, 1), rA2, a2 + hstep, voffA);
;             PG8_WAIT_V(8); PG8_WAIT_L(0); PG8_BAR; PG8_MMA(0, 0, At, B0); PG8_MMA(0, 1, At, B1); PG8_BAR; PG8_SCHED;
;             PG8_LDA(At, 1, 1); PG8_STAGE(PG8_SB(1, 0), rB2, b3, voffB); PG8_STAGE(PG8_SB(1, 1), rB2, b3 + hstep, voffB); PG8_STAGE(PG8_SA(1, 0), rA2, a3, voffA);
;             PG8_WAIT_V(8); PG8_WAIT_L(0); PG8_BAR; PG8_MMA(1, 0, At, B0); PG8_MMA(1, 1, At, B1); PG8_BAR; PG8_SCHED;
	s_setprio 1
	v_mfma_f32_16x16x128_f8f6f4 v[128:131], v[0:7], v[8:15], v[120:123]
	v_mfma_f32_16x16x128_f8f6f4 v[124:127], v[16:23], v[8:15], v[124:127]
	v_mfma_f32_16x16x128_f8f6f4 v[108:111], v[0:7], v[24:31], v[108:111]
	v_mfma_f32_16x16x128_f8f6f4 v[104:107], v[16:23], v[24:31], v[104:107]
	v_mfma_f32_16x16x128_f8f6f4 v[92:95], v[0:7], v[32:39], v[148:151]
	v_mfma_f32_16x16x128_f8f6f4 v[88:91], v[16:23], v[32:39], v[186:189]
	v_mfma_f32_16x16x128_f8f6f4 v[76:79], v[0:7], v[40:47], v[218:221]
	v_mfma_f32_16x16x128_f8f6f4 v[72:75], v[16:23], v[40:47], v[226:229]
	v_mfma_f32_16x16x128_f8f6f4 v[116:119], v[132:139], v[8:15], v[116:119]
	v_mfma_f32_16x16x128_f8f6f4 v[112:115], v[140:147], v[8:15], v[112:115]
	v_mfma_f32_16x16x128_f8f6f4 v[100:103], v[132:139], v[24:31], v[100:103]
	v_mfma_f32_16x16x128_f8f6f4 v[96:99], v[140:147], v[24:31], v[96:99]
	v_mfma_f32_16x16x128_f8f6f4 v[84:87], v[132:139], v[32:39], v[178:181]
	v_mfma_f32_16x16x128_f8f6f4 v[80:83], v[140:147], v[32:39], v[182:185]
	v_mfma_f32_16x16x128_f8f6f4 v[68:71], v[132:139], v[40:47], v[194:197]
	v_mfma_f32_16x16x128_f8f6f4 v[64:67], v[140:147], v[40:47], v[198:201]
	s_setprio 0
	s_barrier
	s_mov_b32 m0, s45
	s_bitset1_b32 s55, 7
	buffer_load_dwordx4 v223, s[12:15], s55 offen lds
	s_mov_b32 m0, s46
	ds_read_b128 v[32:35], v161 offset:49152
	buffer_load_dwordx4 v157, s[12:15], s55 offen lds
	s_add_i32 s55, s55, s30
	s_mov_b32 m0, s52
	ds_read_b128 v[36:39], v161 offset:50176
	buffer_load_dwordx4 v223, s[12:15], s55 offen lds
	s_mov_b32 m0, s53
	ds_read_b128 v[162:165], v161 offset:51200
	buffer_load_dwordx4 v157, s[12:15], s55 offen lds
	s_mov_b32 m0, s47
	ds_read_b128 v[166:169], v161 offset:52224
	buffer_load_dwordx4 v222, s[36:39], s54 offen lds
	s_mov_b32 m0, s48
	ds_read_b128 v[170:173], v161 offset:53248
	buffer_load_dwordx4 v156, s[36:39], s54 offen lds
	ds_read_b128 v[174:177], v161 offset:54272
	ds_read_b128 v[178:181], v161 offset:55296
	ds_read_b128 v[182:185], v161 offset:56320
	s_waitcnt vmcnt(8)
	s_waitcnt lgkmcnt(0)
	s_barrier
	s_setprio 1
	v_mfma_f32_16x16x128_f8f6f4 v[60:63], v[0:7], v[32:39], v[60:63]
	v_mfma_f32_16x16x128_f8f6f4 v[56:59], v[16:23], v[32:39], v[56:59]
	v_mfma_f32_16x16x128_f8f6f4 v[44:47], v[0:7], v[162:169], v[202:205]
	v_mfma_f32_16x16x128_f8f6f4 v[40:43], v[16:23], v[162:169], v[206:209]
	v_mfma_f32_16x16x128_f8f6f4 v[28:31], v[0:7], v[170:177], v[210:213]
	v_mfma_f32_16x16x128_f8f6f4 v[24:27], v[16:23], v[170:177], v[214:217]
	v_mfma_f32_16x16x128_f8f6f4 v[12:15], v[0:7], v[178:185], v[230:233]
	v_mfma_f32_16x16x128_f8f6f4 v[8:11], v[16:23], v[178:185], v[234:237]
	v_mfma_f32_16x16x128_f8f6f4 v[52:55], v[132:139], v[32:39], v[52:55]
	v_mfma_f32_16x16x128_f8f6f4 v[48:51], v[140:147], v[32:39], v[48:51]
	v_mfma_f32_16x16x128_f8f6f4 v[36:39], v[132:139], v[162:169], v[238:241]
	v_mfma_f32_16x16x128_f8f6f4 v[32:35], v[140:147], v[162:169], v[242:245]
	v_mfma_f32_16x16x128_f8f6f4 v[20:23], v[132:139], v[170:177], v[246:249]
	v_mfma_f32_16x16x128_f8f6f4 v[16:19], v[140:147], v[170:177], v[250:253]
	v_mfma_f32_16x16x128_f8f6f4 v[4:7], v[132:139], v[178:185], v[190:193]
	v_mfma_f32_16x16x128_f8f6f4 v[0:3], v[140:147], v[178:185], v[152:155]
	s_setprio 0
	s_barrier
	s_add_i32 s11, s11, 2
	s_addk_i32 s4, 0x100
	s_addk_i32 s5, 0x100
	s_cmp_ge_i32 s11, s58
	s_cbranch_scc0 .LBB0_926
	s_branch .Lzp_after_926
.LBB0_926:
	v_add_u32_e32 v120, 0x10000, v160
	ds_read_b128 v[132:135], v120
	ds_read_b128 v[136:139], v120 offset:1024
	ds_read_b128 v[140:143], v120 offset:2048
	ds_read_b128 v[144:147], v120 offset:3072
	v_add_u32_e32 v120, 0x14000, v160
	ds_read_b128 v[162:165], v120
	ds_read_b128 v[166:169], v120 offset:1024
	ds_read_b128 v[170:173], v120 offset:2048
	ds_read_b128 v[174:177], v120 offset:3072
	s_add_i32 s14, s4, 0x80
	s_cmp_eq_u32 s60, s11
	s_cselect_b32 s66, s2, s14
	s_cselect_b32 s55, s3, s5
	s_or_b32 s54, s66, 0x80
	s_add_i32 s14, s30, s4
	s_mov_b32 m0, s61
	ds_read_b128 v[178:181], v161
	ds_read_b128 v[182:185], v161 offset:1024
	ds_read_b128 v[194:197], v161 offset:2048
	ds_read_b128 v[198:201], v161 offset:3072
	ds_read_b128 v[202:205], v161 offset:4096
	ds_read_b128 v[206:209], v161 offset:5120
	ds_read_b128 v[210:213], v161 offset:6144
	ds_read_b128 v[214:217], v161 offset:7168
	buffer_load_dwordx4 v222, s[36:39], s14 offen lds
	s_mov_b32 m0, s62
	s_nop 0
	buffer_load_dwordx4 v156, s[36:39], s14 offen lds
	s_waitcnt vmcnt(8)
	s_waitcnt lgkmcnt(0)
	s_barrier
	s_setprio 1
	v_mfma_f32_16x16x128_f8f6f4 v[124:127], v[140:147], v[178:185], v[124:127]
	v_mfma_f32_16x16x128_f8f6f4 v[108:111], v[132:139], v[194:201], v[108:111]
	v_mfma_f32_16x16x128_f8f6f4 v[104:107], v[140:147], v[194:201], v[104:107]
	v_mfma_f32_16x16x128_f8f6f4 v[120:123], v[132:139], v[178:185], v[128:131]
	v_mfma_f32_16x16x128_f8f6f4 v[148:151], v[132:139], v[202:209], v[92:95]
	v_mfma_f32_16x16x128_f8f6f4 v[186:189], v[140:147], v[202:209], v[88:91]
	v_mfma_f32_16x16x128_f8f6f4 v[218:221], v[132:139], v[210:217], v[76:79]
	v_mfma_f32_16x16x128_f8f6f4 v[226:229], v[140:147], v[210:217], v[72:75]
	v_mfma_f32_16x16x128_f8f6f4 v[116:119], v[162:169], v[178:185], v[116:119]
	v_mfma_f32_16x16x128_f8f6f4 v[112:115], v[170:177], v[178:185], v[112:115]
	v_mfma_f32_16x16x128_f8f6f4 v[100:103], v[162:169], v[194:201], v[100:103]
	v_mfma_f32_16x16x128_f8f6f4 v[96:99], v[170:177], v[194:201], v[96:99]
	v_mfma_f32_16x16x128_f8f6f4 v[178:181], v[162:169], v[202:209], v[84:87]
	v_mfma_f32_16x16x128_f8f6f4 v[182:185], v[170:177], v[202:209], v[80:83]
	v_mfma_f32_16x16x128_f8f6f4 v[194:197], v[162:169], v[210:217], v[68:71]
	v_mfma_f32_16x16x128_f8f6f4 v[198:201], v[170:177], v[210:217], v[64:67]
	s_setprio 0
	s_barrier
; #define PG8_STAGE(bufoff, rs_, soff_, voff) do { _Pragma("unroll") for (int _i = 0; _i < 2; ++_i) \
;         __builtin_amdgcn_raw_ptr_buffer_load_lds(rs_, (LAS void*)(lds + (bufoff) + ldsw + _i * 8192), 16, (int)(voff)[_i], (int)(soff_), 0, 0); } while (0)
; #define PG8_LDA(dst, b, h) do { _Pragma("unroll") for (int m = 0; m < 4; ++m) dst[m] = PG8_LD2(lds + PG8_SA(b, h) + aoff + m * 2048); } while (0)
; #define PG8_LDB(dst, b, h) do { _Pragma("unroll") for (int n = 0; n < 2; ++n) dst[n] = PG8_LD2(lds + PG8_SB(b, h) + boff + n * 2048); } while (0)
; #define PG8_WAIT_V(n) asm volatile("s_waitcnt vmcnt(" #n ")" ::: "memory")
; #define PG8_WAIT_L(n) asm volatile("s_waitcnt lgkmcnt(" #n ")" ::: "memory")
; #define PG8_BAR __builtin_amdgcn_s_barrier()
; #define PG8_SCHED __builtin_amdgcn_sched_barrier(0)
; template <class Epi, class Sched, bool ALIGN_EPI = false, bool SP2 = false, bool FP8 = false>
; __device__ __forceinline__ void gemm_phase(LAS unsigned char* lds, const Gemm g, const Sched& S, const Epi& E, int wbase) {
;     ...
;             PG8_LDB(B0, 0, 0); PG8_LDB(B1, 0, 1); PG8_SCHED; PG8_LDA(At, 0, 0); PG8_STAGE(PG8_SA(1, 1), rAc, a1 + hstep, voffA);
;             PG8_WAIT_V(8); PG8_WAIT_L(0); PG8_BAR; PG8_MMA(0, 0, At, B0); PG8_MMA(0, 1, At, B1); PG8_BAR; PG8_SCHED;
;             PG8_LDA(At, 0, 1); PG8_STAGE(PG8_SB(0, 0), rB2, b2, voffB); PG8_STAGE(PG8_SB(0, 1), rB2, b2 + hstep, voffB); PG8_STAGE(PG8_SA(0, 0), rA2, a2, voffA);
;             PG8_WAIT_V(8); PG8_WAIT_L(0); PG8_BAR; PG8_MMA(1, 0, At, B0); PG8_MMA(1, 1, At, B1); PG8_BAR; PG8_SCHED;
;             PG8_LDB(B0, 1, 0); PG8_LDB(B1, 1, 1); PG8_SCHED; PG8_LDA(At, 1, 0); PG8_STAGE(PG8_SA(0, 1), rA2, a2 + hstep, voffA);
;             PG8_WAIT_V(8); PG8_WAIT_L(0); PG8_BAR; PG8_MMA(0, 0, At, B0); PG8_MMA(0, 1, At, B1); PG8_BAR; PG8_SCHED;
;             PG8_LDA(At, 1, 1); PG8_STAGE(PG8_SB(1, 0), rB2, b3, voffB); PG8_STAGE(PG8_SB(1, 1), rB2, b3 + hstep, voffB); PG8_STAGE(PG8_SA(1, 0), rA2, a3, voffA);
;             PG8_WAIT_V(8); PG8_WAIT_L(0); PG8_BAR; PG8_MMA(1, 0, At, B0); PG8_MMA(1, 1, At, B1); PG8_BAR; PG8_SCHED;
	s_mov_b32 m0, s33
	s_mov_b32 s14, s38
	s_mov_b32 s15, s39
	s_nop 1
	buffer_load_dwordx4 v223, s[12:15], s55 offen lds
	s_mov_b32 m0, s34
	ds_read_b128 v[64:67], v161 offset:16384
	s_add_i32 s67, s55, s30
	buffer_load_dwordx4 v157, s[12:15], s55 offen lds
	s_mov_b32 m0, s35
	ds_read_b128 v[68:71], v161 offset:17408
	buffer_load_dwordx4 v223, s[12:15], s67 offen lds
	s_mov_b32 m0, s41
	ds_read_b128 v[72:75], v161 offset:18432
	buffer_load_dwordx4 v157, s[12:15], s67 offen lds
	s_mov_b32 m0, s31
	ds_read_b128 v[76:79], v161 offset:19456
	buffer_load_dwordx4 v222, s[36:39], s66 offen lds
	s_mov_b32 m0, s42
	ds_read_b128 v[80:83], v161 offset:20480
	buffer_load_dwordx4 v156, s[36:39], s66 offen lds
	ds_read_b128 v[84:87], v161 offset:21504
	ds_read_b128 v[88:91], v161 offset:22528
	ds_read_b128 v[92:95], v161 offset:23552
	s_waitcnt vmcnt(8)
	s_waitcnt lgkmcnt(0)
	s_barrier
	s_setprio 1
	v_mfma_f32_16x16x128_f8f6f4 v[60:63], v[132:139], v[64:71], v[60:63]
	v_mfma_f32_16x16x128_f8f6f4 v[56:59], v[140:147], v[64:71], v[56:59]
	v_mfma_f32_16x16x128_f8f6f4 v[202:205], v[132:139], v[72:79], v[44:47]
	v_mfma_f32_16x16x128_f8f6f4 v[206:209], v[140:147], v[72:79], v[40:43]
	v_mfma_f32_16x16x128_f8f6f4 v[210:213], v[132:139], v[80:87], v[28:31]
	v_mfma_f32_16x16x128_f8f6f4 v[214:217], v[140:147], v[80:87], v[24:27]
	v_mfma_f32_16x16x128_f8f6f4 v[230:233], v[132:139], v[88:95], v[12:15]
	v_mfma_f32_16x16x128_f8f6f4 v[234:237], v[140:147], v[88:95], v[8:11]
	v_mfma_f32_16x16x128_f8f6f4 v[52:55], v[162:169], v[64:71], v[52:55]
	v_mfma_f32_16x16x128_f8f6f4 v[48:51], v[170:177], v[64:71], v[48:51]
	v_mfma_f32_16x16x128_f8f6f4 v[238:241], v[162:169], v[72:79], v[36:39]
	v_mfma_f32_16x16x128_f8f6f4 v[242:245], v[170:177], v[72:79], v[32:35]
	v_mfma_f32_16x16x128_f8f6f4 v[246:249], v[162:169], v[80:87], v[20:23]
	v_mfma_f32_16x16x128_f8f6f4 v[250:253], v[170:177], v[80:87], v[16:19]
	v_mfma_f32_16x16x128_f8f6f4 v[190:193], v[162:169], v[88:95], v[4:7]
	v_mfma_f32_16x16x128_f8f6f4 v[152:155], v[170:177], v[88:95], v[0:3]
	s_setprio 0
	s_barrier
	v_add_u32_e32 v8, 0x18000, v160
	s_nop 3
	ds_read_b128 v[0:3], v8
	ds_read_b128 v[4:7], v8 offset:1024
	ds_read_b128 v[16:19], v8 offset:2048
	ds_read_b128 v[20:23], v8 offset:3072
	v_add_u32_e32 v8, 0x1c000, v160
	ds_read_b128 v[132:135], v8
	ds_read_b128 v[136:139], v8 offset:1024
	ds_read_b128 v[140:143], v8 offset:2048
	ds_read_b128 v[144:147], v8 offset:3072
	s_add_i32 s66, s66, s30
	s_mov_b32 m0, s43
	ds_read_b128 v[8:11], v161 offset:32768
	ds_read_b128 v[12:15], v161 offset:33792
	ds_read_b128 v[24:27], v161 offset:34816
	ds_read_b128 v[28:31], v161 offset:35840
	ds_read_b128 v[32:35], v161 offset:36864
	ds_read_b128 v[36:39], v161 offset:37888
	ds_read_b128 v[40:43], v161 offset:38912
	ds_read_b128 v[44:47], v161 offset:39936
	buffer_load_dwordx4 v222, s[36:39], s66 offen lds
	s_mov_b32 m0, s44
	s_nop 0
	buffer_load_dwordx4 v156, s[36:39], s66 offen lds
	s_waitcnt vmcnt(8)
	s_waitcnt lgkmcnt(0)
	s_barrier
	s_setprio 1
	v_mfma_f32_16x16x128_f8f6f4 v[128:131], v[0:7], v[8:15], v[120:123]
	v_mfma_f32_16x16x128_f8f6f4 v[124:127], v[16:23], v[8:15], v[124:127]
	v_mfma_f32_16x16x128_f8f6f4 v[108:111], v[0:7], v[24:31], v[108:111]
	v_mfma_f32_16x16x128_f8f6f4 v[104:107], v[16:23], v[24:31], v[104:107]
	v_mfma_f32_16x16x128_f8f6f4 v[92:95], v[0:7], v[32:39], v[148:151]
	v_mfma_f32_16x16x128_f8f6f4 v[88:91], v[16:23], v[32:39], v[186:189]
	v_mfma_f32_16x16x128_f8f6f4 v[76:79], v[0:7], v[40:47], v[218:221]
	v_mfma_f32_16x16x128_f8f6f4 v[72:75], v[16:23], v[40:47], v[226:229]
	v_mfma_f32_16x16x128_f8f6f4 v[116:119], v[132:139], v[8:15], v[116:119]
	v_mfma_f32_16x16x128_f8f6f4 v[112:115], v[140:147], v[8:15], v[112:115]
	v_mfma_f32_16x16x128_f8f6f4 v[100:103], v[132:139], v[24:31], v[100:103]
	v_mfma_f32_16x16x128_f8f6f4 v[96:99], v[140:147], v[24:31], v[96:99]
	v_mfma_f32_16x16x128_f8f6f4 v[84:87], v[132:139], v[32:39], v[178:181]
	v_mfma_f32_16x16x128_f8f6f4 v[80:83], v[140:147], v[32:39], v[182:185]
	v_mfma_f32_16x16x128_f8f6f4 v[68:71], v[132:139], v[40:47], v[194:197]
	v_mfma_f32_16x16x128_f8f6f4 v[64:67], v[140:147], v[40:47], v[198:201]
	s_setprio 0
	s_barrier
	s_mov_b32 m0, s45
	s_bitset1_b32 s55, 7
	buffer_load_dwordx4 v223, s[12:15], s55 offen lds
	s_mov_b32 m0, s46
	ds_read_b128 v[32:35], v161 offset:49152
	buffer_load_dwordx4 v157, s[12:15], s55 offen lds
	s_add_i32 s55, s55, s30
	s_mov_b32 m0, s52
	ds_read_b128 v[36:39], v161 offset:50176
	buffer_load_dwordx4 v223, s[12:15], s55 offen lds
	s_mov_b32 m0, s53
	ds_read_b128 v[162:165], v161 offset:51200
	buffer_load_dwordx4 v157, s[12:15], s55 offen lds
	s_mov_b32 m0, s47
	ds_read_b128 v[166:169], v161 offset:52224
	buffer_load_dwordx4 v222, s[36:39], s54 offen lds
	s_mov_b32 m0, s48
	ds_read_b128 v[170:173], v161 offset:53248
	buffer_load_dwordx4 v156, s[36:39], s54 offen lds
	ds_read_b128 v[174:177], v161 offset:54272
	ds_read_b128 v[178:181], v161 offset:55296
	ds_read_b128 v[182:185], v161 offset:56320
	s_waitcnt vmcnt(8)
	s_waitcnt lgkmcnt(0)
	s_barrier
	s_setprio 1
	v_mfma_f32_16x16x128_f8f6f4 v[60:63], v[0:7], v[32:39], v[60:63]
	v_mfma_f32_16x16x128_f8f6f4 v[56:59], v[16:23], v[32:39], v[56:59]
	v_mfma_f32_16x16x128_f8f6f4 v[44:47], v[0:7], v[162:169], v[202:205]
	v_mfma_f32_16x16x128_f8f6f4 v[40:43], v[16:23], v[162:169], v[206:209]
	v_mfma_f32_16x16x128_f8f6f4 v[28:31], v[0:7], v[170:177], v[210:213]
	v_mfma_f32_16x16x128_f8f6f4 v[24:27], v[16:23], v[170:177], v[214:217]
	v_mfma_f32_16x16x128_f8f6f4 v[12:15], v[0:7], v[178:185], v[230:233]
	v_mfma_f32_16x16x128_f8f6f4 v[8:11], v[16:23], v[178:185], v[234:237]
	v_mfma_f32_16x16x128_f8f6f4 v[52:55], v[132:139], v[32:39], v[52:55]
	v_mfma_f32_16x16x128_f8f6f4 v[48:51], v[140:147], v[32:39], v[48:51]
	v_mfma_f32_16x16x128_f8f6f4 v[36:39], v[132:139], v[162:169], v[238:241]
	v_mfma_f32_16x16x128_f8f6f4 v[32:35], v[140:147], v[162:169], v[242:245]
	v_mfma_f32_16x16x128_f8f6f4 v[20:23], v[132:139], v[170:177], v[246:249]
	v_mfma_f32_16x16x128_f8f6f4 v[16:19], v[140:147], v[170:177], v[250:253]
	v_mfma_f32_16x16x128_f8f6f4 v[4:7], v[132:139], v[178:185], v[190:193]
	v_mfma_f32_16x16x128_f8f6f4 v[0:3], v[140:147], v[178:185], v[152:155]
	s_setprio 0
	s_barrier
	s_add_i32 s11, s11, 2
	s_addk_i32 s4, 0x100
	s_addk_i32 s5, 0x100
	s_cmp_ge_i32 s11, s58
	s_cbranch_scc0 .LBB0_926

;     __device__ __forceinline__ unsigned a_off(const Unit& u, const Gemm& g) const { return (unsigned)u.pm * (unsigned)(BM * 2) * (unsigned)g.K; }
;     __device__ __forceinline__ unsigned b_off(const Unit& u, const Gemm& g) const { return (unsigned)u.pn * (unsigned)(BM * 2) * (unsigned)g.K; }
;     __device__ __forceinline__ bool next(int i, Unit& u) const { return so.next(i, u); }
;     __device__ __forceinline__ unsigned a_off(const Unit& u, const Gemm& g) const { return (unsigned)u.pm * (unsigned)(BM * 2) * (unsigned)g.K; }
;     __device__ __forceinline__ bool next(int i, Unit& u) const { const bool ok = so.next(i >> 1, u); u.part = i & 1; return ok; }
; template <class Epi, class Sched, bool ALIGN_EPI = false, bool SP2 = false, bool FP8 = false>
; __device__ __forceinline__ void gemm_phase(LAS unsigned char* lds, const Gemm g, const Sched& S, const Epi& E, int wbase) {
;     ...
;         const bool has_next = S.next(ui + 1, nxt);
;         const unsigned nA = has_next ? S.a_off(nxt, g) : cA, nB = has_next ? S.b_off(nxt, g) : cB;
;         const rsrc_t rAn = (Sched::TWO && has_next) ? (nxt.part ? rA1 : rA0) : rAc, rBn = (Sched::TWO && has_next) ? (nxt.part ? rB1 : rB0) : rBc;
;         float pre_[8] = {0.f, 0.f, 0.f, 0.f, 0.f, 0.f, 0.f, 0.f};
;         if constexpr (Epi::HAS_PRE) E.pre_load(pre_, cur, wr);
;         for (int t = 0; t < nt; t += 2) {
;             const bool last = (t == nt - 2);
;             const unsigned a1 = cA + (unsigned)(t + 1) * kstep;
;             const unsigned a2 = last ? nA : cA + (unsigned)(t + 2) * kstep, b2 = last ? nB : cB + (unsigned)(t + 2) * kstep; const rsrc_t rA2 = (Sched::TWO && last) ? rAn : rAc, rB2 = (Sched::TWO && last) ? rBn : rBc;
;             const unsigned a3 = a2 + kstep, b3 = b2 + kstep;
;             if (last && has_next) S.a_ready(nxt);
;             if constexpr (SP2) {
;             PG8_LDB(B0, 0, 0); PG8_LDB(B1, 0, 1); PG8_SCHED; PG8_LDA(At, 0, 0); PG8_STAGE(PG8_SA(1, 1), rAc, a1 + hstep, voffA);
;             PG8_WAIT_V(8); PG8_WAIT_L(0); PG8_BAR; PG8_MMA(0, 0, At, B0); PG8_MMA(0, 1, At, B1); PG8_BAR; PG8_SCHED;
;             PG8_LDA(At, 0, 1); PG8_STAGE(PG8_SB(0, 0), rB2, b2, voffB); PG8_STAGE(PG8_SB(0, 1), rB2, b2 + hstep, voffB); PG8_STAGE(PG8_SA(0, 0), rA2, a2, voffA);
;             PG8_WAIT_V(8); PG8_WAIT_L(0); PG8_BAR; PG8_MMA(1, 0, At, B0); PG8_MMA(1, 1, At, B1); PG8_BAR; PG8_SCHED;
.LBB0_1002:
	s_lshl_b32 s81, s80, 19
	s_andn2_b64 vcc, exec, s[24:25]
	s_lshl_b32 s82, s79, 19
	s_cbranch_vccnz .LBB0_1058
	s_and_b64 s[2:3], s[28:29], exec
	s_waitcnt vmcnt(37)
	s_waitcnt vmcnt(36)
	s_waitcnt vmcnt(35)
	s_waitcnt vmcnt(32)
	s_waitcnt vmcnt(31)
	s_waitcnt vmcnt(27)
	s_waitcnt vmcnt(26)
	s_waitcnt vmcnt(24)
	s_waitcnt vmcnt(23)
	s_cselect_b32 s2, s81, s4
	s_cselect_b32 s3, s82, s5
	s_addk_i32 s4, 0x80
	s_addk_i32 s5, 0x100
	s_mov_b32 s11, 0
	s_waitcnt vmcnt(0)
	v_add_u32_e32 v132, 0x10000, v180
	v_add_u32_e32 v156, 0x14000, v180
	ds_read_b128 v[96:99], v132
	ds_read_b128 v[108:111], v132 offset:1024
	ds_read_b128 v[120:123], v132 offset:2048
	ds_read_b128 v[132:135], v132 offset:3072
	ds_read_b128 v[136:139], v156
	ds_read_b128 v[144:147], v156 offset:1024
	ds_read_b128 v[152:155], v156 offset:2048
	ds_read_b128 v[156:159], v156 offset:3072
	s_add_i32 s14, s4, 0x80
	s_cmp_eq_u32 s62, s11
	s_cselect_b32 s66, s2, s14
	s_cselect_b32 s55, s3, s5
	s_or_b32 s54, s66, 0x80
	s_add_i32 s14, s33, s4
	s_mov_b32 m0, s63
	ds_read_b128 v[160:163], v181
	ds_read_b128 v[164:167], v181 offset:1024
	ds_read_b128 v[168:171], v181 offset:2048
	ds_read_b128 v[182:185], v181 offset:3072
	ds_read_b128 v[186:189], v181 offset:4096
	ds_read_b128 v[190:193], v181 offset:5120
	ds_read_b128 v[194:197], v181 offset:6144
	ds_read_b128 v[198:201], v181 offset:7168
	buffer_load_dwordx4 v174, s[36:39], s14 offen lds
	s_mov_b32 m0, s65
	s_nop 0
	buffer_load_dwordx4 v176, s[36:39], s14 offen lds
	s_waitcnt vmcnt(8)
	s_waitcnt lgkmcnt(0)
	s_barrier
	s_setprio 1
	v_mfma_f32_16x16x32_bf16 v[148:151], v[96:99], v[160:163], 0
	v_mfma_f32_16x16x32_bf16 v[140:143], v[120:123], v[160:163], 0
	v_mfma_f32_16x16x32_bf16 v[116:119], v[96:99], v[168:171], 0
	v_mfma_f32_16x16x32_bf16 v[112:115], v[120:123], v[168:171], 0
	v_mfma_f32_16x16x32_bf16 v[92:95], v[96:99], v[186:189], 0
	v_mfma_f32_16x16x32_bf16 v[88:91], v[120:123], v[186:189], 0
	v_mfma_f32_16x16x32_bf16 v[76:79], v[96:99], v[194:197], 0
	v_mfma_f32_16x16x32_bf16 v[72:75], v[120:123], v[194:197], 0
	v_mfma_f32_16x16x32_bf16 v[148:151], v[108:111], v[164:167], v[148:151]
	v_mfma_f32_16x16x32_bf16 v[140:143], v[132:135], v[164:167], v[140:143]
	v_mfma_f32_16x16x32_bf16 v[116:119], v[108:111], v[182:185], v[116:119]
	v_mfma_f32_16x16x32_bf16 v[112:115], v[132:135], v[182:185], v[112:115]
	v_mfma_f32_16x16x32_bf16 v[92:95], v[108:111], v[190:193], v[92:95]
	v_mfma_f32_16x16x32_bf16 v[88:91], v[132:135], v[190:193], v[88:91]
	v_mfma_f32_16x16x32_bf16 v[76:79], v[108:111], v[198:201], v[76:79]
	v_mfma_f32_16x16x32_bf16 v[72:75], v[132:135], v[198:201], v[72:75]
	v_mfma_f32_16x16x32_bf16 v[128:131], v[136:139], v[160:163], 0
	v_mfma_f32_16x16x32_bf16 v[124:127], v[152:155], v[160:163], 0
	v_mfma_f32_16x16x32_bf16 v[104:107], v[136:139], v[168:171], 0
	v_mfma_f32_16x16x32_bf16 v[100:103], v[152:155], v[168:171], 0
	v_mfma_f32_16x16x32_bf16 v[84:87], v[136:139], v[186:189], 0
	v_mfma_f32_16x16x32_bf16 v[80:83], v[152:155], v[186:189], 0
	v_mfma_f32_16x16x32_bf16 v[68:71], v[136:139], v[194:197], 0
	v_mfma_f32_16x16x32_bf16 v[64:67], v[152:155], v[194:197], 0
	v_mfma_f32_16x16x32_bf16 v[128:131], v[144:147], v[164:167], v[128:131]
	v_mfma_f32_16x16x32_bf16 v[124:127], v[156:159], v[164:167], v[124:127]
	v_mfma_f32_16x16x32_bf16 v[104:107], v[144:147], v[182:185], v[104:107]
	v_mfma_f32_16x16x32_bf16 v[100:103], v[156:159], v[182:185], v[100:103]
	v_mfma_f32_16x16x32_bf16 v[84:87], v[144:147], v[190:193], v[84:87]
	v_mfma_f32_16x16x32_bf16 v[80:83], v[156:159], v[190:193], v[80:83]
	v_mfma_f32_16x16x32_bf16 v[68:71], v[144:147], v[198:201], v[68:71]
	v_mfma_f32_16x16x32_bf16 v[64:67], v[156:159], v[198:201], v[64:67]
	s_setprio 0
	s_barrier
	s_mov_b32 m0, s35
	s_mov_b32 s14, s38
	s_mov_b32 s15, s39
	buffer_load_dwordx4 v175, s[12:15], s55 offen lds
	s_mov_b32 m0, s41
	ds_read_b128 v[160:163], v181 offset:16384
	s_add_i32 s67, s55, s33
	buffer_load_dwordx4 v177, s[12:15], s55 offen lds
	s_mov_b32 m0, s42
	ds_read_b128 v[164:167], v181 offset:17408
	buffer_load_dwordx4 v175, s[12:15], s67 offen lds
	s_mov_b32 m0, s43
	ds_read_b128 v[168:171], v181 offset:18432
	buffer_load_dwordx4 v177, s[12:15], s67 offen lds
	s_mov_b32 m0, s34
	ds_read_b128 v[182:185], v181 offset:19456
	buffer_load_dwordx4 v174, s[36:39], s66 offen lds
	s_mov_b32 m0, s44
	ds_read_b128 v[186:189], v181 offset:20480
	buffer_load_dwordx4 v176, s[36:39], s66 offen lds
	ds_read_b128 v[190:193], v181 offset:21504
	ds_read_b128 v[194:197], v181 offset:22528
	ds_read_b128 v[198:201], v181 offset:23552
	s_waitcnt vmcnt(8)
	s_waitcnt lgkmcnt(0)
	s_barrier
; #define PG8_STAGE(bufoff, rs_, soff_, voff) do { _Pragma("unroll") for (int _i = 0; _i < 2; ++_i) \
;         __builtin_amdgcn_raw_ptr_buffer_load_lds(rs_, (LAS void*)(lds + (bufoff) + ldsw + _i * 8192), 16, (int)(voff)[_i], (int)(soff_), 0, 0); } while (0)
; #define PG8_LDA(dst, b, h) do { _Pragma("unroll") for (int m = 0; m < 4; ++m) dst[m] = PG8_LD2(lds + PG8_SA(b, h) + aoff + m * 2048); } while (0)
; #define PG8_LDB(dst, b, h) do { _Pragma("unroll") for (int n = 0; n < 2; ++n) dst[n] = PG8_LD2(lds + PG8_SB(b, h) + boff + n * 2048); } while (0)
; #define PG8_WAIT_V(n) asm volatile("s_waitcnt vmcnt(" #n ")" ::: "memory")
; #define PG8_WAIT_L(n) asm volatile("s_waitcnt lgkmcnt(" #n ")" ::: "memory")
; #define PG8_BAR __builtin_amdgcn_s_barrier()
; #define PG8_SCHED __builtin_amdgcn_sched_barrier(0)
; template <class Epi, class Sched, bool ALIGN_EPI = false, bool SP2 = false, bool FP8 = false>
; __device__ __forceinline__ void gemm_phase(LAS unsigned char* lds, const Gemm g, const Sched& S, const Epi& E, int wbase) {
;     ...
;             PG8_WAIT_V(8); PG8_WAIT_L(0); PG8_BAR; PG8_MMA(1, 0, At, B0); PG8_MMA(1, 1, At, B1); PG8_BAR; PG8_SCHED;
;             PG8_LDB(B0, 1, 0); PG8_LDB(B1, 1, 1); PG8_SCHED; PG8_LDA(At, 1, 0); PG8_STAGE(PG8_SA(0, 1), rA2, a2 + hstep, voffA);
;             PG8_WAIT_V(8); PG8_WAIT_L(0); PG8_BAR; PG8_MMA(0, 0, At, B0); PG8_MMA(0, 1, At, B1); PG8_BAR; PG8_SCHED;
	s_setprio 1
	v_mfma_f32_16x16x32_bf16 v[60:63], v[96:99], v[160:163], 0
	v_mfma_f32_16x16x32_bf16 v[56:59], v[120:123], v[160:163], 0
	v_mfma_f32_16x16x32_bf16 v[44:47], v[96:99], v[168:171], 0
	v_mfma_f32_16x16x32_bf16 v[40:43], v[120:123], v[168:171], 0
	v_mfma_f32_16x16x32_bf16 v[28:31], v[96:99], v[186:189], 0
	v_mfma_f32_16x16x32_bf16 v[24:27], v[120:123], v[186:189], 0
	v_mfma_f32_16x16x32_bf16 v[12:15], v[96:99], v[194:197], 0
	v_mfma_f32_16x16x32_bf16 v[8:11], v[120:123], v[194:197], 0
	v_mfma_f32_16x16x32_bf16 v[60:63], v[108:111], v[164:167], v[60:63]
	v_mfma_f32_16x16x32_bf16 v[56:59], v[132:135], v[164:167], v[56:59]
	v_mfma_f32_16x16x32_bf16 v[44:47], v[108:111], v[182:185], v[44:47]
	v_mfma_f32_16x16x32_bf16 v[40:43], v[132:135], v[182:185], v[40:43]
	v_mfma_f32_16x16x32_bf16 v[28:31], v[108:111], v[190:193], v[28:31]
	v_mfma_f32_16x16x32_bf16 v[24:27], v[132:135], v[190:193], v[24:27]
	v_mfma_f32_16x16x32_bf16 v[12:15], v[108:111], v[198:201], v[12:15]
	v_mfma_f32_16x16x32_bf16 v[8:11], v[132:135], v[198:201], v[8:11]
	v_mfma_f32_16x16x32_bf16 v[52:55], v[136:139], v[160:163], 0
	v_mfma_f32_16x16x32_bf16 v[48:51], v[152:155], v[160:163], 0
	v_mfma_f32_16x16x32_bf16 v[36:39], v[136:139], v[168:171], 0
	v_mfma_f32_16x16x32_bf16 v[32:35], v[152:155], v[168:171], 0
	v_mfma_f32_16x16x32_bf16 v[20:23], v[136:139], v[186:189], 0
	v_mfma_f32_16x16x32_bf16 v[16:19], v[152:155], v[186:189], 0
	v_mfma_f32_16x16x32_bf16 v[4:7], v[136:139], v[194:197], 0
	v_mfma_f32_16x16x32_bf16 v[0:3], v[152:155], v[194:197], 0
	v_mfma_f32_16x16x32_bf16 v[52:55], v[144:147], v[164:167], v[52:55]
	v_mfma_f32_16x16x32_bf16 v[48:51], v[156:159], v[164:167], v[48:51]
	v_mfma_f32_16x16x32_bf16 v[36:39], v[144:147], v[182:185], v[36:39]
	v_mfma_f32_16x16x32_bf16 v[32:35], v[156:159], v[182:185], v[32:35]
	v_mfma_f32_16x16x32_bf16 v[20:23], v[144:147], v[190:193], v[20:23]
	v_mfma_f32_16x16x32_bf16 v[16:19], v[156:159], v[190:193], v[16:19]
	v_mfma_f32_16x16x32_bf16 v[4:7], v[144:147], v[198:201], v[4:7]
	v_mfma_f32_16x16x32_bf16 v[0:3], v[156:159], v[198:201], v[0:3]
	s_setprio 0
	s_barrier
	v_add_u32_e32 v132, 0x18000, v180
	v_add_u32_e32 v156, 0x1c000, v180
	ds_read_b128 v[96:99], v132
	ds_read_b128 v[108:111], v132 offset:1024
	ds_read_b128 v[120:123], v132 offset:2048
	ds_read_b128 v[132:135], v132 offset:3072
	ds_read_b128 v[136:139], v156
	ds_read_b128 v[144:147], v156 offset:1024
	ds_read_b128 v[152:155], v156 offset:2048
	ds_read_b128 v[156:159], v156 offset:3072
	s_add_i32 s66, s66, s33
	s_mov_b32 m0, s45
	ds_read_b128 v[160:163], v181 offset:32768
	ds_read_b128 v[164:167], v181 offset:33792
	ds_read_b128 v[168:171], v181 offset:34816
	ds_read_b128 v[182:185], v181 offset:35840
	ds_read_b128 v[186:189], v181 offset:36864
	ds_read_b128 v[190:193], v181 offset:37888
	ds_read_b128 v[194:197], v181 offset:38912
	ds_read_b128 v[198:201], v181 offset:39936
	buffer_load_dwordx4 v174, s[36:39], s66 offen lds
	s_mov_b32 m0, s46
	s_nop 0
	buffer_load_dwordx4 v176, s[36:39], s66 offen lds
	s_waitcnt vmcnt(8)
	s_waitcnt lgkmcnt(0)
	s_barrier
	s_setprio 1
	v_mfma_f32_16x16x32_bf16 v[148:151], v[96:99], v[160:163], v[148:151]
	v_mfma_f32_16x16x32_bf16 v[140:143], v[120:123], v[160:163], v[140:143]
	v_mfma_f32_16x16x32_bf16 v[116:119], v[96:99], v[168:171], v[116:119]
	v_mfma_f32_16x16x32_bf16 v[112:115], v[120:123], v[168:171], v[112:115]
	v_mfma_f32_16x16x32_bf16 v[92:95], v[96:99], v[186:189], v[92:95]
	v_mfma_f32_16x16x32_bf16 v[88:91], v[120:123], v[186:189], v[88:91]
	v_mfma_f32_16x16x32_bf16 v[76:79], v[96:99], v[194:197], v[76:79]
	v_mfma_f32_16x16x32_bf16 v[72:75], v[120:123], v[194:197], v[72:75]
	v_mfma_f32_16x16x32_bf16 v[148:151], v[108:111], v[164:167], v[148:151]
	v_mfma_f32_16x16x32_bf16 v[140:143], v[132:135], v[164:167], v[140:143]
	v_mfma_f32_16x16x32_bf16 v[116:119], v[108:111], v[182:185], v[116:119]
	v_mfma_f32_16x16x32_bf16 v[112:115], v[132:135], v[182:185], v[112:115]
	v_mfma_f32_16x16x32_bf16 v[92:95], v[108:111], v[190:193], v[92:95]
	v_mfma_f32_16x16x32_bf16 v[88:91], v[132:135], v[190:193], v[88:91]
	v_mfma_f32_16x16x32_bf16 v[76:79], v[108:111], v[198:201], v[76:79]
	v_mfma_f32_16x16x32_bf16 v[72:75], v[132:135], v[198:201], v[72:75]
	v_mfma_f32_16x16x32_bf16 v[128:131], v[136:139], v[160:163], v[128:131]
	v_mfma_f32_16x16x32_bf16 v[124:127], v[152:155], v[160:163], v[124:127]
	v_mfma_f32_16x16x32_bf16 v[104:107], v[136:139], v[168:171], v[104:107]
	v_mfma_f32_16x16x32_bf16 v[100:103], v[152:155], v[168:171], v[100:103]
	v_mfma_f32_16x16x32_bf16 v[84:87], v[136:139], v[186:189], v[84:87]
	v_mfma_f32_16x16x32_bf16 v[80:83], v[152:155], v[186:189], v[80:83]
	v_mfma_f32_16x16x32_bf16 v[68:71], v[136:139], v[194:197], v[68:71]
	v_mfma_f32_16x16x32_bf16 v[64:67], v[152:155], v[194:197], v[64:67]
	v_mfma_f32_16x16x32_bf16 v[128:131], v[144:147], v[164:167], v[128:131]
	v_mfma_f32_16x16x32_bf16 v[124:127], v[156:159], v[164:167], v[124:127]
	v_mfma_f32_16x16x32_bf16 v[104:107], v[144:147], v[182:185], v[104:107]
	v_mfma_f32_16x16x32_bf16 v[100:103], v[156:159], v[182:185], v[100:103]
	v_mfma_f32_16x16x32_bf16 v[84:87], v[144:147], v[190:193], v[84:87]
	v_mfma_f32_16x16x32_bf16 v[80:83], v[156:159], v[190:193], v[80:83]
	v_mfma_f32_16x16x32_bf16 v[68:71], v[144:147], v[198:201], v[68:71]
	v_mfma_f32_16x16x32_bf16 v[64:67], v[156:159], v[198:201], v[64:67]
	s_setprio 0
	s_barrier
; #define PG8_STAGE(bufoff, rs_, soff_, voff) do { _Pragma("unroll") for (int _i = 0; _i < 2; ++_i) \
;         __builtin_amdgcn_raw_ptr_buffer_load_lds(rs_, (LAS void*)(lds + (bufoff) + ldsw + _i * 8192), 16, (int)(voff)[_i], (int)(soff_), 0, 0); } while (0)
; #define PG8_LDA(dst, b, h) do { _Pragma("unroll") for (int m = 0; m < 4; ++m) dst[m] = PG8_LD2(lds + PG8_SA(b, h) + aoff + m * 2048); } while (0)
; #define PG8_LDB(dst, b, h) do { _Pragma("unroll") for (int n = 0; n < 2; ++n) dst[n] = PG8_LD2(lds + PG8_SB(b, h) + boff + n * 2048); } while (0)
; #define PG8_WAIT_V(n) asm volatile("s_waitcnt vmcnt(" #n ")" ::: "memory")
; #define PG8_WAIT_L(n) asm volatile("s_waitcnt lgkmcnt(" #n ")" ::: "memory")
; #define PG8_BAR __builtin_amdgcn_s_barrier()
; #define PG8_SCHED __builtin_amdgcn_sched_barrier(0)
; template <class Epi, class Sched, bool ALIGN_EPI = false, bool SP2 = false, bool FP8 = false>
; __device__ __forceinline__ void gemm_phase(LAS unsigned char* lds, const Gemm g, const Sched& S, const Epi& E, int wbase) {
;     ...
;             PG8_LDB(B0, 0, 0); PG8_LDB(B1, 0, 1); PG8_SCHED; PG8_LDA(At, 0, 0); PG8_STAGE(PG8_SA(1, 1), rAc, a1 + hstep, voffA);
;             PG8_WAIT_V(8); PG8_WAIT_L(0); PG8_BAR; PG8_MMA(0, 0, At, B0); PG8_MMA(0, 1, At, B1); PG8_BAR; PG8_SCHED;
;             PG8_LDA(At, 0, 1); PG8_STAGE(PG8_SB(0, 0), rB2, b2, voffB); PG8_STAGE(PG8_SB(0, 1), rB2, b2 + hstep, voffB); PG8_STAGE(PG8_SA(0, 0), rA2, a2, voffA);
;             PG8_WAIT_V(8); PG8_WAIT_L(0); PG8_BAR; PG8_MMA(1, 0, At, B0); PG8_MMA(1, 1, At, B1); PG8_BAR; PG8_SCHED;
;             PG8_LDB(B0, 1, 0); PG8_LDB(B1, 1, 1); PG8_SCHED; PG8_LDA(At, 1, 0); PG8_STAGE(PG8_SA(0, 1), rA2, a2 + hstep, voffA);
;             PG8_WAIT_V(8); PG8_WAIT_L(0); PG8_BAR; PG8_MMA(0, 0, At, B0); PG8_MMA(0, 1, At, B1); PG8_BAR; PG8_SCHED;
;             PG8_LDA(At, 1, 1); PG8_STAGE(PG8_SB(1, 0), rB2, b3, voffB); PG8_STAGE(PG8_SB(1, 1), rB2, b3 + hstep, voffB); PG8_STAGE(PG8_SA(1, 0), rA2, a3, voffA);
;             PG8_WAIT_V(8); PG8_WAIT_L(0); PG8_BAR; PG8_MMA(1, 0, At, B0); PG8_MMA(1, 1, At, B1); PG8_BAR; PG8_SCHED;
	s_mov_b32 m0, s47
	s_bitset1_b32 s55, 7
	buffer_load_dwordx4 v175, s[12:15], s55 offen lds
	s_mov_b32 m0, s48
	ds_read_b128 v[160:163], v181 offset:49152
	buffer_load_dwordx4 v177, s[12:15], s55 offen lds
	s_add_i32 s55, s55, s33
	s_mov_b32 m0, s56
	ds_read_b128 v[164:167], v181 offset:50176
	buffer_load_dwordx4 v175, s[12:15], s55 offen lds
	s_mov_b32 m0, s57
	ds_read_b128 v[168:171], v181 offset:51200
	buffer_load_dwordx4 v177, s[12:15], s55 offen lds
	s_mov_b32 m0, s52
	ds_read_b128 v[182:185], v181 offset:52224
	buffer_load_dwordx4 v174, s[36:39], s54 offen lds
	s_mov_b32 m0, s53
	ds_read_b128 v[186:189], v181 offset:53248
	buffer_load_dwordx4 v176, s[36:39], s54 offen lds
	ds_read_b128 v[190:193], v181 offset:54272
	ds_read_b128 v[194:197], v181 offset:55296
	ds_read_b128 v[198:201], v181 offset:56320
	s_waitcnt vmcnt(8)
	s_waitcnt lgkmcnt(0)
	s_barrier
	s_setprio 1
	v_mfma_f32_16x16x32_bf16 v[60:63], v[96:99], v[160:163], v[60:63]
	v_mfma_f32_16x16x32_bf16 v[56:59], v[120:123], v[160:163], v[56:59]
	v_mfma_f32_16x16x32_bf16 v[44:47], v[96:99], v[168:171], v[44:47]
	v_mfma_f32_16x16x32_bf16 v[40:43], v[120:123], v[168:171], v[40:43]
	v_mfma_f32_16x16x32_bf16 v[28:31], v[96:99], v[186:189], v[28:31]
	v_mfma_f32_16x16x32_bf16 v[24:27], v[120:123], v[186:189], v[24:27]
	v_mfma_f32_16x16x32_bf16 v[12:15], v[96:99], v[194:197], v[12:15]
	v_mfma_f32_16x16x32_bf16 v[8:11], v[120:123], v[194:197], v[8:11]
	v_mfma_f32_16x16x32_bf16 v[60:63], v[108:111], v[164:167], v[60:63]
	v_mfma_f32_16x16x32_bf16 v[56:59], v[132:135], v[164:167], v[56:59]
	v_mfma_f32_16x16x32_bf16 v[44:47], v[108:111], v[182:185], v[44:47]
	v_mfma_f32_16x16x32_bf16 v[40:43], v[132:135], v[182:185], v[40:43]
	v_mfma_f32_16x16x32_bf16 v[28:31], v[108:111], v[190:193], v[28:31]
	v_mfma_f32_16x16x32_bf16 v[24:27], v[132:135], v[190:193], v[24:27]
	v_mfma_f32_16x16x32_bf16 v[12:15], v[108:111], v[198:201], v[12:15]
	v_mfma_f32_16x16x32_bf16 v[8:11], v[132:135], v[198:201], v[8:11]
	v_mfma_f32_16x16x32_bf16 v[52:55], v[136:139], v[160:163], v[52:55]
	v_mfma_f32_16x16x32_bf16 v[48:51], v[152:155], v[160:163], v[48:51]
	v_mfma_f32_16x16x32_bf16 v[36:39], v[136:139], v[168:171], v[36:39]
	v_mfma_f32_16x16x32_bf16 v[32:35], v[152:155], v[168:171], v[32:35]
	v_mfma_f32_16x16x32_bf16 v[20:23], v[136:139], v[186:189], v[20:23]
	v_mfma_f32_16x16x32_bf16 v[16:19], v[152:155], v[186:189], v[16:19]
	v_mfma_f32_16x16x32_bf16 v[4:7], v[136:139], v[194:197], v[4:7]
	v_mfma_f32_16x16x32_bf16 v[0:3], v[152:155], v[194:197], v[0:3]
	v_mfma_f32_16x16x32_bf16 v[52:55], v[144:147], v[164:167], v[52:55]
	v_mfma_f32_16x16x32_bf16 v[48:51], v[156:159], v[164:167], v[48:51]
	v_mfma_f32_16x16x32_bf16 v[36:39], v[144:147], v[182:185], v[36:39]
	v_mfma_f32_16x16x32_bf16 v[32:35], v[156:159], v[182:185], v[32:35]
	v_mfma_f32_16x16x32_bf16 v[20:23], v[144:147], v[190:193], v[20:23]
	v_mfma_f32_16x16x32_bf16 v[16:19], v[156:159], v[190:193], v[16:19]
	v_mfma_f32_16x16x32_bf16 v[4:7], v[144:147], v[198:201], v[4:7]
	v_mfma_f32_16x16x32_bf16 v[0:3], v[156:159], v[198:201], v[0:3]
	s_setprio 0
	s_barrier
	s_add_i32 s11, s11, 2
	s_addk_i32 s4, 0x100
	s_addk_i32 s5, 0x100
	s_cmp_ge_i32 s11, s60
	s_cbranch_scc0 .LBB0_1004
	s_branch .Lzp_after_1004
.LBB0_1004:
	v_add_u32_e32 v132, 0x10000, v180
	v_add_u32_e32 v156, 0x14000, v180
	ds_read_b128 v[96:99], v132
	ds_read_b128 v[108:111], v132 offset:1024
	ds_read_b128 v[120:123], v132 offset:2048
	ds_read_b128 v[132:135], v132 offset:3072
	ds_read_b128 v[136:139], v156
	ds_read_b128 v[144:147], v156 offset:1024
	ds_read_b128 v[152:155], v156 offset:2048
	ds_read_b128 v[156:159], v156 offset:3072
	s_add_i32 s14, s4, 0x80
	s_cmp_eq_u32 s62, s11
	s_cselect_b32 s66, s2, s14
	s_cselect_b32 s55, s3, s5
	s_or_b32 s54, s66, 0x80
	s_add_i32 s14, s33, s4
	s_mov_b32 m0, s63
	ds_read_b128 v[160:163], v181
	ds_read_b128 v[164:167], v181 offset:1024
	ds_read_b128 v[168:171], v181 offset:2048
	ds_read_b128 v[182:185], v181 offset:3072
	ds_read_b128 v[186:189], v181 offset:4096
	ds_read_b128 v[190:193], v181 offset:5120
	ds_read_b128 v[194:197], v181 offset:6144
	ds_read_b128 v[198:201], v181 offset:7168
	buffer_load_dwordx4 v174, s[36:39], s14 offen lds
	s_mov_b32 m0, s65
	s_nop 0
	buffer_load_dwordx4 v176, s[36:39], s14 offen lds
	s_waitcnt vmcnt(8)
	s_waitcnt lgkmcnt(0)
	s_barrier
	s_setprio 1
	v_mfma_f32_16x16x32_bf16 v[148:151], v[96:99], v[160:163], v[148:151]
	v_mfma_f32_16x16x32_bf16 v[140:143], v[120:123], v[160:163], v[140:143]
	v_mfma_f32_16x16x32_bf16 v[116:119], v[96:99], v[168:171], v[116:119]
	v_mfma_f32_16x16x32_bf16 v[112:115], v[120:123], v[168:171], v[112:115]
	v_mfma_f32_16x16x32_bf16 v[92:95], v[96:99], v[186:189], v[92:95]
	v_mfma_f32_16x16x32_bf16 v[88:91], v[120:123], v[186:189], v[88:91]
	v_mfma_f32_16x16x32_bf16 v[76:79], v[96:99], v[194:197], v[76:79]
	v_mfma_f32_16x16x32_bf16 v[72:75], v[120:123], v[194:197], v[72:75]
	v_mfma_f32_16x16x32_bf16 v[148:151], v[108:111], v[164:167], v[148:151]
	v_mfma_f32_16x16x32_bf16 v[140:143], v[132:135], v[164:167], v[140:143]
	v_mfma_f32_16x16x32_bf16 v[116:119], v[108:111], v[182:185], v[116:119]
	v_mfma_f32_16x16x32_bf16 v[112:115], v[132:135], v[182:185], v[112:115]
	v_mfma_f32_16x16x32_bf16 v[92:95], v[108:111], v[190:193], v[92:95]
	v_mfma_f32_16x16x32_bf16 v[88:91], v[132:135], v[190:193], v[88:91]
	v_mfma_f32_16x16x32_bf16 v[76:79], v[108:111], v[198:201], v[76:79]
	v_mfma_f32_16x16x32_bf16 v[72:75], v[132:135], v[198:201], v[72:75]
	v_mfma_f32_16x16x32_bf16 v[128:131], v[136:139], v[160:163], v[128:131]
	v_mfma_f32_16x16x32_bf16 v[124:127], v[152:155], v[160:163], v[124:127]
	v_mfma_f32_16x16x32_bf16 v[104:107], v[136:139], v[168:171], v[104:107]
	v_mfma_f32_16x16x32_bf16 v[100:103], v[152:155], v[168:171], v[100:103]
	v_mfma_f32_16x16x32_bf16 v[84:87], v[136:139], v[186:189], v[84:87]
	v_mfma_f32_16x16x32_bf16 v[80:83], v[152:155], v[186:189], v[80:83]
	v_mfma_f32_16x16x32_bf16 v[68:71], v[136:139], v[194:197], v[68:71]
	v_mfma_f32_16x16x32_bf16 v[64:67], v[152:155], v[194:197], v[64:67]
	v_mfma_f32_16x16x32_bf16 v[128:131], v[144:147], v[164:167], v[128:131]
	v_mfma_f32_16x16x32_bf16 v[124:127], v[156:159], v[164:167], v[124:127]
	v_mfma_f32_16x16x32_bf16 v[104:107], v[144:147], v[182:185], v[104:107]
	v_mfma_f32_16x16x32_bf16 v[100:103], v[156:159], v[182:185], v[100:103]
	v_mfma_f32_16x16x32_bf16 v[84:87], v[144:147], v[190:193], v[84:87]
	v_mfma_f32_16x16x32_bf16 v[80:83], v[156:159], v[190:193], v[80:83]
	v_mfma_f32_16x16x32_bf16 v[68:71], v[144:147], v[198:201], v[68:71]
	v_mfma_f32_16x16x32_bf16 v[64:67], v[156:159], v[198:201], v[64:67]
	s_setprio 0
	s_barrier
; #define PG8_STAGE(bufoff, rs_, soff_, voff) do { _Pragma("unroll") for (int _i = 0; _i < 2; ++_i) \
;         __builtin_amdgcn_raw_ptr_buffer_load_lds(rs_, (LAS void*)(lds + (bufoff) + ldsw + _i * 8192), 16, (int)(voff)[_i], (int)(soff_), 0, 0); } while (0)
; #define PG8_LDA(dst, b, h) do { _Pragma("unroll") for (int m = 0; m < 4; ++m) dst[m] = PG8_LD2(lds + PG8_SA(b, h) + aoff + m * 2048); } while (0)
; #define PG8_LDB(dst, b, h) do { _Pragma("unroll") for (int n = 0; n < 2; ++n) dst[n] = PG8_LD2(lds + PG8_SB(b, h) + boff + n * 2048); } while (0)
; #define PG8_WAIT_V(n) asm volatile("s_waitcnt vmcnt(" #n ")" ::: "memory")
; #define PG8_WAIT_L(n) asm volatile("s_waitcnt lgkmcnt(" #n ")" ::: "memory")
; #define PG8_BAR __builtin_amdgcn_s_barrier()
; #define PG8_SCHED __builtin_amdgcn_sched_barrier(0)
; template <class Epi, class Sched, bool ALIGN_EPI = false, bool SP2 = false, bool FP8 = false>
; __device__ __forceinline__ void gemm_phase(LAS unsigned char* lds, const Gemm g, const Sched& S, const Epi& E, int wbase) {
;     ...
;             PG8_LDA(At, 0, 1); PG8_STAGE(PG8_SB(0, 0), rB2, b2, voffB); PG8_STAGE(PG8_SB(0, 1), rB2, b2 + hstep, voffB); PG8_STAGE(PG8_SA(0, 0), rA2, a2, voffA);
;             PG8_WAIT_V(8); PG8_WAIT_L(0); PG8_BAR; PG8_MMA(1, 0, At, B0); PG8_MMA(1, 1, At, B1); PG8_BAR; PG8_SCHED;
;             PG8_LDB(B0, 1, 0); PG8_LDB(B1, 1, 1); PG8_SCHED; PG8_LDA(At, 1, 0); PG8_STAGE(PG8_SA(0, 1), rA2, a2 + hstep, voffA);
;             PG8_WAIT_V(8); PG8_WAIT_L(0); PG8_BAR; PG8_MMA(0, 0, At, B0); PG8_MMA(0, 1, At, B1); PG8_BAR; PG8_SCHED;
	s_mov_b32 m0, s35
	s_mov_b32 s14, s38
	s_mov_b32 s15, s39
	buffer_load_dwordx4 v175, s[12:15], s55 offen lds
	s_mov_b32 m0, s41
	ds_read_b128 v[160:163], v181 offset:16384
	s_add_i32 s67, s55, s33
	buffer_load_dwordx4 v177, s[12:15], s55 offen lds
	s_mov_b32 m0, s42
	ds_read_b128 v[164:167], v181 offset:17408
	buffer_load_dwordx4 v175, s[12:15], s67 offen lds
	s_mov_b32 m0, s43
	ds_read_b128 v[168:171], v181 offset:18432
	buffer_load_dwordx4 v177, s[12:15], s67 offen lds
	s_mov_b32 m0, s34
	ds_read_b128 v[182:185], v181 offset:19456
	buffer_load_dwordx4 v174, s[36:39], s66 offen lds
	s_mov_b32 m0, s44
	ds_read_b128 v[186:189], v181 offset:20480
	buffer_load_dwordx4 v176, s[36:39], s66 offen lds
	ds_read_b128 v[190:193], v181 offset:21504
	ds_read_b128 v[194:197], v181 offset:22528
	ds_read_b128 v[198:201], v181 offset:23552
	s_waitcnt vmcnt(8)
	s_waitcnt lgkmcnt(0)
	s_barrier
	s_setprio 1
	v_mfma_f32_16x16x32_bf16 v[60:63], v[96:99], v[160:163], v[60:63]
	v_mfma_f32_16x16x32_bf16 v[56:59], v[120:123], v[160:163], v[56:59]
	v_mfma_f32_16x16x32_bf16 v[44:47], v[96:99], v[168:171], v[44:47]
	v_mfma_f32_16x16x32_bf16 v[40:43], v[120:123], v[168:171], v[40:43]
	v_mfma_f32_16x16x32_bf16 v[28:31], v[96:99], v[186:189], v[28:31]
	v_mfma_f32_16x16x32_bf16 v[24:27], v[120:123], v[186:189], v[24:27]
	v_mfma_f32_16x16x32_bf16 v[12:15], v[96:99], v[194:197], v[12:15]
	v_mfma_f32_16x16x32_bf16 v[8:11], v[120:123], v[194:197], v[8:11]
	v_mfma_f32_16x16x32_bf16 v[60:63], v[108:111], v[164:167], v[60:63]
	v_mfma_f32_16x16x32_bf16 v[56:59], v[132:135], v[164:167], v[56:59]
	v_mfma_f32_16x16x32_bf16 v[44:47], v[108:111], v[182:185], v[44:47]
	v_mfma_f32_16x16x32_bf16 v[40:43], v[132:135], v[182:185], v[40:43]
	v_mfma_f32_16x16x32_bf16 v[28:31], v[108:111], v[190:193], v[28:31]
	v_mfma_f32_16x16x32_bf16 v[24:27], v[132:135], v[190:193], v[24:27]
	v_mfma_f32_16x16x32_bf16 v[12:15], v[108:111], v[198:201], v[12:15]
	v_mfma_f32_16x16x32_bf16 v[8:11], v[132:135], v[198:201], v[8:11]
	v_mfma_f32_16x16x32_bf16 v[52:55], v[136:139], v[160:163], v[52:55]
	v_mfma_f32_16x16x32_bf16 v[48:51], v[152:155], v[160:163], v[48:51]
	v_mfma_f32_16x16x32_bf16 v[36:39], v[136:139], v[168:171], v[36:39]
	v_mfma_f32_16x16x32_bf16 v[32:35], v[152:155], v[168:171], v[32:35]
	v_mfma_f32_16x16x32_bf16 v[20:23], v[136:139], v[186:189], v[20:23]
	v_mfma_f32_16x16x32_bf16 v[16:19], v[152:155], v[186:189], v[16:19]
	v_mfma_f32_16x16x32_bf16 v[4:7], v[136:139], v[194:197], v[4:7]
	v_mfma_f32_16x16x32_bf16 v[0:3], v[152:155], v[194:197], v[0:3]
	v_mfma_f32_16x16x32_bf16 v[52:55], v[144:147], v[164:167], v[52:55]
	v_mfma_f32_16x16x32_bf16 v[48:51], v[156:159], v[164:167], v[48:51]
	v_mfma_f32_16x16x32_bf16 v[36:39], v[144:147], v[182:185], v[36:39]
	v_mfma_f32_16x16x32_bf16 v[32:35], v[156:159], v[182:185], v[32:35]
	v_mfma_f32_16x16x32_bf16 v[20:23], v[144:147], v[190:193], v[20:23]
	v_mfma_f32_16x16x32_bf16 v[16:19], v[156:159], v[190:193], v[16:19]
	v_mfma_f32_16x16x32_bf16 v[4:7], v[144:147], v[198:201], v[4:7]
	v_mfma_f32_16x16x32_bf16 v[0:3], v[156:159], v[198:201], v[0:3]
	s_setprio 0
	s_barrier
	v_add_u32_e32 v132, 0x18000, v180
	v_add_u32_e32 v156, 0x1c000, v180
	ds_read_b128 v[96:99], v132
	ds_read_b128 v[108:111], v132 offset:1024
	ds_read_b128 v[120:123], v132 offset:2048
	ds_read_b128 v[132:135], v132 offset:3072
	ds_read_b128 v[136:139], v156
	ds_read_b128 v[144:147], v156 offset:1024
	ds_read_b128 v[152:155], v156 offset:2048
	ds_read_b128 v[156:159], v156 offset:3072
	s_add_i32 s66, s66, s33
	s_mov_b32 m0, s45
	ds_read_b128 v[160:163], v181 offset:32768
	ds_read_b128 v[164:167], v181 offset:33792
	ds_read_b128 v[168:171], v181 offset:34816
	ds_read_b128 v[182:185], v181 offset:35840
	ds_read_b128 v[186:189], v181 offset:36864
	ds_read_b128 v[190:193], v181 offset:37888
	ds_read_b128 v[194:197], v181 offset:38912
	ds_read_b128 v[198:201], v181 offset:39936
	buffer_load_dwordx4 v174, s[36:39], s66 offen lds
	s_mov_b32 m0, s46
	s_nop 0
	buffer_load_dwordx4 v176, s[36:39], s66 offen lds
	s_waitcnt vmcnt(8)
	s_waitcnt lgkmcnt(0)
	s_barrier
; #define PG8_STAGE(bufoff, rs_, soff_, voff) do { _Pragma("unroll") for (int _i = 0; _i < 2; ++_i) \
;         __builtin_amdgcn_raw_ptr_buffer_load_lds(rs_, (LAS void*)(lds + (bufoff) + ldsw + _i * 8192), 16, (int)(voff)[_i], (int)(soff_), 0, 0); } while (0)
; #define PG8_LDA(dst, b, h) do { _Pragma("unroll") for (int m = 0; m < 4; ++m) dst[m] = PG8_LD2(lds + PG8_SA(b, h) + aoff + m * 2048); } while (0)
; #define PG8_WAIT_V(n) asm volatile("s_waitcnt vmcnt(" #n ")" ::: "memory")
; #define PG8_WAIT_L(n) asm volatile("s_waitcnt lgkmcnt(" #n ")" ::: "memory")
; #define PG8_BAR __builtin_amdgcn_s_barrier()
; #define PG8_SCHED __builtin_amdgcn_sched_barrier(0)
; template <class Epi, class Sched, bool ALIGN_EPI = false, bool SP2 = false, bool FP8 = false>
; __device__ __forceinline__ void gemm_phase(LAS unsigned char* lds, const Gemm g, const Sched& S, const Epi& E, int wbase) {
;     ...
;             PG8_WAIT_V(8); PG8_WAIT_L(0); PG8_BAR; PG8_MMA(0, 0, At, B0); PG8_MMA(0, 1, At, B1); PG8_BAR; PG8_SCHED;
;             PG8_LDA(At, 1, 1); PG8_STAGE(PG8_SB(1, 0), rB2, b3, voffB); PG8_STAGE(PG8_SB(1, 1), rB2, b3 + hstep, voffB); PG8_STAGE(PG8_SA(1, 0), rA2, a3, voffA);
;             PG8_WAIT_V(8); PG8_WAIT_L(0); PG8_BAR; PG8_MMA(1, 0, At, B0); PG8_MMA(1, 1, At, B1); PG8_BAR; PG8_SCHED;
	s_setprio 1
	v_mfma_f32_16x16x32_bf16 v[148:151], v[96:99], v[160:163], v[148:151]
	v_mfma_f32_16x16x32_bf16 v[140:143], v[120:123], v[160:163], v[140:143]
	v_mfma_f32_16x16x32_bf16 v[116:119], v[96:99], v[168:171], v[116:119]
	v_mfma_f32_16x16x32_bf16 v[112:115], v[120:123], v[168:171], v[112:115]
	v_mfma_f32_16x16x32_bf16 v[92:95], v[96:99], v[186:189], v[92:95]
	v_mfma_f32_16x16x32_bf16 v[88:91], v[120:123], v[186:189], v[88:91]
	v_mfma_f32_16x16x32_bf16 v[76:79], v[96:99], v[194:197], v[76:79]
	v_mfma_f32_16x16x32_bf16 v[72:75], v[120:123], v[194:197], v[72:75]
	v_mfma_f32_16x16x32_bf16 v[148:151], v[108:111], v[164:167], v[148:151]
	v_mfma_f32_16x16x32_bf16 v[140:143], v[132:135], v[164:167], v[140:143]
	v_mfma_f32_16x16x32_bf16 v[116:119], v[108:111], v[182:185], v[116:119]
	v_mfma_f32_16x16x32_bf16 v[112:115], v[132:135], v[182:185], v[112:115]
	v_mfma_f32_16x16x32_bf16 v[92:95], v[108:111], v[190:193], v[92:95]
	v_mfma_f32_16x16x32_bf16 v[88:91], v[132:135], v[190:193], v[88:91]
	v_mfma_f32_16x16x32_bf16 v[76:79], v[108:111], v[198:201], v[76:79]
	v_mfma_f32_16x16x32_bf16 v[72:75], v[132:135], v[198:201], v[72:75]
	v_mfma_f32_16x16x32_bf16 v[128:131], v[136:139], v[160:163], v[128:131]
	v_mfma_f32_16x16x32_bf16 v[124:127], v[152:155], v[160:163], v[124:127]
	v_mfma_f32_16x16x32_bf16 v[104:107], v[136:139], v[168:171], v[104:107]
	v_mfma_f32_16x16x32_bf16 v[100:103], v[152:155], v[168:171], v[100:103]
	v_mfma_f32_16x16x32_bf16 v[84:87], v[136:139], v[186:189], v[84:87]
	v_mfma_f32_16x16x32_bf16 v[80:83], v[152:155], v[186:189], v[80:83]
	v_mfma_f32_16x16x32_bf16 v[68:71], v[136:139], v[194:197], v[68:71]
	v_mfma_f32_16x16x32_bf16 v[64:67], v[152:155], v[194:197], v[64:67]
	v_mfma_f32_16x16x32_bf16 v[128:131], v[144:147], v[164:167], v[128:131]
	v_mfma_f32_16x16x32_bf16 v[124:127], v[156:159], v[164:167], v[124:127]
	v_mfma_f32_16x16x32_bf16 v[104:107], v[144:147], v[182:185], v[104:107]
	v_mfma_f32_16x16x32_bf16 v[100:103], v[156:159], v[182:185], v[100:103]
	v_mfma_f32_16x16x32_bf16 v[84:87], v[144:147], v[190:193], v[84:87]
	v_mfma_f32_16x16x32_bf16 v[80:83], v[156:159], v[190:193], v[80:83]
	v_mfma_f32_16x16x32_bf16 v[68:71], v[144:147], v[198:201], v[68:71]
	v_mfma_f32_16x16x32_bf16 v[64:67], v[156:159], v[198:201], v[64:67]
	s_setprio 0
	s_barrier
	s_mov_b32 m0, s47
	s_bitset1_b32 s55, 7
	buffer_load_dwordx4 v175, s[12:15], s55 offen lds
	s_mov_b32 m0, s48
	ds_read_b128 v[160:163], v181 offset:49152
	buffer_load_dwordx4 v177, s[12:15], s55 offen lds
	s_add_i32 s55, s55, s33
	s_mov_b32 m0, s56
	ds_read_b128 v[164:167], v181 offset:50176
	buffer_load_dwordx4 v175, s[12:15], s55 offen lds
	s_mov_b32 m0, s57
	ds_read_b128 v[168:171], v181 offset:51200
	buffer_load_dwordx4 v177, s[12:15], s55 offen lds
	s_mov_b32 m0, s52
	ds_read_b128 v[182:185], v181 offset:52224
	buffer_load_dwordx4 v174, s[36:39], s54 offen lds
	s_mov_b32 m0, s53
	ds_read_b128 v[186:189], v181 offset:53248
	buffer_load_dwordx4 v176, s[36:39], s54 offen lds
	ds_read_b128 v[190:193], v181 offset:54272
	ds_read_b128 v[194:197], v181 offset:55296
	ds_read_b128 v[198:201], v181 offset:56320
	s_waitcnt vmcnt(8)
	s_waitcnt lgkmcnt(0)
	s_barrier
	s_setprio 1
	v_mfma_f32_16x16x32_bf16 v[60:63], v[96:99], v[160:163], v[60:63]
	v_mfma_f32_16x16x32_bf16 v[56:59], v[120:123], v[160:163], v[56:59]
	v_mfma_f32_16x16x32_bf16 v[44:47], v[96:99], v[168:171], v[44:47]
	v_mfma_f32_16x16x32_bf16 v[40:43], v[120:123], v[168:171], v[40:43]
	v_mfma_f32_16x16x32_bf16 v[28:31], v[96:99], v[186:189], v[28:31]
	v_mfma_f32_16x16x32_bf16 v[24:27], v[120:123], v[186:189], v[24:27]
	v_mfma_f32_16x16x32_bf16 v[12:15], v[96:99], v[194:197], v[12:15]
	v_mfma_f32_16x16x32_bf16 v[8:11], v[120:123], v[194:197], v[8:11]
	v_mfma_f32_16x16x32_bf16 v[60:63], v[108:111], v[164:167], v[60:63]
	v_mfma_f32_16x16x32_bf16 v[56:59], v[132:135], v[164:167], v[56:59]
	v_mfma_f32_16x16x32_bf16 v[44:47], v[108:111], v[182:185], v[44:47]
	v_mfma_f32_16x16x32_bf16 v[40:43], v[132:135], v[182:185], v[40:43]
	v_mfma_f32_16x16x32_bf16 v[28:31], v[108:111], v[190:193], v[28:31]
	v_mfma_f32_16x16x32_bf16 v[24:27], v[132:135], v[190:193], v[24:27]
	v_mfma_f32_16x16x32_bf16 v[12:15], v[108:111], v[198:201], v[12:15]
	v_mfma_f32_16x16x32_bf16 v[8:11], v[132:135], v[198:201], v[8:11]
	v_mfma_f32_16x16x32_bf16 v[52:55], v[136:139], v[160:163], v[52:55]
	v_mfma_f32_16x16x32_bf16 v[48:51], v[152:155], v[160:163], v[48:51]
	v_mfma_f32_16x16x32_bf16 v[36:39], v[136:139], v[168:171], v[36:39]
	v_mfma_f32_16x16x32_bf16 v[32:35], v[152:155], v[168:171], v[32:35]
	v_mfma_f32_16x16x32_bf16 v[20:23], v[136:139], v[186:189], v[20:23]
	v_mfma_f32_16x16x32_bf16 v[16:19], v[152:155], v[186:189], v[16:19]
	v_mfma_f32_16x16x32_bf16 v[4:7], v[136:139], v[194:197], v[4:7]
	v_mfma_f32_16x16x32_bf16 v[0:3], v[152:155], v[194:197], v[0:3]
	v_mfma_f32_16x16x32_bf16 v[52:55], v[144:147], v[164:167], v[52:55]
	v_mfma_f32_16x16x32_bf16 v[48:51], v[156:159], v[164:167], v[48:51]
	v_mfma_f32_16x16x32_bf16 v[36:39], v[144:147], v[182:185], v[36:39]
	v_mfma_f32_16x16x32_bf16 v[32:35], v[156:159], v[182:185], v[32:35]
	v_mfma_f32_16x16x32_bf16 v[20:23], v[144:147], v[190:193], v[20:23]
	v_mfma_f32_16x16x32_bf16 v[16:19], v[156:159], v[190:193], v[16:19]
	v_mfma_f32_16x16x32_bf16 v[4:7], v[144:147], v[198:201], v[4:7]
	v_mfma_f32_16x16x32_bf16 v[0:3], v[156:159], v[198:201], v[0:3]
	s_setprio 0
	s_barrier
	s_add_i32 s11, s11, 2
	s_addk_i32 s4, 0x100
	s_addk_i32 s5, 0x100
	s_cmp_ge_i32 s11, s60
	s_cbranch_scc0 .LBB0_1004

;     __device__ __forceinline__ unsigned a_off(const Unit& u, const Gemm& g) const { return (unsigned)u.pm * (unsigned)(BM * 2) * (unsigned)g.K; }
;     __device__ __forceinline__ unsigned b_off(const Unit& u, const Gemm& g) const { return (unsigned)u.pn * (unsigned)(BM * 2) * (unsigned)g.K; }
;     __device__ __forceinline__ bool next(int i, Unit& u) const { return so.next(i, u); }
;     __device__ __forceinline__ unsigned a_off(const Unit& u, const Gemm& g) const { return (unsigned)u.pm * (unsigned)(BM * 2) * (unsigned)g.K; }
;     __device__ __forceinline__ bool next(int i, Unit& u) const { const bool ok = so.next(i >> 1, u); u.part = i & 1; return ok; }
; template <class Epi, class Sched, bool ALIGN_EPI = false, bool SP2 = false, bool FP8 = false>
; __device__ __forceinline__ void gemm_phase(LAS unsigned char* lds, const Gemm g, const Sched& S, const Epi& E, int wbase) {
;     ...
;         const bool has_next = S.next(ui + 1, nxt);
;         const unsigned nA = has_next ? S.a_off(nxt, g) : cA, nB = has_next ? S.b_off(nxt, g) : cB;
;         const rsrc_t rAn = (Sched::TWO && has_next) ? (nxt.part ? rA1 : rA0) : rAc, rBn = (Sched::TWO && has_next) ? (nxt.part ? rB1 : rB0) : rBc;
;         float pre_[8] = {0.f, 0.f, 0.f, 0.f, 0.f, 0.f, 0.f, 0.f};
;         if constexpr (Epi::HAS_PRE) E.pre_load(pre_, cur, wr);
;         for (int t = 0; t < nt; t += 2) {
;             const bool last = (t == nt - 2);
;             const unsigned a1 = cA + (unsigned)(t + 1) * kstep;
;             const unsigned a2 = last ? nA : cA + (unsigned)(t + 2) * kstep, b2 = last ? nB : cB + (unsigned)(t + 2) * kstep; const rsrc_t rA2 = (Sched::TWO && last) ? rAn : rAc, rB2 = (Sched::TWO && last) ? rBn : rBc;
;             const unsigned a3 = a2 + kstep, b3 = b2 + kstep;
;             if (last && has_next) S.a_ready(nxt);
;             if constexpr (SP2) {
;             PG8_LDB(B0, 0, 0); PG8_LDB(B1, 0, 1); PG8_SCHED; PG8_LDA(At, 0, 0); PG8_STAGE(PG8_SA(1, 1), rAc, a1 + hstep, voffA);
;             PG8_WAIT_V(8); PG8_WAIT_L(0); PG8_BAR; PG8_MMA(0, 0, At, B0); PG8_MMA(0, 1, At, B1); PG8_BAR; PG8_SCHED;
;             PG8_LDA(At, 0, 1); PG8_STAGE(PG8_SB(0, 0), rB2, b2, voffB); PG8_STAGE(PG8_SB(0, 1), rB2, b2 + hstep, voffB); PG8_STAGE(PG8_SA(0, 0), rA2, a2, voffA);
;             PG8_WAIT_V(8); PG8_WAIT_L(0); PG8_BAR; PG8_MMA(1, 0, At, B0); PG8_MMA(1, 1, At, B1); PG8_BAR; PG8_SCHED;
.LBB0_1626:
	s_lshl_b32 s56, s53, 19
	s_andn2_b64 vcc, exec, s[12:13]
	s_lshl_b32 s57, s52, 19
	s_cbranch_vccnz .LBB0_1634
	s_and_b64 s[6:7], s[18:19], exec
	s_waitcnt vmcnt(37)
	s_waitcnt vmcnt(35)
	s_waitcnt vmcnt(31)
	s_waitcnt vmcnt(27)
	s_waitcnt vmcnt(23)
	s_waitcnt vmcnt(22)
	s_cselect_b32 s59, s56, s55
	s_cselect_b32 s60, s57, s54
	s_add_i32 s61, s55, 0x80
	s_add_i32 s62, s54, 0x100
	s_mov_b32 s63, 0
	v_add_u32_e32 v136, 0x10000, v161
	ds_read_b128 v[128:131], v136
	ds_read_b128 v[132:135], v136 offset:1024
	ds_read_b128 v[164:167], v136 offset:2048
	ds_read_b128 v[168:171], v136 offset:3072
	v_add_u32_e32 v136, 0x14000, v161
	ds_read_b128 v[172:175], v136
	ds_read_b128 v[176:179], v136 offset:1024
	ds_read_b128 v[180:183], v136 offset:2048
	ds_read_b128 v[184:187], v136 offset:3072
	s_add_i32 s6, s61, 0x80
	s_cmp_eq_u32 s46, s63
	s_cselect_b32 s65, s59, s6
	s_cselect_b32 s55, s60, s62
	s_or_b32 s54, s65, 0x80
	s_add_i32 s6, s22, s61
	s_mov_b32 m0, s47
	ds_read_b128 v[188:191], v162
	ds_read_b128 v[192:195], v162 offset:1024
	ds_read_b128 v[196:199], v162 offset:2048
	ds_read_b128 v[200:203], v162 offset:3072
	ds_read_b128 v[204:207], v162 offset:4096
	ds_read_b128 v[208:211], v162 offset:5120
	ds_read_b128 v[212:215], v162 offset:6144
	ds_read_b128 v[216:219], v162 offset:7168
	buffer_load_dwordx4 v137, s[36:39], s6 offen lds
	s_mov_b32 m0, s48
	s_nop 0
	buffer_load_dwordx4 v145, s[36:39], s6 offen lds
	s_waitcnt vmcnt(8)
	s_waitcnt lgkmcnt(0)
	s_barrier
	s_setprio 1
	v_mfma_f32_16x16x32_bf16 v[120:123], v[128:131], v[188:191], 0
	v_mfma_f32_16x16x32_bf16 v[124:127], v[164:167], v[188:191], 0
	v_mfma_f32_16x16x32_bf16 v[104:107], v[128:131], v[196:199], 0
	v_mfma_f32_16x16x32_bf16 v[108:111], v[164:167], v[196:199], 0
	v_mfma_f32_16x16x32_bf16 v[88:91], v[128:131], v[204:207], 0
	v_mfma_f32_16x16x32_bf16 v[92:95], v[164:167], v[204:207], 0
	v_mfma_f32_16x16x32_bf16 v[72:75], v[128:131], v[212:215], 0
	v_mfma_f32_16x16x32_bf16 v[76:79], v[164:167], v[212:215], 0
	v_mfma_f32_16x16x32_bf16 v[120:123], v[132:135], v[192:195], v[120:123]
	v_mfma_f32_16x16x32_bf16 v[124:127], v[168:171], v[192:195], v[124:127]
	v_mfma_f32_16x16x32_bf16 v[104:107], v[132:135], v[200:203], v[104:107]
	v_mfma_f32_16x16x32_bf16 v[108:111], v[168:171], v[200:203], v[108:111]
	v_mfma_f32_16x16x32_bf16 v[88:91], v[132:135], v[208:211], v[88:91]
	v_mfma_f32_16x16x32_bf16 v[92:95], v[168:171], v[208:211], v[92:95]
	v_mfma_f32_16x16x32_bf16 v[72:75], v[132:135], v[216:219], v[72:75]
	v_mfma_f32_16x16x32_bf16 v[76:79], v[168:171], v[216:219], v[76:79]
	v_mfma_f32_16x16x32_bf16 v[112:115], v[172:175], v[188:191], 0
	v_mfma_f32_16x16x32_bf16 v[116:119], v[180:183], v[188:191], 0
	v_mfma_f32_16x16x32_bf16 v[96:99], v[172:175], v[196:199], 0
	v_mfma_f32_16x16x32_bf16 v[100:103], v[180:183], v[196:199], 0
	v_mfma_f32_16x16x32_bf16 v[80:83], v[172:175], v[204:207], 0
	v_mfma_f32_16x16x32_bf16 v[84:87], v[180:183], v[204:207], 0
	v_mfma_f32_16x16x32_bf16 v[64:67], v[172:175], v[212:215], 0
	v_mfma_f32_16x16x32_bf16 v[68:71], v[180:183], v[212:215], 0
	v_mfma_f32_16x16x32_bf16 v[112:115], v[176:179], v[192:195], v[112:115]
	v_mfma_f32_16x16x32_bf16 v[116:119], v[184:187], v[192:195], v[116:119]
	v_mfma_f32_16x16x32_bf16 v[96:99], v[176:179], v[200:203], v[96:99]
	v_mfma_f32_16x16x32_bf16 v[100:103], v[184:187], v[200:203], v[100:103]
	v_mfma_f32_16x16x32_bf16 v[80:83], v[176:179], v[208:211], v[80:83]
	v_mfma_f32_16x16x32_bf16 v[84:87], v[184:187], v[208:211], v[84:87]
	v_mfma_f32_16x16x32_bf16 v[64:67], v[176:179], v[216:219], v[64:67]
	v_mfma_f32_16x16x32_bf16 v[68:71], v[184:187], v[216:219], v[68:71]
	s_setprio 0
	s_barrier
	s_mov_b32 m0, s24
	s_mov_b32 s6, s38
	s_mov_b32 s7, s39
	buffer_load_dwordx4 v141, s[4:7], s55 offen lds
	s_mov_b32 m0, s25
	ds_read_b128 v[188:191], v162 offset:16384
	s_add_i32 s66, s55, s22
	buffer_load_dwordx4 v149, s[4:7], s55 offen lds
	s_mov_b32 m0, s26
	ds_read_b128 v[192:195], v162 offset:17408
	buffer_load_dwordx4 v141, s[4:7], s66 offen lds
	s_mov_b32 m0, s27
	ds_read_b128 v[196:199], v162 offset:18432
	buffer_load_dwordx4 v149, s[4:7], s66 offen lds
	s_mov_b32 m0, s23
	ds_read_b128 v[200:203], v162 offset:19456
	buffer_load_dwordx4 v137, s[36:39], s65 offen lds
	s_mov_b32 m0, s28
	ds_read_b128 v[204:207], v162 offset:20480
	buffer_load_dwordx4 v145, s[36:39], s65 offen lds
	ds_read_b128 v[208:211], v162 offset:21504
	ds_read_b128 v[212:215], v162 offset:22528
	ds_read_b128 v[216:219], v162 offset:23552
	s_waitcnt vmcnt(8)
	s_waitcnt lgkmcnt(0)
	s_barrier
	s_setprio 1
	v_mfma_f32_16x16x32_bf16 v[56:59], v[128:131], v[188:191], 0
	v_mfma_f32_16x16x32_bf16 v[60:63], v[164:167], v[188:191], 0
	v_mfma_f32_16x16x32_bf16 v[40:43], v[128:131], v[196:199], 0
	v_mfma_f32_16x16x32_bf16 v[44:47], v[164:167], v[196:199], 0
	v_mfma_f32_16x16x32_bf16 v[24:27], v[128:131], v[204:207], 0
	v_mfma_f32_16x16x32_bf16 v[28:31], v[164:167], v[204:207], 0
	v_mfma_f32_16x16x32_bf16 v[8:11], v[128:131], v[212:215], 0
	v_mfma_f32_16x16x32_bf16 v[12:15], v[164:167], v[212:215], 0
	v_mfma_f32_16x16x32_bf16 v[56:59], v[132:135], v[192:195], v[56:59]
	v_mfma_f32_16x16x32_bf16 v[60:63], v[168:171], v[192:195], v[60:63]
	v_mfma_f32_16x16x32_bf16 v[40:43], v[132:135], v[200:203], v[40:43]
	v_mfma_f32_16x16x32_bf16 v[44:47], v[168:171], v[200:203], v[44:47]
	v_mfma_f32_16x16x32_bf16 v[24:27], v[132:135], v[208:211], v[24:27]
	v_mfma_f32_16x16x32_bf16 v[28:31], v[168:171], v[208:211], v[28:31]
	v_mfma_f32_16x16x32_bf16 v[8:11], v[132:135], v[216:219], v[8:11]
	v_mfma_f32_16x16x32_bf16 v[12:15], v[168:171], v[216:219], v[12:15]
	v_mfma_f32_16x16x32_bf16 v[48:51], v[172:175], v[188:191], 0
	v_mfma_f32_16x16x32_bf16 v[52:55], v[180:183], v[188:191], 0
	v_mfma_f32_16x16x32_bf16 v[32:35], v[172:175], v[196:199], 0
	v_mfma_f32_16x16x32_bf16 v[36:39], v[180:183], v[196:199], 0
	v_mfma_f32_16x16x32_bf16 v[16:19], v[172:175], v[204:207], 0
	v_mfma_f32_16x16x32_bf16 v[20:23], v[180:183], v[204:207], 0
	v_mfma_f32_16x16x32_bf16 v[4:7], v[172:175], v[212:215], 0
	v_mfma_f32_16x16x32_bf16 v[0:3], v[180:183], v[212:215], 0
	v_mfma_f32_16x16x32_bf16 v[48:51], v[176:179], v[192:195], v[48:51]
	v_mfma_f32_16x16x32_bf16 v[52:55], v[184:187], v[192:195], v[52:55]
	v_mfma_f32_16x16x32_bf16 v[32:35], v[176:179], v[200:203], v[32:35]
	v_mfma_f32_16x16x32_bf16 v[36:39], v[184:187], v[200:203], v[36:39]
	v_mfma_f32_16x16x32_bf16 v[16:19], v[176:179], v[208:211], v[16:19]
	v_mfma_f32_16x16x32_bf16 v[20:23], v[184:187], v[208:211], v[20:23]
	v_mfma_f32_16x16x32_bf16 v[4:7], v[176:179], v[216:219], v[4:7]
	v_mfma_f32_16x16x32_bf16 v[0:3], v[184:187], v[216:219], v[0:3]
	s_setprio 0
	s_barrier
; #define PG8_STAGE(bufoff, rs_, soff_, voff) do { _Pragma("unroll") for (int _i = 0; _i < 2; ++_i) \
;         __builtin_amdgcn_raw_ptr_buffer_load_lds(rs_, (LAS void*)(lds + (bufoff) + ldsw + _i * 8192), 16, (int)(voff)[_i], (int)(soff_), 0, 0); } while (0)
; #define PG8_LDA(dst, b, h) do { _Pragma("unroll") for (int m = 0; m < 4; ++m) dst[m] = PG8_LD2(lds + PG8_SA(b, h) + aoff + m * 2048); } while (0)
; #define PG8_LDB(dst, b, h) do { _Pragma("unroll") for (int n = 0; n < 2; ++n) dst[n] = PG8_LD2(lds + PG8_SB(b, h) + boff + n * 2048); } while (0)
; #define PG8_WAIT_V(n) asm volatile("s_waitcnt vmcnt(" #n ")" ::: "memory")
; #define PG8_WAIT_L(n) asm volatile("s_waitcnt lgkmcnt(" #n ")" ::: "memory")
; #define PG8_BAR __builtin_amdgcn_s_barrier()
; #define PG8_SCHED __builtin_amdgcn_sched_barrier(0)
; template <class Epi, class Sched, bool ALIGN_EPI = false, bool SP2 = false, bool FP8 = false>
; __device__ __forceinline__ void gemm_phase(LAS unsigned char* lds, const Gemm g, const Sched& S, const Epi& E, int wbase) {
;     ...
;             PG8_LDB(B0, 1, 0); PG8_LDB(B1, 1, 1); PG8_SCHED; PG8_LDA(At, 1, 0); PG8_STAGE(PG8_SA(0, 1), rA2, a2 + hstep, voffA);
;             PG8_WAIT_V(8); PG8_WAIT_L(0); PG8_BAR; PG8_MMA(0, 0, At, B0); PG8_MMA(0, 1, At, B1); PG8_BAR; PG8_SCHED;
;             PG8_LDA(At, 1, 1); PG8_STAGE(PG8_SB(1, 0), rB2, b3, voffB); PG8_STAGE(PG8_SB(1, 1), rB2, b3 + hstep, voffB); PG8_STAGE(PG8_SA(1, 0), rA2, a3, voffA);
;             PG8_WAIT_V(8); PG8_WAIT_L(0); PG8_BAR; PG8_MMA(1, 0, At, B0); PG8_MMA(1, 1, At, B1); PG8_BAR; PG8_SCHED;
	v_add_u32_e32 v136, 0x18000, v161
	ds_read_b128 v[128:131], v136
	ds_read_b128 v[132:135], v136 offset:1024
	ds_read_b128 v[164:167], v136 offset:2048
	ds_read_b128 v[168:171], v136 offset:3072
	v_add_u32_e32 v136, 0x1c000, v161
	ds_read_b128 v[172:175], v136
	ds_read_b128 v[176:179], v136 offset:1024
	ds_read_b128 v[180:183], v136 offset:2048
	ds_read_b128 v[184:187], v136 offset:3072
	s_add_i32 s65, s65, s22
	s_mov_b32 m0, s29
	ds_read_b128 v[188:191], v162 offset:32768
	ds_read_b128 v[192:195], v162 offset:33792
	ds_read_b128 v[196:199], v162 offset:34816
	ds_read_b128 v[200:203], v162 offset:35840
	ds_read_b128 v[204:207], v162 offset:36864
	ds_read_b128 v[208:211], v162 offset:37888
	ds_read_b128 v[212:215], v162 offset:38912
	ds_read_b128 v[216:219], v162 offset:39936
	buffer_load_dwordx4 v137, s[36:39], s65 offen lds
	s_mov_b32 m0, s30
	s_nop 0
	buffer_load_dwordx4 v145, s[36:39], s65 offen lds
	s_waitcnt vmcnt(8)
	s_waitcnt lgkmcnt(0)
	s_barrier
	s_setprio 1
	v_mfma_f32_16x16x32_bf16 v[120:123], v[128:131], v[188:191], v[120:123]
	v_mfma_f32_16x16x32_bf16 v[124:127], v[164:167], v[188:191], v[124:127]
	v_mfma_f32_16x16x32_bf16 v[104:107], v[128:131], v[196:199], v[104:107]
	v_mfma_f32_16x16x32_bf16 v[108:111], v[164:167], v[196:199], v[108:111]
	v_mfma_f32_16x16x32_bf16 v[88:91], v[128:131], v[204:207], v[88:91]
	v_mfma_f32_16x16x32_bf16 v[92:95], v[164:167], v[204:207], v[92:95]
	v_mfma_f32_16x16x32_bf16 v[72:75], v[128:131], v[212:215], v[72:75]
	v_mfma_f32_16x16x32_bf16 v[76:79], v[164:167], v[212:215], v[76:79]
	v_mfma_f32_16x16x32_bf16 v[120:123], v[132:135], v[192:195], v[120:123]
	v_mfma_f32_16x16x32_bf16 v[124:127], v[168:171], v[192:195], v[124:127]
	v_mfma_f32_16x16x32_bf16 v[104:107], v[132:135], v[200:203], v[104:107]
	v_mfma_f32_16x16x32_bf16 v[108:111], v[168:171], v[200:203], v[108:111]
	v_mfma_f32_16x16x32_bf16 v[88:91], v[132:135], v[208:211], v[88:91]
	v_mfma_f32_16x16x32_bf16 v[92:95], v[168:171], v[208:211], v[92:95]
	v_mfma_f32_16x16x32_bf16 v[72:75], v[132:135], v[216:219], v[72:75]
	v_mfma_f32_16x16x32_bf16 v[76:79], v[168:171], v[216:219], v[76:79]
	v_mfma_f32_16x16x32_bf16 v[112:115], v[172:175], v[188:191], v[112:115]
	v_mfma_f32_16x16x32_bf16 v[116:119], v[180:183], v[188:191], v[116:119]
	v_mfma_f32_16x16x32_bf16 v[96:99], v[172:175], v[196:199], v[96:99]
	v_mfma_f32_16x16x32_bf16 v[100:103], v[180:183], v[196:199], v[100:103]
	v_mfma_f32_16x16x32_bf16 v[80:83], v[172:175], v[204:207], v[80:83]
	v_mfma_f32_16x16x32_bf16 v[84:87], v[180:183], v[204:207], v[84:87]
	v_mfma_f32_16x16x32_bf16 v[64:67], v[172:175], v[212:215], v[64:67]
	v_mfma_f32_16x16x32_bf16 v[68:71], v[180:183], v[212:215], v[68:71]
	v_mfma_f32_16x16x32_bf16 v[112:115], v[176:179], v[192:195], v[112:115]
	v_mfma_f32_16x16x32_bf16 v[116:119], v[184:187], v[192:195], v[116:119]
	v_mfma_f32_16x16x32_bf16 v[96:99], v[176:179], v[200:203], v[96:99]
	v_mfma_f32_16x16x32_bf16 v[100:103], v[184:187], v[200:203], v[100:103]
	v_mfma_f32_16x16x32_bf16 v[80:83], v[176:179], v[208:211], v[80:83]
	v_mfma_f32_16x16x32_bf16 v[84:87], v[184:187], v[208:211], v[84:87]
	v_mfma_f32_16x16x32_bf16 v[64:67], v[176:179], v[216:219], v[64:67]
	v_mfma_f32_16x16x32_bf16 v[68:71], v[184:187], v[216:219], v[68:71]
	s_setprio 0
	s_barrier
	s_mov_b32 m0, s31
	s_bitset1_b32 s55, 7
	buffer_load_dwordx4 v141, s[4:7], s55 offen lds
	s_mov_b32 m0, s33
	ds_read_b128 v[188:191], v162 offset:49152
	buffer_load_dwordx4 v149, s[4:7], s55 offen lds
	s_add_i32 s55, s55, s22
	s_mov_b32 m0, s41
	ds_read_b128 v[192:195], v162 offset:50176
	buffer_load_dwordx4 v141, s[4:7], s55 offen lds
	s_mov_b32 m0, s42
	ds_read_b128 v[196:199], v162 offset:51200
	buffer_load_dwordx4 v149, s[4:7], s55 offen lds
	s_mov_b32 m0, s34
	ds_read_b128 v[200:203], v162 offset:52224
	buffer_load_dwordx4 v137, s[36:39], s54 offen lds
	s_mov_b32 m0, s35
	ds_read_b128 v[204:207], v162 offset:53248
	buffer_load_dwordx4 v145, s[36:39], s54 offen lds
	ds_read_b128 v[208:211], v162 offset:54272
	ds_read_b128 v[212:215], v162 offset:55296
	ds_read_b128 v[216:219], v162 offset:56320
	s_waitcnt vmcnt(8)
	s_waitcnt lgkmcnt(0)
	s_barrier
	s_setprio 1
	v_mfma_f32_16x16x32_bf16 v[56:59], v[128:131], v[188:191], v[56:59]
	v_mfma_f32_16x16x32_bf16 v[60:63], v[164:167], v[188:191], v[60:63]
	v_mfma_f32_16x16x32_bf16 v[40:43], v[128:131], v[196:199], v[40:43]
	v_mfma_f32_16x16x32_bf16 v[44:47], v[164:167], v[196:199], v[44:47]
	v_mfma_f32_16x16x32_bf16 v[24:27], v[128:131], v[204:207], v[24:27]
	v_mfma_f32_16x16x32_bf16 v[28:31], v[164:167], v[204:207], v[28:31]
	v_mfma_f32_16x16x32_bf16 v[8:11], v[128:131], v[212:215], v[8:11]
	v_mfma_f32_16x16x32_bf16 v[12:15], v[164:167], v[212:215], v[12:15]
	v_mfma_f32_16x16x32_bf16 v[56:59], v[132:135], v[192:195], v[56:59]
	v_mfma_f32_16x16x32_bf16 v[60:63], v[168:171], v[192:195], v[60:63]
	v_mfma_f32_16x16x32_bf16 v[40:43], v[132:135], v[200:203], v[40:43]
	v_mfma_f32_16x16x32_bf16 v[44:47], v[168:171], v[200:203], v[44:47]
	v_mfma_f32_16x16x32_bf16 v[24:27], v[132:135], v[208:211], v[24:27]
	v_mfma_f32_16x16x32_bf16 v[28:31], v[168:171], v[208:211], v[28:31]
	v_mfma_f32_16x16x32_bf16 v[8:11], v[132:135], v[216:219], v[8:11]
	v_mfma_f32_16x16x32_bf16 v[12:15], v[168:171], v[216:219], v[12:15]
	v_mfma_f32_16x16x32_bf16 v[48:51], v[172:175], v[188:191], v[48:51]
	v_mfma_f32_16x16x32_bf16 v[52:55], v[180:183], v[188:191], v[52:55]
	v_mfma_f32_16x16x32_bf16 v[32:35], v[172:175], v[196:199], v[32:35]
	v_mfma_f32_16x16x32_bf16 v[36:39], v[180:183], v[196:199], v[36:39]
	v_mfma_f32_16x16x32_bf16 v[16:19], v[172:175], v[204:207], v[16:19]
	v_mfma_f32_16x16x32_bf16 v[20:23], v[180:183], v[204:207], v[20:23]
	v_mfma_f32_16x16x32_bf16 v[4:7], v[172:175], v[212:215], v[4:7]
	v_mfma_f32_16x16x32_bf16 v[0:3], v[180:183], v[212:215], v[0:3]
	v_mfma_f32_16x16x32_bf16 v[48:51], v[176:179], v[192:195], v[48:51]
	v_mfma_f32_16x16x32_bf16 v[52:55], v[184:187], v[192:195], v[52:55]
	v_mfma_f32_16x16x32_bf16 v[32:35], v[176:179], v[200:203], v[32:35]
	v_mfma_f32_16x16x32_bf16 v[36:39], v[184:187], v[200:203], v[36:39]
	v_mfma_f32_16x16x32_bf16 v[16:19], v[176:179], v[208:211], v[16:19]
	v_mfma_f32_16x16x32_bf16 v[20:23], v[184:187], v[208:211], v[20:23]
	v_mfma_f32_16x16x32_bf16 v[4:7], v[176:179], v[216:219], v[4:7]
	v_mfma_f32_16x16x32_bf16 v[0:3], v[184:187], v[216:219], v[0:3]
	s_setprio 0
	s_barrier
	s_add_i32 s63, s63, 2
	s_addk_i32 s61, 0x100
	s_addk_i32 s62, 0x100
	s_cmp_ge_i32 s63, s44
	s_cbranch_scc0 .LBB0_1628
	s_branch .Lzp_after_1628
; #define PG8_STAGE(bufoff, rs_, soff_, voff) do { _Pragma("unroll") for (int _i = 0; _i < 2; ++_i) \
;         __builtin_amdgcn_raw_ptr_buffer_load_lds(rs_, (LAS void*)(lds + (bufoff) + ldsw + _i * 8192), 16, (int)(voff)[_i], (int)(soff_), 0, 0); } while (0)
; #define PG8_LDA(dst, b, h) do { _Pragma("unroll") for (int m = 0; m < 4; ++m) dst[m] = PG8_LD2(lds + PG8_SA(b, h) + aoff + m * 2048); } while (0)
; #define PG8_LDB(dst, b, h) do { _Pragma("unroll") for (int n = 0; n < 2; ++n) dst[n] = PG8_LD2(lds + PG8_SB(b, h) + boff + n * 2048); } while (0)
; #define PG8_WAIT_V(n) asm volatile("s_waitcnt vmcnt(" #n ")" ::: "memory")
; #define PG8_WAIT_L(n) asm volatile("s_waitcnt lgkmcnt(" #n ")" ::: "memory")
; #define PG8_BAR __builtin_amdgcn_s_barrier()
; #define PG8_SCHED __builtin_amdgcn_sched_barrier(0)
; template <class Epi, class Sched, bool ALIGN_EPI = false, bool SP2 = false, bool FP8 = false>
; __device__ __forceinline__ void gemm_phase(LAS unsigned char* lds, const Gemm g, const Sched& S, const Epi& E, int wbase) {
;     ...
;             PG8_LDB(B0, 0, 0); PG8_LDB(B1, 0, 1); PG8_SCHED; PG8_LDA(At, 0, 0); PG8_STAGE(PG8_SA(1, 1), rAc, a1 + hstep, voffA);
;             PG8_WAIT_V(8); PG8_WAIT_L(0); PG8_BAR; PG8_MMA(0, 0, At, B0); PG8_MMA(0, 1, At, B1); PG8_BAR; PG8_SCHED;
;             PG8_LDA(At, 0, 1); PG8_STAGE(PG8_SB(0, 0), rB2, b2, voffB); PG8_STAGE(PG8_SB(0, 1), rB2, b2 + hstep, voffB); PG8_STAGE(PG8_SA(0, 0), rA2, a2, voffA);
;             PG8_WAIT_V(8); PG8_WAIT_L(0); PG8_BAR; PG8_MMA(1, 0, At, B0); PG8_MMA(1, 1, At, B1); PG8_BAR; PG8_SCHED;
.LBB0_1628:
	v_add_u32_e32 v136, 0x10000, v161
	ds_read_b128 v[128:131], v136
	ds_read_b128 v[132:135], v136 offset:1024
	ds_read_b128 v[164:167], v136 offset:2048
	ds_read_b128 v[168:171], v136 offset:3072
	v_add_u32_e32 v136, 0x14000, v161
	ds_read_b128 v[172:175], v136
	ds_read_b128 v[176:179], v136 offset:1024
	ds_read_b128 v[180:183], v136 offset:2048
	ds_read_b128 v[184:187], v136 offset:3072
	s_add_i32 s6, s61, 0x80
	s_cmp_eq_u32 s46, s63
	s_cselect_b32 s65, s59, s6
	s_cselect_b32 s55, s60, s62
	s_or_b32 s54, s65, 0x80
	s_add_i32 s6, s22, s61
	s_mov_b32 m0, s47
	ds_read_b128 v[188:191], v162
	ds_read_b128 v[192:195], v162 offset:1024
	ds_read_b128 v[196:199], v162 offset:2048
	ds_read_b128 v[200:203], v162 offset:3072
	ds_read_b128 v[204:207], v162 offset:4096
	ds_read_b128 v[208:211], v162 offset:5120
	ds_read_b128 v[212:215], v162 offset:6144
	ds_read_b128 v[216:219], v162 offset:7168
	buffer_load_dwordx4 v137, s[36:39], s6 offen lds
	s_mov_b32 m0, s48
	s_nop 0
	buffer_load_dwordx4 v145, s[36:39], s6 offen lds
	s_waitcnt vmcnt(8)
	s_waitcnt lgkmcnt(0)
	s_barrier
	s_setprio 1
	v_mfma_f32_16x16x32_bf16 v[120:123], v[128:131], v[188:191], v[120:123]
	v_mfma_f32_16x16x32_bf16 v[124:127], v[164:167], v[188:191], v[124:127]
	v_mfma_f32_16x16x32_bf16 v[104:107], v[128:131], v[196:199], v[104:107]
	v_mfma_f32_16x16x32_bf16 v[108:111], v[164:167], v[196:199], v[108:111]
	v_mfma_f32_16x16x32_bf16 v[88:91], v[128:131], v[204:207], v[88:91]
	v_mfma_f32_16x16x32_bf16 v[92:95], v[164:167], v[204:207], v[92:95]
	v_mfma_f32_16x16x32_bf16 v[72:75], v[128:131], v[212:215], v[72:75]
	v_mfma_f32_16x16x32_bf16 v[76:79], v[164:167], v[212:215], v[76:79]
	v_mfma_f32_16x16x32_bf16 v[120:123], v[132:135], v[192:195], v[120:123]
	v_mfma_f32_16x16x32_bf16 v[124:127], v[168:171], v[192:195], v[124:127]
	v_mfma_f32_16x16x32_bf16 v[104:107], v[132:135], v[200:203], v[104:107]
	v_mfma_f32_16x16x32_bf16 v[108:111], v[168:171], v[200:203], v[108:111]
	v_mfma_f32_16x16x32_bf16 v[88:91], v[132:135], v[208:211], v[88:91]
	v_mfma_f32_16x16x32_bf16 v[92:95], v[168:171], v[208:211], v[92:95]
	v_mfma_f32_16x16x32_bf16 v[72:75], v[132:135], v[216:219], v[72:75]
	v_mfma_f32_16x16x32_bf16 v[76:79], v[168:171], v[216:219], v[76:79]
	v_mfma_f32_16x16x32_bf16 v[112:115], v[172:175], v[188:191], v[112:115]
	v_mfma_f32_16x16x32_bf16 v[116:119], v[180:183], v[188:191], v[116:119]
	v_mfma_f32_16x16x32_bf16 v[96:99], v[172:175], v[196:199], v[96:99]
	v_mfma_f32_16x16x32_bf16 v[100:103], v[180:183], v[196:199], v[100:103]
	v_mfma_f32_16x16x32_bf16 v[80:83], v[172:175], v[204:207], v[80:83]
	v_mfma_f32_16x16x32_bf16 v[84:87], v[180:183], v[204:207], v[84:87]
	v_mfma_f32_16x16x32_bf16 v[64:67], v[172:175], v[212:215], v[64:67]
	v_mfma_f32_16x16x32_bf16 v[68:71], v[180:183], v[212:215], v[68:71]
	v_mfma_f32_16x16x32_bf16 v[112:115], v[176:179], v[192:195], v[112:115]
	v_mfma_f32_16x16x32_bf16 v[116:119], v[184:187], v[192:195], v[116:119]
	v_mfma_f32_16x16x32_bf16 v[96:99], v[176:179], v[200:203], v[96:99]
	v_mfma_f32_16x16x32_bf16 v[100:103], v[184:187], v[200:203], v[100:103]
	v_mfma_f32_16x16x32_bf16 v[80:83], v[176:179], v[208:211], v[80:83]
	v_mfma_f32_16x16x32_bf16 v[84:87], v[184:187], v[208:211], v[84:87]
	v_mfma_f32_16x16x32_bf16 v[64:67], v[176:179], v[216:219], v[64:67]
	v_mfma_f32_16x16x32_bf16 v[68:71], v[184:187], v[216:219], v[68:71]
	s_setprio 0
	s_barrier
	s_mov_b32 m0, s24
	s_mov_b32 s6, s38
	s_mov_b32 s7, s39
	buffer_load_dwordx4 v141, s[4:7], s55 offen lds
	s_mov_b32 m0, s25
	ds_read_b128 v[188:191], v162 offset:16384
	s_add_i32 s66, s55, s22
	buffer_load_dwordx4 v149, s[4:7], s55 offen lds
	s_mov_b32 m0, s26
	ds_read_b128 v[192:195], v162 offset:17408
	buffer_load_dwordx4 v141, s[4:7], s66 offen lds
	s_mov_b32 m0, s27
	ds_read_b128 v[196:199], v162 offset:18432
	buffer_load_dwordx4 v149, s[4:7], s66 offen lds
	s_mov_b32 m0, s23
	ds_read_b128 v[200:203], v162 offset:19456
	buffer_load_dwordx4 v137, s[36:39], s65 offen lds
	s_mov_b32 m0, s28
	ds_read_b128 v[204:207], v162 offset:20480
	buffer_load_dwordx4 v145, s[36:39], s65 offen lds
	ds_read_b128 v[208:211], v162 offset:21504
	ds_read_b128 v[212:215], v162 offset:22528
	ds_read_b128 v[216:219], v162 offset:23552
	s_waitcnt vmcnt(8)
	s_waitcnt lgkmcnt(0)
	s_barrier
	s_setprio 1
	v_mfma_f32_16x16x32_bf16 v[56:59], v[128:131], v[188:191], v[56:59]
	v_mfma_f32_16x16x32_bf16 v[60:63], v[164:167], v[188:191], v[60:63]
	v_mfma_f32_16x16x32_bf16 v[40:43], v[128:131], v[196:199], v[40:43]
	v_mfma_f32_16x16x32_bf16 v[44:47], v[164:167], v[196:199], v[44:47]
	v_mfma_f32_16x16x32_bf16 v[24:27], v[128:131], v[204:207], v[24:27]
	v_mfma_f32_16x16x32_bf16 v[28:31], v[164:167], v[204:207], v[28:31]
	v_mfma_f32_16x16x32_bf16 v[8:11], v[128:131], v[212:215], v[8:11]
	v_mfma_f32_16x16x32_bf16 v[12:15], v[164:167], v[212:215], v[12:15]
	v_mfma_f32_16x16x32_bf16 v[56:59], v[132:135], v[192:195], v[56:59]
	v_mfma_f32_16x16x32_bf16 v[60:63], v[168:171], v[192:195], v[60:63]
	v_mfma_f32_16x16x32_bf16 v[40:43], v[132:135], v[200:203], v[40:43]
	v_mfma_f32_16x16x32_bf16 v[44:47], v[168:171], v[200:203], v[44:47]
	v_mfma_f32_16x16x32_bf16 v[24:27], v[132:135], v[208:211], v[24:27]
	v_mfma_f32_16x16x32_bf16 v[28:31], v[168:171], v[208:211], v[28:31]
	v_mfma_f32_16x16x32_bf16 v[8:11], v[132:135], v[216:219], v[8:11]
	v_mfma_f32_16x16x32_bf16 v[12:15], v[168:171], v[216:219], v[12:15]
	v_mfma_f32_16x16x32_bf16 v[48:51], v[172:175], v[188:191], v[48:51]
	v_mfma_f32_16x16x32_bf16 v[52:55], v[180:183], v[188:191], v[52:55]
	v_mfma_f32_16x16x32_bf16 v[32:35], v[172:175], v[196:199], v[32:35]
	v_mfma_f32_16x16x32_bf16 v[36:39], v[180:183], v[196:199], v[36:39]
	v_mfma_f32_16x16x32_bf16 v[16:19], v[172:175], v[204:207], v[16:19]
	v_mfma_f32_16x16x32_bf16 v[20:23], v[180:183], v[204:207], v[20:23]
	v_mfma_f32_16x16x32_bf16 v[4:7], v[172:175], v[212:215], v[4:7]
	v_mfma_f32_16x16x32_bf16 v[0:3], v[180:183], v[212:215], v[0:3]
	v_mfma_f32_16x16x32_bf16 v[48:51], v[176:179], v[192:195], v[48:51]
	v_mfma_f32_16x16x32_bf16 v[52:55], v[184:187], v[192:195], v[52:55]
	v_mfma_f32_16x16x32_bf16 v[32:35], v[176:179], v[200:203], v[32:35]
	v_mfma_f32_16x16x32_bf16 v[36:39], v[184:187], v[200:203], v[36:39]
	v_mfma_f32_16x16x32_bf16 v[16:19], v[176:179], v[208:211], v[16:19]
	v_mfma_f32_16x16x32_bf16 v[20:23], v[184:187], v[208:211], v[20:23]
	v_mfma_f32_16x16x32_bf16 v[4:7], v[176:179], v[216:219], v[4:7]
	v_mfma_f32_16x16x32_bf16 v[0:3], v[184:187], v[216:219], v[0:3]
	s_setprio 0
	s_barrier
; #define PG8_STAGE(bufoff, rs_, soff_, voff) do { _Pragma("unroll") for (int _i = 0; _i < 2; ++_i) \
;         __builtin_amdgcn_raw_ptr_buffer_load_lds(rs_, (LAS void*)(lds + (bufoff) + ldsw + _i * 8192), 16, (int)(voff)[_i], (int)(soff_), 0, 0); } while (0)
; #define PG8_LDA(dst, b, h) do { _Pragma("unroll") for (int m = 0; m < 4; ++m) dst[m] = PG8_LD2(lds + PG8_SA(b, h) + aoff + m * 2048); } while (0)
; #define PG8_LDB(dst, b, h) do { _Pragma("unroll") for (int n = 0; n < 2; ++n) dst[n] = PG8_LD2(lds + PG8_SB(b, h) + boff + n * 2048); } while (0)
; #define PG8_WAIT_V(n) asm volatile("s_waitcnt vmcnt(" #n ")" ::: "memory")
; #define PG8_WAIT_L(n) asm volatile("s_waitcnt lgkmcnt(" #n ")" ::: "memory")
; #define PG8_BAR __builtin_amdgcn_s_barrier()
; #define PG8_SCHED __builtin_amdgcn_sched_barrier(0)
; template <class Epi, class Sched, bool ALIGN_EPI = false, bool SP2 = false, bool FP8 = false>
; __device__ __forceinline__ void gemm_phase(LAS unsigned char* lds, const Gemm g, const Sched& S, const Epi& E, int wbase) {
;     ...
;             PG8_LDB(B0, 1, 0); PG8_LDB(B1, 1, 1); PG8_SCHED; PG8_LDA(At, 1, 0); PG8_STAGE(PG8_SA(0, 1), rA2, a2 + hstep, voffA);
;             PG8_WAIT_V(8); PG8_WAIT_L(0); PG8_BAR; PG8_MMA(0, 0, At, B0); PG8_MMA(0, 1, At, B1); PG8_BAR; PG8_SCHED;
;             PG8_LDA(At, 1, 1); PG8_STAGE(PG8_SB(1, 0), rB2, b3, voffB); PG8_STAGE(PG8_SB(1, 1), rB2, b3 + hstep, voffB); PG8_STAGE(PG8_SA(1, 0), rA2, a3, voffA);
;             PG8_WAIT_V(8); PG8_WAIT_L(0); PG8_BAR; PG8_MMA(1, 0, At, B0); PG8_MMA(1, 1, At, B1); PG8_BAR; PG8_SCHED;
	v_add_u32_e32 v136, 0x18000, v161
	ds_read_b128 v[128:131], v136
	ds_read_b128 v[132:135], v136 offset:1024
	ds_read_b128 v[164:167], v136 offset:2048
	ds_read_b128 v[168:171], v136 offset:3072
	v_add_u32_e32 v136, 0x1c000, v161
	ds_read_b128 v[172:175], v136
	ds_read_b128 v[176:179], v136 offset:1024
	ds_read_b128 v[180:183], v136 offset:2048
	ds_read_b128 v[184:187], v136 offset:3072
	s_add_i32 s65, s65, s22
	s_mov_b32 m0, s29
	ds_read_b128 v[188:191], v162 offset:32768
	ds_read_b128 v[192:195], v162 offset:33792
	ds_read_b128 v[196:199], v162 offset:34816
	ds_read_b128 v[200:203], v162 offset:35840
	ds_read_b128 v[204:207], v162 offset:36864
	ds_read_b128 v[208:211], v162 offset:37888
	ds_read_b128 v[212:215], v162 offset:38912
	ds_read_b128 v[216:219], v162 offset:39936
	buffer_load_dwordx4 v137, s[36:39], s65 offen lds
	s_mov_b32 m0, s30
	s_nop 0
	buffer_load_dwordx4 v145, s[36:39], s65 offen lds
	s_waitcnt vmcnt(8)
	s_waitcnt lgkmcnt(0)
	s_barrier
	s_setprio 1
	v_mfma_f32_16x16x32_bf16 v[120:123], v[128:131], v[188:191], v[120:123]
	v_mfma_f32_16x16x32_bf16 v[124:127], v[164:167], v[188:191], v[124:127]
	v_mfma_f32_16x16x32_bf16 v[104:107], v[128:131], v[196:199], v[104:107]
	v_mfma_f32_16x16x32_bf16 v[108:111], v[164:167], v[196:199], v[108:111]
	v_mfma_f32_16x16x32_bf16 v[88:91], v[128:131], v[204:207], v[88:91]
	v_mfma_f32_16x16x32_bf16 v[92:95], v[164:167], v[204:207], v[92:95]
	v_mfma_f32_16x16x32_bf16 v[72:75], v[128:131], v[212:215], v[72:75]
	v_mfma_f32_16x16x32_bf16 v[76:79], v[164:167], v[212:215], v[76:79]
	v_mfma_f32_16x16x32_bf16 v[120:123], v[132:135], v[192:195], v[120:123]
	v_mfma_f32_16x16x32_bf16 v[124:127], v[168:171], v[192:195], v[124:127]
	v_mfma_f32_16x16x32_bf16 v[104:107], v[132:135], v[200:203], v[104:107]
	v_mfma_f32_16x16x32_bf16 v[108:111], v[168:171], v[200:203], v[108:111]
	v_mfma_f32_16x16x32_bf16 v[88:91], v[132:135], v[208:211], v[88:91]
	v_mfma_f32_16x16x32_bf16 v[92:95], v[168:171], v[208:211], v[92:95]
	v_mfma_f32_16x16x32_bf16 v[72:75], v[132:135], v[216:219], v[72:75]
	v_mfma_f32_16x16x32_bf16 v[76:79], v[168:171], v[216:219], v[76:79]
	v_mfma_f32_16x16x32_bf16 v[112:115], v[172:175], v[188:191], v[112:115]
	v_mfma_f32_16x16x32_bf16 v[116:119], v[180:183], v[188:191], v[116:119]
	v_mfma_f32_16x16x32_bf16 v[96:99], v[172:175], v[196:199], v[96:99]
	v_mfma_f32_16x16x32_bf16 v[100:103], v[180:183], v[196:199], v[100:103]
	v_mfma_f32_16x16x32_bf16 v[80:83], v[172:175], v[204:207], v[80:83]
	v_mfma_f32_16x16x32_bf16 v[84:87], v[180:183], v[204:207], v[84:87]
	v_mfma_f32_16x16x32_bf16 v[64:67], v[172:175], v[212:215], v[64:67]
	v_mfma_f32_16x16x32_bf16 v[68:71], v[180:183], v[212:215], v[68:71]
	v_mfma_f32_16x16x32_bf16 v[112:115], v[176:179], v[192:195], v[112:115]
	v_mfma_f32_16x16x32_bf16 v[116:119], v[184:187], v[192:195], v[116:119]
	v_mfma_f32_16x16x32_bf16 v[96:99], v[176:179], v[200:203], v[96:99]
	v_mfma_f32_16x16x32_bf16 v[100:103], v[184:187], v[200:203], v[100:103]
	v_mfma_f32_16x16x32_bf16 v[80:83], v[176:179], v[208:211], v[80:83]
	v_mfma_f32_16x16x32_bf16 v[84:87], v[184:187], v[208:211], v[84:87]
	v_mfma_f32_16x16x32_bf16 v[64:67], v[176:179], v[216:219], v[64:67]
	v_mfma_f32_16x16x32_bf16 v[68:71], v[184:187], v[216:219], v[68:71]
	s_setprio 0
	s_barrier
	s_mov_b32 m0, s31
	s_bitset1_b32 s55, 7
	buffer_load_dwordx4 v141, s[4:7], s55 offen lds
	s_mov_b32 m0, s33
	ds_read_b128 v[188:191], v162 offset:49152
	buffer_load_dwordx4 v149, s[4:7], s55 offen lds
	s_add_i32 s55, s55, s22
	s_mov_b32 m0, s41
	ds_read_b128 v[192:195], v162 offset:50176
	buffer_load_dwordx4 v141, s[4:7], s55 offen lds
	s_mov_b32 m0, s42
	ds_read_b128 v[196:199], v162 offset:51200
	buffer_load_dwordx4 v149, s[4:7], s55 offen lds
	s_mov_b32 m0, s34
	ds_read_b128 v[200:203], v162 offset:52224
	buffer_load_dwordx4 v137, s[36:39], s54 offen lds
	s_mov_b32 m0, s35
	ds_read_b128 v[204:207], v162 offset:53248
	buffer_load_dwordx4 v145, s[36:39], s54 offen lds
	ds_read_b128 v[208:211], v162 offset:54272
	ds_read_b128 v[212:215], v162 offset:55296
	ds_read_b128 v[216:219], v162 offset:56320
	s_waitcnt vmcnt(8)
	s_waitcnt lgkmcnt(0)
	s_barrier
	s_setprio 1
	v_mfma_f32_16x16x32_bf16 v[56:59], v[128:131], v[188:191], v[56:59]
	v_mfma_f32_16x16x32_bf16 v[60:63], v[164:167], v[188:191], v[60:63]
	v_mfma_f32_16x16x32_bf16 v[40:43], v[128:131], v[196:199], v[40:43]
	v_mfma_f32_16x16x32_bf16 v[44:47], v[164:167], v[196:199], v[44:47]
	v_mfma_f32_16x16x32_bf16 v[24:27], v[128:131], v[204:207], v[24:27]
	v_mfma_f32_16x16x32_bf16 v[28:31], v[164:167], v[204:207], v[28:31]
	v_mfma_f32_16x16x32_bf16 v[8:11], v[128:131], v[212:215], v[8:11]
	v_mfma_f32_16x16x32_bf16 v[12:15], v[164:167], v[212:215], v[12:15]
	v_mfma_f32_16x16x32_bf16 v[56:59], v[132:135], v[192:195], v[56:59]
	v_mfma_f32_16x16x32_bf16 v[60:63], v[168:171], v[192:195], v[60:63]
	v_mfma_f32_16x16x32_bf16 v[40:43], v[132:135], v[200:203], v[40:43]
	v_mfma_f32_16x16x32_bf16 v[44:47], v[168:171], v[200:203], v[44:47]
	v_mfma_f32_16x16x32_bf16 v[24:27], v[132:135], v[208:211], v[24:27]
	v_mfma_f32_16x16x32_bf16 v[28:31], v[168:171], v[208:211], v[28:31]
	v_mfma_f32_16x16x32_bf16 v[8:11], v[132:135], v[216:219], v[8:11]
	v_mfma_f32_16x16x32_bf16 v[12:15], v[168:171], v[216:219], v[12:15]
	v_mfma_f32_16x16x32_bf16 v[48:51], v[172:175], v[188:191], v[48:51]
	v_mfma_f32_16x16x32_bf16 v[52:55], v[180:183], v[188:191], v[52:55]
	v_mfma_f32_16x16x32_bf16 v[32:35], v[172:175], v[196:199], v[32:35]
	v_mfma_f32_16x16x32_bf16 v[36:39], v[180:183], v[196:199], v[36:39]
	v_mfma_f32_16x16x32_bf16 v[16:19], v[172:175], v[204:207], v[16:19]
	v_mfma_f32_16x16x32_bf16 v[20:23], v[180:183], v[204:207], v[20:23]
	v_mfma_f32_16x16x32_bf16 v[4:7], v[172:175], v[212:215], v[4:7]
	v_mfma_f32_16x16x32_bf16 v[0:3], v[180:183], v[212:215], v[0:3]
	v_mfma_f32_16x16x32_bf16 v[48:51], v[176:179], v[192:195], v[48:51]
	v_mfma_f32_16x16x32_bf16 v[52:55], v[184:187], v[192:195], v[52:55]
	v_mfma_f32_16x16x32_bf16 v[32:35], v[176:179], v[200:203], v[32:35]
	v_mfma_f32_16x16x32_bf16 v[36:39], v[184:187], v[200:203], v[36:39]
	v_mfma_f32_16x16x32_bf16 v[16:19], v[176:179], v[208:211], v[16:19]
	v_mfma_f32_16x16x32_bf16 v[20:23], v[184:187], v[208:211], v[20:23]
	v_mfma_f32_16x16x32_bf16 v[4:7], v[176:179], v[216:219], v[4:7]
	v_mfma_f32_16x16x32_bf16 v[0:3], v[184:187], v[216:219], v[0:3]
	s_setprio 0
	s_barrier
	s_add_i32 s63, s63, 2
	s_addk_i32 s61, 0x100
	s_addk_i32 s62, 0x100
	s_cmp_ge_i32 s63, s44
	s_cbranch_scc0 .LBB0_1628

;     __device__ __forceinline__ unsigned a_off(const Unit& u, const Gemm& g) const { return (unsigned)u.pm * (unsigned)(BM * 2) * (unsigned)g.K; }
;     __device__ __forceinline__ unsigned b_off(const Unit& u, const Gemm& g) const { return (unsigned)u.pn * (unsigned)(BM * 2) * (unsigned)g.K; }
;     __device__ __forceinline__ bool next(int i, Unit& u) const { return so.next(i, u); }
;     __device__ __forceinline__ unsigned a_off(const Unit& u, const Gemm& g) const { return (unsigned)u.pm * (unsigned)(BM * 2) * (unsigned)g.K; }
;     __device__ __forceinline__ bool next(int i, Unit& u) const { const bool ok = so.next(i >> 1, u); u.part = i & 1; return ok; }
; template <class Epi, class Sched, bool ALIGN_EPI = false, bool SP2 = false, bool FP8 = false>
; __device__ __forceinline__ void gemm_phase(LAS unsigned char* lds, const Gemm g, const Sched& S, const Epi& E, int wbase) {
;     ...
;         const bool has_next = S.next(ui + 1, nxt);
;         const unsigned nA = has_next ? S.a_off(nxt, g) : cA, nB = has_next ? S.b_off(nxt, g) : cB;
;         const rsrc_t rAn = (Sched::TWO && has_next) ? (nxt.part ? rA1 : rA0) : rAc, rBn = (Sched::TWO && has_next) ? (nxt.part ? rB1 : rB0) : rBc;
;         float pre_[8] = {0.f, 0.f, 0.f, 0.f, 0.f, 0.f, 0.f, 0.f};
;         if constexpr (Epi::HAS_PRE) E.pre_load(pre_, cur, wr);
;         for (int t = 0; t < nt; t += 2) {
;             const bool last = (t == nt - 2);
;             const unsigned a1 = cA + (unsigned)(t + 1) * kstep;
;             const unsigned a2 = last ? nA : cA + (unsigned)(t + 2) * kstep, b2 = last ? nB : cB + (unsigned)(t + 2) * kstep; const rsrc_t rA2 = (Sched::TWO && last) ? rAn : rAc, rB2 = (Sched::TWO && last) ? rBn : rBc;
;             const unsigned a3 = a2 + kstep, b3 = b2 + kstep;
;             if (last && has_next) S.a_ready(nxt);
;             if constexpr (SP2) {
;             PG8_LDB(B0, 0, 0); PG8_LDB(B1, 0, 1); PG8_SCHED; PG8_LDA(At, 0, 0); PG8_STAGE(PG8_SA(1, 1), rAc, a1 + hstep, voffA);
;             PG8_WAIT_V(8); PG8_WAIT_L(0); PG8_BAR; PG8_MMA(0, 0, At, B0); PG8_MMA(0, 1, At, B1); PG8_BAR; PG8_SCHED;
;             PG8_LDA(At, 0, 1); PG8_STAGE(PG8_SB(0, 0), rB2, b2, voffB); PG8_STAGE(PG8_SB(0, 1), rB2, b2 + hstep, voffB); PG8_STAGE(PG8_SA(0, 0), rA2, a2, voffA);
;             PG8_WAIT_V(8); PG8_WAIT_L(0); PG8_BAR; PG8_MMA(1, 0, At, B0); PG8_MMA(1, 1, At, B1); PG8_BAR; PG8_SCHED;
.LBB0_1699:
	s_mul_i32 s61, s60, 0x1c0000
	s_andn2_b64 vcc, exec, s[14:15]
	s_mul_i32 s62, s59, 0x1c0000
	s_cbranch_vccnz .LBB0_1703
	s_and_b64 s[6:7], s[18:19], exec
	s_waitcnt vmcnt(37)
	s_waitcnt vmcnt(36)
	s_waitcnt vmcnt(35)
	s_waitcnt vmcnt(32)
	s_waitcnt vmcnt(31)
	s_waitcnt vmcnt(28)
	s_waitcnt vmcnt(27)
	s_waitcnt vmcnt(23)
	s_waitcnt vmcnt(22)
	s_cselect_b32 s21, s61, s55
	s_cselect_b32 s63, s62, s54
	s_add_i32 s65, s55, 0x80
	s_add_i32 s66, s54, 0x100
	s_mov_b32 s67, 0
	v_add_u32_e32 v140, 0x10000, v176
	v_add_u32_e32 v156, 0x14000, v176
	ds_read_b128 v[112:115], v140
	ds_read_b128 v[124:127], v140 offset:1024
	ds_read_b128 v[136:139], v140 offset:2048
	ds_read_b128 v[140:143], v140 offset:3072
	ds_read_b128 v[144:147], v156
	ds_read_b128 v[148:151], v156 offset:1024
	ds_read_b128 v[152:155], v156 offset:2048
	ds_read_b128 v[156:159], v156 offset:3072
	s_add_i32 s6, s65, 0x80
	s_cmp_eq_u32 s52, s67
	s_cselect_b32 s68, s21, s6
	s_cselect_b32 s55, s63, s66
	s_or_b32 s54, s68, 0x80
	s_add_i32 s6, s25, s65
	s_mov_b32 m0, s53
	ds_read_b128 v[160:163], v177
	ds_read_b128 v[164:167], v177 offset:1024
	ds_read_b128 v[178:181], v177 offset:2048
	ds_read_b128 v[182:185], v177 offset:3072
	ds_read_b128 v[186:189], v177 offset:4096
	ds_read_b128 v[190:193], v177 offset:5120
	ds_read_b128 v[194:197], v177 offset:6144
	ds_read_b128 v[198:201], v177 offset:7168
	buffer_load_dwordx4 v170, s[36:39], s6 offen lds
	s_mov_b32 m0, s56
	s_nop 0
	buffer_load_dwordx4 v172, s[36:39], s6 offen lds
	s_waitcnt vmcnt(8)
	s_waitcnt lgkmcnt(0)
	s_barrier
	s_setprio 1
	v_mfma_f32_16x16x32_bf16 v[132:135], v[112:115], v[160:163], 0
	v_mfma_f32_16x16x32_bf16 v[128:131], v[136:139], v[160:163], 0
	v_mfma_f32_16x16x32_bf16 v[108:111], v[112:115], v[178:181], 0
	v_mfma_f32_16x16x32_bf16 v[104:107], v[136:139], v[178:181], 0
	v_mfma_f32_16x16x32_bf16 v[92:95], v[112:115], v[186:189], 0
	v_mfma_f32_16x16x32_bf16 v[88:91], v[136:139], v[186:189], 0
	v_mfma_f32_16x16x32_bf16 v[76:79], v[112:115], v[194:197], 0
	v_mfma_f32_16x16x32_bf16 v[72:75], v[136:139], v[194:197], 0
	v_mfma_f32_16x16x32_bf16 v[132:135], v[124:127], v[164:167], v[132:135]
	v_mfma_f32_16x16x32_bf16 v[128:131], v[140:143], v[164:167], v[128:131]
	v_mfma_f32_16x16x32_bf16 v[108:111], v[124:127], v[182:185], v[108:111]
	v_mfma_f32_16x16x32_bf16 v[104:107], v[140:143], v[182:185], v[104:107]
	v_mfma_f32_16x16x32_bf16 v[92:95], v[124:127], v[190:193], v[92:95]
	v_mfma_f32_16x16x32_bf16 v[88:91], v[140:143], v[190:193], v[88:91]
	v_mfma_f32_16x16x32_bf16 v[76:79], v[124:127], v[198:201], v[76:79]
	v_mfma_f32_16x16x32_bf16 v[72:75], v[140:143], v[198:201], v[72:75]
	v_mfma_f32_16x16x32_bf16 v[120:123], v[144:147], v[160:163], 0
	v_mfma_f32_16x16x32_bf16 v[116:119], v[152:155], v[160:163], 0
	v_mfma_f32_16x16x32_bf16 v[100:103], v[144:147], v[178:181], 0
	v_mfma_f32_16x16x32_bf16 v[96:99], v[152:155], v[178:181], 0
	v_mfma_f32_16x16x32_bf16 v[84:87], v[144:147], v[186:189], 0
	v_mfma_f32_16x16x32_bf16 v[80:83], v[152:155], v[186:189], 0
	v_mfma_f32_16x16x32_bf16 v[68:71], v[144:147], v[194:197], 0
	v_mfma_f32_16x16x32_bf16 v[64:67], v[152:155], v[194:197], 0
	v_mfma_f32_16x16x32_bf16 v[120:123], v[148:151], v[164:167], v[120:123]
	v_mfma_f32_16x16x32_bf16 v[116:119], v[156:159], v[164:167], v[116:119]
	v_mfma_f32_16x16x32_bf16 v[100:103], v[148:151], v[182:185], v[100:103]
	v_mfma_f32_16x16x32_bf16 v[96:99], v[156:159], v[182:185], v[96:99]
	v_mfma_f32_16x16x32_bf16 v[84:87], v[148:151], v[190:193], v[84:87]
	v_mfma_f32_16x16x32_bf16 v[80:83], v[156:159], v[190:193], v[80:83]
	v_mfma_f32_16x16x32_bf16 v[68:71], v[148:151], v[198:201], v[68:71]
	v_mfma_f32_16x16x32_bf16 v[64:67], v[156:159], v[198:201], v[64:67]
	s_setprio 0
	s_barrier
	s_mov_b32 m0, s27
	s_mov_b32 s6, s38
	s_mov_b32 s7, s39
	buffer_load_dwordx4 v171, s[4:7], s55 offen lds
	s_mov_b32 m0, s28
	ds_read_b128 v[160:163], v177 offset:16384
	s_add_i32 s69, s55, s25
	buffer_load_dwordx4 v173, s[4:7], s55 offen lds
	s_mov_b32 m0, s29
	ds_read_b128 v[164:167], v177 offset:17408
	buffer_load_dwordx4 v171, s[4:7], s69 offen lds
	s_mov_b32 m0, s30
	ds_read_b128 v[178:181], v177 offset:18432
	buffer_load_dwordx4 v173, s[4:7], s69 offen lds
	s_mov_b32 m0, s26
	ds_read_b128 v[182:185], v177 offset:19456
	buffer_load_dwordx4 v170, s[36:39], s68 offen lds
	s_mov_b32 m0, s31
	ds_read_b128 v[186:189], v177 offset:20480
	buffer_load_dwordx4 v172, s[36:39], s68 offen lds
	ds_read_b128 v[190:193], v177 offset:21504
	ds_read_b128 v[194:197], v177 offset:22528
	ds_read_b128 v[198:201], v177 offset:23552
	s_waitcnt vmcnt(8)
	s_waitcnt lgkmcnt(0)
	s_barrier
; #define PG8_STAGE(bufoff, rs_, soff_, voff) do { _Pragma("unroll") for (int _i = 0; _i < 2; ++_i) \
;         __builtin_amdgcn_raw_ptr_buffer_load_lds(rs_, (LAS void*)(lds + (bufoff) + ldsw + _i * 8192), 16, (int)(voff)[_i], (int)(soff_), 0, 0); } while (0)
; #define PG8_LDA(dst, b, h) do { _Pragma("unroll") for (int m = 0; m < 4; ++m) dst[m] = PG8_LD2(lds + PG8_SA(b, h) + aoff + m * 2048); } while (0)
; #define PG8_LDB(dst, b, h) do { _Pragma("unroll") for (int n = 0; n < 2; ++n) dst[n] = PG8_LD2(lds + PG8_SB(b, h) + boff + n * 2048); } while (0)
; #define PG8_WAIT_V(n) asm volatile("s_waitcnt vmcnt(" #n ")" ::: "memory")
; #define PG8_WAIT_L(n) asm volatile("s_waitcnt lgkmcnt(" #n ")" ::: "memory")
; #define PG8_BAR __builtin_amdgcn_s_barrier()
; #define PG8_SCHED __builtin_amdgcn_sched_barrier(0)
; template <class Epi, class Sched, bool ALIGN_EPI = false, bool SP2 = false, bool FP8 = false>
; __device__ __forceinline__ void gemm_phase(LAS unsigned char* lds, const Gemm g, const Sched& S, const Epi& E, int wbase) {
;     ...
;             PG8_WAIT_V(8); PG8_WAIT_L(0); PG8_BAR; PG8_MMA(1, 0, At, B0); PG8_MMA(1, 1, At, B1); PG8_BAR; PG8_SCHED;
;             PG8_LDB(B0, 1, 0); PG8_LDB(B1, 1, 1); PG8_SCHED; PG8_LDA(At, 1, 0); PG8_STAGE(PG8_SA(0, 1), rA2, a2 + hstep, voffA);
;             PG8_WAIT_V(8); PG8_WAIT_L(0); PG8_BAR; PG8_MMA(0, 0, At, B0); PG8_MMA(0, 1, At, B1); PG8_BAR; PG8_SCHED;
	s_setprio 1
	v_mfma_f32_16x16x32_bf16 v[60:63], v[112:115], v[160:163], 0
	v_mfma_f32_16x16x32_bf16 v[56:59], v[136:139], v[160:163], 0
	v_mfma_f32_16x16x32_bf16 v[44:47], v[112:115], v[178:181], 0
	v_mfma_f32_16x16x32_bf16 v[40:43], v[136:139], v[178:181], 0
	v_mfma_f32_16x16x32_bf16 v[28:31], v[112:115], v[186:189], 0
	v_mfma_f32_16x16x32_bf16 v[24:27], v[136:139], v[186:189], 0
	v_mfma_f32_16x16x32_bf16 v[12:15], v[112:115], v[194:197], 0
	v_mfma_f32_16x16x32_bf16 v[8:11], v[136:139], v[194:197], 0
	v_mfma_f32_16x16x32_bf16 v[60:63], v[124:127], v[164:167], v[60:63]
	v_mfma_f32_16x16x32_bf16 v[56:59], v[140:143], v[164:167], v[56:59]
	v_mfma_f32_16x16x32_bf16 v[44:47], v[124:127], v[182:185], v[44:47]
	v_mfma_f32_16x16x32_bf16 v[40:43], v[140:143], v[182:185], v[40:43]
	v_mfma_f32_16x16x32_bf16 v[28:31], v[124:127], v[190:193], v[28:31]
	v_mfma_f32_16x16x32_bf16 v[24:27], v[140:143], v[190:193], v[24:27]
	v_mfma_f32_16x16x32_bf16 v[12:15], v[124:127], v[198:201], v[12:15]
	v_mfma_f32_16x16x32_bf16 v[8:11], v[140:143], v[198:201], v[8:11]
	v_mfma_f32_16x16x32_bf16 v[52:55], v[144:147], v[160:163], 0
	v_mfma_f32_16x16x32_bf16 v[48:51], v[152:155], v[160:163], 0
	v_mfma_f32_16x16x32_bf16 v[36:39], v[144:147], v[178:181], 0
	v_mfma_f32_16x16x32_bf16 v[32:35], v[152:155], v[178:181], 0
	v_mfma_f32_16x16x32_bf16 v[20:23], v[144:147], v[186:189], 0
	v_mfma_f32_16x16x32_bf16 v[16:19], v[152:155], v[186:189], 0
	v_mfma_f32_16x16x32_bf16 v[4:7], v[144:147], v[194:197], 0
	v_mfma_f32_16x16x32_bf16 v[0:3], v[152:155], v[194:197], 0
	v_mfma_f32_16x16x32_bf16 v[52:55], v[148:151], v[164:167], v[52:55]
	v_mfma_f32_16x16x32_bf16 v[48:51], v[156:159], v[164:167], v[48:51]
	v_mfma_f32_16x16x32_bf16 v[36:39], v[148:151], v[182:185], v[36:39]
	v_mfma_f32_16x16x32_bf16 v[32:35], v[156:159], v[182:185], v[32:35]
	v_mfma_f32_16x16x32_bf16 v[20:23], v[148:151], v[190:193], v[20:23]
	v_mfma_f32_16x16x32_bf16 v[16:19], v[156:159], v[190:193], v[16:19]
	v_mfma_f32_16x16x32_bf16 v[4:7], v[148:151], v[198:201], v[4:7]
	v_mfma_f32_16x16x32_bf16 v[0:3], v[156:159], v[198:201], v[0:3]
	s_setprio 0
	s_barrier
	v_add_u32_e32 v140, 0x18000, v176
	v_add_u32_e32 v156, 0x1c000, v176
	ds_read_b128 v[112:115], v140
	ds_read_b128 v[124:127], v140 offset:1024
	ds_read_b128 v[136:139], v140 offset:2048
	ds_read_b128 v[140:143], v140 offset:3072
	ds_read_b128 v[144:147], v156
	ds_read_b128 v[148:151], v156 offset:1024
	ds_read_b128 v[152:155], v156 offset:2048
	ds_read_b128 v[156:159], v156 offset:3072
	s_add_i32 s68, s68, s25
	s_mov_b32 m0, s33
	ds_read_b128 v[160:163], v177 offset:32768
	ds_read_b128 v[164:167], v177 offset:33792
	ds_read_b128 v[178:181], v177 offset:34816
	ds_read_b128 v[182:185], v177 offset:35840
	ds_read_b128 v[186:189], v177 offset:36864
	ds_read_b128 v[190:193], v177 offset:37888
	ds_read_b128 v[194:197], v177 offset:38912
	ds_read_b128 v[198:201], v177 offset:39936
	buffer_load_dwordx4 v170, s[36:39], s68 offen lds
	s_mov_b32 m0, s34
	s_nop 0
	buffer_load_dwordx4 v172, s[36:39], s68 offen lds
	s_waitcnt vmcnt(8)
	s_waitcnt lgkmcnt(0)
	s_barrier
	s_setprio 1
	v_mfma_f32_16x16x32_bf16 v[132:135], v[112:115], v[160:163], v[132:135]
	v_mfma_f32_16x16x32_bf16 v[128:131], v[136:139], v[160:163], v[128:131]
	v_mfma_f32_16x16x32_bf16 v[108:111], v[112:115], v[178:181], v[108:111]
	v_mfma_f32_16x16x32_bf16 v[104:107], v[136:139], v[178:181], v[104:107]
	v_mfma_f32_16x16x32_bf16 v[92:95], v[112:115], v[186:189], v[92:95]
	v_mfma_f32_16x16x32_bf16 v[88:91], v[136:139], v[186:189], v[88:91]
	v_mfma_f32_16x16x32_bf16 v[76:79], v[112:115], v[194:197], v[76:79]
	v_mfma_f32_16x16x32_bf16 v[72:75], v[136:139], v[194:197], v[72:75]
	v_mfma_f32_16x16x32_bf16 v[132:135], v[124:127], v[164:167], v[132:135]
	v_mfma_f32_16x16x32_bf16 v[128:131], v[140:143], v[164:167], v[128:131]
	v_mfma_f32_16x16x32_bf16 v[108:111], v[124:127], v[182:185], v[108:111]
	v_mfma_f32_16x16x32_bf16 v[104:107], v[140:143], v[182:185], v[104:107]
	v_mfma_f32_16x16x32_bf16 v[92:95], v[124:127], v[190:193], v[92:95]
	v_mfma_f32_16x16x32_bf16 v[88:91], v[140:143], v[190:193], v[88:91]
	v_mfma_f32_16x16x32_bf16 v[76:79], v[124:127], v[198:201], v[76:79]
	v_mfma_f32_16x16x32_bf16 v[72:75], v[140:143], v[198:201], v[72:75]
	v_mfma_f32_16x16x32_bf16 v[120:123], v[144:147], v[160:163], v[120:123]
	v_mfma_f32_16x16x32_bf16 v[116:119], v[152:155], v[160:163], v[116:119]
	v_mfma_f32_16x16x32_bf16 v[100:103], v[144:147], v[178:181], v[100:103]
	v_mfma_f32_16x16x32_bf16 v[96:99], v[152:155], v[178:181], v[96:99]
	v_mfma_f32_16x16x32_bf16 v[84:87], v[144:147], v[186:189], v[84:87]
	v_mfma_f32_16x16x32_bf16 v[80:83], v[152:155], v[186:189], v[80:83]
	v_mfma_f32_16x16x32_bf16 v[68:71], v[144:147], v[194:197], v[68:71]
	v_mfma_f32_16x16x32_bf16 v[64:67], v[152:155], v[194:197], v[64:67]
	v_mfma_f32_16x16x32_bf16 v[120:123], v[148:151], v[164:167], v[120:123]
	v_mfma_f32_16x16x32_bf16 v[116:119], v[156:159], v[164:167], v[116:119]
	v_mfma_f32_16x16x32_bf16 v[100:103], v[148:151], v[182:185], v[100:103]
	v_mfma_f32_16x16x32_bf16 v[96:99], v[156:159], v[182:185], v[96:99]
	v_mfma_f32_16x16x32_bf16 v[84:87], v[148:151], v[190:193], v[84:87]
	v_mfma_f32_16x16x32_bf16 v[80:83], v[156:159], v[190:193], v[80:83]
	v_mfma_f32_16x16x32_bf16 v[68:71], v[148:151], v[198:201], v[68:71]
	v_mfma_f32_16x16x32_bf16 v[64:67], v[156:159], v[198:201], v[64:67]
	s_setprio 0
	s_barrier
; #define PG8_STAGE(bufoff, rs_, soff_, voff) do { _Pragma("unroll") for (int _i = 0; _i < 2; ++_i) \
;         __builtin_amdgcn_raw_ptr_buffer_load_lds(rs_, (LAS void*)(lds + (bufoff) + ldsw + _i * 8192), 16, (int)(voff)[_i], (int)(soff_), 0, 0); } while (0)
; #define PG8_LDA(dst, b, h) do { _Pragma("unroll") for (int m = 0; m < 4; ++m) dst[m] = PG8_LD2(lds + PG8_SA(b, h) + aoff + m * 2048); } while (0)
; #define PG8_LDB(dst, b, h) do { _Pragma("unroll") for (int n = 0; n < 2; ++n) dst[n] = PG8_LD2(lds + PG8_SB(b, h) + boff + n * 2048); } while (0)
; #define PG8_WAIT_V(n) asm volatile("s_waitcnt vmcnt(" #n ")" ::: "memory")
; #define PG8_WAIT_L(n) asm volatile("s_waitcnt lgkmcnt(" #n ")" ::: "memory")
; #define PG8_BAR __builtin_amdgcn_s_barrier()
; #define PG8_SCHED __builtin_amdgcn_sched_barrier(0)
; template <class Epi, class Sched, bool ALIGN_EPI = false, bool SP2 = false, bool FP8 = false>
; __device__ __forceinline__ void gemm_phase(LAS unsigned char* lds, const Gemm g, const Sched& S, const Epi& E, int wbase) {
;     ...
;             PG8_LDB(B0, 0, 0); PG8_LDB(B1, 0, 1); PG8_SCHED; PG8_LDA(At, 0, 0); PG8_STAGE(PG8_SA(1, 1), rAc, a1 + hstep, voffA);
;             PG8_WAIT_V(8); PG8_WAIT_L(0); PG8_BAR; PG8_MMA(0, 0, At, B0); PG8_MMA(0, 1, At, B1); PG8_BAR; PG8_SCHED;
;             PG8_LDA(At, 0, 1); PG8_STAGE(PG8_SB(0, 0), rB2, b2, voffB); PG8_STAGE(PG8_SB(0, 1), rB2, b2 + hstep, voffB); PG8_STAGE(PG8_SA(0, 0), rA2, a2, voffA);
;             PG8_WAIT_V(8); PG8_WAIT_L(0); PG8_BAR; PG8_MMA(1, 0, At, B0); PG8_MMA(1, 1, At, B1); PG8_BAR; PG8_SCHED;
;             PG8_LDB(B0, 1, 0); PG8_LDB(B1, 1, 1); PG8_SCHED; PG8_LDA(At, 1, 0); PG8_STAGE(PG8_SA(0, 1), rA2, a2 + hstep, voffA);
;             PG8_WAIT_V(8); PG8_WAIT_L(0); PG8_BAR; PG8_MMA(0, 0, At, B0); PG8_MMA(0, 1, At, B1); PG8_BAR; PG8_SCHED;
;             PG8_LDA(At, 1, 1); PG8_STAGE(PG8_SB(1, 0), rB2, b3, voffB); PG8_STAGE(PG8_SB(1, 1), rB2, b3 + hstep, voffB); PG8_STAGE(PG8_SA(1, 0), rA2, a3, voffA);
;             PG8_WAIT_V(8); PG8_WAIT_L(0); PG8_BAR; PG8_MMA(1, 0, At, B0); PG8_MMA(1, 1, At, B1); PG8_BAR; PG8_SCHED;
	s_mov_b32 m0, s1
	s_bitset1_b32 s55, 7
	buffer_load_dwordx4 v171, s[4:7], s55 offen lds
	s_mov_b32 m0, s35
	ds_read_b128 v[160:163], v177 offset:49152
	buffer_load_dwordx4 v173, s[4:7], s55 offen lds
	s_add_i32 s55, s55, s25
	s_mov_b32 m0, s43
	ds_read_b128 v[164:167], v177 offset:50176
	buffer_load_dwordx4 v171, s[4:7], s55 offen lds
	s_mov_b32 m0, s44
	ds_read_b128 v[178:181], v177 offset:51200
	buffer_load_dwordx4 v173, s[4:7], s55 offen lds
	s_mov_b32 m0, s41
	ds_read_b128 v[182:185], v177 offset:52224
	buffer_load_dwordx4 v170, s[36:39], s54 offen lds
	s_mov_b32 m0, s42
	ds_read_b128 v[186:189], v177 offset:53248
	buffer_load_dwordx4 v172, s[36:39], s54 offen lds
	ds_read_b128 v[190:193], v177 offset:54272
	ds_read_b128 v[194:197], v177 offset:55296
	ds_read_b128 v[198:201], v177 offset:56320
	s_waitcnt vmcnt(8)
	s_waitcnt lgkmcnt(0)
	s_barrier
	s_setprio 1
	v_mfma_f32_16x16x32_bf16 v[60:63], v[112:115], v[160:163], v[60:63]
	v_mfma_f32_16x16x32_bf16 v[56:59], v[136:139], v[160:163], v[56:59]
	v_mfma_f32_16x16x32_bf16 v[44:47], v[112:115], v[178:181], v[44:47]
	v_mfma_f32_16x16x32_bf16 v[40:43], v[136:139], v[178:181], v[40:43]
	v_mfma_f32_16x16x32_bf16 v[28:31], v[112:115], v[186:189], v[28:31]
	v_mfma_f32_16x16x32_bf16 v[24:27], v[136:139], v[186:189], v[24:27]
	v_mfma_f32_16x16x32_bf16 v[12:15], v[112:115], v[194:197], v[12:15]
	v_mfma_f32_16x16x32_bf16 v[8:11], v[136:139], v[194:197], v[8:11]
	v_mfma_f32_16x16x32_bf16 v[60:63], v[124:127], v[164:167], v[60:63]
	v_mfma_f32_16x16x32_bf16 v[56:59], v[140:143], v[164:167], v[56:59]
	v_mfma_f32_16x16x32_bf16 v[44:47], v[124:127], v[182:185], v[44:47]
	v_mfma_f32_16x16x32_bf16 v[40:43], v[140:143], v[182:185], v[40:43]
	v_mfma_f32_16x16x32_bf16 v[28:31], v[124:127], v[190:193], v[28:31]
	v_mfma_f32_16x16x32_bf16 v[24:27], v[140:143], v[190:193], v[24:27]
	v_mfma_f32_16x16x32_bf16 v[12:15], v[124:127], v[198:201], v[12:15]
	v_mfma_f32_16x16x32_bf16 v[8:11], v[140:143], v[198:201], v[8:11]
	v_mfma_f32_16x16x32_bf16 v[52:55], v[144:147], v[160:163], v[52:55]
	v_mfma_f32_16x16x32_bf16 v[48:51], v[152:155], v[160:163], v[48:51]
	v_mfma_f32_16x16x32_bf16 v[36:39], v[144:147], v[178:181], v[36:39]
	v_mfma_f32_16x16x32_bf16 v[32:35], v[152:155], v[178:181], v[32:35]
	v_mfma_f32_16x16x32_bf16 v[20:23], v[144:147], v[186:189], v[20:23]
	v_mfma_f32_16x16x32_bf16 v[16:19], v[152:155], v[186:189], v[16:19]
	v_mfma_f32_16x16x32_bf16 v[4:7], v[144:147], v[194:197], v[4:7]
	v_mfma_f32_16x16x32_bf16 v[0:3], v[152:155], v[194:197], v[0:3]
	v_mfma_f32_16x16x32_bf16 v[52:55], v[148:151], v[164:167], v[52:55]
	v_mfma_f32_16x16x32_bf16 v[48:51], v[156:159], v[164:167], v[48:51]
	v_mfma_f32_16x16x32_bf16 v[36:39], v[148:151], v[182:185], v[36:39]
	v_mfma_f32_16x16x32_bf16 v[32:35], v[156:159], v[182:185], v[32:35]
	v_mfma_f32_16x16x32_bf16 v[20:23], v[148:151], v[190:193], v[20:23]
	v_mfma_f32_16x16x32_bf16 v[16:19], v[156:159], v[190:193], v[16:19]
	v_mfma_f32_16x16x32_bf16 v[4:7], v[148:151], v[198:201], v[4:7]
	v_mfma_f32_16x16x32_bf16 v[0:3], v[156:159], v[198:201], v[0:3]
	s_setprio 0
	s_barrier
	s_add_i32 s67, s67, 2
	s_addk_i32 s65, 0x100
	s_addk_i32 s66, 0x100
	s_cmp_ge_i32 s67, s47
	s_cbranch_scc0 .LBB0_1701
	s_branch .Lzp_after_1701
.LBB0_1701:
	v_add_u32_e32 v140, 0x10000, v176
	v_add_u32_e32 v156, 0x14000, v176
	ds_read_b128 v[112:115], v140
	ds_read_b128 v[124:127], v140 offset:1024
	ds_read_b128 v[136:139], v140 offset:2048
	ds_read_b128 v[140:143], v140 offset:3072
	ds_read_b128 v[144:147], v156
	ds_read_b128 v[148:151], v156 offset:1024
	ds_read_b128 v[152:155], v156 offset:2048
	ds_read_b128 v[156:159], v156 offset:3072
	s_add_i32 s6, s65, 0x80
	s_cmp_eq_u32 s52, s67
	s_cselect_b32 s68, s21, s6
	s_cselect_b32 s55, s63, s66
	s_or_b32 s54, s68, 0x80
	s_add_i32 s6, s25, s65
	s_mov_b32 m0, s53
	ds_read_b128 v[160:163], v177
	ds_read_b128 v[164:167], v177 offset:1024
	ds_read_b128 v[178:181], v177 offset:2048
	ds_read_b128 v[182:185], v177 offset:3072
	ds_read_b128 v[186:189], v177 offset:4096
	ds_read_b128 v[190:193], v177 offset:5120
	ds_read_b128 v[194:197], v177 offset:6144
	ds_read_b128 v[198:201], v177 offset:7168
	buffer_load_dwordx4 v170, s[36:39], s6 offen lds
	s_mov_b32 m0, s56
	s_nop 0
	buffer_load_dwordx4 v172, s[36:39], s6 offen lds
	s_waitcnt vmcnt(8)
	s_waitcnt lgkmcnt(0)
	s_barrier
	s_setprio 1
	v_mfma_f32_16x16x32_bf16 v[132:135], v[112:115], v[160:163], v[132:135]
	v_mfma_f32_16x16x32_bf16 v[128:131], v[136:139], v[160:163], v[128:131]
	v_mfma_f32_16x16x32_bf16 v[108:111], v[112:115], v[178:181], v[108:111]
	v_mfma_f32_16x16x32_bf16 v[104:107], v[136:139], v[178:181], v[104:107]
	v_mfma_f32_16x16x32_bf16 v[92:95], v[112:115], v[186:189], v[92:95]
	v_mfma_f32_16x16x32_bf16 v[88:91], v[136:139], v[186:189], v[88:91]
	v_mfma_f32_16x16x32_bf16 v[76:79], v[112:115], v[194:197], v[76:79]
	v_mfma_f32_16x16x32_bf16 v[72:75], v[136:139], v[194:197], v[72:75]
	v_mfma_f32_16x16x32_bf16 v[132:135], v[124:127], v[164:167], v[132:135]
	v_mfma_f32_16x16x32_bf16 v[128:131], v[140:143], v[164:167], v[128:131]
	v_mfma_f32_16x16x32_bf16 v[108:111], v[124:127], v[182:185], v[108:111]
	v_mfma_f32_16x16x32_bf16 v[104:107], v[140:143], v[182:185], v[104:107]
	v_mfma_f32_16x16x32_bf16 v[92:95], v[124:127], v[190:193], v[92:95]
	v_mfma_f32_16x16x32_bf16 v[88:91], v[140:143], v[190:193], v[88:91]
	v_mfma_f32_16x16x32_bf16 v[76:79], v[124:127], v[198:201], v[76:79]
	v_mfma_f32_16x16x32_bf16 v[72:75], v[140:143], v[198:201], v[72:75]
	v_mfma_f32_16x16x32_bf16 v[120:123], v[144:147], v[160:163], v[120:123]
	v_mfma_f32_16x16x32_bf16 v[116:119], v[152:155], v[160:163], v[116:119]
	v_mfma_f32_16x16x32_bf16 v[100:103], v[144:147], v[178:181], v[100:103]
	v_mfma_f32_16x16x32_bf16 v[96:99], v[152:155], v[178:181], v[96:99]
	v_mfma_f32_16x16x32_bf16 v[84:87], v[144:147], v[186:189], v[84:87]
	v_mfma_f32_16x16x32_bf16 v[80:83], v[152:155], v[186:189], v[80:83]
	v_mfma_f32_16x16x32_bf16 v[68:71], v[144:147], v[194:197], v[68:71]
	v_mfma_f32_16x16x32_bf16 v[64:67], v[152:155], v[194:197], v[64:67]
	v_mfma_f32_16x16x32_bf16 v[120:123], v[148:151], v[164:167], v[120:123]
	v_mfma_f32_16x16x32_bf16 v[116:119], v[156:159], v[164:167], v[116:119]
	v_mfma_f32_16x16x32_bf16 v[100:103], v[148:151], v[182:185], v[100:103]
	v_mfma_f32_16x16x32_bf16 v[96:99], v[156:159], v[182:185], v[96:99]
	v_mfma_f32_16x16x32_bf16 v[84:87], v[148:151], v[190:193], v[84:87]
	v_mfma_f32_16x16x32_bf16 v[80:83], v[156:159], v[190:193], v[80:83]
	v_mfma_f32_16x16x32_bf16 v[68:71], v[148:151], v[198:201], v[68:71]
	v_mfma_f32_16x16x32_bf16 v[64:67], v[156:159], v[198:201], v[64:67]
	s_setprio 0
	s_barrier
; #define PG8_STAGE(bufoff, rs_, soff_, voff) do { _Pragma("unroll") for (int _i = 0; _i < 2; ++_i) \
;         __builtin_amdgcn_raw_ptr_buffer_load_lds(rs_, (LAS void*)(lds + (bufoff) + ldsw + _i * 8192), 16, (int)(voff)[_i], (int)(soff_), 0, 0); } while (0)
; #define PG8_LDA(dst, b, h) do { _Pragma("unroll") for (int m = 0; m < 4; ++m) dst[m] = PG8_LD2(lds + PG8_SA(b, h) + aoff + m * 2048); } while (0)
; #define PG8_LDB(dst, b, h) do { _Pragma("unroll") for (int n = 0; n < 2; ++n) dst[n] = PG8_LD2(lds + PG8_SB(b, h) + boff + n * 2048); } while (0)
; #define PG8_WAIT_V(n) asm volatile("s_waitcnt vmcnt(" #n ")" ::: "memory")
; #define PG8_WAIT_L(n) asm volatile("s_waitcnt lgkmcnt(" #n ")" ::: "memory")
; #define PG8_BAR __builtin_amdgcn_s_barrier()
; #define PG8_SCHED __builtin_amdgcn_sched_barrier(0)
; template <class Epi, class Sched, bool ALIGN_EPI = false, bool SP2 = false, bool FP8 = false>
; __device__ __forceinline__ void gemm_phase(LAS unsigned char* lds, const Gemm g, const Sched& S, const Epi& E, int wbase) {
;     ...
;             PG8_LDA(At, 0, 1); PG8_STAGE(PG8_SB(0, 0), rB2, b2, voffB); PG8_STAGE(PG8_SB(0, 1), rB2, b2 + hstep, voffB); PG8_STAGE(PG8_SA(0, 0), rA2, a2, voffA);
;             PG8_WAIT_V(8); PG8_WAIT_L(0); PG8_BAR; PG8_MMA(1, 0, At, B0); PG8_MMA(1, 1, At, B1); PG8_BAR; PG8_SCHED;
;             PG8_LDB(B0, 1, 0); PG8_LDB(B1, 1, 1); PG8_SCHED; PG8_LDA(At, 1, 0); PG8_STAGE(PG8_SA(0, 1), rA2, a2 + hstep, voffA);
;             PG8_WAIT_V(8); PG8_WAIT_L(0); PG8_BAR; PG8_MMA(0, 0, At, B0); PG8_MMA(0, 1, At, B1); PG8_BAR; PG8_SCHED;
	s_mov_b32 m0, s27
	s_mov_b32 s6, s38
	s_mov_b32 s7, s39
	buffer_load_dwordx4 v171, s[4:7], s55 offen lds
	s_mov_b32 m0, s28
	ds_read_b128 v[160:163], v177 offset:16384
	s_add_i32 s69, s55, s25
	buffer_load_dwordx4 v173, s[4:7], s55 offen lds
	s_mov_b32 m0, s29
	ds_read_b128 v[164:167], v177 offset:17408
	buffer_load_dwordx4 v171, s[4:7], s69 offen lds
	s_mov_b32 m0, s30
	ds_read_b128 v[178:181], v177 offset:18432
	buffer_load_dwordx4 v173, s[4:7], s69 offen lds
	s_mov_b32 m0, s26
	ds_read_b128 v[182:185], v177 offset:19456
	buffer_load_dwordx4 v170, s[36:39], s68 offen lds
	s_mov_b32 m0, s31
	ds_read_b128 v[186:189], v177 offset:20480
	buffer_load_dwordx4 v172, s[36:39], s68 offen lds
	ds_read_b128 v[190:193], v177 offset:21504
	ds_read_b128 v[194:197], v177 offset:22528
	ds_read_b128 v[198:201], v177 offset:23552
	s_waitcnt vmcnt(8)
	s_waitcnt lgkmcnt(0)
	s_barrier
	s_setprio 1
	v_mfma_f32_16x16x32_bf16 v[60:63], v[112:115], v[160:163], v[60:63]
	v_mfma_f32_16x16x32_bf16 v[56:59], v[136:139], v[160:163], v[56:59]
	v_mfma_f32_16x16x32_bf16 v[44:47], v[112:115], v[178:181], v[44:47]
	v_mfma_f32_16x16x32_bf16 v[40:43], v[136:139], v[178:181], v[40:43]
	v_mfma_f32_16x16x32_bf16 v[28:31], v[112:115], v[186:189], v[28:31]
	v_mfma_f32_16x16x32_bf16 v[24:27], v[136:139], v[186:189], v[24:27]
	v_mfma_f32_16x16x32_bf16 v[12:15], v[112:115], v[194:197], v[12:15]
	v_mfma_f32_16x16x32_bf16 v[8:11], v[136:139], v[194:197], v[8:11]
	v_mfma_f32_16x16x32_bf16 v[60:63], v[124:127], v[164:167], v[60:63]
	v_mfma_f32_16x16x32_bf16 v[56:59], v[140:143], v[164:167], v[56:59]
	v_mfma_f32_16x16x32_bf16 v[44:47], v[124:127], v[182:185], v[44:47]
	v_mfma_f32_16x16x32_bf16 v[40:43], v[140:143], v[182:185], v[40:43]
	v_mfma_f32_16x16x32_bf16 v[28:31], v[124:127], v[190:193], v[28:31]
	v_mfma_f32_16x16x32_bf16 v[24:27], v[140:143], v[190:193], v[24:27]
	v_mfma_f32_16x16x32_bf16 v[12:15], v[124:127], v[198:201], v[12:15]
	v_mfma_f32_16x16x32_bf16 v[8:11], v[140:143], v[198:201], v[8:11]
	v_mfma_f32_16x16x32_bf16 v[52:55], v[144:147], v[160:163], v[52:55]
	v_mfma_f32_16x16x32_bf16 v[48:51], v[152:155], v[160:163], v[48:51]
	v_mfma_f32_16x16x32_bf16 v[36:39], v[144:147], v[178:181], v[36:39]
	v_mfma_f32_16x16x32_bf16 v[32:35], v[152:155], v[178:181], v[32:35]
	v_mfma_f32_16x16x32_bf16 v[20:23], v[144:147], v[186:189], v[20:23]
	v_mfma_f32_16x16x32_bf16 v[16:19], v[152:155], v[186:189], v[16:19]
	v_mfma_f32_16x16x32_bf16 v[4:7], v[144:147], v[194:197], v[4:7]
	v_mfma_f32_16x16x32_bf16 v[0:3], v[152:155], v[194:197], v[0:3]
	v_mfma_f32_16x16x32_bf16 v[52:55], v[148:151], v[164:167], v[52:55]
	v_mfma_f32_16x16x32_bf16 v[48:51], v[156:159], v[164:167], v[48:51]
	v_mfma_f32_16x16x32_bf16 v[36:39], v[148:151], v[182:185], v[36:39]
	v_mfma_f32_16x16x32_bf16 v[32:35], v[156:159], v[182:185], v[32:35]
	v_mfma_f32_16x16x32_bf16 v[20:23], v[148:151], v[190:193], v[20:23]
	v_mfma_f32_16x16x32_bf16 v[16:19], v[156:159], v[190:193], v[16:19]
	v_mfma_f32_16x16x32_bf16 v[4:7], v[148:151], v[198:201], v[4:7]
	v_mfma_f32_16x16x32_bf16 v[0:3], v[156:159], v[198:201], v[0:3]
	s_setprio 0
	s_barrier
	v_add_u32_e32 v140, 0x18000, v176
	v_add_u32_e32 v156, 0x1c000, v176
	ds_read_b128 v[112:115], v140
	ds_read_b128 v[124:127], v140 offset:1024
	ds_read_b128 v[136:139], v140 offset:2048
	ds_read_b128 v[140:143], v140 offset:3072
	ds_read_b128 v[144:147], v156
	ds_read_b128 v[148:151], v156 offset:1024
	ds_read_b128 v[152:155], v156 offset:2048
	ds_read_b128 v[156:159], v156 offset:3072
	s_add_i32 s68, s68, s25
	s_mov_b32 m0, s33
	ds_read_b128 v[160:163], v177 offset:32768
	ds_read_b128 v[164:167], v177 offset:33792
	ds_read_b128 v[178:181], v177 offset:34816
	ds_read_b128 v[182:185], v177 offset:35840
	ds_read_b128 v[186:189], v177 offset:36864
	ds_read_b128 v[190:193], v177 offset:37888
	ds_read_b128 v[194:197], v177 offset:38912
	ds_read_b128 v[198:201], v177 offset:39936
	buffer_load_dwordx4 v170, s[36:39], s68 offen lds
	s_mov_b32 m0, s34
	s_nop 0
	buffer_load_dwordx4 v172, s[36:39], s68 offen lds
	s_waitcnt vmcnt(8)
	s_waitcnt lgkmcnt(0)
	s_barrier
; #define PG8_STAGE(bufoff, rs_, soff_, voff) do { _Pragma("unroll") for (int _i = 0; _i < 2; ++_i) \
;         __builtin_amdgcn_raw_ptr_buffer_load_lds(rs_, (LAS void*)(lds + (bufoff) + ldsw + _i * 8192), 16, (int)(voff)[_i], (int)(soff_), 0, 0); } while (0)
; #define PG8_LDA(dst, b, h) do { _Pragma("unroll") for (int m = 0; m < 4; ++m) dst[m] = PG8_LD2(lds + PG8_SA(b, h) + aoff + m * 2048); } while (0)
; #define PG8_WAIT_V(n) asm volatile("s_waitcnt vmcnt(" #n ")" ::: "memory")
; #define PG8_WAIT_L(n) asm volatile("s_waitcnt lgkmcnt(" #n ")" ::: "memory")
; #define PG8_BAR __builtin_amdgcn_s_barrier()
; #define PG8_SCHED __builtin_amdgcn_sched_barrier(0)
; template <class Epi, class Sched, bool ALIGN_EPI = false, bool SP2 = false, bool FP8 = false>
; __device__ __forceinline__ void gemm_phase(LAS unsigned char* lds, const Gemm g, const Sched& S, const Epi& E, int wbase) {
;     ...
;             PG8_WAIT_V(8); PG8_WAIT_L(0); PG8_BAR; PG8_MMA(0, 0, At, B0); PG8_MMA(0, 1, At, B1); PG8_BAR; PG8_SCHED;
;             PG8_LDA(At, 1, 1); PG8_STAGE(PG8_SB(1, 0), rB2, b3, voffB); PG8_STAGE(PG8_SB(1, 1), rB2, b3 + hstep, voffB); PG8_STAGE(PG8_SA(1, 0), rA2, a3, voffA);
;             PG8_WAIT_V(8); PG8_WAIT_L(0); PG8_BAR; PG8_MMA(1, 0, At, B0); PG8_MMA(1, 1, At, B1); PG8_BAR; PG8_SCHED;
	s_setprio 1
	v_mfma_f32_16x16x32_bf16 v[132:135], v[112:115], v[160:163], v[132:135]
	v_mfma_f32_16x16x32_bf16 v[128:131], v[136:139], v[160:163], v[128:131]
	v_mfma_f32_16x16x32_bf16 v[108:111], v[112:115], v[178:181], v[108:111]
	v_mfma_f32_16x16x32_bf16 v[104:107], v[136:139], v[178:181], v[104:107]
	v_mfma_f32_16x16x32_bf16 v[92:95], v[112:115], v[186:189], v[92:95]
	v_mfma_f32_16x16x32_bf16 v[88:91], v[136:139], v[186:189], v[88:91]
	v_mfma_f32_16x16x32_bf16 v[76:79], v[112:115], v[194:197], v[76:79]
	v_mfma_f32_16x16x32_bf16 v[72:75], v[136:139], v[194:197], v[72:75]
	v_mfma_f32_16x16x32_bf16 v[132:135], v[124:127], v[164:167], v[132:135]
	v_mfma_f32_16x16x32_bf16 v[128:131], v[140:143], v[164:167], v[128:131]
	v_mfma_f32_16x16x32_bf16 v[108:111], v[124:127], v[182:185], v[108:111]
	v_mfma_f32_16x16x32_bf16 v[104:107], v[140:143], v[182:185], v[104:107]
	v_mfma_f32_16x16x32_bf16 v[92:95], v[124:127], v[190:193], v[92:95]
	v_mfma_f32_16x16x32_bf16 v[88:91], v[140:143], v[190:193], v[88:91]
	v_mfma_f32_16x16x32_bf16 v[76:79], v[124:127], v[198:201], v[76:79]
	v_mfma_f32_16x16x32_bf16 v[72:75], v[140:143], v[198:201], v[72:75]
	v_mfma_f32_16x16x32_bf16 v[120:123], v[144:147], v[160:163], v[120:123]
	v_mfma_f32_16x16x32_bf16 v[116:119], v[152:155], v[160:163], v[116:119]
	v_mfma_f32_16x16x32_bf16 v[100:103], v[144:147], v[178:181], v[100:103]
	v_mfma_f32_16x16x32_bf16 v[96:99], v[152:155], v[178:181], v[96:99]
	v_mfma_f32_16x16x32_bf16 v[84:87], v[144:147], v[186:189], v[84:87]
	v_mfma_f32_16x16x32_bf16 v[80:83], v[152:155], v[186:189], v[80:83]
	v_mfma_f32_16x16x32_bf16 v[68:71], v[144:147], v[194:197], v[68:71]
	v_mfma_f32_16x16x32_bf16 v[64:67], v[152:155], v[194:197], v[64:67]
	v_mfma_f32_16x16x32_bf16 v[120:123], v[148:151], v[164:167], v[120:123]
	v_mfma_f32_16x16x32_bf16 v[116:119], v[156:159], v[164:167], v[116:119]
	v_mfma_f32_16x16x32_bf16 v[100:103], v[148:151], v[182:185], v[100:103]
	v_mfma_f32_16x16x32_bf16 v[96:99], v[156:159], v[182:185], v[96:99]
	v_mfma_f32_16x16x32_bf16 v[84:87], v[148:151], v[190:193], v[84:87]
	v_mfma_f32_16x16x32_bf16 v[80:83], v[156:159], v[190:193], v[80:83]
	v_mfma_f32_16x16x32_bf16 v[68:71], v[148:151], v[198:201], v[68:71]
	v_mfma_f32_16x16x32_bf16 v[64:67], v[156:159], v[198:201], v[64:67]
	s_setprio 0
	s_barrier
	s_mov_b32 m0, s1
	s_bitset1_b32 s55, 7
	buffer_load_dwordx4 v171, s[4:7], s55 offen lds
	s_mov_b32 m0, s35
	ds_read_b128 v[160:163], v177 offset:49152
	buffer_load_dwordx4 v173, s[4:7], s55 offen lds
	s_add_i32 s55, s55, s25
	s_mov_b32 m0, s43
	ds_read_b128 v[164:167], v177 offset:50176
	buffer_load_dwordx4 v171, s[4:7], s55 offen lds
	s_mov_b32 m0, s44
	ds_read_b128 v[178:181], v177 offset:51200
	buffer_load_dwordx4 v173, s[4:7], s55 offen lds
	s_mov_b32 m0, s41
	ds_read_b128 v[182:185], v177 offset:52224
	buffer_load_dwordx4 v170, s[36:39], s54 offen lds
	s_mov_b32 m0, s42
	ds_read_b128 v[186:189], v177 offset:53248
	buffer_load_dwordx4 v172, s[36:39], s54 offen lds
	ds_read_b128 v[190:193], v177 offset:54272
	ds_read_b128 v[194:197], v177 offset:55296
	ds_read_b128 v[198:201], v177 offset:56320
	s_waitcnt vmcnt(8)
	s_waitcnt lgkmcnt(0)
	s_barrier
	s_setprio 1
	v_mfma_f32_16x16x32_bf16 v[60:63], v[112:115], v[160:163], v[60:63]
	v_mfma_f32_16x16x32_bf16 v[56:59], v[136:139], v[160:163], v[56:59]
	v_mfma_f32_16x16x32_bf16 v[44:47], v[112:115], v[178:181], v[44:47]
	v_mfma_f32_16x16x32_bf16 v[40:43], v[136:139], v[178:181], v[40:43]
	v_mfma_f32_16x16x32_bf16 v[28:31], v[112:115], v[186:189], v[28:31]
	v_mfma_f32_16x16x32_bf16 v[24:27], v[136:139], v[186:189], v[24:27]
	v_mfma_f32_16x16x32_bf16 v[12:15], v[112:115], v[194:197], v[12:15]
	v_mfma_f32_16x16x32_bf16 v[8:11], v[136:139], v[194:197], v[8:11]
	v_mfma_f32_16x16x32_bf16 v[60:63], v[124:127], v[164:167], v[60:63]
	v_mfma_f32_16x16x32_bf16 v[56:59], v[140:143], v[164:167], v[56:59]
	v_mfma_f32_16x16x32_bf16 v[44:47], v[124:127], v[182:185], v[44:47]
	v_mfma_f32_16x16x32_bf16 v[40:43], v[140:143], v[182:185], v[40:43]
	v_mfma_f32_16x16x32_bf16 v[28:31], v[124:127], v[190:193], v[28:31]
	v_mfma_f32_16x16x32_bf16 v[24:27], v[140:143], v[190:193], v[24:27]
	v_mfma_f32_16x16x32_bf16 v[12:15], v[124:127], v[198:201], v[12:15]
	v_mfma_f32_16x16x32_bf16 v[8:11], v[140:143], v[198:201], v[8:11]
	v_mfma_f32_16x16x32_bf16 v[52:55], v[144:147], v[160:163], v[52:55]
	v_mfma_f32_16x16x32_bf16 v[48:51], v[152:155], v[160:163], v[48:51]
	v_mfma_f32_16x16x32_bf16 v[36:39], v[144:147], v[178:181], v[36:39]
	v_mfma_f32_16x16x32_bf16 v[32:35], v[152:155], v[178:181], v[32:35]
	v_mfma_f32_16x16x32_bf16 v[20:23], v[144:147], v[186:189], v[20:23]
	v_mfma_f32_16x16x32_bf16 v[16:19], v[152:155], v[186:189], v[16:19]
	v_mfma_f32_16x16x32_bf16 v[4:7], v[144:147], v[194:197], v[4:7]
	v_mfma_f32_16x16x32_bf16 v[0:3], v[152:155], v[194:197], v[0:3]
	v_mfma_f32_16x16x32_bf16 v[52:55], v[148:151], v[164:167], v[52:55]
	v_mfma_f32_16x16x32_bf16 v[48:51], v[156:159], v[164:167], v[48:51]
	v_mfma_f32_16x16x32_bf16 v[36:39], v[148:151], v[182:185], v[36:39]
	v_mfma_f32_16x16x32_bf16 v[32:35], v[156:159], v[182:185], v[32:35]
	v_mfma_f32_16x16x32_bf16 v[20:23], v[148:151], v[190:193], v[20:23]
	v_mfma_f32_16x16x32_bf16 v[16:19], v[156:159], v[190:193], v[16:19]
	v_mfma_f32_16x16x32_bf16 v[4:7], v[148:151], v[198:201], v[4:7]
	v_mfma_f32_16x16x32_bf16 v[0:3], v[156:159], v[198:201], v[0:3]
	s_setprio 0
	s_barrier
	s_add_i32 s67, s67, 2
	s_addk_i32 s65, 0x100
	s_addk_i32 s66, 0x100
	s_cmp_ge_i32 s67, s47
	s_cbranch_scc0 .LBB0_1701

;     __device__ __forceinline__ unsigned a_off(const Unit& u, const Gemm& g) const { return (unsigned)u.pm * (unsigned)(BM * 2) * (unsigned)g.K; }
;     __device__ __forceinline__ unsigned b_off(const Unit& u, const Gemm& g) const { return (unsigned)u.pn * (unsigned)(BM * 2) * (unsigned)g.K; }
;     __device__ __forceinline__ bool next(int i, Unit& u) const { return so.next(i, u); }
; template <class Epi, class Sched, bool ALIGN_EPI = false, bool SP2 = false, bool FP8 = false>
; __device__ __forceinline__ void gemm_phase(LAS unsigned char* lds, const Gemm g, const Sched& S, const Epi& E, int wbase) {
;     ...
;         const bool has_next = S.next(ui + 1, nxt);
;         const unsigned nA = has_next ? S.a_off(nxt, g) : cA, nB = has_next ? S.b_off(nxt, g) : cB;
;         const rsrc_t rAn = (Sched::TWO && has_next) ? (nxt.part ? rA1 : rA0) : rAc, rBn = (Sched::TWO && has_next) ? (nxt.part ? rB1 : rB0) : rBc;
;         float pre_[8] = {0.f, 0.f, 0.f, 0.f, 0.f, 0.f, 0.f, 0.f};
;         if constexpr (Epi::HAS_PRE) E.pre_load(pre_, cur, wr);
;         for (int t = 0; t < nt; t += 2) {
;             const bool last = (t == nt - 2);
;             const unsigned a1 = cA + (unsigned)(t + 1) * kstep;
;             const unsigned a2 = last ? nA : cA + (unsigned)(t + 2) * kstep, b2 = last ? nB : cB + (unsigned)(t + 2) * kstep; const rsrc_t rA2 = (Sched::TWO && last) ? rAn : rAc, rB2 = (Sched::TWO && last) ? rBn : rBc;
;             const unsigned a3 = a2 + kstep, b3 = b2 + kstep;
;             if (last && has_next) S.a_ready(nxt);
;             if constexpr (SP2) {
;             PG8_LDB(B0, 0, 0); PG8_LDB(B1, 0, 1); PG8_SCHED; PG8_LDA(At, 0, 0); PG8_STAGE(PG8_SA(1, 1), rAc, a1 + hstep, voffA);
;             PG8_WAIT_V(8); PG8_WAIT_L(0); PG8_BAR; PG8_MMA(0, 0, At, B0); PG8_MMA(0, 1, At, B1); PG8_BAR; PG8_SCHED;
;             PG8_LDA(At, 0, 1); PG8_STAGE(PG8_SB(0, 0), rB2, b2, voffB); PG8_STAGE(PG8_SB(0, 1), rB2, b2 + hstep, voffB); PG8_STAGE(PG8_SA(0, 0), rA2, a2, voffA);
;             PG8_WAIT_V(8); PG8_WAIT_L(0); PG8_BAR; PG8_MMA(1, 0, At, B0); PG8_MMA(1, 1, At, B1); PG8_BAR; PG8_SCHED;
;             PG8_LDB(B0, 1, 0); PG8_LDB(B1, 1, 1); PG8_SCHED; PG8_LDA(At, 1, 0); PG8_STAGE(PG8_SA(0, 1), rA2, a2 + hstep, voffA);
;             PG8_WAIT_V(8); PG8_WAIT_L(0); PG8_BAR; PG8_MMA(0, 0, At, B0); PG8_MMA(0, 1, At, B1); PG8_BAR; PG8_SCHED;
.LBB0_1779:
	s_lshl_b32 s53, s52, 18
	s_andn2_b64 vcc, exec, s[14:15]
	s_lshl_b32 s56, s48, 18
	s_cbranch_vccnz .LBB0_1783
	s_and_b64 s[6:7], s[18:19], exec
	s_waitcnt vmcnt(37)
	s_waitcnt vmcnt(35)
	s_waitcnt vmcnt(31)
	s_waitcnt vmcnt(27)
	s_waitcnt vmcnt(23)
	s_waitcnt vmcnt(22)
	v_mov_b32_e32 v225, 1
	v_mov_b32_e32 v223, v233
	v_mov_b32_e32 v222, 0x358637bd
	s_cselect_b32 s59, s53, s55
	s_cselect_b32 s60, s56, s54
	s_add_i32 s61, s55, 0x80
	s_add_i32 s62, s54, 0x100
	s_mov_b32 s63, 0
	v_add_u32_e32 v140, 0x10000, v154
	v_add_u32_e32 v144, 0x14000, v154
	ds_read_b128 v[128:131], v140
	ds_read_b128 v[132:135], v140 offset:1024
	ds_read_b128 v[136:139], v140 offset:2048
	ds_read_b128 v[140:143], v140 offset:3072
	ds_read_b128 v[156:159], v144
	ds_read_b128 v[160:163], v144 offset:1024
	ds_read_b128 v[164:167], v144 offset:2048
	ds_read_b128 v[168:171], v144 offset:3072
	s_add_i32 s6, s61, 0x80
	s_cmp_eq_u32 s45, s63
	s_cselect_b32 s65, s59, s6
	s_cselect_b32 s55, s60, s62
	s_or_b32 s54, s65, 0x80
	s_add_i32 s6, s21, s61
	s_mov_b32 m0, s46
	ds_read_b128 v[172:175], v155
	ds_read_b128 v[176:179], v155 offset:1024
	ds_read_b128 v[180:183], v155 offset:2048
	ds_read_b128 v[184:187], v155 offset:3072
	ds_read_b128 v[194:197], v155 offset:4096
	ds_read_b128 v[198:201], v155 offset:5120
	ds_read_b128 v[202:205], v155 offset:6144
	ds_read_b128 v[206:209], v155 offset:7168
	buffer_load_dwordx4 v148, s[36:39], s6 offen lds
	s_mov_b32 m0, s47
	s_nop 0
	buffer_load_dwordx4 v150, s[36:39], s6 offen lds
	s_waitcnt vmcnt(8)
	s_waitcnt lgkmcnt(0)
	s_barrier
	s_setprio 1
	v_mfma_f32_16x16x128_f8f6f4 v[120:123], v[128:135], v[172:179], 0
	v_mfma_f32_16x16x128_f8f6f4 v[124:127], v[136:143], v[172:179], 0
	v_mfma_f32_16x16x128_f8f6f4 v[104:107], v[128:135], v[180:187], 0
	v_mfma_f32_16x16x128_f8f6f4 v[108:111], v[136:143], v[180:187], 0
	v_mfma_f32_16x16x128_f8f6f4 v[144:147], v[128:135], v[194:201], 0
	v_mfma_f32_16x16x128_f8f6f4 v[188:191], v[136:143], v[194:201], 0
	v_mfma_f32_16x16x128_f8f6f4 v[210:213], v[128:135], v[202:209], 0
	v_mfma_f32_16x16x128_f8f6f4 v[214:217], v[136:143], v[202:209], 0
	v_mfma_f32_16x16x128_f8f6f4 v[112:115], v[156:163], v[172:179], 0
	v_mfma_f32_16x16x128_f8f6f4 v[116:119], v[164:171], v[172:179], 0
	v_mfma_f32_16x16x128_f8f6f4 v[96:99], v[156:163], v[180:187], 0
	v_mfma_f32_16x16x128_f8f6f4 v[100:103], v[164:171], v[180:187], 0
	v_mfma_f32_16x16x128_f8f6f4 v[172:175], v[156:163], v[194:201], 0
	v_mfma_f32_16x16x128_f8f6f4 v[176:179], v[164:171], v[194:201], 0
	v_mfma_f32_16x16x128_f8f6f4 v[180:183], v[156:163], v[202:209], 0
	v_mfma_f32_16x16x128_f8f6f4 v[184:187], v[164:171], v[202:209], 0
	s_setprio 0
	s_barrier
	s_mov_b32 m0, s23
	s_mov_b32 s6, s38
	s_mov_b32 s7, s39
	s_nop 0
	buffer_load_dwordx4 v149, s[4:7], s55 offen lds
	s_mov_b32 m0, s24
	ds_read_b128 v[64:67], v155 offset:16384
	s_add_i32 s66, s55, s21
	buffer_load_dwordx4 v151, s[4:7], s55 offen lds
	s_mov_b32 m0, s25
	ds_read_b128 v[68:71], v155 offset:17408
	buffer_load_dwordx4 v149, s[4:7], s66 offen lds
	s_mov_b32 m0, s26
	ds_read_b128 v[72:75], v155 offset:18432
	buffer_load_dwordx4 v151, s[4:7], s66 offen lds
	s_mov_b32 m0, s22
	ds_read_b128 v[76:79], v155 offset:19456
	buffer_load_dwordx4 v148, s[36:39], s65 offen lds
	s_mov_b32 m0, s27
	ds_read_b128 v[80:83], v155 offset:20480
	buffer_load_dwordx4 v150, s[36:39], s65 offen lds
	ds_read_b128 v[84:87], v155 offset:21504
	ds_read_b128 v[88:91], v155 offset:22528
	ds_read_b128 v[92:95], v155 offset:23552
	s_waitcnt vmcnt(8)
	s_waitcnt lgkmcnt(0)
	s_barrier
	s_setprio 1
	v_mfma_f32_16x16x128_f8f6f4 v[56:59], v[128:135], v[64:71], 0
	v_mfma_f32_16x16x128_f8f6f4 v[60:63], v[136:143], v[64:71], 0
	v_mfma_f32_16x16x128_f8f6f4 v[8:11], v[128:135], v[88:95], 0
	v_mfma_f32_16x16x128_f8f6f4 v[192:195], v[128:135], v[72:79], 0
	v_mfma_f32_16x16x128_f8f6f4 v[196:199], v[136:143], v[72:79], 0
	v_mfma_f32_16x16x128_f8f6f4 v[200:203], v[128:135], v[80:87], 0
	v_mfma_f32_16x16x128_f8f6f4 v[204:207], v[136:143], v[80:87], 0
	v_mfma_f32_16x16x128_f8f6f4 v[218:221], v[136:143], v[88:95], 0
	v_mfma_f32_16x16x128_f8f6f4 v[52:55], v[164:171], v[64:71], 0
	v_mfma_f32_16x16x128_f8f6f4 v[226:229], v[156:163], v[64:71], 0
	v_mfma_f32_16x16x128_f8f6f4 v[230:233], v[156:163], v[72:79], 0
	v_mfma_f32_16x16x128_f8f6f4 v[234:237], v[164:171], v[72:79], 0
	v_mfma_f32_16x16x128_f8f6f4 v[238:241], v[156:163], v[80:87], 0
	v_mfma_f32_16x16x128_f8f6f4 v[242:245], v[164:171], v[80:87], 0
	v_mfma_f32_16x16x128_f8f6f4 v[246:249], v[156:163], v[88:95], 0
	v_mfma_f32_16x16x128_f8f6f4 v[250:253], v[164:171], v[88:95], 0
	s_setprio 0
	s_barrier
	s_nop 1
	v_add_u32_e32 v16, 0x18000, v154
	v_add_u32_e32 v20, 0x1c000, v154
	s_nop 0
	ds_read_b128 v[0:3], v16
	ds_read_b128 v[4:7], v16 offset:1024
	ds_read_b128 v[12:15], v16 offset:2048
	ds_read_b128 v[16:19], v16 offset:3072
	ds_read_b128 v[128:131], v20
	ds_read_b128 v[132:135], v20 offset:1024
	ds_read_b128 v[136:139], v20 offset:2048
	ds_read_b128 v[140:143], v20 offset:3072
	s_add_i32 s65, s65, s21
	s_mov_b32 m0, s28
	ds_read_b128 v[20:23], v155 offset:32768
	ds_read_b128 v[24:27], v155 offset:33792
	ds_read_b128 v[28:31], v155 offset:34816
	ds_read_b128 v[32:35], v155 offset:35840
	ds_read_b128 v[36:39], v155 offset:36864
	ds_read_b128 v[40:43], v155 offset:37888
	ds_read_b128 v[44:47], v155 offset:38912
	ds_read_b128 v[48:51], v155 offset:39936
	buffer_load_dwordx4 v148, s[36:39], s65 offen lds
	s_mov_b32 m0, s29
	s_nop 0
	buffer_load_dwordx4 v150, s[36:39], s65 offen lds
	s_waitcnt vmcnt(8)
	s_waitcnt lgkmcnt(0)
	s_barrier
; #define PG8_STAGE(bufoff, rs_, soff_, voff) do { _Pragma("unroll") for (int _i = 0; _i < 2; ++_i) \
;         __builtin_amdgcn_raw_ptr_buffer_load_lds(rs_, (LAS void*)(lds + (bufoff) + ldsw + _i * 8192), 16, (int)(voff)[_i], (int)(soff_), 0, 0); } while (0)
; #define PG8_LDA(dst, b, h) do { _Pragma("unroll") for (int m = 0; m < 4; ++m) dst[m] = PG8_LD2(lds + PG8_SA(b, h) + aoff + m * 2048); } while (0)
; #define PG8_WAIT_V(n) asm volatile("s_waitcnt vmcnt(" #n ")" ::: "memory")
; #define PG8_WAIT_L(n) asm volatile("s_waitcnt lgkmcnt(" #n ")" ::: "memory")
; #define PG8_BAR __builtin_amdgcn_s_barrier()
; #define PG8_SCHED __builtin_amdgcn_sched_barrier(0)
; template <class Epi, class Sched, bool ALIGN_EPI = false, bool SP2 = false, bool FP8 = false>
; __device__ __forceinline__ void gemm_phase(LAS unsigned char* lds, const Gemm g, const Sched& S, const Epi& E, int wbase) {
;     ...
;             PG8_WAIT_V(8); PG8_WAIT_L(0); PG8_BAR; PG8_MMA(0, 0, At, B0); PG8_MMA(0, 1, At, B1); PG8_BAR; PG8_SCHED;
;             PG8_LDA(At, 1, 1); PG8_STAGE(PG8_SB(1, 0), rB2, b3, voffB); PG8_STAGE(PG8_SB(1, 1), rB2, b3 + hstep, voffB); PG8_STAGE(PG8_SA(1, 0), rA2, a3, voffA);
;             PG8_WAIT_V(8); PG8_WAIT_L(0); PG8_BAR; PG8_MMA(1, 0, At, B0); PG8_MMA(1, 1, At, B1); PG8_BAR; PG8_SCHED;
	s_setprio 1
	v_mfma_f32_16x16x128_f8f6f4 v[120:123], v[0:7], v[20:27], v[120:123]
	v_mfma_f32_16x16x128_f8f6f4 v[124:127], v[12:19], v[20:27], v[124:127]
	v_mfma_f32_16x16x128_f8f6f4 v[104:107], v[0:7], v[28:35], v[104:107]
	v_mfma_f32_16x16x128_f8f6f4 v[108:111], v[12:19], v[28:35], v[108:111]
	v_mfma_f32_16x16x128_f8f6f4 v[88:91], v[0:7], v[36:43], v[144:147]
	v_mfma_f32_16x16x128_f8f6f4 v[92:95], v[12:19], v[36:43], v[188:191]
	v_mfma_f32_16x16x128_f8f6f4 v[72:75], v[0:7], v[44:51], v[210:213]
	v_mfma_f32_16x16x128_f8f6f4 v[76:79], v[12:19], v[44:51], v[214:217]
	v_mfma_f32_16x16x128_f8f6f4 v[112:115], v[128:135], v[20:27], v[112:115]
	v_mfma_f32_16x16x128_f8f6f4 v[116:119], v[136:143], v[20:27], v[116:119]
	v_mfma_f32_16x16x128_f8f6f4 v[96:99], v[128:135], v[28:35], v[96:99]
	v_mfma_f32_16x16x128_f8f6f4 v[100:103], v[136:143], v[28:35], v[100:103]
	v_mfma_f32_16x16x128_f8f6f4 v[80:83], v[128:135], v[36:43], v[172:175]
	v_mfma_f32_16x16x128_f8f6f4 v[84:87], v[136:143], v[36:43], v[176:179]
	v_mfma_f32_16x16x128_f8f6f4 v[64:67], v[128:135], v[44:51], v[180:183]
	v_mfma_f32_16x16x128_f8f6f4 v[68:71], v[136:143], v[44:51], v[184:187]
	s_setprio 0
	s_barrier
	s_mov_b32 m0, s30
	s_bitset1_b32 s55, 7
	buffer_load_dwordx4 v149, s[4:7], s55 offen lds
	s_mov_b32 m0, s31
	ds_read_b128 v[32:35], v155 offset:49152
	buffer_load_dwordx4 v151, s[4:7], s55 offen lds
	s_add_i32 s55, s55, s21
	s_mov_b32 m0, s35
	ds_read_b128 v[36:39], v155 offset:50176
	buffer_load_dwordx4 v149, s[4:7], s55 offen lds
	s_mov_b32 m0, s41
	ds_read_b128 v[156:159], v155 offset:51200
	buffer_load_dwordx4 v151, s[4:7], s55 offen lds
	s_mov_b32 m0, s33
	ds_read_b128 v[160:163], v155 offset:52224
	buffer_load_dwordx4 v148, s[36:39], s54 offen lds
	s_mov_b32 m0, s34
	ds_read_b128 v[164:167], v155 offset:53248
	buffer_load_dwordx4 v150, s[36:39], s54 offen lds
	ds_read_b128 v[168:171], v155 offset:54272
	ds_read_b128 v[172:175], v155 offset:55296
	ds_read_b128 v[176:179], v155 offset:56320
	s_waitcnt vmcnt(8)
	s_waitcnt lgkmcnt(0)
	s_barrier
	s_setprio 1
	v_mfma_f32_16x16x128_f8f6f4 v[56:59], v[0:7], v[32:39], v[56:59]
	v_mfma_f32_16x16x128_f8f6f4 v[60:63], v[12:19], v[32:39], v[60:63]
	v_mfma_f32_16x16x128_f8f6f4 v[40:43], v[0:7], v[156:163], v[192:195]
	v_mfma_f32_16x16x128_f8f6f4 v[44:47], v[12:19], v[156:163], v[196:199]
	v_mfma_f32_16x16x128_f8f6f4 v[24:27], v[0:7], v[164:171], v[200:203]
	v_mfma_f32_16x16x128_f8f6f4 v[28:31], v[12:19], v[164:171], v[204:207]
	v_mfma_f32_16x16x128_f8f6f4 v[8:11], v[0:7], v[172:179], v[8:11]
	v_mfma_f32_16x16x128_f8f6f4 v[12:15], v[12:19], v[172:179], v[218:221]
	v_mfma_f32_16x16x128_f8f6f4 v[48:51], v[128:135], v[32:39], v[226:229]
	v_mfma_f32_16x16x128_f8f6f4 v[52:55], v[136:143], v[32:39], v[52:55]
	v_mfma_f32_16x16x128_f8f6f4 v[32:35], v[128:135], v[156:163], v[230:233]
	v_mfma_f32_16x16x128_f8f6f4 v[36:39], v[136:143], v[156:163], v[234:237]
	v_mfma_f32_16x16x128_f8f6f4 v[16:19], v[128:135], v[164:171], v[238:241]
	v_mfma_f32_16x16x128_f8f6f4 v[20:23], v[136:143], v[164:171], v[242:245]
	v_mfma_f32_16x16x128_f8f6f4 v[4:7], v[128:135], v[172:179], v[246:249]
	v_mfma_f32_16x16x128_f8f6f4 v[0:3], v[136:143], v[172:179], v[250:253]
	s_setprio 0
	s_barrier
	s_add_i32 s63, s63, 2
	s_addk_i32 s61, 0x100
	s_addk_i32 s62, 0x100
	s_cmp_ge_i32 s63, s43
	s_cbranch_scc0 .LBB0_1781
	s_branch .Lzp_after_1781
.LBB0_1781:
	v_add_u32_e32 v140, 0x10000, v154
	v_add_u32_e32 v144, 0x14000, v154
	ds_read_b128 v[128:131], v140
	ds_read_b128 v[132:135], v140 offset:1024
	ds_read_b128 v[136:139], v140 offset:2048
	ds_read_b128 v[140:143], v140 offset:3072
	ds_read_b128 v[156:159], v144
	ds_read_b128 v[160:163], v144 offset:1024
	ds_read_b128 v[164:167], v144 offset:2048
	ds_read_b128 v[168:171], v144 offset:3072
	s_add_i32 s6, s61, 0x80
	s_cmp_eq_u32 s45, s63
	s_cselect_b32 s65, s59, s6
	s_cselect_b32 s55, s60, s62
	s_or_b32 s54, s65, 0x80
	s_add_i32 s6, s21, s61
	s_mov_b32 m0, s46
	ds_read_b128 v[172:175], v155
	ds_read_b128 v[176:179], v155 offset:1024
	ds_read_b128 v[180:183], v155 offset:2048
	ds_read_b128 v[184:187], v155 offset:3072
	ds_read_b128 v[194:197], v155 offset:4096
	ds_read_b128 v[198:201], v155 offset:5120
	ds_read_b128 v[202:205], v155 offset:6144
	ds_read_b128 v[206:209], v155 offset:7168
	buffer_load_dwordx4 v148, s[36:39], s6 offen lds
	s_mov_b32 m0, s47
	s_nop 0
	buffer_load_dwordx4 v150, s[36:39], s6 offen lds
	s_waitcnt vmcnt(8)
	s_waitcnt lgkmcnt(0)
	s_barrier
	s_setprio 1
	v_mfma_f32_16x16x128_f8f6f4 v[120:123], v[128:135], v[172:179], v[120:123]
	v_mfma_f32_16x16x128_f8f6f4 v[124:127], v[136:143], v[172:179], v[124:127]
	v_mfma_f32_16x16x128_f8f6f4 v[104:107], v[128:135], v[180:187], v[104:107]
	v_mfma_f32_16x16x128_f8f6f4 v[108:111], v[136:143], v[180:187], v[108:111]
	v_mfma_f32_16x16x128_f8f6f4 v[144:147], v[128:135], v[194:201], v[88:91]
	v_mfma_f32_16x16x128_f8f6f4 v[188:191], v[136:143], v[194:201], v[92:95]
	v_mfma_f32_16x16x128_f8f6f4 v[210:213], v[128:135], v[202:209], v[72:75]
	v_mfma_f32_16x16x128_f8f6f4 v[214:217], v[136:143], v[202:209], v[76:79]
	v_mfma_f32_16x16x128_f8f6f4 v[112:115], v[156:163], v[172:179], v[112:115]
	v_mfma_f32_16x16x128_f8f6f4 v[116:119], v[164:171], v[172:179], v[116:119]
	v_mfma_f32_16x16x128_f8f6f4 v[96:99], v[156:163], v[180:187], v[96:99]
	v_mfma_f32_16x16x128_f8f6f4 v[100:103], v[164:171], v[180:187], v[100:103]
	v_mfma_f32_16x16x128_f8f6f4 v[172:175], v[156:163], v[194:201], v[80:83]
	v_mfma_f32_16x16x128_f8f6f4 v[176:179], v[164:171], v[194:201], v[84:87]
	v_mfma_f32_16x16x128_f8f6f4 v[180:183], v[156:163], v[202:209], v[64:67]
	v_mfma_f32_16x16x128_f8f6f4 v[184:187], v[164:171], v[202:209], v[68:71]
	s_setprio 0
	s_barrier
; #define PG8_STAGE(bufoff, rs_, soff_, voff) do { _Pragma("unroll") for (int _i = 0; _i < 2; ++_i) \
;         __builtin_amdgcn_raw_ptr_buffer_load_lds(rs_, (LAS void*)(lds + (bufoff) + ldsw + _i * 8192), 16, (int)(voff)[_i], (int)(soff_), 0, 0); } while (0)
; #define PG8_LDA(dst, b, h) do { _Pragma("unroll") for (int m = 0; m < 4; ++m) dst[m] = PG8_LD2(lds + PG8_SA(b, h) + aoff + m * 2048); } while (0)
; #define PG8_LDB(dst, b, h) do { _Pragma("unroll") for (int n = 0; n < 2; ++n) dst[n] = PG8_LD2(lds + PG8_SB(b, h) + boff + n * 2048); } while (0)
; #define PG8_WAIT_V(n) asm volatile("s_waitcnt vmcnt(" #n ")" ::: "memory")
; #define PG8_WAIT_L(n) asm volatile("s_waitcnt lgkmcnt(" #n ")" ::: "memory")
; #define PG8_BAR __builtin_amdgcn_s_barrier()
; #define PG8_SCHED __builtin_amdgcn_sched_barrier(0)
; template <class Epi, class Sched, bool ALIGN_EPI = false, bool SP2 = false, bool FP8 = false>
; __device__ __forceinline__ void gemm_phase(LAS unsigned char* lds, const Gemm g, const Sched& S, const Epi& E, int wbase) {
;     ...
;             PG8_LDA(At, 0, 1); PG8_STAGE(PG8_SB(0, 0), rB2, b2, voffB); PG8_STAGE(PG8_SB(0, 1), rB2, b2 + hstep, voffB); PG8_STAGE(PG8_SA(0, 0), rA2, a2, voffA);
;             PG8_WAIT_V(8); PG8_WAIT_L(0); PG8_BAR; PG8_MMA(1, 0, At, B0); PG8_MMA(1, 1, At, B1); PG8_BAR; PG8_SCHED;
;             PG8_LDB(B0, 1, 0); PG8_LDB(B1, 1, 1); PG8_SCHED; PG8_LDA(At, 1, 0); PG8_STAGE(PG8_SA(0, 1), rA2, a2 + hstep, voffA);
;             PG8_WAIT_V(8); PG8_WAIT_L(0); PG8_BAR; PG8_MMA(0, 0, At, B0); PG8_MMA(0, 1, At, B1); PG8_BAR; PG8_SCHED;
;             PG8_LDA(At, 1, 1); PG8_STAGE(PG8_SB(1, 0), rB2, b3, voffB); PG8_STAGE(PG8_SB(1, 1), rB2, b3 + hstep, voffB); PG8_STAGE(PG8_SA(1, 0), rA2, a3, voffA);
;             PG8_WAIT_V(8); PG8_WAIT_L(0); PG8_BAR; PG8_MMA(1, 0, At, B0); PG8_MMA(1, 1, At, B1); PG8_BAR; PG8_SCHED;
	s_mov_b32 m0, s23
	s_mov_b32 s6, s38
	s_mov_b32 s7, s39
	s_nop 0
	buffer_load_dwordx4 v149, s[4:7], s55 offen lds
	s_mov_b32 m0, s24
	ds_read_b128 v[64:67], v155 offset:16384
	s_add_i32 s66, s55, s21
	buffer_load_dwordx4 v151, s[4:7], s55 offen lds
	s_mov_b32 m0, s25
	ds_read_b128 v[68:71], v155 offset:17408
	buffer_load_dwordx4 v149, s[4:7], s66 offen lds
	s_mov_b32 m0, s26
	ds_read_b128 v[72:75], v155 offset:18432
	buffer_load_dwordx4 v151, s[4:7], s66 offen lds
	s_mov_b32 m0, s22
	ds_read_b128 v[76:79], v155 offset:19456
	buffer_load_dwordx4 v148, s[36:39], s65 offen lds
	s_mov_b32 m0, s27
	ds_read_b128 v[80:83], v155 offset:20480
	buffer_load_dwordx4 v150, s[36:39], s65 offen lds
	ds_read_b128 v[84:87], v155 offset:21504
	ds_read_b128 v[88:91], v155 offset:22528
	ds_read_b128 v[92:95], v155 offset:23552
	s_waitcnt vmcnt(8)
	s_waitcnt lgkmcnt(0)
	s_barrier
	s_setprio 1
	v_mfma_f32_16x16x128_f8f6f4 v[56:59], v[128:135], v[64:71], v[56:59]
	v_mfma_f32_16x16x128_f8f6f4 v[60:63], v[136:143], v[64:71], v[60:63]
	v_mfma_f32_16x16x128_f8f6f4 v[8:11], v[128:135], v[88:95], v[8:11]
	v_mfma_f32_16x16x128_f8f6f4 v[192:195], v[128:135], v[72:79], v[40:43]
	v_mfma_f32_16x16x128_f8f6f4 v[196:199], v[136:143], v[72:79], v[44:47]
	v_mfma_f32_16x16x128_f8f6f4 v[200:203], v[128:135], v[80:87], v[24:27]
	v_mfma_f32_16x16x128_f8f6f4 v[204:207], v[136:143], v[80:87], v[28:31]
	v_mfma_f32_16x16x128_f8f6f4 v[218:221], v[136:143], v[88:95], v[12:15]
	v_mfma_f32_16x16x128_f8f6f4 v[52:55], v[164:171], v[64:71], v[52:55]
	v_mfma_f32_16x16x128_f8f6f4 v[226:229], v[156:163], v[64:71], v[48:51]
	v_mfma_f32_16x16x128_f8f6f4 v[230:233], v[156:163], v[72:79], v[32:35]
	v_mfma_f32_16x16x128_f8f6f4 v[234:237], v[164:171], v[72:79], v[36:39]
	v_mfma_f32_16x16x128_f8f6f4 v[238:241], v[156:163], v[80:87], v[16:19]
	v_mfma_f32_16x16x128_f8f6f4 v[242:245], v[164:171], v[80:87], v[20:23]
	v_mfma_f32_16x16x128_f8f6f4 v[246:249], v[156:163], v[88:95], v[4:7]
	v_mfma_f32_16x16x128_f8f6f4 v[250:253], v[164:171], v[88:95], v[0:3]
	s_setprio 0
	s_barrier
	s_nop 1
	v_add_u32_e32 v16, 0x18000, v154
	v_add_u32_e32 v20, 0x1c000, v154
	s_nop 0
	ds_read_b128 v[0:3], v16
	ds_read_b128 v[4:7], v16 offset:1024
	ds_read_b128 v[12:15], v16 offset:2048
	ds_read_b128 v[16:19], v16 offset:3072
	ds_read_b128 v[128:131], v20
	ds_read_b128 v[132:135], v20 offset:1024
	ds_read_b128 v[136:139], v20 offset:2048
	ds_read_b128 v[140:143], v20 offset:3072
	s_add_i32 s65, s65, s21
	s_mov_b32 m0, s28
	ds_read_b128 v[20:23], v155 offset:32768
	ds_read_b128 v[24:27], v155 offset:33792
	ds_read_b128 v[28:31], v155 offset:34816
	ds_read_b128 v[32:35], v155 offset:35840
	ds_read_b128 v[36:39], v155 offset:36864
	ds_read_b128 v[40:43], v155 offset:37888
	ds_read_b128 v[44:47], v155 offset:38912
	ds_read_b128 v[48:51], v155 offset:39936
	buffer_load_dwordx4 v148, s[36:39], s65 offen lds
	s_mov_b32 m0, s29
	s_nop 0
	buffer_load_dwordx4 v150, s[36:39], s65 offen lds
	s_waitcnt vmcnt(8)
	s_waitcnt lgkmcnt(0)
	s_barrier
	s_setprio 1
	v_mfma_f32_16x16x128_f8f6f4 v[120:123], v[0:7], v[20:27], v[120:123]
	v_mfma_f32_16x16x128_f8f6f4 v[124:127], v[12:19], v[20:27], v[124:127]
	v_mfma_f32_16x16x128_f8f6f4 v[104:107], v[0:7], v[28:35], v[104:107]
	v_mfma_f32_16x16x128_f8f6f4 v[108:111], v[12:19], v[28:35], v[108:111]
	v_mfma_f32_16x16x128_f8f6f4 v[88:91], v[0:7], v[36:43], v[144:147]
	v_mfma_f32_16x16x128_f8f6f4 v[92:95], v[12:19], v[36:43], v[188:191]
	v_mfma_f32_16x16x128_f8f6f4 v[72:75], v[0:7], v[44:51], v[210:213]
	v_mfma_f32_16x16x128_f8f6f4 v[76:79], v[12:19], v[44:51], v[214:217]
	v_mfma_f32_16x16x128_f8f6f4 v[112:115], v[128:135], v[20:27], v[112:115]
	v_mfma_f32_16x16x128_f8f6f4 v[116:119], v[136:143], v[20:27], v[116:119]
	v_mfma_f32_16x16x128_f8f6f4 v[96:99], v[128:135], v[28:35], v[96:99]
	v_mfma_f32_16x16x128_f8f6f4 v[100:103], v[136:143], v[28:35], v[100:103]
	v_mfma_f32_16x16x128_f8f6f4 v[80:83], v[128:135], v[36:43], v[172:175]
	v_mfma_f32_16x16x128_f8f6f4 v[84:87], v[136:143], v[36:43], v[176:179]
	v_mfma_f32_16x16x128_f8f6f4 v[64:67], v[128:135], v[44:51], v[180:183]
	v_mfma_f32_16x16x128_f8f6f4 v[68:71], v[136:143], v[44:51], v[184:187]
	s_setprio 0
	s_barrier
	s_mov_b32 m0, s30
	s_bitset1_b32 s55, 7
	buffer_load_dwordx4 v149, s[4:7], s55 offen lds
	s_mov_b32 m0, s31
	ds_read_b128 v[32:35], v155 offset:49152
	buffer_load_dwordx4 v151, s[4:7], s55 offen lds
	s_add_i32 s55, s55, s21
	s_mov_b32 m0, s35
	ds_read_b128 v[36:39], v155 offset:50176
	buffer_load_dwordx4 v149, s[4:7], s55 offen lds
	s_mov_b32 m0, s41
	ds_read_b128 v[156:159], v155 offset:51200
	buffer_load_dwordx4 v151, s[4:7], s55 offen lds
	s_mov_b32 m0, s33
	ds_read_b128 v[160:163], v155 offset:52224
	buffer_load_dwordx4 v148, s[36:39], s54 offen lds
	s_mov_b32 m0, s34
	ds_read_b128 v[164:167], v155 offset:53248
	buffer_load_dwordx4 v150, s[36:39], s54 offen lds
	ds_read_b128 v[168:171], v155 offset:54272
	ds_read_b128 v[172:175], v155 offset:55296
	ds_read_b128 v[176:179], v155 offset:56320
	s_waitcnt vmcnt(8)
	s_waitcnt lgkmcnt(0)
	s_barrier
	s_setprio 1
	v_mfma_f32_16x16x128_f8f6f4 v[56:59], v[0:7], v[32:39], v[56:59]
	v_mfma_f32_16x16x128_f8f6f4 v[60:63], v[12:19], v[32:39], v[60:63]
	v_mfma_f32_16x16x128_f8f6f4 v[40:43], v[0:7], v[156:163], v[192:195]
	v_mfma_f32_16x16x128_f8f6f4 v[44:47], v[12:19], v[156:163], v[196:199]
	v_mfma_f32_16x16x128_f8f6f4 v[24:27], v[0:7], v[164:171], v[200:203]
	v_mfma_f32_16x16x128_f8f6f4 v[28:31], v[12:19], v[164:171], v[204:207]
	v_mfma_f32_16x16x128_f8f6f4 v[8:11], v[0:7], v[172:179], v[8:11]
	v_mfma_f32_16x16x128_f8f6f4 v[12:15], v[12:19], v[172:179], v[218:221]
	v_mfma_f32_16x16x128_f8f6f4 v[48:51], v[128:135], v[32:39], v[226:229]
	v_mfma_f32_16x16x128_f8f6f4 v[52:55], v[136:143], v[32:39], v[52:55]
	v_mfma_f32_16x16x128_f8f6f4 v[32:35], v[128:135], v[156:163], v[230:233]
	v_mfma_f32_16x16x128_f8f6f4 v[36:39], v[136:143], v[156:163], v[234:237]
	v_mfma_f32_16x16x128_f8f6f4 v[16:19], v[128:135], v[164:171], v[238:241]
	v_mfma_f32_16x16x128_f8f6f4 v[20:23], v[136:143], v[164:171], v[242:245]
	v_mfma_f32_16x16x128_f8f6f4 v[4:7], v[128:135], v[172:179], v[246:249]
	v_mfma_f32_16x16x128_f8f6f4 v[0:3], v[136:143], v[172:179], v[250:253]
	s_setprio 0
	s_barrier
	s_add_i32 s63, s63, 2
	s_addk_i32 s61, 0x100
	s_addk_i32 s62, 0x100
	s_cmp_ge_i32 s63, s43
	s_cbranch_scc0 .LBB0_1781

;     __device__ __forceinline__ unsigned a_off(const Unit& u, const Gemm& g) const { return (unsigned)u.pm * (unsigned)(BM * 2) * (unsigned)g.K; }
;     __device__ __forceinline__ unsigned b_off(const Unit& u, const Gemm& g) const { return (unsigned)u.pn * (unsigned)(BM * 2) * (unsigned)g.K; }
;     __device__ __forceinline__ bool next(int i, Unit& u) const { return so.next(i, u); }
; template <class Epi, class Sched, bool ALIGN_EPI = false, bool SP2 = false, bool FP8 = false>
; __device__ __forceinline__ void gemm_phase(LAS unsigned char* lds, const Gemm g, const Sched& S, const Epi& E, int wbase) {
;     ...
;         const bool has_next = S.next(ui + 1, nxt);
;         const unsigned nA = has_next ? S.a_off(nxt, g) : cA, nB = has_next ? S.b_off(nxt, g) : cB;
;         const rsrc_t rAn = (Sched::TWO && has_next) ? (nxt.part ? rA1 : rA0) : rAc, rBn = (Sched::TWO && has_next) ? (nxt.part ? rB1 : rB0) : rBc;
;         float pre_[8] = {0.f, 0.f, 0.f, 0.f, 0.f, 0.f, 0.f, 0.f};
;         if constexpr (Epi::HAS_PRE) E.pre_load(pre_, cur, wr);
;         for (int t = 0; t < nt; t += 2) {
;             const bool last = (t == nt - 2);
;             const unsigned a1 = cA + (unsigned)(t + 1) * kstep;
;             const unsigned a2 = last ? nA : cA + (unsigned)(t + 2) * kstep, b2 = last ? nB : cB + (unsigned)(t + 2) * kstep; const rsrc_t rA2 = (Sched::TWO && last) ? rAn : rAc, rB2 = (Sched::TWO && last) ? rBn : rBc;
;             const unsigned a3 = a2 + kstep, b3 = b2 + kstep;
;             if (last && has_next) S.a_ready(nxt);
;             if constexpr (SP2) {
;             PG8_LDB(B0, 0, 0); PG8_LDB(B1, 0, 1); PG8_SCHED; PG8_LDA(At, 0, 0); PG8_STAGE(PG8_SA(1, 1), rAc, a1 + hstep, voffA);
;             PG8_WAIT_V(8); PG8_WAIT_L(0); PG8_BAR; PG8_MMA(0, 0, At, B0); PG8_MMA(0, 1, At, B1); PG8_BAR; PG8_SCHED;
;             PG8_LDA(At, 0, 1); PG8_STAGE(PG8_SB(0, 0), rB2, b2, voffB); PG8_STAGE(PG8_SB(0, 1), rB2, b2 + hstep, voffB); PG8_STAGE(PG8_SA(0, 0), rA2, a2, voffA);
;             PG8_WAIT_V(8); PG8_WAIT_L(0); PG8_BAR; PG8_MMA(1, 0, At, B0); PG8_MMA(1, 1, At, B1); PG8_BAR; PG8_SCHED;
;             PG8_LDB(B0, 1, 0); PG8_LDB(B1, 1, 1); PG8_SCHED; PG8_LDA(At, 1, 0); PG8_STAGE(PG8_SA(0, 1), rA2, a2 + hstep, voffA);
;             PG8_WAIT_V(8); PG8_WAIT_L(0); PG8_BAR; PG8_MMA(0, 0, At, B0); PG8_MMA(0, 1, At, B1); PG8_BAR; PG8_SCHED;
.LBB0_1852:
	s_mul_i32 s61, s60, 0xe0000
	s_andn2_b64 vcc, exec, s[14:15]
	s_mul_i32 s62, s59, 0xe0000
	s_cbranch_vccnz .LBB0_1856
	s_and_b64 s[6:7], s[18:19], exec
	s_waitcnt vmcnt(37)
	s_waitcnt vmcnt(36)
	s_waitcnt vmcnt(35)
	s_waitcnt vmcnt(32)
	s_waitcnt vmcnt(31)
	s_waitcnt vmcnt(28)
	s_waitcnt vmcnt(27)
	s_waitcnt vmcnt(24)
	s_waitcnt vmcnt(23)
	s_waitcnt vmcnt(22)
	v_mov_b32_e32 v223, 0xff61b1e6
	v_mov_b32_e32 v222, 1
	v_mov_b32_e32 v169, v233
	v_mov_b32_e32 v168, 0x358637bd
	s_cselect_b32 s21, s61, s55
	s_cselect_b32 s63, s62, s54
	s_add_i32 s65, s55, 0x80
	s_add_i32 s66, s54, 0x100
	s_mov_b32 s67, 0
	v_add_u32_e32 v140, 0x10000, v176
	v_add_u32_e32 v156, 0x14000, v176
	ds_read_b128 v[128:131], v140
	ds_read_b128 v[132:135], v140 offset:1024
	ds_read_b128 v[136:139], v140 offset:2048
	ds_read_b128 v[140:143], v140 offset:3072
	ds_read_b128 v[144:147], v156
	ds_read_b128 v[148:151], v156 offset:1024
	ds_read_b128 v[152:155], v156 offset:2048
	ds_read_b128 v[156:159], v156 offset:3072
	s_add_i32 s6, s65, 0x80
	s_cmp_eq_u32 s52, s67
	s_cselect_b32 s68, s21, s6
	s_cselect_b32 s55, s63, s66
	s_or_b32 s54, s68, 0x80
	s_add_i32 s6, s24, s65
	s_mov_b32 m0, s53
	ds_read_b128 v[160:163], v177
	ds_read_b128 v[164:167], v177 offset:1024
	ds_read_b128 v[178:181], v177 offset:2048
	ds_read_b128 v[182:185], v177 offset:3072
	ds_read_b128 v[194:197], v177 offset:4096
	ds_read_b128 v[198:201], v177 offset:5120
	ds_read_b128 v[202:205], v177 offset:6144
	ds_read_b128 v[206:209], v177 offset:7168
	buffer_load_dwordx4 v170, s[36:39], s6 offen lds
	s_mov_b32 m0, s56
	s_nop 0
	buffer_load_dwordx4 v172, s[36:39], s6 offen lds
	s_waitcnt vmcnt(8)
	s_waitcnt lgkmcnt(0)
	s_barrier
	s_setprio 1
	v_mfma_f32_16x16x128_f8f6f4 v[124:127], v[128:135], v[160:167], 0
	v_mfma_f32_16x16x128_f8f6f4 v[120:123], v[136:143], v[160:167], 0
	v_mfma_f32_16x16x128_f8f6f4 v[108:111], v[128:135], v[178:185], 0
	v_mfma_f32_16x16x128_f8f6f4 v[104:107], v[136:143], v[178:185], 0
	v_mfma_f32_16x16x128_f8f6f4 v[186:189], v[128:135], v[194:201], 0
	v_mfma_f32_16x16x128_f8f6f4 v[190:193], v[136:143], v[194:201], 0
	v_mfma_f32_16x16x128_f8f6f4 v[210:213], v[128:135], v[202:209], 0
	v_mfma_f32_16x16x128_f8f6f4 v[214:217], v[136:143], v[202:209], 0
	v_mfma_f32_16x16x128_f8f6f4 v[116:119], v[144:151], v[160:167], 0
	v_mfma_f32_16x16x128_f8f6f4 v[112:115], v[152:159], v[160:167], 0
	v_mfma_f32_16x16x128_f8f6f4 v[100:103], v[144:151], v[178:185], 0
	v_mfma_f32_16x16x128_f8f6f4 v[96:99], v[152:159], v[178:185], 0
	v_mfma_f32_16x16x128_f8f6f4 v[160:163], v[144:151], v[194:201], 0
	v_mfma_f32_16x16x128_f8f6f4 v[164:167], v[152:159], v[194:201], 0
	v_mfma_f32_16x16x128_f8f6f4 v[178:181], v[144:151], v[202:209], 0
	v_mfma_f32_16x16x128_f8f6f4 v[182:185], v[152:159], v[202:209], 0
	s_setprio 0
	s_barrier
	s_mov_b32 m0, s26
	s_mov_b32 s6, s38
	s_mov_b32 s7, s39
	s_nop 1
	buffer_load_dwordx4 v171, s[4:7], s55 offen lds
	s_mov_b32 m0, s27
	ds_read_b128 v[64:67], v177 offset:16384
	s_add_i32 s69, s55, s24
	buffer_load_dwordx4 v173, s[4:7], s55 offen lds
	s_mov_b32 m0, s28
	ds_read_b128 v[68:71], v177 offset:17408
	buffer_load_dwordx4 v171, s[4:7], s69 offen lds
	s_mov_b32 m0, s29
	ds_read_b128 v[72:75], v177 offset:18432
	buffer_load_dwordx4 v173, s[4:7], s69 offen lds
	s_mov_b32 m0, s25
	ds_read_b128 v[76:79], v177 offset:19456
	buffer_load_dwordx4 v170, s[36:39], s68 offen lds
	s_mov_b32 m0, s30
	ds_read_b128 v[80:83], v177 offset:20480
	buffer_load_dwordx4 v172, s[36:39], s68 offen lds
	ds_read_b128 v[84:87], v177 offset:21504
	ds_read_b128 v[88:91], v177 offset:22528
	ds_read_b128 v[92:95], v177 offset:23552
	s_waitcnt vmcnt(8)
	s_waitcnt lgkmcnt(0)
	s_barrier
	s_setprio 1
	v_mfma_f32_16x16x128_f8f6f4 v[60:63], v[128:135], v[64:71], 0
	v_mfma_f32_16x16x128_f8f6f4 v[56:59], v[136:143], v[64:71], 0
	v_mfma_f32_16x16x128_f8f6f4 v[194:197], v[128:135], v[72:79], 0
	v_mfma_f32_16x16x128_f8f6f4 v[198:201], v[136:143], v[72:79], 0
	v_mfma_f32_16x16x128_f8f6f4 v[202:205], v[128:135], v[80:87], 0
	v_mfma_f32_16x16x128_f8f6f4 v[206:209], v[136:143], v[80:87], 0
	v_mfma_f32_16x16x128_f8f6f4 v[218:221], v[128:135], v[88:95], 0
	v_mfma_f32_16x16x128_f8f6f4 v[226:229], v[136:143], v[88:95], 0
	v_mfma_f32_16x16x128_f8f6f4 v[52:55], v[144:151], v[64:71], 0
	v_mfma_f32_16x16x128_f8f6f4 v[48:51], v[152:159], v[64:71], 0
	v_mfma_f32_16x16x128_f8f6f4 v[230:233], v[144:151], v[72:79], 0
	v_mfma_f32_16x16x128_f8f6f4 v[234:237], v[152:159], v[72:79], 0
	v_mfma_f32_16x16x128_f8f6f4 v[238:241], v[144:151], v[80:87], 0
	v_mfma_f32_16x16x128_f8f6f4 v[242:245], v[152:159], v[80:87], 0
	v_mfma_f32_16x16x128_f8f6f4 v[246:249], v[144:151], v[88:95], 0
	v_mfma_f32_16x16x128_f8f6f4 v[250:253], v[152:159], v[88:95], 0
	s_setprio 0
	s_barrier
	v_add_u32_e32 v8, 0x18000, v176
	s_nop 3
	ds_read_b128 v[0:3], v8
	ds_read_b128 v[4:7], v8 offset:1024
	ds_read_b128 v[16:19], v8 offset:2048
	ds_read_b128 v[20:23], v8 offset:3072
	v_add_u32_e32 v8, 0x1c000, v176
	ds_read_b128 v[128:131], v8
	ds_read_b128 v[132:135], v8 offset:1024
	ds_read_b128 v[136:139], v8 offset:2048
	ds_read_b128 v[140:143], v8 offset:3072
	s_add_i32 s68, s68, s24
	s_mov_b32 m0, s31
	ds_read_b128 v[8:11], v177 offset:32768
	ds_read_b128 v[12:15], v177 offset:33792
	ds_read_b128 v[24:27], v177 offset:34816
	ds_read_b128 v[28:31], v177 offset:35840
	ds_read_b128 v[32:35], v177 offset:36864
	ds_read_b128 v[36:39], v177 offset:37888
	ds_read_b128 v[40:43], v177 offset:38912
	ds_read_b128 v[44:47], v177 offset:39936
	buffer_load_dwordx4 v170, s[36:39], s68 offen lds
	s_mov_b32 m0, s33
	s_nop 0
	buffer_load_dwordx4 v172, s[36:39], s68 offen lds
	s_waitcnt vmcnt(8)
	s_waitcnt lgkmcnt(0)
	s_barrier
; #define PG8_STAGE(bufoff, rs_, soff_, voff) do { _Pragma("unroll") for (int _i = 0; _i < 2; ++_i) \
;         __builtin_amdgcn_raw_ptr_buffer_load_lds(rs_, (LAS void*)(lds + (bufoff) + ldsw + _i * 8192), 16, (int)(voff)[_i], (int)(soff_), 0, 0); } while (0)
; #define PG8_LDA(dst, b, h) do { _Pragma("unroll") for (int m = 0; m < 4; ++m) dst[m] = PG8_LD2(lds + PG8_SA(b, h) + aoff + m * 2048); } while (0)
; #define PG8_WAIT_V(n) asm volatile("s_waitcnt vmcnt(" #n ")" ::: "memory")
; #define PG8_WAIT_L(n) asm volatile("s_waitcnt lgkmcnt(" #n ")" ::: "memory")
; #define PG8_BAR __builtin_amdgcn_s_barrier()
; #define PG8_SCHED __builtin_amdgcn_sched_barrier(0)
; template <class Epi, class Sched, bool ALIGN_EPI = false, bool SP2 = false, bool FP8 = false>
; __device__ __forceinline__ void gemm_phase(LAS unsigned char* lds, const Gemm g, const Sched& S, const Epi& E, int wbase) {
;     ...
;             PG8_WAIT_V(8); PG8_WAIT_L(0); PG8_BAR; PG8_MMA(0, 0, At, B0); PG8_MMA(0, 1, At, B1); PG8_BAR; PG8_SCHED;
;             PG8_LDA(At, 1, 1); PG8_STAGE(PG8_SB(1, 0), rB2, b3, voffB); PG8_STAGE(PG8_SB(1, 1), rB2, b3 + hstep, voffB); PG8_STAGE(PG8_SA(1, 0), rA2, a3, voffA);
;             PG8_WAIT_V(8); PG8_WAIT_L(0); PG8_BAR; PG8_MMA(1, 0, At, B0); PG8_MMA(1, 1, At, B1); PG8_BAR; PG8_SCHED;
	s_setprio 1
	v_mfma_f32_16x16x128_f8f6f4 v[124:127], v[0:7], v[8:15], v[124:127]
	v_mfma_f32_16x16x128_f8f6f4 v[120:123], v[16:23], v[8:15], v[120:123]
	v_mfma_f32_16x16x128_f8f6f4 v[108:111], v[0:7], v[24:31], v[108:111]
	v_mfma_f32_16x16x128_f8f6f4 v[104:107], v[16:23], v[24:31], v[104:107]
	v_mfma_f32_16x16x128_f8f6f4 v[92:95], v[0:7], v[32:39], v[186:189]
	v_mfma_f32_16x16x128_f8f6f4 v[88:91], v[16:23], v[32:39], v[190:193]
	v_mfma_f32_16x16x128_f8f6f4 v[76:79], v[0:7], v[40:47], v[210:213]
	v_mfma_f32_16x16x128_f8f6f4 v[72:75], v[16:23], v[40:47], v[214:217]
	v_mfma_f32_16x16x128_f8f6f4 v[116:119], v[128:135], v[8:15], v[116:119]
	v_mfma_f32_16x16x128_f8f6f4 v[112:115], v[136:143], v[8:15], v[112:115]
	v_mfma_f32_16x16x128_f8f6f4 v[100:103], v[128:135], v[24:31], v[100:103]
	v_mfma_f32_16x16x128_f8f6f4 v[96:99], v[136:143], v[24:31], v[96:99]
	v_mfma_f32_16x16x128_f8f6f4 v[84:87], v[128:135], v[32:39], v[160:163]
	v_mfma_f32_16x16x128_f8f6f4 v[80:83], v[136:143], v[32:39], v[164:167]
	v_mfma_f32_16x16x128_f8f6f4 v[68:71], v[128:135], v[40:47], v[178:181]
	v_mfma_f32_16x16x128_f8f6f4 v[64:67], v[136:143], v[40:47], v[182:185]
	s_setprio 0
	s_barrier
	s_mov_b32 m0, s34
	s_bitset1_b32 s55, 7
	buffer_load_dwordx4 v171, s[4:7], s55 offen lds
	s_mov_b32 m0, s35
	ds_read_b128 v[32:35], v177 offset:49152
	buffer_load_dwordx4 v173, s[4:7], s55 offen lds
	s_add_i32 s55, s55, s24
	s_mov_b32 m0, s43
	ds_read_b128 v[36:39], v177 offset:50176
	buffer_load_dwordx4 v171, s[4:7], s55 offen lds
	s_mov_b32 m0, s44
	ds_read_b128 v[144:147], v177 offset:51200
	buffer_load_dwordx4 v173, s[4:7], s55 offen lds
	s_mov_b32 m0, s41
	ds_read_b128 v[148:151], v177 offset:52224
	buffer_load_dwordx4 v170, s[36:39], s54 offen lds
	s_mov_b32 m0, s42
	ds_read_b128 v[152:155], v177 offset:53248
	buffer_load_dwordx4 v172, s[36:39], s54 offen lds
	ds_read_b128 v[156:159], v177 offset:54272
	ds_read_b128 v[160:163], v177 offset:55296
	ds_read_b128 v[164:167], v177 offset:56320
	s_waitcnt vmcnt(8)
	s_waitcnt lgkmcnt(0)
	s_barrier
	s_setprio 1
	v_mfma_f32_16x16x128_f8f6f4 v[60:63], v[0:7], v[32:39], v[60:63]
	v_mfma_f32_16x16x128_f8f6f4 v[56:59], v[16:23], v[32:39], v[56:59]
	v_mfma_f32_16x16x128_f8f6f4 v[44:47], v[0:7], v[144:151], v[194:197]
	v_mfma_f32_16x16x128_f8f6f4 v[40:43], v[16:23], v[144:151], v[198:201]
	v_mfma_f32_16x16x128_f8f6f4 v[28:31], v[0:7], v[152:159], v[202:205]
	v_mfma_f32_16x16x128_f8f6f4 v[24:27], v[16:23], v[152:159], v[206:209]
	v_mfma_f32_16x16x128_f8f6f4 v[12:15], v[0:7], v[160:167], v[218:221]
	v_mfma_f32_16x16x128_f8f6f4 v[8:11], v[16:23], v[160:167], v[226:229]
	v_mfma_f32_16x16x128_f8f6f4 v[52:55], v[128:135], v[32:39], v[52:55]
	v_mfma_f32_16x16x128_f8f6f4 v[48:51], v[136:143], v[32:39], v[48:51]
	v_mfma_f32_16x16x128_f8f6f4 v[36:39], v[128:135], v[144:151], v[230:233]
	v_mfma_f32_16x16x128_f8f6f4 v[32:35], v[136:143], v[144:151], v[234:237]
	v_mfma_f32_16x16x128_f8f6f4 v[20:23], v[128:135], v[152:159], v[238:241]
	v_mfma_f32_16x16x128_f8f6f4 v[16:19], v[136:143], v[152:159], v[242:245]
	v_mfma_f32_16x16x128_f8f6f4 v[4:7], v[128:135], v[160:167], v[246:249]
	v_mfma_f32_16x16x128_f8f6f4 v[0:3], v[136:143], v[160:167], v[250:253]
	s_setprio 0
	s_barrier
	s_add_i32 s67, s67, 2
	s_addk_i32 s65, 0x100
	s_addk_i32 s66, 0x100
	s_cmp_ge_i32 s67, s47
	s_cbranch_scc0 .LBB0_1854
	s_branch .Lzp_after_1854
.LBB0_1854:
	v_add_u32_e32 v140, 0x10000, v176
	v_add_u32_e32 v156, 0x14000, v176
	ds_read_b128 v[128:131], v140
	ds_read_b128 v[132:135], v140 offset:1024
	ds_read_b128 v[136:139], v140 offset:2048
	ds_read_b128 v[140:143], v140 offset:3072
	ds_read_b128 v[144:147], v156
	ds_read_b128 v[148:151], v156 offset:1024
	ds_read_b128 v[152:155], v156 offset:2048
	ds_read_b128 v[156:159], v156 offset:3072
	s_add_i32 s6, s65, 0x80
	s_cmp_eq_u32 s52, s67
	s_cselect_b32 s68, s21, s6
	s_cselect_b32 s55, s63, s66
	s_or_b32 s54, s68, 0x80
	s_add_i32 s6, s24, s65
	s_mov_b32 m0, s53
	ds_read_b128 v[160:163], v177
	ds_read_b128 v[164:167], v177 offset:1024
	ds_read_b128 v[178:181], v177 offset:2048
	ds_read_b128 v[182:185], v177 offset:3072
	ds_read_b128 v[194:197], v177 offset:4096
	ds_read_b128 v[198:201], v177 offset:5120
	ds_read_b128 v[202:205], v177 offset:6144
	ds_read_b128 v[206:209], v177 offset:7168
	buffer_load_dwordx4 v170, s[36:39], s6 offen lds
	s_mov_b32 m0, s56
	s_nop 0
	buffer_load_dwordx4 v172, s[36:39], s6 offen lds
	s_waitcnt vmcnt(8)
	s_waitcnt lgkmcnt(0)
	s_barrier
	s_setprio 1
	v_mfma_f32_16x16x128_f8f6f4 v[124:127], v[128:135], v[160:167], v[124:127]
	v_mfma_f32_16x16x128_f8f6f4 v[120:123], v[136:143], v[160:167], v[120:123]
	v_mfma_f32_16x16x128_f8f6f4 v[108:111], v[128:135], v[178:185], v[108:111]
	v_mfma_f32_16x16x128_f8f6f4 v[104:107], v[136:143], v[178:185], v[104:107]
	v_mfma_f32_16x16x128_f8f6f4 v[186:189], v[128:135], v[194:201], v[92:95]
	v_mfma_f32_16x16x128_f8f6f4 v[190:193], v[136:143], v[194:201], v[88:91]
	v_mfma_f32_16x16x128_f8f6f4 v[210:213], v[128:135], v[202:209], v[76:79]
	v_mfma_f32_16x16x128_f8f6f4 v[214:217], v[136:143], v[202:209], v[72:75]
	v_mfma_f32_16x16x128_f8f6f4 v[116:119], v[144:151], v[160:167], v[116:119]
	v_mfma_f32_16x16x128_f8f6f4 v[112:115], v[152:159], v[160:167], v[112:115]
	v_mfma_f32_16x16x128_f8f6f4 v[100:103], v[144:151], v[178:185], v[100:103]
	v_mfma_f32_16x16x128_f8f6f4 v[96:99], v[152:159], v[178:185], v[96:99]
	v_mfma_f32_16x16x128_f8f6f4 v[160:163], v[144:151], v[194:201], v[84:87]
	v_mfma_f32_16x16x128_f8f6f4 v[164:167], v[152:159], v[194:201], v[80:83]
	v_mfma_f32_16x16x128_f8f6f4 v[178:181], v[144:151], v[202:209], v[68:71]
	v_mfma_f32_16x16x128_f8f6f4 v[182:185], v[152:159], v[202:209], v[64:67]
	s_setprio 0
	s_barrier
; #define PG8_STAGE(bufoff, rs_, soff_, voff) do { _Pragma("unroll") for (int _i = 0; _i < 2; ++_i) \
;         __builtin_amdgcn_raw_ptr_buffer_load_lds(rs_, (LAS void*)(lds + (bufoff) + ldsw + _i * 8192), 16, (int)(voff)[_i], (int)(soff_), 0, 0); } while (0)
; #define PG8_LDA(dst, b, h) do { _Pragma("unroll") for (int m = 0; m < 4; ++m) dst[m] = PG8_LD2(lds + PG8_SA(b, h) + aoff + m * 2048); } while (0)
; #define PG8_LDB(dst, b, h) do { _Pragma("unroll") for (int n = 0; n < 2; ++n) dst[n] = PG8_LD2(lds + PG8_SB(b, h) + boff + n * 2048); } while (0)
; #define PG8_WAIT_V(n) asm volatile("s_waitcnt vmcnt(" #n ")" ::: "memory")
; #define PG8_WAIT_L(n) asm volatile("s_waitcnt lgkmcnt(" #n ")" ::: "memory")
; #define PG8_BAR __builtin_amdgcn_s_barrier()
; #define PG8_SCHED __builtin_amdgcn_sched_barrier(0)
; template <class Epi, class Sched, bool ALIGN_EPI = false, bool SP2 = false, bool FP8 = false>
; __device__ __forceinline__ void gemm_phase(LAS unsigned char* lds, const Gemm g, const Sched& S, const Epi& E, int wbase) {
;     ...
;             PG8_LDA(At, 0, 1); PG8_STAGE(PG8_SB(0, 0), rB2, b2, voffB); PG8_STAGE(PG8_SB(0, 1), rB2, b2 + hstep, voffB); PG8_STAGE(PG8_SA(0, 0), rA2, a2, voffA);
;             PG8_WAIT_V(8); PG8_WAIT_L(0); PG8_BAR; PG8_MMA(1, 0, At, B0); PG8_MMA(1, 1, At, B1); PG8_BAR; PG8_SCHED;
;             PG8_LDB(B0, 1, 0); PG8_LDB(B1, 1, 1); PG8_SCHED; PG8_LDA(At, 1, 0); PG8_STAGE(PG8_SA(0, 1), rA2, a2 + hstep, voffA);
;             PG8_WAIT_V(8); PG8_WAIT_L(0); PG8_BAR; PG8_MMA(0, 0, At, B0); PG8_MMA(0, 1, At, B1); PG8_BAR; PG8_SCHED;
;             PG8_LDA(At, 1, 1); PG8_STAGE(PG8_SB(1, 0), rB2, b3, voffB); PG8_STAGE(PG8_SB(1, 1), rB2, b3 + hstep, voffB); PG8_STAGE(PG8_SA(1, 0), rA2, a3, voffA);
;             PG8_WAIT_V(8); PG8_WAIT_L(0); PG8_BAR; PG8_MMA(1, 0, At, B0); PG8_MMA(1, 1, At, B1); PG8_BAR; PG8_SCHED;
	s_mov_b32 m0, s26
	s_mov_b32 s6, s38
	s_mov_b32 s7, s39
	s_nop 1
	buffer_load_dwordx4 v171, s[4:7], s55 offen lds
	s_mov_b32 m0, s27
	ds_read_b128 v[64:67], v177 offset:16384
	s_add_i32 s69, s55, s24
	buffer_load_dwordx4 v173, s[4:7], s55 offen lds
	s_mov_b32 m0, s28
	ds_read_b128 v[68:71], v177 offset:17408
	buffer_load_dwordx4 v171, s[4:7], s69 offen lds
	s_mov_b32 m0, s29
	ds_read_b128 v[72:75], v177 offset:18432
	buffer_load_dwordx4 v173, s[4:7], s69 offen lds
	s_mov_b32 m0, s25
	ds_read_b128 v[76:79], v177 offset:19456
	buffer_load_dwordx4 v170, s[36:39], s68 offen lds
	s_mov_b32 m0, s30
	ds_read_b128 v[80:83], v177 offset:20480
	buffer_load_dwordx4 v172, s[36:39], s68 offen lds
	ds_read_b128 v[84:87], v177 offset:21504
	ds_read_b128 v[88:91], v177 offset:22528
	ds_read_b128 v[92:95], v177 offset:23552
	s_waitcnt vmcnt(8)
	s_waitcnt lgkmcnt(0)
	s_barrier
	s_setprio 1
	v_mfma_f32_16x16x128_f8f6f4 v[60:63], v[128:135], v[64:71], v[60:63]
	v_mfma_f32_16x16x128_f8f6f4 v[56:59], v[136:143], v[64:71], v[56:59]
	v_mfma_f32_16x16x128_f8f6f4 v[194:197], v[128:135], v[72:79], v[44:47]
	v_mfma_f32_16x16x128_f8f6f4 v[198:201], v[136:143], v[72:79], v[40:43]
	v_mfma_f32_16x16x128_f8f6f4 v[202:205], v[128:135], v[80:87], v[28:31]
	v_mfma_f32_16x16x128_f8f6f4 v[206:209], v[136:143], v[80:87], v[24:27]
	v_mfma_f32_16x16x128_f8f6f4 v[218:221], v[128:135], v[88:95], v[12:15]
	v_mfma_f32_16x16x128_f8f6f4 v[226:229], v[136:143], v[88:95], v[8:11]
	v_mfma_f32_16x16x128_f8f6f4 v[52:55], v[144:151], v[64:71], v[52:55]
	v_mfma_f32_16x16x128_f8f6f4 v[48:51], v[152:159], v[64:71], v[48:51]
	v_mfma_f32_16x16x128_f8f6f4 v[230:233], v[144:151], v[72:79], v[36:39]
	v_mfma_f32_16x16x128_f8f6f4 v[234:237], v[152:159], v[72:79], v[32:35]
	v_mfma_f32_16x16x128_f8f6f4 v[238:241], v[144:151], v[80:87], v[20:23]
	v_mfma_f32_16x16x128_f8f6f4 v[242:245], v[152:159], v[80:87], v[16:19]
	v_mfma_f32_16x16x128_f8f6f4 v[246:249], v[144:151], v[88:95], v[4:7]
	v_mfma_f32_16x16x128_f8f6f4 v[250:253], v[152:159], v[88:95], v[0:3]
	s_setprio 0
	s_barrier
	v_add_u32_e32 v8, 0x18000, v176
	s_nop 3
	ds_read_b128 v[0:3], v8
	ds_read_b128 v[4:7], v8 offset:1024
	ds_read_b128 v[16:19], v8 offset:2048
	ds_read_b128 v[20:23], v8 offset:3072
	v_add_u32_e32 v8, 0x1c000, v176
	ds_read_b128 v[128:131], v8
	ds_read_b128 v[132:135], v8 offset:1024
	ds_read_b128 v[136:139], v8 offset:2048
	ds_read_b128 v[140:143], v8 offset:3072
	s_add_i32 s68, s68, s24
	s_mov_b32 m0, s31
	ds_read_b128 v[8:11], v177 offset:32768
	ds_read_b128 v[12:15], v177 offset:33792
	ds_read_b128 v[24:27], v177 offset:34816
	ds_read_b128 v[28:31], v177 offset:35840
	ds_read_b128 v[32:35], v177 offset:36864
	ds_read_b128 v[36:39], v177 offset:37888
	ds_read_b128 v[40:43], v177 offset:38912
	ds_read_b128 v[44:47], v177 offset:39936
	buffer_load_dwordx4 v170, s[36:39], s68 offen lds
	s_mov_b32 m0, s33
	s_nop 0
	buffer_load_dwordx4 v172, s[36:39], s68 offen lds
	s_waitcnt vmcnt(8)
	s_waitcnt lgkmcnt(0)
	s_barrier
	s_setprio 1
	v_mfma_f32_16x16x128_f8f6f4 v[124:127], v[0:7], v[8:15], v[124:127]
	v_mfma_f32_16x16x128_f8f6f4 v[120:123], v[16:23], v[8:15], v[120:123]
	v_mfma_f32_16x16x128_f8f6f4 v[108:111], v[0:7], v[24:31], v[108:111]
	v_mfma_f32_16x16x128_f8f6f4 v[104:107], v[16:23], v[24:31], v[104:107]
	v_mfma_f32_16x16x128_f8f6f4 v[92:95], v[0:7], v[32:39], v[186:189]
	v_mfma_f32_16x16x128_f8f6f4 v[88:91], v[16:23], v[32:39], v[190:193]
	v_mfma_f32_16x16x128_f8f6f4 v[76:79], v[0:7], v[40:47], v[210:213]
	v_mfma_f32_16x16x128_f8f6f4 v[72:75], v[16:23], v[40:47], v[214:217]
	v_mfma_f32_16x16x128_f8f6f4 v[116:119], v[128:135], v[8:15], v[116:119]
	v_mfma_f32_16x16x128_f8f6f4 v[112:115], v[136:143], v[8:15], v[112:115]
	v_mfma_f32_16x16x128_f8f6f4 v[100:103], v[128:135], v[24:31], v[100:103]
	v_mfma_f32_16x16x128_f8f6f4 v[96:99], v[136:143], v[24:31], v[96:99]
	v_mfma_f32_16x16x128_f8f6f4 v[84:87], v[128:135], v[32:39], v[160:163]
	v_mfma_f32_16x16x128_f8f6f4 v[80:83], v[136:143], v[32:39], v[164:167]
	v_mfma_f32_16x16x128_f8f6f4 v[68:71], v[128:135], v[40:47], v[178:181]
	v_mfma_f32_16x16x128_f8f6f4 v[64:67], v[136:143], v[40:47], v[182:185]
	s_setprio 0
	s_barrier
	s_mov_b32 m0, s34
	s_bitset1_b32 s55, 7
	buffer_load_dwordx4 v171, s[4:7], s55 offen lds
	s_mov_b32 m0, s35
	ds_read_b128 v[32:35], v177 offset:49152
	buffer_load_dwordx4 v173, s[4:7], s55 offen lds
	s_add_i32 s55, s55, s24
	s_mov_b32 m0, s43
	ds_read_b128 v[36:39], v177 offset:50176
	buffer_load_dwordx4 v171, s[4:7], s55 offen lds
	s_mov_b32 m0, s44
	ds_read_b128 v[144:147], v177 offset:51200
	buffer_load_dwordx4 v173, s[4:7], s55 offen lds
	s_mov_b32 m0, s41
	ds_read_b128 v[148:151], v177 offset:52224
	buffer_load_dwordx4 v170, s[36:39], s54 offen lds
	s_mov_b32 m0, s42
	ds_read_b128 v[152:155], v177 offset:53248
	buffer_load_dwordx4 v172, s[36:39], s54 offen lds
	ds_read_b128 v[156:159], v177 offset:54272
	ds_read_b128 v[160:163], v177 offset:55296
	ds_read_b128 v[164:167], v177 offset:56320
	s_waitcnt vmcnt(8)
	s_waitcnt lgkmcnt(0)
	s_barrier
	s_setprio 1
	v_mfma_f32_16x16x128_f8f6f4 v[60:63], v[0:7], v[32:39], v[60:63]
	v_mfma_f32_16x16x128_f8f6f4 v[56:59], v[16:23], v[32:39], v[56:59]
	v_mfma_f32_16x16x128_f8f6f4 v[44:47], v[0:7], v[144:151], v[194:197]
	v_mfma_f32_16x16x128_f8f6f4 v[40:43], v[16:23], v[144:151], v[198:201]
	v_mfma_f32_16x16x128_f8f6f4 v[28:31], v[0:7], v[152:159], v[202:205]
	v_mfma_f32_16x16x128_f8f6f4 v[24:27], v[16:23], v[152:159], v[206:209]
	v_mfma_f32_16x16x128_f8f6f4 v[12:15], v[0:7], v[160:167], v[218:221]
	v_mfma_f32_16x16x128_f8f6f4 v[8:11], v[16:23], v[160:167], v[226:229]
	v_mfma_f32_16x16x128_f8f6f4 v[52:55], v[128:135], v[32:39], v[52:55]
	v_mfma_f32_16x16x128_f8f6f4 v[48:51], v[136:143], v[32:39], v[48:51]
	v_mfma_f32_16x16x128_f8f6f4 v[36:39], v[128:135], v[144:151], v[230:233]
	v_mfma_f32_16x16x128_f8f6f4 v[32:35], v[136:143], v[144:151], v[234:237]
	v_mfma_f32_16x16x128_f8f6f4 v[20:23], v[128:135], v[152:159], v[238:241]
	v_mfma_f32_16x16x128_f8f6f4 v[16:19], v[136:143], v[152:159], v[242:245]
	v_mfma_f32_16x16x128_f8f6f4 v[4:7], v[128:135], v[160:167], v[246:249]
	v_mfma_f32_16x16x128_f8f6f4 v[0:3], v[136:143], v[160:167], v[250:253]
	s_setprio 0
	s_barrier
	s_add_i32 s67, s67, 2
	s_addk_i32 s65, 0x100
	s_addk_i32 s66, 0x100
	s_cmp_ge_i32 s67, s47
	s_cbranch_scc0 .LBB0_1854

;     __device__ __forceinline__ unsigned a_off(const Unit& u, const Gemm& g) const { return (unsigned)u.pm * (unsigned)(BM * 2) * (unsigned)g.K; }
; template <class Epi, class Sched, bool ALIGN_EPI = false, bool SP2 = false, bool FP8 = false>
; __device__ __forceinline__ void gemm_phase(LAS unsigned char* lds, const Gemm g, const Sched& S, const Epi& E, int wbase) {
;     ...
;         const bool has_next = S.next(ui + 1, nxt);
;         const unsigned nA = has_next ? S.a_off(nxt, g) : cA, nB = has_next ? S.b_off(nxt, g) : cB;
;         const rsrc_t rAn = (Sched::TWO && has_next) ? (nxt.part ? rA1 : rA0) : rAc, rBn = (Sched::TWO && has_next) ? (nxt.part ? rB1 : rB0) : rBc;
;         float pre_[8] = {0.f, 0.f, 0.f, 0.f, 0.f, 0.f, 0.f, 0.f};
;         if constexpr (Epi::HAS_PRE) E.pre_load(pre_, cur, wr);
;         for (int t = 0; t < nt; t += 2) {
;             const bool last = (t == nt - 2);
;             const unsigned a1 = cA + (unsigned)(t + 1) * kstep;
;             const unsigned a2 = last ? nA : cA + (unsigned)(t + 2) * kstep, b2 = last ? nB : cB + (unsigned)(t + 2) * kstep; const rsrc_t rA2 = (Sched::TWO && last) ? rAn : rAc, rB2 = (Sched::TWO && last) ? rBn : rBc;
;             const unsigned a3 = a2 + kstep, b3 = b2 + kstep;
;             if (last && has_next) S.a_ready(nxt);
;             if constexpr (SP2) {
;             PG8_LDB(B0, 0, 0); PG8_LDB(B1, 0, 1); PG8_SCHED; PG8_LDA(At, 0, 0); PG8_STAGE(PG8_SA(1, 1), rAc, a1 + hstep, voffA);
;             PG8_WAIT_V(8); PG8_WAIT_L(0); PG8_BAR; PG8_MMA(0, 0, At, B0); PG8_MMA(0, 1, At, B1); PG8_BAR; PG8_SCHED;
;             PG8_LDA(At, 0, 1); PG8_STAGE(PG8_SB(0, 0), rB2, b2, voffB); PG8_STAGE(PG8_SB(0, 1), rB2, b2 + hstep, voffB); PG8_STAGE(PG8_SA(0, 0), rA2, a2, voffA);
;             PG8_WAIT_V(8); PG8_WAIT_L(0); PG8_BAR; PG8_MMA(1, 0, At, B0); PG8_MMA(1, 1, At, B1); PG8_BAR; PG8_SCHED;
;             PG8_LDB(B0, 1, 0); PG8_LDB(B1, 1, 1); PG8_SCHED; PG8_LDA(At, 1, 0); PG8_STAGE(PG8_SA(0, 1), rA2, a2 + hstep, voffA);
;             PG8_WAIT_V(8); PG8_WAIT_L(0); PG8_BAR; PG8_MMA(0, 0, At, B0); PG8_MMA(0, 1, At, B1); PG8_BAR; PG8_SCHED;
;             PG8_LDA(At, 1, 1); PG8_STAGE(PG8_SB(1, 0), rB2, b3, voffB); PG8_STAGE(PG8_SB(1, 1), rB2, b3 + hstep, voffB); PG8_STAGE(PG8_SA(1, 0), rA2, a3, voffA);
;             PG8_WAIT_V(8); PG8_WAIT_L(0); PG8_BAR; PG8_MMA(1, 0, At, B0); PG8_MMA(1, 1, At, B1); PG8_BAR; PG8_SCHED;
.LBB0_1942:
	s_mov_b32 s68, s94
	s_lshl_b32 s85, s84, 19
	s_andn2_b64 vcc, exec, s[22:23]
	s_lshl_b32 s94, s83, 19
	s_cbranch_vccnz .LBB0_1966
	s_and_b64 s[6:7], s[26:27], exec
	s_waitcnt vmcnt(37)
	s_waitcnt vmcnt(36)
	s_waitcnt vmcnt(35)
	s_waitcnt vmcnt(32)
	s_waitcnt vmcnt(31)
	s_waitcnt vmcnt(28)
	s_waitcnt vmcnt(27)
	s_waitcnt vmcnt(24)
	s_waitcnt vmcnt(23)
	s_cselect_b32 s29, s85, s55
	s_cselect_b32 s60, s94, s54
	s_add_i32 s61, s55, 0x80
	s_add_i32 s62, s54, 0x100
	s_mov_b32 s63, 0
	s_waitcnt vmcnt(0)
	v_add_u32_e32 v136, 0x10000, v174
	v_add_u32_e32 v156, 0x14000, v174
	ds_read_b128 v[120:123], v136
	ds_read_b128 v[124:127], v136 offset:1024
	ds_read_b128 v[132:135], v136 offset:2048
	ds_read_b128 v[136:139], v136 offset:3072
	ds_read_b128 v[144:147], v156
	ds_read_b128 v[148:151], v156 offset:1024
	ds_read_b128 v[152:155], v156 offset:2048
	ds_read_b128 v[156:159], v156 offset:3072
	s_add_i32 s6, s61, 0x80
	s_cmp_eq_u32 s77, s63
	s_cselect_b32 s66, s29, s6
	s_cselect_b32 s55, s60, s62
	s_or_b32 s54, s66, 0x80
	s_add_i32 s6, s33, s61
	s_mov_b32 m0, s79
	ds_read_b128 v[160:163], v175
	ds_read_b128 v[164:167], v175 offset:1024
	ds_read_b128 v[176:179], v175 offset:2048
	ds_read_b128 v[180:183], v175 offset:3072
	ds_read_b128 v[184:187], v175 offset:4096
	ds_read_b128 v[188:191], v175 offset:5120
	ds_read_b128 v[192:195], v175 offset:6144
	ds_read_b128 v[196:199], v175 offset:7168
	buffer_load_dwordx4 v168, s[36:39], s6 offen lds
	s_mov_b32 m0, s82
	s_nop 0
	buffer_load_dwordx4 v170, s[36:39], s6 offen lds
	s_waitcnt vmcnt(8)
	s_waitcnt lgkmcnt(0)
	s_barrier
	s_setprio 1
	v_mfma_f32_16x16x32_bf16 v[140:143], v[120:123], v[160:163], 0
	v_mfma_f32_16x16x32_bf16 v[128:131], v[132:135], v[160:163], 0
	v_mfma_f32_16x16x32_bf16 v[108:111], v[120:123], v[176:179], 0
	v_mfma_f32_16x16x32_bf16 v[104:107], v[132:135], v[176:179], 0
	v_mfma_f32_16x16x32_bf16 v[92:95], v[120:123], v[184:187], 0
	v_mfma_f32_16x16x32_bf16 v[88:91], v[132:135], v[184:187], 0
	v_mfma_f32_16x16x32_bf16 v[76:79], v[120:123], v[192:195], 0
	v_mfma_f32_16x16x32_bf16 v[72:75], v[132:135], v[192:195], 0
	v_mfma_f32_16x16x32_bf16 v[140:143], v[124:127], v[164:167], v[140:143]
	v_mfma_f32_16x16x32_bf16 v[128:131], v[136:139], v[164:167], v[128:131]
	v_mfma_f32_16x16x32_bf16 v[108:111], v[124:127], v[180:183], v[108:111]
	v_mfma_f32_16x16x32_bf16 v[104:107], v[136:139], v[180:183], v[104:107]
	v_mfma_f32_16x16x32_bf16 v[92:95], v[124:127], v[188:191], v[92:95]
	v_mfma_f32_16x16x32_bf16 v[88:91], v[136:139], v[188:191], v[88:91]
	v_mfma_f32_16x16x32_bf16 v[76:79], v[124:127], v[196:199], v[76:79]
	v_mfma_f32_16x16x32_bf16 v[72:75], v[136:139], v[196:199], v[72:75]
	v_mfma_f32_16x16x32_bf16 v[116:119], v[144:147], v[160:163], 0
	v_mfma_f32_16x16x32_bf16 v[112:115], v[152:155], v[160:163], 0
	v_mfma_f32_16x16x32_bf16 v[100:103], v[144:147], v[176:179], 0
	v_mfma_f32_16x16x32_bf16 v[96:99], v[152:155], v[176:179], 0
	v_mfma_f32_16x16x32_bf16 v[84:87], v[144:147], v[184:187], 0
	v_mfma_f32_16x16x32_bf16 v[80:83], v[152:155], v[184:187], 0
	v_mfma_f32_16x16x32_bf16 v[68:71], v[144:147], v[192:195], 0
	v_mfma_f32_16x16x32_bf16 v[64:67], v[152:155], v[192:195], 0
	v_mfma_f32_16x16x32_bf16 v[116:119], v[148:151], v[164:167], v[116:119]
	v_mfma_f32_16x16x32_bf16 v[112:115], v[156:159], v[164:167], v[112:115]
	v_mfma_f32_16x16x32_bf16 v[100:103], v[148:151], v[180:183], v[100:103]
	v_mfma_f32_16x16x32_bf16 v[96:99], v[156:159], v[180:183], v[96:99]
	v_mfma_f32_16x16x32_bf16 v[84:87], v[148:151], v[188:191], v[84:87]
	v_mfma_f32_16x16x32_bf16 v[80:83], v[156:159], v[188:191], v[80:83]
	v_mfma_f32_16x16x32_bf16 v[68:71], v[148:151], v[196:199], v[68:71]
	v_mfma_f32_16x16x32_bf16 v[64:67], v[156:159], v[196:199], v[64:67]
	s_setprio 0
	s_barrier
	s_mov_b32 m0, s35
	s_mov_b32 s6, s38
	s_mov_b32 s7, s39
	buffer_load_dwordx4 v169, s[4:7], s55 offen lds
	s_mov_b32 m0, s41
	ds_read_b128 v[160:163], v175 offset:16384
	s_add_i32 s67, s55, s33
	buffer_load_dwordx4 v171, s[4:7], s55 offen lds
	s_mov_b32 m0, s42
	ds_read_b128 v[164:167], v175 offset:17408
	buffer_load_dwordx4 v169, s[4:7], s67 offen lds
	s_mov_b32 m0, s43
	ds_read_b128 v[176:179], v175 offset:18432
	buffer_load_dwordx4 v171, s[4:7], s67 offen lds
	s_mov_b32 m0, s34
	ds_read_b128 v[180:183], v175 offset:19456
	buffer_load_dwordx4 v168, s[36:39], s66 offen lds
	s_mov_b32 m0, s44
	ds_read_b128 v[184:187], v175 offset:20480
	buffer_load_dwordx4 v170, s[36:39], s66 offen lds
	ds_read_b128 v[188:191], v175 offset:21504
	ds_read_b128 v[192:195], v175 offset:22528
	ds_read_b128 v[196:199], v175 offset:23552
	s_waitcnt vmcnt(8)
	s_waitcnt lgkmcnt(0)
	s_barrier
; #define PG8_STAGE(bufoff, rs_, soff_, voff) do { _Pragma("unroll") for (int _i = 0; _i < 2; ++_i) \
;         __builtin_amdgcn_raw_ptr_buffer_load_lds(rs_, (LAS void*)(lds + (bufoff) + ldsw + _i * 8192), 16, (int)(voff)[_i], (int)(soff_), 0, 0); } while (0)
; #define PG8_LDA(dst, b, h) do { _Pragma("unroll") for (int m = 0; m < 4; ++m) dst[m] = PG8_LD2(lds + PG8_SA(b, h) + aoff + m * 2048); } while (0)
; #define PG8_LDB(dst, b, h) do { _Pragma("unroll") for (int n = 0; n < 2; ++n) dst[n] = PG8_LD2(lds + PG8_SB(b, h) + boff + n * 2048); } while (0)
; #define PG8_WAIT_V(n) asm volatile("s_waitcnt vmcnt(" #n ")" ::: "memory")
; #define PG8_WAIT_L(n) asm volatile("s_waitcnt lgkmcnt(" #n ")" ::: "memory")
; #define PG8_BAR __builtin_amdgcn_s_barrier()
; #define PG8_SCHED __builtin_amdgcn_sched_barrier(0)
; template <class Epi, class Sched, bool ALIGN_EPI = false, bool SP2 = false, bool FP8 = false>
; __device__ __forceinline__ void gemm_phase(LAS unsigned char* lds, const Gemm g, const Sched& S, const Epi& E, int wbase) {
;     ...
;             PG8_WAIT_V(8); PG8_WAIT_L(0); PG8_BAR; PG8_MMA(1, 0, At, B0); PG8_MMA(1, 1, At, B1); PG8_BAR; PG8_SCHED;
;             PG8_LDB(B0, 1, 0); PG8_LDB(B1, 1, 1); PG8_SCHED; PG8_LDA(At, 1, 0); PG8_STAGE(PG8_SA(0, 1), rA2, a2 + hstep, voffA);
;             PG8_WAIT_V(8); PG8_WAIT_L(0); PG8_BAR; PG8_MMA(0, 0, At, B0); PG8_MMA(0, 1, At, B1); PG8_BAR; PG8_SCHED;
	s_setprio 1
	v_mfma_f32_16x16x32_bf16 v[60:63], v[120:123], v[160:163], 0
	v_mfma_f32_16x16x32_bf16 v[56:59], v[132:135], v[160:163], 0
	v_mfma_f32_16x16x32_bf16 v[44:47], v[120:123], v[176:179], 0
	v_mfma_f32_16x16x32_bf16 v[40:43], v[132:135], v[176:179], 0
	v_mfma_f32_16x16x32_bf16 v[28:31], v[120:123], v[184:187], 0
	v_mfma_f32_16x16x32_bf16 v[24:27], v[132:135], v[184:187], 0
	v_mfma_f32_16x16x32_bf16 v[12:15], v[120:123], v[192:195], 0
	v_mfma_f32_16x16x32_bf16 v[8:11], v[132:135], v[192:195], 0
	v_mfma_f32_16x16x32_bf16 v[60:63], v[124:127], v[164:167], v[60:63]
	v_mfma_f32_16x16x32_bf16 v[56:59], v[136:139], v[164:167], v[56:59]
	v_mfma_f32_16x16x32_bf16 v[44:47], v[124:127], v[180:183], v[44:47]
	v_mfma_f32_16x16x32_bf16 v[40:43], v[136:139], v[180:183], v[40:43]
	v_mfma_f32_16x16x32_bf16 v[28:31], v[124:127], v[188:191], v[28:31]
	v_mfma_f32_16x16x32_bf16 v[24:27], v[136:139], v[188:191], v[24:27]
	v_mfma_f32_16x16x32_bf16 v[12:15], v[124:127], v[196:199], v[12:15]
	v_mfma_f32_16x16x32_bf16 v[8:11], v[136:139], v[196:199], v[8:11]
	v_mfma_f32_16x16x32_bf16 v[52:55], v[144:147], v[160:163], 0
	v_mfma_f32_16x16x32_bf16 v[48:51], v[152:155], v[160:163], 0
	v_mfma_f32_16x16x32_bf16 v[36:39], v[144:147], v[176:179], 0
	v_mfma_f32_16x16x32_bf16 v[32:35], v[152:155], v[176:179], 0
	v_mfma_f32_16x16x32_bf16 v[20:23], v[144:147], v[184:187], 0
	v_mfma_f32_16x16x32_bf16 v[16:19], v[152:155], v[184:187], 0
	v_mfma_f32_16x16x32_bf16 v[4:7], v[144:147], v[192:195], 0
	v_mfma_f32_16x16x32_bf16 v[0:3], v[152:155], v[192:195], 0
	v_mfma_f32_16x16x32_bf16 v[52:55], v[148:151], v[164:167], v[52:55]
	v_mfma_f32_16x16x32_bf16 v[48:51], v[156:159], v[164:167], v[48:51]
	v_mfma_f32_16x16x32_bf16 v[36:39], v[148:151], v[180:183], v[36:39]
	v_mfma_f32_16x16x32_bf16 v[32:35], v[156:159], v[180:183], v[32:35]
	v_mfma_f32_16x16x32_bf16 v[20:23], v[148:151], v[188:191], v[20:23]
	v_mfma_f32_16x16x32_bf16 v[16:19], v[156:159], v[188:191], v[16:19]
	v_mfma_f32_16x16x32_bf16 v[4:7], v[148:151], v[196:199], v[4:7]
	v_mfma_f32_16x16x32_bf16 v[0:3], v[156:159], v[196:199], v[0:3]
	s_setprio 0
	s_barrier
	v_add_u32_e32 v136, 0x18000, v174
	v_add_u32_e32 v156, 0x1c000, v174
	ds_read_b128 v[120:123], v136
	ds_read_b128 v[124:127], v136 offset:1024
	ds_read_b128 v[132:135], v136 offset:2048
	ds_read_b128 v[136:139], v136 offset:3072
	ds_read_b128 v[144:147], v156
	ds_read_b128 v[148:151], v156 offset:1024
	ds_read_b128 v[152:155], v156 offset:2048
	ds_read_b128 v[156:159], v156 offset:3072
	s_add_i32 s66, s66, s33
	s_mov_b32 m0, s45
	ds_read_b128 v[160:163], v175 offset:32768
	ds_read_b128 v[164:167], v175 offset:33792
	ds_read_b128 v[176:179], v175 offset:34816
	ds_read_b128 v[180:183], v175 offset:35840
	ds_read_b128 v[184:187], v175 offset:36864
	ds_read_b128 v[188:191], v175 offset:37888
	ds_read_b128 v[192:195], v175 offset:38912
	ds_read_b128 v[196:199], v175 offset:39936
	buffer_load_dwordx4 v168, s[36:39], s66 offen lds
	s_mov_b32 m0, s46
	s_nop 0
	buffer_load_dwordx4 v170, s[36:39], s66 offen lds
	s_waitcnt vmcnt(8)
	s_waitcnt lgkmcnt(0)
	s_barrier
	s_setprio 1
	v_mfma_f32_16x16x32_bf16 v[140:143], v[120:123], v[160:163], v[140:143]
	v_mfma_f32_16x16x32_bf16 v[128:131], v[132:135], v[160:163], v[128:131]
	v_mfma_f32_16x16x32_bf16 v[108:111], v[120:123], v[176:179], v[108:111]
	v_mfma_f32_16x16x32_bf16 v[104:107], v[132:135], v[176:179], v[104:107]
	v_mfma_f32_16x16x32_bf16 v[92:95], v[120:123], v[184:187], v[92:95]
	v_mfma_f32_16x16x32_bf16 v[88:91], v[132:135], v[184:187], v[88:91]
	v_mfma_f32_16x16x32_bf16 v[76:79], v[120:123], v[192:195], v[76:79]
	v_mfma_f32_16x16x32_bf16 v[72:75], v[132:135], v[192:195], v[72:75]
	v_mfma_f32_16x16x32_bf16 v[140:143], v[124:127], v[164:167], v[140:143]
	v_mfma_f32_16x16x32_bf16 v[128:131], v[136:139], v[164:167], v[128:131]
	v_mfma_f32_16x16x32_bf16 v[108:111], v[124:127], v[180:183], v[108:111]
	v_mfma_f32_16x16x32_bf16 v[104:107], v[136:139], v[180:183], v[104:107]
	v_mfma_f32_16x16x32_bf16 v[92:95], v[124:127], v[188:191], v[92:95]
	v_mfma_f32_16x16x32_bf16 v[88:91], v[136:139], v[188:191], v[88:91]
	v_mfma_f32_16x16x32_bf16 v[76:79], v[124:127], v[196:199], v[76:79]
	v_mfma_f32_16x16x32_bf16 v[72:75], v[136:139], v[196:199], v[72:75]
	v_mfma_f32_16x16x32_bf16 v[116:119], v[144:147], v[160:163], v[116:119]
	v_mfma_f32_16x16x32_bf16 v[112:115], v[152:155], v[160:163], v[112:115]
	v_mfma_f32_16x16x32_bf16 v[100:103], v[144:147], v[176:179], v[100:103]
	v_mfma_f32_16x16x32_bf16 v[96:99], v[152:155], v[176:179], v[96:99]
	v_mfma_f32_16x16x32_bf16 v[84:87], v[144:147], v[184:187], v[84:87]
	v_mfma_f32_16x16x32_bf16 v[80:83], v[152:155], v[184:187], v[80:83]
	v_mfma_f32_16x16x32_bf16 v[68:71], v[144:147], v[192:195], v[68:71]
	v_mfma_f32_16x16x32_bf16 v[64:67], v[152:155], v[192:195], v[64:67]
	v_mfma_f32_16x16x32_bf16 v[116:119], v[148:151], v[164:167], v[116:119]
	v_mfma_f32_16x16x32_bf16 v[112:115], v[156:159], v[164:167], v[112:115]
	v_mfma_f32_16x16x32_bf16 v[100:103], v[148:151], v[180:183], v[100:103]
	v_mfma_f32_16x16x32_bf16 v[96:99], v[156:159], v[180:183], v[96:99]
	v_mfma_f32_16x16x32_bf16 v[84:87], v[148:151], v[188:191], v[84:87]
	v_mfma_f32_16x16x32_bf16 v[80:83], v[156:159], v[188:191], v[80:83]
	v_mfma_f32_16x16x32_bf16 v[68:71], v[148:151], v[196:199], v[68:71]
	v_mfma_f32_16x16x32_bf16 v[64:67], v[156:159], v[196:199], v[64:67]
	s_setprio 0
	s_barrier
; #define PG8_STAGE(bufoff, rs_, soff_, voff) do { _Pragma("unroll") for (int _i = 0; _i < 2; ++_i) \
;         __builtin_amdgcn_raw_ptr_buffer_load_lds(rs_, (LAS void*)(lds + (bufoff) + ldsw + _i * 8192), 16, (int)(voff)[_i], (int)(soff_), 0, 0); } while (0)
; #define PG8_LDA(dst, b, h) do { _Pragma("unroll") for (int m = 0; m < 4; ++m) dst[m] = PG8_LD2(lds + PG8_SA(b, h) + aoff + m * 2048); } while (0)
; #define PG8_LDB(dst, b, h) do { _Pragma("unroll") for (int n = 0; n < 2; ++n) dst[n] = PG8_LD2(lds + PG8_SB(b, h) + boff + n * 2048); } while (0)
; #define PG8_WAIT_V(n) asm volatile("s_waitcnt vmcnt(" #n ")" ::: "memory")
; #define PG8_WAIT_L(n) asm volatile("s_waitcnt lgkmcnt(" #n ")" ::: "memory")
; #define PG8_BAR __builtin_amdgcn_s_barrier()
; #define PG8_SCHED __builtin_amdgcn_sched_barrier(0)
; template <class Epi, class Sched, bool ALIGN_EPI = false, bool SP2 = false, bool FP8 = false>
; __device__ __forceinline__ void gemm_phase(LAS unsigned char* lds, const Gemm g, const Sched& S, const Epi& E, int wbase) {
;     ...
;             if constexpr (SP2) {
;             PG8_LDB(B0, 0, 0); PG8_LDB(B1, 0, 1); PG8_SCHED; PG8_LDA(At, 0, 0); PG8_STAGE(PG8_SA(1, 1), rAc, a1 + hstep, voffA);
;             PG8_WAIT_V(8); PG8_WAIT_L(0); PG8_BAR; PG8_MMA(0, 0, At, B0); PG8_MMA(0, 1, At, B1); PG8_BAR; PG8_SCHED;
;     ...
;             PG8_LDA(At, 1, 1); PG8_STAGE(PG8_SB(1, 0), rB2, b3, voffB); PG8_STAGE(PG8_SB(1, 1), rB2, b3 + hstep, voffB); PG8_STAGE(PG8_SA(1, 0), rA2, a3, voffA);
;             PG8_WAIT_V(8); PG8_WAIT_L(0); PG8_BAR; PG8_MMA(1, 0, At, B0); PG8_MMA(1, 1, At, B1); PG8_BAR; PG8_SCHED;
	s_mov_b32 m0, s47
	s_bitset1_b32 s55, 7
	buffer_load_dwordx4 v169, s[4:7], s55 offen lds
	s_mov_b32 m0, s48
	ds_read_b128 v[160:163], v175 offset:49152
	buffer_load_dwordx4 v171, s[4:7], s55 offen lds
	s_add_i32 s55, s55, s33
	s_mov_b32 m0, s56
	ds_read_b128 v[164:167], v175 offset:50176
	buffer_load_dwordx4 v169, s[4:7], s55 offen lds
	s_mov_b32 m0, s57
	ds_read_b128 v[176:179], v175 offset:51200
	buffer_load_dwordx4 v171, s[4:7], s55 offen lds
	s_mov_b32 m0, s52
	ds_read_b128 v[180:183], v175 offset:52224
	buffer_load_dwordx4 v168, s[36:39], s54 offen lds
	s_mov_b32 m0, s53
	ds_read_b128 v[184:187], v175 offset:53248
	buffer_load_dwordx4 v170, s[36:39], s54 offen lds
	ds_read_b128 v[188:191], v175 offset:54272
	ds_read_b128 v[192:195], v175 offset:55296
	ds_read_b128 v[196:199], v175 offset:56320
	s_waitcnt vmcnt(8)
	s_waitcnt lgkmcnt(0)
	s_barrier
	s_setprio 1
	v_mfma_f32_16x16x32_bf16 v[60:63], v[120:123], v[160:163], v[60:63]
	v_mfma_f32_16x16x32_bf16 v[56:59], v[132:135], v[160:163], v[56:59]
	v_mfma_f32_16x16x32_bf16 v[44:47], v[120:123], v[176:179], v[44:47]
	v_mfma_f32_16x16x32_bf16 v[40:43], v[132:135], v[176:179], v[40:43]
	v_mfma_f32_16x16x32_bf16 v[28:31], v[120:123], v[184:187], v[28:31]
	v_mfma_f32_16x16x32_bf16 v[24:27], v[132:135], v[184:187], v[24:27]
	v_mfma_f32_16x16x32_bf16 v[12:15], v[120:123], v[192:195], v[12:15]
	v_mfma_f32_16x16x32_bf16 v[8:11], v[132:135], v[192:195], v[8:11]
	v_mfma_f32_16x16x32_bf16 v[60:63], v[124:127], v[164:167], v[60:63]
	v_mfma_f32_16x16x32_bf16 v[56:59], v[136:139], v[164:167], v[56:59]
	v_mfma_f32_16x16x32_bf16 v[44:47], v[124:127], v[180:183], v[44:47]
	v_mfma_f32_16x16x32_bf16 v[40:43], v[136:139], v[180:183], v[40:43]
	v_mfma_f32_16x16x32_bf16 v[28:31], v[124:127], v[188:191], v[28:31]
	v_mfma_f32_16x16x32_bf16 v[24:27], v[136:139], v[188:191], v[24:27]
	v_mfma_f32_16x16x32_bf16 v[12:15], v[124:127], v[196:199], v[12:15]
	v_mfma_f32_16x16x32_bf16 v[8:11], v[136:139], v[196:199], v[8:11]
	v_mfma_f32_16x16x32_bf16 v[52:55], v[144:147], v[160:163], v[52:55]
	v_mfma_f32_16x16x32_bf16 v[48:51], v[152:155], v[160:163], v[48:51]
	v_mfma_f32_16x16x32_bf16 v[36:39], v[144:147], v[176:179], v[36:39]
	v_mfma_f32_16x16x32_bf16 v[32:35], v[152:155], v[176:179], v[32:35]
	v_mfma_f32_16x16x32_bf16 v[20:23], v[144:147], v[184:187], v[20:23]
	v_mfma_f32_16x16x32_bf16 v[16:19], v[152:155], v[184:187], v[16:19]
	v_mfma_f32_16x16x32_bf16 v[4:7], v[144:147], v[192:195], v[4:7]
	v_mfma_f32_16x16x32_bf16 v[0:3], v[152:155], v[192:195], v[0:3]
	v_mfma_f32_16x16x32_bf16 v[52:55], v[148:151], v[164:167], v[52:55]
	v_mfma_f32_16x16x32_bf16 v[48:51], v[156:159], v[164:167], v[48:51]
	v_mfma_f32_16x16x32_bf16 v[36:39], v[148:151], v[180:183], v[36:39]
	v_mfma_f32_16x16x32_bf16 v[32:35], v[156:159], v[180:183], v[32:35]
	v_mfma_f32_16x16x32_bf16 v[20:23], v[148:151], v[188:191], v[20:23]
	v_mfma_f32_16x16x32_bf16 v[16:19], v[156:159], v[188:191], v[16:19]
	v_mfma_f32_16x16x32_bf16 v[4:7], v[148:151], v[196:199], v[4:7]
	v_mfma_f32_16x16x32_bf16 v[0:3], v[156:159], v[196:199], v[0:3]
	s_setprio 0
	s_barrier
	s_add_i32 s63, s63, 2
	s_addk_i32 s61, 0x100
	s_addk_i32 s62, 0x100
	s_cmp_ge_i32 s63, s65
	s_cbranch_scc0 .LBB0_1944
	s_branch .Lzp_after_1944
.LBB0_1944:
	v_add_u32_e32 v136, 0x10000, v174
	v_add_u32_e32 v156, 0x14000, v174
	ds_read_b128 v[120:123], v136
	ds_read_b128 v[124:127], v136 offset:1024
	ds_read_b128 v[132:135], v136 offset:2048
	ds_read_b128 v[136:139], v136 offset:3072
	ds_read_b128 v[144:147], v156
	ds_read_b128 v[148:151], v156 offset:1024
	ds_read_b128 v[152:155], v156 offset:2048
	ds_read_b128 v[156:159], v156 offset:3072
	s_add_i32 s6, s61, 0x80
	s_cmp_eq_u32 s77, s63
	s_cselect_b32 s66, s29, s6
	s_cselect_b32 s55, s60, s62
	s_or_b32 s54, s66, 0x80
	s_add_i32 s6, s33, s61
	s_mov_b32 m0, s79
	ds_read_b128 v[160:163], v175
	ds_read_b128 v[164:167], v175 offset:1024
	ds_read_b128 v[176:179], v175 offset:2048
	ds_read_b128 v[180:183], v175 offset:3072
	ds_read_b128 v[184:187], v175 offset:4096
	ds_read_b128 v[188:191], v175 offset:5120
	ds_read_b128 v[192:195], v175 offset:6144
	ds_read_b128 v[196:199], v175 offset:7168
	buffer_load_dwordx4 v168, s[36:39], s6 offen lds
	s_mov_b32 m0, s82
	s_nop 0
	buffer_load_dwordx4 v170, s[36:39], s6 offen lds
	s_waitcnt vmcnt(8)
	s_waitcnt lgkmcnt(0)
	s_barrier
	s_setprio 1
	v_mfma_f32_16x16x32_bf16 v[140:143], v[120:123], v[160:163], v[140:143]
	v_mfma_f32_16x16x32_bf16 v[128:131], v[132:135], v[160:163], v[128:131]
	v_mfma_f32_16x16x32_bf16 v[108:111], v[120:123], v[176:179], v[108:111]
	v_mfma_f32_16x16x32_bf16 v[104:107], v[132:135], v[176:179], v[104:107]
	v_mfma_f32_16x16x32_bf16 v[92:95], v[120:123], v[184:187], v[92:95]
	v_mfma_f32_16x16x32_bf16 v[88:91], v[132:135], v[184:187], v[88:91]
	v_mfma_f32_16x16x32_bf16 v[76:79], v[120:123], v[192:195], v[76:79]
	v_mfma_f32_16x16x32_bf16 v[72:75], v[132:135], v[192:195], v[72:75]
	v_mfma_f32_16x16x32_bf16 v[140:143], v[124:127], v[164:167], v[140:143]
	v_mfma_f32_16x16x32_bf16 v[128:131], v[136:139], v[164:167], v[128:131]
	v_mfma_f32_16x16x32_bf16 v[108:111], v[124:127], v[180:183], v[108:111]
	v_mfma_f32_16x16x32_bf16 v[104:107], v[136:139], v[180:183], v[104:107]
	v_mfma_f32_16x16x32_bf16 v[92:95], v[124:127], v[188:191], v[92:95]
	v_mfma_f32_16x16x32_bf16 v[88:91], v[136:139], v[188:191], v[88:91]
	v_mfma_f32_16x16x32_bf16 v[76:79], v[124:127], v[196:199], v[76:79]
	v_mfma_f32_16x16x32_bf16 v[72:75], v[136:139], v[196:199], v[72:75]
	v_mfma_f32_16x16x32_bf16 v[116:119], v[144:147], v[160:163], v[116:119]
	v_mfma_f32_16x16x32_bf16 v[112:115], v[152:155], v[160:163], v[112:115]
	v_mfma_f32_16x16x32_bf16 v[100:103], v[144:147], v[176:179], v[100:103]
	v_mfma_f32_16x16x32_bf16 v[96:99], v[152:155], v[176:179], v[96:99]
	v_mfma_f32_16x16x32_bf16 v[84:87], v[144:147], v[184:187], v[84:87]
	v_mfma_f32_16x16x32_bf16 v[80:83], v[152:155], v[184:187], v[80:83]
	v_mfma_f32_16x16x32_bf16 v[68:71], v[144:147], v[192:195], v[68:71]
	v_mfma_f32_16x16x32_bf16 v[64:67], v[152:155], v[192:195], v[64:67]
	v_mfma_f32_16x16x32_bf16 v[116:119], v[148:151], v[164:167], v[116:119]
	v_mfma_f32_16x16x32_bf16 v[112:115], v[156:159], v[164:167], v[112:115]
	v_mfma_f32_16x16x32_bf16 v[100:103], v[148:151], v[180:183], v[100:103]
	v_mfma_f32_16x16x32_bf16 v[96:99], v[156:159], v[180:183], v[96:99]
	v_mfma_f32_16x16x32_bf16 v[84:87], v[148:151], v[188:191], v[84:87]
	v_mfma_f32_16x16x32_bf16 v[80:83], v[156:159], v[188:191], v[80:83]
	v_mfma_f32_16x16x32_bf16 v[68:71], v[148:151], v[196:199], v[68:71]
	v_mfma_f32_16x16x32_bf16 v[64:67], v[156:159], v[196:199], v[64:67]
	s_setprio 0
	s_barrier
; #define PG8_STAGE(bufoff, rs_, soff_, voff) do { _Pragma("unroll") for (int _i = 0; _i < 2; ++_i) \
;         __builtin_amdgcn_raw_ptr_buffer_load_lds(rs_, (LAS void*)(lds + (bufoff) + ldsw + _i * 8192), 16, (int)(voff)[_i], (int)(soff_), 0, 0); } while (0)
; #define PG8_LDA(dst, b, h) do { _Pragma("unroll") for (int m = 0; m < 4; ++m) dst[m] = PG8_LD2(lds + PG8_SA(b, h) + aoff + m * 2048); } while (0)
; #define PG8_LDB(dst, b, h) do { _Pragma("unroll") for (int n = 0; n < 2; ++n) dst[n] = PG8_LD2(lds + PG8_SB(b, h) + boff + n * 2048); } while (0)
; #define PG8_WAIT_V(n) asm volatile("s_waitcnt vmcnt(" #n ")" ::: "memory")
; #define PG8_WAIT_L(n) asm volatile("s_waitcnt lgkmcnt(" #n ")" ::: "memory")
; #define PG8_BAR __builtin_amdgcn_s_barrier()
; #define PG8_SCHED __builtin_amdgcn_sched_barrier(0)
; template <class Epi, class Sched, bool ALIGN_EPI = false, bool SP2 = false, bool FP8 = false>
; __device__ __forceinline__ void gemm_phase(LAS unsigned char* lds, const Gemm g, const Sched& S, const Epi& E, int wbase) {
;     ...
;             PG8_LDA(At, 0, 1); PG8_STAGE(PG8_SB(0, 0), rB2, b2, voffB); PG8_STAGE(PG8_SB(0, 1), rB2, b2 + hstep, voffB); PG8_STAGE(PG8_SA(0, 0), rA2, a2, voffA);
;             PG8_WAIT_V(8); PG8_WAIT_L(0); PG8_BAR; PG8_MMA(1, 0, At, B0); PG8_MMA(1, 1, At, B1); PG8_BAR; PG8_SCHED;
;             PG8_LDB(B0, 1, 0); PG8_LDB(B1, 1, 1); PG8_SCHED; PG8_LDA(At, 1, 0); PG8_STAGE(PG8_SA(0, 1), rA2, a2 + hstep, voffA);
;             PG8_WAIT_V(8); PG8_WAIT_L(0); PG8_BAR; PG8_MMA(0, 0, At, B0); PG8_MMA(0, 1, At, B1); PG8_BAR; PG8_SCHED;
	s_mov_b32 m0, s35
	s_mov_b32 s6, s38
	s_mov_b32 s7, s39
	buffer_load_dwordx4 v169, s[4:7], s55 offen lds
	s_mov_b32 m0, s41
	ds_read_b128 v[160:163], v175 offset:16384
	s_add_i32 s67, s55, s33
	buffer_load_dwordx4 v171, s[4:7], s55 offen lds
	s_mov_b32 m0, s42
	ds_read_b128 v[164:167], v175 offset:17408
	buffer_load_dwordx4 v169, s[4:7], s67 offen lds
	s_mov_b32 m0, s43
	ds_read_b128 v[176:179], v175 offset:18432
	buffer_load_dwordx4 v171, s[4:7], s67 offen lds
	s_mov_b32 m0, s34
	ds_read_b128 v[180:183], v175 offset:19456
	buffer_load_dwordx4 v168, s[36:39], s66 offen lds
	s_mov_b32 m0, s44
	ds_read_b128 v[184:187], v175 offset:20480
	buffer_load_dwordx4 v170, s[36:39], s66 offen lds
	ds_read_b128 v[188:191], v175 offset:21504
	ds_read_b128 v[192:195], v175 offset:22528
	ds_read_b128 v[196:199], v175 offset:23552
	s_waitcnt vmcnt(8)
	s_waitcnt lgkmcnt(0)
	s_barrier
	s_setprio 1
	v_mfma_f32_16x16x32_bf16 v[60:63], v[120:123], v[160:163], v[60:63]
	v_mfma_f32_16x16x32_bf16 v[56:59], v[132:135], v[160:163], v[56:59]
	v_mfma_f32_16x16x32_bf16 v[44:47], v[120:123], v[176:179], v[44:47]
	v_mfma_f32_16x16x32_bf16 v[40:43], v[132:135], v[176:179], v[40:43]
	v_mfma_f32_16x16x32_bf16 v[28:31], v[120:123], v[184:187], v[28:31]
	v_mfma_f32_16x16x32_bf16 v[24:27], v[132:135], v[184:187], v[24:27]
	v_mfma_f32_16x16x32_bf16 v[12:15], v[120:123], v[192:195], v[12:15]
	v_mfma_f32_16x16x32_bf16 v[8:11], v[132:135], v[192:195], v[8:11]
	v_mfma_f32_16x16x32_bf16 v[60:63], v[124:127], v[164:167], v[60:63]
	v_mfma_f32_16x16x32_bf16 v[56:59], v[136:139], v[164:167], v[56:59]
	v_mfma_f32_16x16x32_bf16 v[44:47], v[124:127], v[180:183], v[44:47]
	v_mfma_f32_16x16x32_bf16 v[40:43], v[136:139], v[180:183], v[40:43]
	v_mfma_f32_16x16x32_bf16 v[28:31], v[124:127], v[188:191], v[28:31]
	v_mfma_f32_16x16x32_bf16 v[24:27], v[136:139], v[188:191], v[24:27]
	v_mfma_f32_16x16x32_bf16 v[12:15], v[124:127], v[196:199], v[12:15]
	v_mfma_f32_16x16x32_bf16 v[8:11], v[136:139], v[196:199], v[8:11]
	v_mfma_f32_16x16x32_bf16 v[52:55], v[144:147], v[160:163], v[52:55]
	v_mfma_f32_16x16x32_bf16 v[48:51], v[152:155], v[160:163], v[48:51]
	v_mfma_f32_16x16x32_bf16 v[36:39], v[144:147], v[176:179], v[36:39]
	v_mfma_f32_16x16x32_bf16 v[32:35], v[152:155], v[176:179], v[32:35]
	v_mfma_f32_16x16x32_bf16 v[20:23], v[144:147], v[184:187], v[20:23]
	v_mfma_f32_16x16x32_bf16 v[16:19], v[152:155], v[184:187], v[16:19]
	v_mfma_f32_16x16x32_bf16 v[4:7], v[144:147], v[192:195], v[4:7]
	v_mfma_f32_16x16x32_bf16 v[0:3], v[152:155], v[192:195], v[0:3]
	v_mfma_f32_16x16x32_bf16 v[52:55], v[148:151], v[164:167], v[52:55]
	v_mfma_f32_16x16x32_bf16 v[48:51], v[156:159], v[164:167], v[48:51]
	v_mfma_f32_16x16x32_bf16 v[36:39], v[148:151], v[180:183], v[36:39]
	v_mfma_f32_16x16x32_bf16 v[32:35], v[156:159], v[180:183], v[32:35]
	v_mfma_f32_16x16x32_bf16 v[20:23], v[148:151], v[188:191], v[20:23]
	v_mfma_f32_16x16x32_bf16 v[16:19], v[156:159], v[188:191], v[16:19]
	v_mfma_f32_16x16x32_bf16 v[4:7], v[148:151], v[196:199], v[4:7]
	v_mfma_f32_16x16x32_bf16 v[0:3], v[156:159], v[196:199], v[0:3]
	s_setprio 0
	s_barrier
	v_add_u32_e32 v136, 0x18000, v174
	v_add_u32_e32 v156, 0x1c000, v174
	ds_read_b128 v[120:123], v136
	ds_read_b128 v[124:127], v136 offset:1024
	ds_read_b128 v[132:135], v136 offset:2048
	ds_read_b128 v[136:139], v136 offset:3072
	ds_read_b128 v[144:147], v156
	ds_read_b128 v[148:151], v156 offset:1024
	ds_read_b128 v[152:155], v156 offset:2048
	ds_read_b128 v[156:159], v156 offset:3072
	s_add_i32 s66, s66, s33
	s_mov_b32 m0, s45
	ds_read_b128 v[160:163], v175 offset:32768
	ds_read_b128 v[164:167], v175 offset:33792
	ds_read_b128 v[176:179], v175 offset:34816
	ds_read_b128 v[180:183], v175 offset:35840
	ds_read_b128 v[184:187], v175 offset:36864
	ds_read_b128 v[188:191], v175 offset:37888
	ds_read_b128 v[192:195], v175 offset:38912
	ds_read_b128 v[196:199], v175 offset:39936
	buffer_load_dwordx4 v168, s[36:39], s66 offen lds
	s_mov_b32 m0, s46
	s_nop 0
	buffer_load_dwordx4 v170, s[36:39], s66 offen lds
	s_waitcnt vmcnt(8)
	s_waitcnt lgkmcnt(0)
	s_barrier
; #define PG8_STAGE(bufoff, rs_, soff_, voff) do { _Pragma("unroll") for (int _i = 0; _i < 2; ++_i) \
;         __builtin_amdgcn_raw_ptr_buffer_load_lds(rs_, (LAS void*)(lds + (bufoff) + ldsw + _i * 8192), 16, (int)(voff)[_i], (int)(soff_), 0, 0); } while (0)
; #define PG8_LDA(dst, b, h) do { _Pragma("unroll") for (int m = 0; m < 4; ++m) dst[m] = PG8_LD2(lds + PG8_SA(b, h) + aoff + m * 2048); } while (0)
; #define PG8_WAIT_V(n) asm volatile("s_waitcnt vmcnt(" #n ")" ::: "memory")
; #define PG8_WAIT_L(n) asm volatile("s_waitcnt lgkmcnt(" #n ")" ::: "memory")
; #define PG8_BAR __builtin_amdgcn_s_barrier()
; #define PG8_SCHED __builtin_amdgcn_sched_barrier(0)
; template <class Epi, class Sched, bool ALIGN_EPI = false, bool SP2 = false, bool FP8 = false>
; __device__ __forceinline__ void gemm_phase(LAS unsigned char* lds, const Gemm g, const Sched& S, const Epi& E, int wbase) {
;     ...
;         for (int t = 0; t < nt; t += 2) {
;     ...
;             PG8_WAIT_V(8); PG8_WAIT_L(0); PG8_BAR; PG8_MMA(0, 0, At, B0); PG8_MMA(0, 1, At, B1); PG8_BAR; PG8_SCHED;
;             PG8_LDA(At, 1, 1); PG8_STAGE(PG8_SB(1, 0), rB2, b3, voffB); PG8_STAGE(PG8_SB(1, 1), rB2, b3 + hstep, voffB); PG8_STAGE(PG8_SA(1, 0), rA2, a3, voffA);
;             PG8_WAIT_V(8); PG8_WAIT_L(0); PG8_BAR; PG8_MMA(1, 0, At, B0); PG8_MMA(1, 1, At, B1); PG8_BAR; PG8_SCHED;
	s_setprio 1
	v_mfma_f32_16x16x32_bf16 v[140:143], v[120:123], v[160:163], v[140:143]
	v_mfma_f32_16x16x32_bf16 v[128:131], v[132:135], v[160:163], v[128:131]
	v_mfma_f32_16x16x32_bf16 v[108:111], v[120:123], v[176:179], v[108:111]
	v_mfma_f32_16x16x32_bf16 v[104:107], v[132:135], v[176:179], v[104:107]
	v_mfma_f32_16x16x32_bf16 v[92:95], v[120:123], v[184:187], v[92:95]
	v_mfma_f32_16x16x32_bf16 v[88:91], v[132:135], v[184:187], v[88:91]
	v_mfma_f32_16x16x32_bf16 v[76:79], v[120:123], v[192:195], v[76:79]
	v_mfma_f32_16x16x32_bf16 v[72:75], v[132:135], v[192:195], v[72:75]
	v_mfma_f32_16x16x32_bf16 v[140:143], v[124:127], v[164:167], v[140:143]
	v_mfma_f32_16x16x32_bf16 v[128:131], v[136:139], v[164:167], v[128:131]
	v_mfma_f32_16x16x32_bf16 v[108:111], v[124:127], v[180:183], v[108:111]
	v_mfma_f32_16x16x32_bf16 v[104:107], v[136:139], v[180:183], v[104:107]
	v_mfma_f32_16x16x32_bf16 v[92:95], v[124:127], v[188:191], v[92:95]
	v_mfma_f32_16x16x32_bf16 v[88:91], v[136:139], v[188:191], v[88:91]
	v_mfma_f32_16x16x32_bf16 v[76:79], v[124:127], v[196:199], v[76:79]
	v_mfma_f32_16x16x32_bf16 v[72:75], v[136:139], v[196:199], v[72:75]
	v_mfma_f32_16x16x32_bf16 v[116:119], v[144:147], v[160:163], v[116:119]
	v_mfma_f32_16x16x32_bf16 v[112:115], v[152:155], v[160:163], v[112:115]
	v_mfma_f32_16x16x32_bf16 v[100:103], v[144:147], v[176:179], v[100:103]
	v_mfma_f32_16x16x32_bf16 v[96:99], v[152:155], v[176:179], v[96:99]
	v_mfma_f32_16x16x32_bf16 v[84:87], v[144:147], v[184:187], v[84:87]
	v_mfma_f32_16x16x32_bf16 v[80:83], v[152:155], v[184:187], v[80:83]
	v_mfma_f32_16x16x32_bf16 v[68:71], v[144:147], v[192:195], v[68:71]
	v_mfma_f32_16x16x32_bf16 v[64:67], v[152:155], v[192:195], v[64:67]
	v_mfma_f32_16x16x32_bf16 v[116:119], v[148:151], v[164:167], v[116:119]
	v_mfma_f32_16x16x32_bf16 v[112:115], v[156:159], v[164:167], v[112:115]
	v_mfma_f32_16x16x32_bf16 v[100:103], v[148:151], v[180:183], v[100:103]
	v_mfma_f32_16x16x32_bf16 v[96:99], v[156:159], v[180:183], v[96:99]
	v_mfma_f32_16x16x32_bf16 v[84:87], v[148:151], v[188:191], v[84:87]
	v_mfma_f32_16x16x32_bf16 v[80:83], v[156:159], v[188:191], v[80:83]
	v_mfma_f32_16x16x32_bf16 v[68:71], v[148:151], v[196:199], v[68:71]
	v_mfma_f32_16x16x32_bf16 v[64:67], v[156:159], v[196:199], v[64:67]
	s_setprio 0
	s_barrier
	s_mov_b32 m0, s47
	s_bitset1_b32 s55, 7
	buffer_load_dwordx4 v169, s[4:7], s55 offen lds
	s_mov_b32 m0, s48
	ds_read_b128 v[160:163], v175 offset:49152
	buffer_load_dwordx4 v171, s[4:7], s55 offen lds
	s_add_i32 s55, s55, s33
	s_mov_b32 m0, s56
	ds_read_b128 v[164:167], v175 offset:50176
	buffer_load_dwordx4 v169, s[4:7], s55 offen lds
	s_mov_b32 m0, s57
	ds_read_b128 v[176:179], v175 offset:51200
	buffer_load_dwordx4 v171, s[4:7], s55 offen lds
	s_mov_b32 m0, s52
	ds_read_b128 v[180:183], v175 offset:52224
	buffer_load_dwordx4 v168, s[36:39], s54 offen lds
	s_mov_b32 m0, s53
	ds_read_b128 v[184:187], v175 offset:53248
	buffer_load_dwordx4 v170, s[36:39], s54 offen lds
	ds_read_b128 v[188:191], v175 offset:54272
	ds_read_b128 v[192:195], v175 offset:55296
	ds_read_b128 v[196:199], v175 offset:56320
	s_waitcnt vmcnt(8)
	s_waitcnt lgkmcnt(0)
	s_barrier
	s_setprio 1
	v_mfma_f32_16x16x32_bf16 v[60:63], v[120:123], v[160:163], v[60:63]
	v_mfma_f32_16x16x32_bf16 v[56:59], v[132:135], v[160:163], v[56:59]
	v_mfma_f32_16x16x32_bf16 v[44:47], v[120:123], v[176:179], v[44:47]
	v_mfma_f32_16x16x32_bf16 v[40:43], v[132:135], v[176:179], v[40:43]
	v_mfma_f32_16x16x32_bf16 v[28:31], v[120:123], v[184:187], v[28:31]
	v_mfma_f32_16x16x32_bf16 v[24:27], v[132:135], v[184:187], v[24:27]
	v_mfma_f32_16x16x32_bf16 v[12:15], v[120:123], v[192:195], v[12:15]
	v_mfma_f32_16x16x32_bf16 v[8:11], v[132:135], v[192:195], v[8:11]
	v_mfma_f32_16x16x32_bf16 v[60:63], v[124:127], v[164:167], v[60:63]
	v_mfma_f32_16x16x32_bf16 v[56:59], v[136:139], v[164:167], v[56:59]
	v_mfma_f32_16x16x32_bf16 v[44:47], v[124:127], v[180:183], v[44:47]
	v_mfma_f32_16x16x32_bf16 v[40:43], v[136:139], v[180:183], v[40:43]
	v_mfma_f32_16x16x32_bf16 v[28:31], v[124:127], v[188:191], v[28:31]
	v_mfma_f32_16x16x32_bf16 v[24:27], v[136:139], v[188:191], v[24:27]
	v_mfma_f32_16x16x32_bf16 v[12:15], v[124:127], v[196:199], v[12:15]
	v_mfma_f32_16x16x32_bf16 v[8:11], v[136:139], v[196:199], v[8:11]
	v_mfma_f32_16x16x32_bf16 v[52:55], v[144:147], v[160:163], v[52:55]
	v_mfma_f32_16x16x32_bf16 v[48:51], v[152:155], v[160:163], v[48:51]
	v_mfma_f32_16x16x32_bf16 v[36:39], v[144:147], v[176:179], v[36:39]
	v_mfma_f32_16x16x32_bf16 v[32:35], v[152:155], v[176:179], v[32:35]
	v_mfma_f32_16x16x32_bf16 v[20:23], v[144:147], v[184:187], v[20:23]
	v_mfma_f32_16x16x32_bf16 v[16:19], v[152:155], v[184:187], v[16:19]
	v_mfma_f32_16x16x32_bf16 v[4:7], v[144:147], v[192:195], v[4:7]
	v_mfma_f32_16x16x32_bf16 v[0:3], v[152:155], v[192:195], v[0:3]
	v_mfma_f32_16x16x32_bf16 v[52:55], v[148:151], v[164:167], v[52:55]
	v_mfma_f32_16x16x32_bf16 v[48:51], v[156:159], v[164:167], v[48:51]
	v_mfma_f32_16x16x32_bf16 v[36:39], v[148:151], v[180:183], v[36:39]
	v_mfma_f32_16x16x32_bf16 v[32:35], v[156:159], v[180:183], v[32:35]
	v_mfma_f32_16x16x32_bf16 v[20:23], v[148:151], v[188:191], v[20:23]
	v_mfma_f32_16x16x32_bf16 v[16:19], v[156:159], v[188:191], v[16:19]
	v_mfma_f32_16x16x32_bf16 v[4:7], v[148:151], v[196:199], v[4:7]
	v_mfma_f32_16x16x32_bf16 v[0:3], v[156:159], v[196:199], v[0:3]
	s_setprio 0
	s_barrier
	s_add_i32 s63, s63, 2
	s_addk_i32 s61, 0x100
	s_addk_i32 s62, 0x100
	s_cmp_ge_i32 s63, s65
	s_cbranch_scc0 .LBB0_1944

;     __device__ __forceinline__ unsigned a_off(const Unit& u, const Gemm& g) const { return (unsigned)u.pm * (unsigned)(BM * 2) * (unsigned)g.K; }
;     __device__ __forceinline__ unsigned b_off(const Unit& u, const Gemm& g) const { return (unsigned)u.pn * (unsigned)(BM * 2) * (unsigned)g.K; }
;     __device__ __forceinline__ bool next(int i, Unit& u) const { return so.next(i, u); }
; template <class Epi, class Sched, bool ALIGN_EPI = false, bool SP2 = false, bool FP8 = false>
; __device__ __forceinline__ void gemm_phase(LAS unsigned char* lds, const Gemm g, const Sched& S, const Epi& E, int wbase) {
;     ...
;         const bool has_next = S.next(ui + 1, nxt);
;         const unsigned nA = has_next ? S.a_off(nxt, g) : cA, nB = has_next ? S.b_off(nxt, g) : cB;
;         const rsrc_t rAn = (Sched::TWO && has_next) ? (nxt.part ? rA1 : rA0) : rAc, rBn = (Sched::TWO && has_next) ? (nxt.part ? rB1 : rB0) : rBc;
;         float pre_[8] = {0.f, 0.f, 0.f, 0.f, 0.f, 0.f, 0.f, 0.f};
;         if constexpr (Epi::HAS_PRE) E.pre_load(pre_, cur, wr);
;         for (int t = 0; t < nt; t += 2) {
;             const bool last = (t == nt - 2);
;             const unsigned a1 = cA + (unsigned)(t + 1) * kstep;
;             const unsigned a2 = last ? nA : cA + (unsigned)(t + 2) * kstep, b2 = last ? nB : cB + (unsigned)(t + 2) * kstep; const rsrc_t rA2 = (Sched::TWO && last) ? rAn : rAc, rB2 = (Sched::TWO && last) ? rBn : rBc;
;             const unsigned a3 = a2 + kstep, b3 = b2 + kstep;
;             if (last && has_next) S.a_ready(nxt);
;             if constexpr (SP2) {
;             PG8_LDB(B0, 0, 0); PG8_LDB(B1, 0, 1); PG8_SCHED; PG8_LDA(At, 0, 0); PG8_STAGE(PG8_SA(1, 1), rAc, a1 + hstep, voffA);
;             PG8_WAIT_V(8); PG8_WAIT_L(0); PG8_BAR; PG8_MMA(0, 0, At, B0); PG8_MMA(0, 1, At, B1); PG8_BAR; PG8_SCHED;
;             PG8_LDA(At, 0, 1); PG8_STAGE(PG8_SB(0, 0), rB2, b2, voffB); PG8_STAGE(PG8_SB(0, 1), rB2, b2 + hstep, voffB); PG8_STAGE(PG8_SA(0, 0), rA2, a2, voffA);
;             PG8_WAIT_V(8); PG8_WAIT_L(0); PG8_BAR; PG8_MMA(1, 0, At, B0); PG8_MMA(1, 1, At, B1); PG8_BAR; PG8_SCHED;
;             PG8_LDB(B0, 1, 0); PG8_LDB(B1, 1, 1); PG8_SCHED; PG8_LDA(At, 1, 0); PG8_STAGE(PG8_SA(0, 1), rA2, a2 + hstep, voffA);
;             PG8_WAIT_V(8); PG8_WAIT_L(0); PG8_BAR; PG8_MMA(0, 0, At, B0); PG8_MMA(0, 1, At, B1); PG8_BAR; PG8_SCHED;
.LBB0_1988:
	s_lshl_b32 s95, s94, 18
	s_andn2_b64 vcc, exec, s[26:27]
	s_lshl_b32 s96, s9, 18
	s_cbranch_vccnz .LBB0_1992
	s_and_b64 s[2:3], s[34:35], exec
	s_waitcnt vmcnt(37)
	s_waitcnt vmcnt(36)
	s_waitcnt vmcnt(35)
	s_waitcnt vmcnt(32)
	s_waitcnt vmcnt(31)
	s_waitcnt vmcnt(28)
	s_waitcnt vmcnt(27)
	s_waitcnt vmcnt(24)
	s_waitcnt vmcnt(23)
	v_mov_b32_e32 v223, 0xff61b1e6
	v_mov_b32_e32 v222, 1
	v_mov_b32_e32 v173, v233
	v_mov_b32_e32 v172, 0x358637bd
	s_cselect_b32 s2, s95, s4
	s_cselect_b32 s3, s96, s5
	s_addk_i32 s4, 0x80
	s_addk_i32 s5, 0x100
	s_mov_b32 s61, 0
	s_waitcnt vmcnt(0)
	v_add_u32_e32 v136, 0x10000, v180
	v_add_u32_e32 v156, 0x14000, v180
	ds_read_b128 v[120:123], v136
	ds_read_b128 v[124:127], v136 offset:1024
	ds_read_b128 v[132:135], v136 offset:2048
	ds_read_b128 v[136:139], v136 offset:3072
	ds_read_b128 v[144:147], v156
	ds_read_b128 v[148:151], v156 offset:1024
	ds_read_b128 v[152:155], v156 offset:2048
	ds_read_b128 v[156:159], v156 offset:3072
	s_add_i32 s14, s4, 0x80
	s_cmp_eq_u32 s84, s61
	s_cselect_b32 s62, s2, s14
	s_cselect_b32 s55, s3, s5
	s_or_b32 s54, s62, 0x80
	s_add_i32 s14, s42, s4
	s_mov_b32 m0, s85
	ds_read_b128 v[160:163], v181
	ds_read_b128 v[164:167], v181 offset:1024
	ds_read_b128 v[182:185], v181 offset:2048
	ds_read_b128 v[186:189], v181 offset:3072
	ds_read_b128 v[194:197], v181 offset:4096
	ds_read_b128 v[198:201], v181 offset:5120
	ds_read_b128 v[202:205], v181 offset:6144
	ds_read_b128 v[206:209], v181 offset:7168
	buffer_load_dwordx4 v174, s[36:39], s14 offen lds
	s_mov_b32 m0, s8
	s_nop 0
	buffer_load_dwordx4 v176, s[36:39], s14 offen lds
	s_waitcnt vmcnt(8)
	s_waitcnt lgkmcnt(0)
	s_barrier
	s_setprio 1
	v_mfma_f32_16x16x128_f8f6f4 v[140:143], v[120:127], v[160:167], 0
	v_mfma_f32_16x16x128_f8f6f4 v[128:131], v[132:139], v[160:167], 0
	v_mfma_f32_16x16x128_f8f6f4 v[108:111], v[120:127], v[182:189], 0
	v_mfma_f32_16x16x128_f8f6f4 v[104:107], v[132:139], v[182:189], 0
	v_mfma_f32_16x16x128_f8f6f4 v[168:171], v[120:127], v[194:201], 0
	v_mfma_f32_16x16x128_f8f6f4 v[190:193], v[132:139], v[194:201], 0
	v_mfma_f32_16x16x128_f8f6f4 v[210:213], v[120:127], v[202:209], 0
	v_mfma_f32_16x16x128_f8f6f4 v[214:217], v[132:139], v[202:209], 0
	v_mfma_f32_16x16x128_f8f6f4 v[116:119], v[144:151], v[160:167], 0
	v_mfma_f32_16x16x128_f8f6f4 v[112:115], v[152:159], v[160:167], 0
	v_mfma_f32_16x16x128_f8f6f4 v[100:103], v[144:151], v[182:189], 0
	v_mfma_f32_16x16x128_f8f6f4 v[96:99], v[152:159], v[182:189], 0
	v_mfma_f32_16x16x128_f8f6f4 v[160:163], v[144:151], v[194:201], 0
	v_mfma_f32_16x16x128_f8f6f4 v[164:167], v[152:159], v[194:201], 0
	v_mfma_f32_16x16x128_f8f6f4 v[182:185], v[144:151], v[202:209], 0
	v_mfma_f32_16x16x128_f8f6f4 v[186:189], v[152:159], v[202:209], 0
	s_setprio 0
	s_barrier
	s_mov_b32 m0, s44
	s_mov_b32 s14, s38
	s_mov_b32 s15, s39
	s_nop 1
	buffer_load_dwordx4 v175, s[12:15], s55 offen lds
	s_mov_b32 m0, s45
	ds_read_b128 v[64:67], v181 offset:16384
	s_add_i32 s63, s55, s42
	buffer_load_dwordx4 v177, s[12:15], s55 offen lds
	s_mov_b32 m0, s46
	ds_read_b128 v[68:71], v181 offset:17408
	buffer_load_dwordx4 v175, s[12:15], s63 offen lds
	s_mov_b32 m0, s47
	ds_read_b128 v[72:75], v181 offset:18432
	buffer_load_dwordx4 v177, s[12:15], s63 offen lds
	s_mov_b32 m0, s43
	ds_read_b128 v[76:79], v181 offset:19456
	buffer_load_dwordx4 v174, s[36:39], s62 offen lds
	s_mov_b32 m0, s48
	ds_read_b128 v[80:83], v181 offset:20480
	buffer_load_dwordx4 v176, s[36:39], s62 offen lds
	ds_read_b128 v[84:87], v181 offset:21504
	ds_read_b128 v[88:91], v181 offset:22528
	ds_read_b128 v[92:95], v181 offset:23552
	s_waitcnt vmcnt(8)
	s_waitcnt lgkmcnt(0)
	s_barrier
	s_setprio 1
	v_mfma_f32_16x16x128_f8f6f4 v[60:63], v[120:127], v[64:71], 0
	v_mfma_f32_16x16x128_f8f6f4 v[56:59], v[132:139], v[64:71], 0
	v_mfma_f32_16x16x128_f8f6f4 v[194:197], v[120:127], v[72:79], 0
	v_mfma_f32_16x16x128_f8f6f4 v[198:201], v[132:139], v[72:79], 0
	v_mfma_f32_16x16x128_f8f6f4 v[202:205], v[120:127], v[80:87], 0
	v_mfma_f32_16x16x128_f8f6f4 v[206:209], v[132:139], v[80:87], 0
	v_mfma_f32_16x16x128_f8f6f4 v[218:221], v[120:127], v[88:95], 0
	v_mfma_f32_16x16x128_f8f6f4 v[226:229], v[132:139], v[88:95], 0
	v_mfma_f32_16x16x128_f8f6f4 v[52:55], v[144:151], v[64:71], 0
	v_mfma_f32_16x16x128_f8f6f4 v[48:51], v[152:159], v[64:71], 0
	v_mfma_f32_16x16x128_f8f6f4 v[230:233], v[144:151], v[72:79], 0
	v_mfma_f32_16x16x128_f8f6f4 v[234:237], v[152:159], v[72:79], 0
	v_mfma_f32_16x16x128_f8f6f4 v[238:241], v[144:151], v[80:87], 0
	v_mfma_f32_16x16x128_f8f6f4 v[242:245], v[152:159], v[80:87], 0
	v_mfma_f32_16x16x128_f8f6f4 v[246:249], v[144:151], v[88:95], 0
	v_mfma_f32_16x16x128_f8f6f4 v[250:253], v[152:159], v[88:95], 0
	s_setprio 0
	s_barrier
	v_add_u32_e32 v8, 0x18000, v180
	s_nop 3
	ds_read_b128 v[0:3], v8
	ds_read_b128 v[4:7], v8 offset:1024
	ds_read_b128 v[16:19], v8 offset:2048
	ds_read_b128 v[20:23], v8 offset:3072
	v_add_u32_e32 v8, 0x1c000, v180
	ds_read_b128 v[120:123], v8
	ds_read_b128 v[124:127], v8 offset:1024
	ds_read_b128 v[132:135], v8 offset:2048
	ds_read_b128 v[136:139], v8 offset:3072
	s_add_i32 s62, s62, s42
	s_mov_b32 m0, s52
	ds_read_b128 v[8:11], v181 offset:32768
	ds_read_b128 v[12:15], v181 offset:33792
	ds_read_b128 v[24:27], v181 offset:34816
	ds_read_b128 v[28:31], v181 offset:35840
	ds_read_b128 v[32:35], v181 offset:36864
	ds_read_b128 v[36:39], v181 offset:37888
	ds_read_b128 v[40:43], v181 offset:38912
	ds_read_b128 v[44:47], v181 offset:39936
	buffer_load_dwordx4 v174, s[36:39], s62 offen lds
	s_mov_b32 m0, s53
	s_nop 0
	buffer_load_dwordx4 v176, s[36:39], s62 offen lds
	s_waitcnt vmcnt(8)
	s_waitcnt lgkmcnt(0)
	s_barrier
; #define PG8_STAGE(bufoff, rs_, soff_, voff) do { _Pragma("unroll") for (int _i = 0; _i < 2; ++_i) \
;         __builtin_amdgcn_raw_ptr_buffer_load_lds(rs_, (LAS void*)(lds + (bufoff) + ldsw + _i * 8192), 16, (int)(voff)[_i], (int)(soff_), 0, 0); } while (0)
; #define PG8_LDA(dst, b, h) do { _Pragma("unroll") for (int m = 0; m < 4; ++m) dst[m] = PG8_LD2(lds + PG8_SA(b, h) + aoff + m * 2048); } while (0)
; #define PG8_LDB(dst, b, h) do { _Pragma("unroll") for (int n = 0; n < 2; ++n) dst[n] = PG8_LD2(lds + PG8_SB(b, h) + boff + n * 2048); } while (0)
; #define PG8_WAIT_V(n) asm volatile("s_waitcnt vmcnt(" #n ")" ::: "memory")
; #define PG8_WAIT_L(n) asm volatile("s_waitcnt lgkmcnt(" #n ")" ::: "memory")
; #define PG8_BAR __builtin_amdgcn_s_barrier()
; #define PG8_SCHED __builtin_amdgcn_sched_barrier(0)
; template <class Epi, class Sched, bool ALIGN_EPI = false, bool SP2 = false, bool FP8 = false>
; __device__ __forceinline__ void gemm_phase(LAS unsigned char* lds, const Gemm g, const Sched& S, const Epi& E, int wbase) {
;     ...
;             if constexpr (SP2) {
;             PG8_LDB(B0, 0, 0); PG8_LDB(B1, 0, 1); PG8_SCHED; PG8_LDA(At, 0, 0); PG8_STAGE(PG8_SA(1, 1), rAc, a1 + hstep, voffA);
;             PG8_WAIT_V(8); PG8_WAIT_L(0); PG8_BAR; PG8_MMA(0, 0, At, B0); PG8_MMA(0, 1, At, B1); PG8_BAR; PG8_SCHED;
;     ...
;             PG8_WAIT_V(8); PG8_WAIT_L(0); PG8_BAR; PG8_MMA(0, 0, At, B0); PG8_MMA(0, 1, At, B1); PG8_BAR; PG8_SCHED;
;             PG8_LDA(At, 1, 1); PG8_STAGE(PG8_SB(1, 0), rB2, b3, voffB); PG8_STAGE(PG8_SB(1, 1), rB2, b3 + hstep, voffB); PG8_STAGE(PG8_SA(1, 0), rA2, a3, voffA);
;             PG8_WAIT_V(8); PG8_WAIT_L(0); PG8_BAR; PG8_MMA(1, 0, At, B0); PG8_MMA(1, 1, At, B1); PG8_BAR; PG8_SCHED;
	s_setprio 1
	v_mfma_f32_16x16x128_f8f6f4 v[140:143], v[0:7], v[8:15], v[140:143]
	v_mfma_f32_16x16x128_f8f6f4 v[128:131], v[16:23], v[8:15], v[128:131]
	v_mfma_f32_16x16x128_f8f6f4 v[108:111], v[0:7], v[24:31], v[108:111]
	v_mfma_f32_16x16x128_f8f6f4 v[104:107], v[16:23], v[24:31], v[104:107]
	v_mfma_f32_16x16x128_f8f6f4 v[92:95], v[0:7], v[32:39], v[168:171]
	v_mfma_f32_16x16x128_f8f6f4 v[88:91], v[16:23], v[32:39], v[190:193]
	v_mfma_f32_16x16x128_f8f6f4 v[76:79], v[0:7], v[40:47], v[210:213]
	v_mfma_f32_16x16x128_f8f6f4 v[72:75], v[16:23], v[40:47], v[214:217]
	v_mfma_f32_16x16x128_f8f6f4 v[116:119], v[120:127], v[8:15], v[116:119]
	v_mfma_f32_16x16x128_f8f6f4 v[112:115], v[132:139], v[8:15], v[112:115]
	v_mfma_f32_16x16x128_f8f6f4 v[100:103], v[120:127], v[24:31], v[100:103]
	v_mfma_f32_16x16x128_f8f6f4 v[96:99], v[132:139], v[24:31], v[96:99]
	v_mfma_f32_16x16x128_f8f6f4 v[84:87], v[120:127], v[32:39], v[160:163]
	v_mfma_f32_16x16x128_f8f6f4 v[80:83], v[132:139], v[32:39], v[164:167]
	v_mfma_f32_16x16x128_f8f6f4 v[68:71], v[120:127], v[40:47], v[182:185]
	v_mfma_f32_16x16x128_f8f6f4 v[64:67], v[132:139], v[40:47], v[186:189]
	s_setprio 0
	s_barrier
	s_mov_b32 m0, s56
	s_bitset1_b32 s55, 7
	buffer_load_dwordx4 v175, s[12:15], s55 offen lds
	s_mov_b32 m0, s57
	ds_read_b128 v[32:35], v181 offset:49152
	buffer_load_dwordx4 v177, s[12:15], s55 offen lds
	s_add_i32 s55, s55, s42
	s_mov_b32 m0, s65
	ds_read_b128 v[36:39], v181 offset:50176
	buffer_load_dwordx4 v175, s[12:15], s55 offen lds
	s_mov_b32 m0, s76
	ds_read_b128 v[144:147], v181 offset:51200
	buffer_load_dwordx4 v177, s[12:15], s55 offen lds
	s_mov_b32 m0, s58
	ds_read_b128 v[148:151], v181 offset:52224
	buffer_load_dwordx4 v174, s[36:39], s54 offen lds
	s_mov_b32 m0, s59
	ds_read_b128 v[152:155], v181 offset:53248
	buffer_load_dwordx4 v176, s[36:39], s54 offen lds
	ds_read_b128 v[156:159], v181 offset:54272
	ds_read_b128 v[160:163], v181 offset:55296
	ds_read_b128 v[164:167], v181 offset:56320
	s_waitcnt vmcnt(8)
	s_waitcnt lgkmcnt(0)
	s_barrier
	s_setprio 1
	v_mfma_f32_16x16x128_f8f6f4 v[60:63], v[0:7], v[32:39], v[60:63]
	v_mfma_f32_16x16x128_f8f6f4 v[56:59], v[16:23], v[32:39], v[56:59]
	v_mfma_f32_16x16x128_f8f6f4 v[44:47], v[0:7], v[144:151], v[194:197]
	v_mfma_f32_16x16x128_f8f6f4 v[40:43], v[16:23], v[144:151], v[198:201]
	v_mfma_f32_16x16x128_f8f6f4 v[28:31], v[0:7], v[152:159], v[202:205]
	v_mfma_f32_16x16x128_f8f6f4 v[24:27], v[16:23], v[152:159], v[206:209]
	v_mfma_f32_16x16x128_f8f6f4 v[12:15], v[0:7], v[160:167], v[218:221]
	v_mfma_f32_16x16x128_f8f6f4 v[8:11], v[16:23], v[160:167], v[226:229]
	v_mfma_f32_16x16x128_f8f6f4 v[52:55], v[120:127], v[32:39], v[52:55]
	v_mfma_f32_16x16x128_f8f6f4 v[48:51], v[132:139], v[32:39], v[48:51]
	v_mfma_f32_16x16x128_f8f6f4 v[36:39], v[120:127], v[144:151], v[230:233]
	v_mfma_f32_16x16x128_f8f6f4 v[32:35], v[132:139], v[144:151], v[234:237]
	v_mfma_f32_16x16x128_f8f6f4 v[20:23], v[120:127], v[152:159], v[238:241]
	v_mfma_f32_16x16x128_f8f6f4 v[16:19], v[132:139], v[152:159], v[242:245]
	v_mfma_f32_16x16x128_f8f6f4 v[4:7], v[120:127], v[160:167], v[246:249]
	v_mfma_f32_16x16x128_f8f6f4 v[0:3], v[132:139], v[160:167], v[250:253]
	s_setprio 0
	s_barrier
	s_add_i32 s61, s61, 2
	s_addk_i32 s4, 0x100
	s_addk_i32 s5, 0x100
	s_cmp_ge_i32 s61, s82
	s_cbranch_scc0 .LBB0_1990
	s_branch .Lzp_after_1990
.LBB0_1990:
	v_add_u32_e32 v136, 0x10000, v180
	v_add_u32_e32 v156, 0x14000, v180
	ds_read_b128 v[120:123], v136
	ds_read_b128 v[124:127], v136 offset:1024
	ds_read_b128 v[132:135], v136 offset:2048
	ds_read_b128 v[136:139], v136 offset:3072
	ds_read_b128 v[144:147], v156
	ds_read_b128 v[148:151], v156 offset:1024
	ds_read_b128 v[152:155], v156 offset:2048
	ds_read_b128 v[156:159], v156 offset:3072
	s_add_i32 s14, s4, 0x80
	s_cmp_eq_u32 s84, s61
	s_cselect_b32 s62, s2, s14
	s_cselect_b32 s55, s3, s5
	s_or_b32 s54, s62, 0x80
	s_add_i32 s14, s42, s4
	s_mov_b32 m0, s85
	ds_read_b128 v[160:163], v181
	ds_read_b128 v[164:167], v181 offset:1024
	ds_read_b128 v[182:185], v181 offset:2048
	ds_read_b128 v[186:189], v181 offset:3072
	ds_read_b128 v[194:197], v181 offset:4096
	ds_read_b128 v[198:201], v181 offset:5120
	ds_read_b128 v[202:205], v181 offset:6144
	ds_read_b128 v[206:209], v181 offset:7168
	buffer_load_dwordx4 v174, s[36:39], s14 offen lds
	s_mov_b32 m0, s8
	s_nop 0
	buffer_load_dwordx4 v176, s[36:39], s14 offen lds
	s_waitcnt vmcnt(8)
	s_waitcnt lgkmcnt(0)
	s_barrier
	s_setprio 1
	v_mfma_f32_16x16x128_f8f6f4 v[140:143], v[120:127], v[160:167], v[140:143]
	v_mfma_f32_16x16x128_f8f6f4 v[128:131], v[132:139], v[160:167], v[128:131]
	v_mfma_f32_16x16x128_f8f6f4 v[108:111], v[120:127], v[182:189], v[108:111]
	v_mfma_f32_16x16x128_f8f6f4 v[104:107], v[132:139], v[182:189], v[104:107]
	v_mfma_f32_16x16x128_f8f6f4 v[168:171], v[120:127], v[194:201], v[92:95]
	v_mfma_f32_16x16x128_f8f6f4 v[190:193], v[132:139], v[194:201], v[88:91]
	v_mfma_f32_16x16x128_f8f6f4 v[210:213], v[120:127], v[202:209], v[76:79]
	v_mfma_f32_16x16x128_f8f6f4 v[214:217], v[132:139], v[202:209], v[72:75]
	v_mfma_f32_16x16x128_f8f6f4 v[116:119], v[144:151], v[160:167], v[116:119]
	v_mfma_f32_16x16x128_f8f6f4 v[112:115], v[152:159], v[160:167], v[112:115]
	v_mfma_f32_16x16x128_f8f6f4 v[100:103], v[144:151], v[182:189], v[100:103]
	v_mfma_f32_16x16x128_f8f6f4 v[96:99], v[152:159], v[182:189], v[96:99]
	v_mfma_f32_16x16x128_f8f6f4 v[160:163], v[144:151], v[194:201], v[84:87]
	v_mfma_f32_16x16x128_f8f6f4 v[164:167], v[152:159], v[194:201], v[80:83]
	v_mfma_f32_16x16x128_f8f6f4 v[182:185], v[144:151], v[202:209], v[68:71]
	v_mfma_f32_16x16x128_f8f6f4 v[186:189], v[152:159], v[202:209], v[64:67]
	s_setprio 0
	s_barrier
; #define PG8_STAGE(bufoff, rs_, soff_, voff) do { _Pragma("unroll") for (int _i = 0; _i < 2; ++_i) \
;         __builtin_amdgcn_raw_ptr_buffer_load_lds(rs_, (LAS void*)(lds + (bufoff) + ldsw + _i * 8192), 16, (int)(voff)[_i], (int)(soff_), 0, 0); } while (0)
; #define PG8_LDA(dst, b, h) do { _Pragma("unroll") for (int m = 0; m < 4; ++m) dst[m] = PG8_LD2(lds + PG8_SA(b, h) + aoff + m * 2048); } while (0)
; #define PG8_LDB(dst, b, h) do { _Pragma("unroll") for (int n = 0; n < 2; ++n) dst[n] = PG8_LD2(lds + PG8_SB(b, h) + boff + n * 2048); } while (0)
; #define PG8_WAIT_V(n) asm volatile("s_waitcnt vmcnt(" #n ")" ::: "memory")
; #define PG8_WAIT_L(n) asm volatile("s_waitcnt lgkmcnt(" #n ")" ::: "memory")
; #define PG8_BAR __builtin_amdgcn_s_barrier()
; #define PG8_SCHED __builtin_amdgcn_sched_barrier(0)
; template <class Epi, class Sched, bool ALIGN_EPI = false, bool SP2 = false, bool FP8 = false>
; __device__ __forceinline__ void gemm_phase(LAS unsigned char* lds, const Gemm g, const Sched& S, const Epi& E, int wbase) {
;     ...
;             PG8_LDA(At, 0, 1); PG8_STAGE(PG8_SB(0, 0), rB2, b2, voffB); PG8_STAGE(PG8_SB(0, 1), rB2, b2 + hstep, voffB); PG8_STAGE(PG8_SA(0, 0), rA2, a2, voffA);
;             PG8_WAIT_V(8); PG8_WAIT_L(0); PG8_BAR; PG8_MMA(1, 0, At, B0); PG8_MMA(1, 1, At, B1); PG8_BAR; PG8_SCHED;
;             PG8_LDB(B0, 1, 0); PG8_LDB(B1, 1, 1); PG8_SCHED; PG8_LDA(At, 1, 0); PG8_STAGE(PG8_SA(0, 1), rA2, a2 + hstep, voffA);
;             PG8_WAIT_V(8); PG8_WAIT_L(0); PG8_BAR; PG8_MMA(0, 0, At, B0); PG8_MMA(0, 1, At, B1); PG8_BAR; PG8_SCHED;
;             PG8_LDA(At, 1, 1); PG8_STAGE(PG8_SB(1, 0), rB2, b3, voffB); PG8_STAGE(PG8_SB(1, 1), rB2, b3 + hstep, voffB); PG8_STAGE(PG8_SA(1, 0), rA2, a3, voffA);
;             PG8_WAIT_V(8); PG8_WAIT_L(0); PG8_BAR; PG8_MMA(1, 0, At, B0); PG8_MMA(1, 1, At, B1); PG8_BAR; PG8_SCHED;
	s_mov_b32 m0, s44
	s_mov_b32 s14, s38
	s_mov_b32 s15, s39
	s_nop 1
	buffer_load_dwordx4 v175, s[12:15], s55 offen lds
	s_mov_b32 m0, s45
	ds_read_b128 v[64:67], v181 offset:16384
	s_add_i32 s63, s55, s42
	buffer_load_dwordx4 v177, s[12:15], s55 offen lds
	s_mov_b32 m0, s46
	ds_read_b128 v[68:71], v181 offset:17408
	buffer_load_dwordx4 v175, s[12:15], s63 offen lds
	s_mov_b32 m0, s47
	ds_read_b128 v[72:75], v181 offset:18432
	buffer_load_dwordx4 v177, s[12:15], s63 offen lds
	s_mov_b32 m0, s43
	ds_read_b128 v[76:79], v181 offset:19456
	buffer_load_dwordx4 v174, s[36:39], s62 offen lds
	s_mov_b32 m0, s48
	ds_read_b128 v[80:83], v181 offset:20480
	buffer_load_dwordx4 v176, s[36:39], s62 offen lds
	ds_read_b128 v[84:87], v181 offset:21504
	ds_read_b128 v[88:91], v181 offset:22528
	ds_read_b128 v[92:95], v181 offset:23552
	s_waitcnt vmcnt(8)
	s_waitcnt lgkmcnt(0)
	s_barrier
	s_setprio 1
	v_mfma_f32_16x16x128_f8f6f4 v[60:63], v[120:127], v[64:71], v[60:63]
	v_mfma_f32_16x16x128_f8f6f4 v[56:59], v[132:139], v[64:71], v[56:59]
	v_mfma_f32_16x16x128_f8f6f4 v[194:197], v[120:127], v[72:79], v[44:47]
	v_mfma_f32_16x16x128_f8f6f4 v[198:201], v[132:139], v[72:79], v[40:43]
	v_mfma_f32_16x16x128_f8f6f4 v[202:205], v[120:127], v[80:87], v[28:31]
	v_mfma_f32_16x16x128_f8f6f4 v[206:209], v[132:139], v[80:87], v[24:27]
	v_mfma_f32_16x16x128_f8f6f4 v[218:221], v[120:127], v[88:95], v[12:15]
	v_mfma_f32_16x16x128_f8f6f4 v[226:229], v[132:139], v[88:95], v[8:11]
	v_mfma_f32_16x16x128_f8f6f4 v[52:55], v[144:151], v[64:71], v[52:55]
	v_mfma_f32_16x16x128_f8f6f4 v[48:51], v[152:159], v[64:71], v[48:51]
	v_mfma_f32_16x16x128_f8f6f4 v[230:233], v[144:151], v[72:79], v[36:39]
	v_mfma_f32_16x16x128_f8f6f4 v[234:237], v[152:159], v[72:79], v[32:35]
	v_mfma_f32_16x16x128_f8f6f4 v[238:241], v[144:151], v[80:87], v[20:23]
	v_mfma_f32_16x16x128_f8f6f4 v[242:245], v[152:159], v[80:87], v[16:19]
	v_mfma_f32_16x16x128_f8f6f4 v[246:249], v[144:151], v[88:95], v[4:7]
	v_mfma_f32_16x16x128_f8f6f4 v[250:253], v[152:159], v[88:95], v[0:3]
	s_setprio 0
	s_barrier
	v_add_u32_e32 v8, 0x18000, v180
	s_nop 3
	ds_read_b128 v[0:3], v8
	ds_read_b128 v[4:7], v8 offset:1024
	ds_read_b128 v[16:19], v8 offset:2048
	ds_read_b128 v[20:23], v8 offset:3072
	v_add_u32_e32 v8, 0x1c000, v180
	ds_read_b128 v[120:123], v8
	ds_read_b128 v[124:127], v8 offset:1024
	ds_read_b128 v[132:135], v8 offset:2048
	ds_read_b128 v[136:139], v8 offset:3072
	s_add_i32 s62, s62, s42
	s_mov_b32 m0, s52
	ds_read_b128 v[8:11], v181 offset:32768
	ds_read_b128 v[12:15], v181 offset:33792
	ds_read_b128 v[24:27], v181 offset:34816
	ds_read_b128 v[28:31], v181 offset:35840
	ds_read_b128 v[32:35], v181 offset:36864
	ds_read_b128 v[36:39], v181 offset:37888
	ds_read_b128 v[40:43], v181 offset:38912
	ds_read_b128 v[44:47], v181 offset:39936
	buffer_load_dwordx4 v174, s[36:39], s62 offen lds
	s_mov_b32 m0, s53
	s_nop 0
	buffer_load_dwordx4 v176, s[36:39], s62 offen lds
	s_waitcnt vmcnt(8)
	s_waitcnt lgkmcnt(0)
	s_barrier
	s_setprio 1
	v_mfma_f32_16x16x128_f8f6f4 v[140:143], v[0:7], v[8:15], v[140:143]
	v_mfma_f32_16x16x128_f8f6f4 v[128:131], v[16:23], v[8:15], v[128:131]
	v_mfma_f32_16x16x128_f8f6f4 v[108:111], v[0:7], v[24:31], v[108:111]
	v_mfma_f32_16x16x128_f8f6f4 v[104:107], v[16:23], v[24:31], v[104:107]
	v_mfma_f32_16x16x128_f8f6f4 v[92:95], v[0:7], v[32:39], v[168:171]
	v_mfma_f32_16x16x128_f8f6f4 v[88:91], v[16:23], v[32:39], v[190:193]
	v_mfma_f32_16x16x128_f8f6f4 v[76:79], v[0:7], v[40:47], v[210:213]
	v_mfma_f32_16x16x128_f8f6f4 v[72:75], v[16:23], v[40:47], v[214:217]
	v_mfma_f32_16x16x128_f8f6f4 v[116:119], v[120:127], v[8:15], v[116:119]
	v_mfma_f32_16x16x128_f8f6f4 v[112:115], v[132:139], v[8:15], v[112:115]
	v_mfma_f32_16x16x128_f8f6f4 v[100:103], v[120:127], v[24:31], v[100:103]
	v_mfma_f32_16x16x128_f8f6f4 v[96:99], v[132:139], v[24:31], v[96:99]
	v_mfma_f32_16x16x128_f8f6f4 v[84:87], v[120:127], v[32:39], v[160:163]
	v_mfma_f32_16x16x128_f8f6f4 v[80:83], v[132:139], v[32:39], v[164:167]
	v_mfma_f32_16x16x128_f8f6f4 v[68:71], v[120:127], v[40:47], v[182:185]
	v_mfma_f32_16x16x128_f8f6f4 v[64:67], v[132:139], v[40:47], v[186:189]
	s_setprio 0
	s_barrier
	s_mov_b32 m0, s56
	s_bitset1_b32 s55, 7
	buffer_load_dwordx4 v175, s[12:15], s55 offen lds
	s_mov_b32 m0, s57
	ds_read_b128 v[32:35], v181 offset:49152
	buffer_load_dwordx4 v177, s[12:15], s55 offen lds
	s_add_i32 s55, s55, s42
	s_mov_b32 m0, s65
	ds_read_b128 v[36:39], v181 offset:50176
	buffer_load_dwordx4 v175, s[12:15], s55 offen lds
	s_mov_b32 m0, s76
	ds_read_b128 v[144:147], v181 offset:51200
	buffer_load_dwordx4 v177, s[12:15], s55 offen lds
	s_mov_b32 m0, s58
	ds_read_b128 v[148:151], v181 offset:52224
	buffer_load_dwordx4 v174, s[36:39], s54 offen lds
	s_mov_b32 m0, s59
	ds_read_b128 v[152:155], v181 offset:53248
	buffer_load_dwordx4 v176, s[36:39], s54 offen lds
	ds_read_b128 v[156:159], v181 offset:54272
	ds_read_b128 v[160:163], v181 offset:55296
	ds_read_b128 v[164:167], v181 offset:56320
	s_waitcnt vmcnt(8)
	s_waitcnt lgkmcnt(0)
	s_barrier
	s_setprio 1
	v_mfma_f32_16x16x128_f8f6f4 v[60:63], v[0:7], v[32:39], v[60:63]
	v_mfma_f32_16x16x128_f8f6f4 v[56:59], v[16:23], v[32:39], v[56:59]
	v_mfma_f32_16x16x128_f8f6f4 v[44:47], v[0:7], v[144:151], v[194:197]
	v_mfma_f32_16x16x128_f8f6f4 v[40:43], v[16:23], v[144:151], v[198:201]
	v_mfma_f32_16x16x128_f8f6f4 v[28:31], v[0:7], v[152:159], v[202:205]
	v_mfma_f32_16x16x128_f8f6f4 v[24:27], v[16:23], v[152:159], v[206:209]
	v_mfma_f32_16x16x128_f8f6f4 v[12:15], v[0:7], v[160:167], v[218:221]
	v_mfma_f32_16x16x128_f8f6f4 v[8:11], v[16:23], v[160:167], v[226:229]
	v_mfma_f32_16x16x128_f8f6f4 v[52:55], v[120:127], v[32:39], v[52:55]
	v_mfma_f32_16x16x128_f8f6f4 v[48:51], v[132:139], v[32:39], v[48:51]
	v_mfma_f32_16x16x128_f8f6f4 v[36:39], v[120:127], v[144:151], v[230:233]
	v_mfma_f32_16x16x128_f8f6f4 v[32:35], v[132:139], v[144:151], v[234:237]
	v_mfma_f32_16x16x128_f8f6f4 v[20:23], v[120:127], v[152:159], v[238:241]
	v_mfma_f32_16x16x128_f8f6f4 v[16:19], v[132:139], v[152:159], v[242:245]
	v_mfma_f32_16x16x128_f8f6f4 v[4:7], v[120:127], v[160:167], v[246:249]
	v_mfma_f32_16x16x128_f8f6f4 v[0:3], v[132:139], v[160:167], v[250:253]
	s_setprio 0
	s_barrier
	s_add_i32 s61, s61, 2
	s_addk_i32 s4, 0x100
	s_addk_i32 s5, 0x100
	s_cmp_ge_i32 s61, s82
	s_cbranch_scc0 .LBB0_1990
